# sigmoid reciprocals 1/(1+exp): v_rcp_f32 + one f32 Newton step + v_div_fixup instead of the 11-instruction IEEE division expansion (525 sites; f32 throughout, error < 1 ulp)
# speedup vs baseline: 1.0116x; 1.0089x over previous
; __device__ __forceinline__ float sigmoidf_(float x) { return 1.f / (1.f + __expf(-x)); }
; __device__ __forceinline__ void rwkv_lin_ph(const int WID_, const bf16* __restrict__ proj, const float* __restrict__ mu, bf16* __restrict__ lin, const int row_lo, const int row_hi) {
;     ...
;         for (int i = 0; i < 4; ++i) { const int m = m0 + i; z[i] = *(const uint2*)(proj + (size_t)m * DSHIFT + 1536 + 4 * lane);
;             zp[i] = make_uint2(0, 0); if ((m & (S - 1)) != 0) zp[i] = *(const uint2*)(proj + (size_t)(m - 1) * DSHIFT + 1536 + 4 * lane); }
; #pragma unroll
;         for (int i = 0; i < 4; ++i) {
;             float c[4] = {__builtin_bit_cast(float, z[i].x << 16), __builtin_bit_cast(float, z[i].x & 0xffff0000u), __builtin_bit_cast(float, z[i].y << 16), __builtin_bit_cast(float, z[i].y & 0xffff0000u)};
;             const float q[4] = {__builtin_bit_cast(float, zp[i].x << 16), __builtin_bit_cast(float, zp[i].x & 0xffff0000u), __builtin_bit_cast(float, zp[i].y << 16), __builtin_bit_cast(float, zp[i].y & 0xffff0000u)};
; #pragma unroll
;             for (int e = 0; e < 4; ++e) { float t = c[e] + (q[e] - c[e]) * mm[e];
;                 if (lane < 16) t = 1.f - 2.f / (1.f + __expf(2.f * t));
;                 else if (lane >= 32) t = sigmoidf_(t);
.LBB0_455:
	v_lshl_add_u64 v[8:9], s[50:51], 0, v[4:5]
	global_load_dwordx2 v[12:13], v[8:9], off
	v_lshl_add_u64 v[8:9], s[46:47], 0, v[4:5]
	global_load_dwordx2 v[10:11], v[8:9], off
	v_lshl_add_u64 v[8:9], s[18:19], 0, v[4:5]
	global_load_dwordx2 v[8:9], v[8:9], off
	s_waitcnt vmcnt(0)
	v_lshlrev_b32_e32 v18, 16, v14
	v_lshlrev_b32_e32 v19, 16, v16
	v_sub_f32_e32 v19, v19, v18
	v_fma_f32 v19, v0, v19, v18
	s_and_saveexec_b64 s[10:11], s[0:1]
	s_xor_b64 s[62:63], exec, s[10:11]
	s_cbranch_execz .LBB0_459
	s_and_saveexec_b64 s[68:69], s[2:3]
	s_cbranch_execz .LBB0_458
	v_mul_f32_e32 v19, 0xbfb8aa3b, v19
	v_exp_f32_e32 v19, v19
	s_nop 0
	v_add_f32_e32 v19, 1.0, v19
	v_rcp_f32_e32 v21, v19
	s_nop 0
	v_fma_f32 v23, -v19, v21, 1.0
	v_fmac_f32_e32 v21, v23, v21
	v_div_fixup_f32 v19, v21, v19, 1.0

; __device__ __forceinline__ float sigmoidf_(float x) { return 1.f / (1.f + __expf(-x)); }
; __device__ __forceinline__ void rwkv_lin_ph(const int WID_, const bf16* __restrict__ proj, const float* __restrict__ mu, bf16* __restrict__ lin, const int row_lo, const int row_hi) {
;     ...
;             for (int e = 0; e < 4; ++e) { float t = c[e] + (q[e] - c[e]) * mm[e];
;                 if (lane < 16) t = 1.f - 2.f / (1.f + __expf(2.f * t));
;                 else if (lane >= 32) t = sigmoidf_(t);
.LBB0_461:
	s_or_b64 exec, exec, s[62:63]
	v_and_b32_e32 v14, 0xffff0000, v14
	v_and_b32_e32 v16, 0xffff0000, v16
	v_sub_f32_e32 v16, v16, v14
	v_fma_f32 v20, v1, v16, v14
	s_and_saveexec_b64 s[10:11], s[0:1]
	s_xor_b64 s[62:63], exec, s[10:11]
	s_cbranch_execz .LBB0_465
	s_and_saveexec_b64 s[68:69], s[2:3]
	s_cbranch_execz .LBB0_464
	v_mul_f32_e32 v16, 0xbfb8aa3b, v20
	v_exp_f32_e32 v16, v16
	s_nop 0
	v_add_f32_e32 v16, 1.0, v16
	v_rcp_f32_e32 v21, v16
	s_nop 0
	v_fma_f32 v23, -v16, v21, 1.0
	v_fmac_f32_e32 v21, v23, v21
	v_div_fixup_f32 v20, v21, v16, 1.0

; __device__ __forceinline__ float sigmoidf_(float x) { return 1.f / (1.f + __expf(-x)); }
; __device__ __forceinline__ void rwkv_lin_ph(const int WID_, const bf16* __restrict__ proj, const float* __restrict__ mu, bf16* __restrict__ lin, const int row_lo, const int row_hi) {
;     ...
;             for (int e = 0; e < 4; ++e) { float t = c[e] + (q[e] - c[e]) * mm[e];
;                 if (lane < 16) t = 1.f - 2.f / (1.f + __expf(2.f * t));
;                 else if (lane >= 32) t = sigmoidf_(t);
.LBB0_467:
	s_or_b64 exec, exec, s[62:63]
	v_lshlrev_b32_e32 v16, 16, v15
	v_lshlrev_b32_e32 v21, 16, v17
	v_sub_f32_e32 v21, v21, v16
	v_fma_f32 v21, v2, v21, v16
	s_and_saveexec_b64 s[10:11], s[0:1]
	s_xor_b64 s[62:63], exec, s[10:11]
	s_cbranch_execz .LBB0_471
	s_and_saveexec_b64 s[68:69], s[2:3]
	s_cbranch_execz .LBB0_470
	v_mul_f32_e32 v21, 0xbfb8aa3b, v21
	v_exp_f32_e32 v21, v21
	s_nop 0
	v_add_f32_e32 v21, 1.0, v21
	v_rcp_f32_e32 v23, v21
	s_nop 0
	v_fma_f32 v25, -v21, v23, 1.0
	v_fmac_f32_e32 v23, v25, v23
	v_div_fixup_f32 v21, v23, v21, 1.0

; __device__ __forceinline__ float sigmoidf_(float x) { return 1.f / (1.f + __expf(-x)); }
; __device__ __forceinline__ void rwkv_lin_ph(const int WID_, const bf16* __restrict__ proj, const float* __restrict__ mu, bf16* __restrict__ lin, const int row_lo, const int row_hi) {
;     ...
;             for (int e = 0; e < 4; ++e) { float t = c[e] + (q[e] - c[e]) * mm[e];
;                 if (lane < 16) t = 1.f - 2.f / (1.f + __expf(2.f * t));
;                 else if (lane >= 32) t = sigmoidf_(t);
.LBB0_473:
	s_or_b64 exec, exec, s[62:63]
	v_and_b32_e32 v15, 0xffff0000, v15
	v_and_b32_e32 v17, 0xffff0000, v17
	v_sub_f32_e32 v17, v17, v15
	v_fma_f32 v17, v3, v17, v15
	s_and_saveexec_b64 s[10:11], s[0:1]
	s_xor_b64 s[62:63], exec, s[10:11]
	s_cbranch_execz .LBB0_477
	s_and_saveexec_b64 s[68:69], s[2:3]
	s_cbranch_execz .LBB0_476
	v_mul_f32_e32 v17, 0xbfb8aa3b, v17
	v_exp_f32_e32 v17, v17
	s_nop 0
	v_add_f32_e32 v17, 1.0, v17
	v_rcp_f32_e32 v23, v17
	s_nop 0
	v_fma_f32 v25, -v17, v23, 1.0
	v_fmac_f32_e32 v23, v25, v23
	v_div_fixup_f32 v17, v23, v17, 1.0

; __device__ __forceinline__ unsigned pk2(float lo, float hi) { const f32x2h v = {lo, hi}; const bf16x2h b = __builtin_convertvector(v, bf16x2h); return __builtin_bit_cast(unsigned, b); }
; __device__ __forceinline__ float sigmoidf_(float x) { return 1.f / (1.f + __expf(-x)); }
; __device__ __forceinline__ void rwkv_lin_ph(const int WID_, const bf16* __restrict__ proj, const float* __restrict__ mu, bf16* __restrict__ lin, const int row_lo, const int row_hi) {
;     ...
;             for (int e = 0; e < 4; ++e) { float t = c[e] + (q[e] - c[e]) * mm[e];
;                 if (lane < 16) t = 1.f - 2.f / (1.f + __expf(2.f * t));
;                 else if (lane >= 32) t = sigmoidf_(t);
;                 c[e] = t; }
;             uint2 o; o.x = pk2(c[0], c[1]); o.y = pk2(c[2], c[3]);
;             *(uint2*)(lin + (size_t)(m0 + i) * 256 + 4 * lane) = o;
.LBB0_479:
	s_or_b64 exec, exec, s[62:63]
	v_cvt_pk_bf16_f32 v21, v21, v17
	v_lshl_add_u64 v[22:23], s[52:53], 0, v[4:5]
	v_lshlrev_b32_e32 v17, 16, v12
	v_add_co_u32_e32 v22, vcc, 0x23000000, v22
	v_sub_f32_e32 v18, v18, v17
	v_cvt_pk_bf16_f32 v20, v19, v20
	v_addc_co_u32_e32 v23, vcc, 0, v23, vcc
	v_fma_f32 v18, v0, v18, v17
	global_store_dwordx2 v[22:23], v[20:21], off
	s_and_saveexec_b64 s[10:11], s[0:1]
	s_xor_b64 s[62:63], exec, s[10:11]
	s_cbranch_execz .LBB0_483
	s_and_saveexec_b64 s[68:69], s[2:3]
	s_cbranch_execz .LBB0_482
	v_mul_f32_e32 v18, 0xbfb8aa3b, v18
	v_exp_f32_e32 v18, v18
	s_nop 0
	v_add_f32_e32 v18, 1.0, v18
	v_rcp_f32_e32 v20, v18
	s_nop 0
	v_fma_f32 v22, -v18, v20, 1.0
	v_fmac_f32_e32 v20, v22, v20
	v_div_fixup_f32 v18, v20, v18, 1.0

; __device__ __forceinline__ float sigmoidf_(float x) { return 1.f / (1.f + __expf(-x)); }
; __device__ __forceinline__ void rwkv_lin_ph(const int WID_, const bf16* __restrict__ proj, const float* __restrict__ mu, bf16* __restrict__ lin, const int row_lo, const int row_hi) {
;     ...
;             for (int e = 0; e < 4; ++e) { float t = c[e] + (q[e] - c[e]) * mm[e];
;                 if (lane < 16) t = 1.f - 2.f / (1.f + __expf(2.f * t));
;                 else if (lane >= 32) t = sigmoidf_(t);
.LBB0_485:
	s_or_b64 exec, exec, s[62:63]
	v_and_b32_e32 v12, 0xffff0000, v12
	v_sub_f32_e32 v14, v14, v12
	v_fma_f32 v19, v1, v14, v12
	s_and_saveexec_b64 s[10:11], s[0:1]
	s_xor_b64 s[62:63], exec, s[10:11]
	s_cbranch_execz .LBB0_489
	s_and_saveexec_b64 s[68:69], s[2:3]
	s_cbranch_execz .LBB0_488
	v_mul_f32_e32 v14, 0xbfb8aa3b, v19
	v_exp_f32_e32 v14, v14
	s_nop 0
	v_add_f32_e32 v14, 1.0, v14
	v_rcp_f32_e32 v20, v14
	s_nop 0
	v_fma_f32 v22, -v14, v20, 1.0
	v_fmac_f32_e32 v20, v22, v20
	v_div_fixup_f32 v19, v20, v14, 1.0

; __device__ __forceinline__ float sigmoidf_(float x) { return 1.f / (1.f + __expf(-x)); }
; __device__ __forceinline__ void rwkv_lin_ph(const int WID_, const bf16* __restrict__ proj, const float* __restrict__ mu, bf16* __restrict__ lin, const int row_lo, const int row_hi) {
;     ...
;             for (int e = 0; e < 4; ++e) { float t = c[e] + (q[e] - c[e]) * mm[e];
;                 if (lane < 16) t = 1.f - 2.f / (1.f + __expf(2.f * t));
;                 else if (lane >= 32) t = sigmoidf_(t);
.LBB0_491:
	s_or_b64 exec, exec, s[62:63]
	v_lshlrev_b32_e32 v14, 16, v13
	v_sub_f32_e32 v16, v16, v14
	v_fma_f32 v20, v2, v16, v14
	s_and_saveexec_b64 s[10:11], s[0:1]
	s_xor_b64 s[62:63], exec, s[10:11]
	s_cbranch_execz .LBB0_495
	s_and_saveexec_b64 s[68:69], s[2:3]
	s_cbranch_execz .LBB0_494
	v_mul_f32_e32 v16, 0xbfb8aa3b, v20
	v_exp_f32_e32 v16, v16
	s_nop 0
	v_add_f32_e32 v16, 1.0, v16
	v_rcp_f32_e32 v21, v16
	s_nop 0
	v_fma_f32 v23, -v16, v21, 1.0
	v_fmac_f32_e32 v21, v23, v21
	v_div_fixup_f32 v20, v21, v16, 1.0

; __device__ __forceinline__ float sigmoidf_(float x) { return 1.f / (1.f + __expf(-x)); }
; __device__ __forceinline__ void rwkv_lin_ph(const int WID_, const bf16* __restrict__ proj, const float* __restrict__ mu, bf16* __restrict__ lin, const int row_lo, const int row_hi) {
;     ...
;             for (int e = 0; e < 4; ++e) { float t = c[e] + (q[e] - c[e]) * mm[e];
;                 if (lane < 16) t = 1.f - 2.f / (1.f + __expf(2.f * t));
;                 else if (lane >= 32) t = sigmoidf_(t);
.LBB0_497:
	s_or_b64 exec, exec, s[62:63]
	v_and_b32_e32 v16, 0xffff0000, v13
	v_sub_f32_e32 v13, v15, v16
	v_fma_f32 v13, v3, v13, v16
	s_and_saveexec_b64 s[10:11], s[0:1]
	s_xor_b64 s[62:63], exec, s[10:11]
	s_cbranch_execz .LBB0_501
	s_and_saveexec_b64 s[68:69], s[2:3]
	s_cbranch_execz .LBB0_500
	v_mul_f32_e32 v13, 0xbfb8aa3b, v13
	v_exp_f32_e32 v13, v13
	s_nop 0
	v_add_f32_e32 v13, 1.0, v13
	v_rcp_f32_e32 v21, v13
	s_nop 0
	v_fma_f32 v23, -v13, v21, 1.0
	v_fmac_f32_e32 v21, v23, v21
	v_div_fixup_f32 v13, v21, v13, 1.0

; __device__ __forceinline__ unsigned pk2(float lo, float hi) { const f32x2h v = {lo, hi}; const bf16x2h b = __builtin_convertvector(v, bf16x2h); return __builtin_bit_cast(unsigned, b); }
; __device__ __forceinline__ float sigmoidf_(float x) { return 1.f / (1.f + __expf(-x)); }
; __device__ __forceinline__ void rwkv_lin_ph(const int WID_, const bf16* __restrict__ proj, const float* __restrict__ mu, bf16* __restrict__ lin, const int row_lo, const int row_hi) {
;     ...
;             for (int e = 0; e < 4; ++e) { float t = c[e] + (q[e] - c[e]) * mm[e];
;                 if (lane < 16) t = 1.f - 2.f / (1.f + __expf(2.f * t));
;                 else if (lane >= 32) t = sigmoidf_(t);
;                 c[e] = t; }
;             uint2 o; o.x = pk2(c[0], c[1]); o.y = pk2(c[2], c[3]);
;             *(uint2*)(lin + (size_t)(m0 + i) * 256 + 4 * lane) = o;
.LBB0_503:
	s_or_b64 exec, exec, s[62:63]
	v_cvt_pk_bf16_f32 v18, v18, v19
	v_cvt_pk_bf16_f32 v19, v20, v13
	v_lshl_add_u64 v[20:21], s[48:49], 0, v[4:5]
	v_lshlrev_b32_e32 v15, 16, v10
	v_add_co_u32_e32 v20, vcc, 0x23000000, v20
	v_sub_f32_e32 v13, v17, v15
	s_nop 0
	v_addc_co_u32_e32 v21, vcc, 0, v21, vcc
	v_fma_f32 v17, v0, v13, v15
	global_store_dwordx2 v[20:21], v[18:19], off
	s_and_saveexec_b64 s[10:11], s[0:1]
	s_xor_b64 s[62:63], exec, s[10:11]
	s_cbranch_execz .LBB0_507
	s_and_saveexec_b64 s[68:69], s[2:3]
	s_cbranch_execz .LBB0_506
	v_mul_f32_e32 v13, 0xbfb8aa3b, v17
	v_exp_f32_e32 v13, v13
	s_nop 0
	v_add_f32_e32 v13, 1.0, v13
	v_rcp_f32_e32 v18, v13
	s_nop 0
	v_fma_f32 v20, -v13, v18, 1.0
	v_fmac_f32_e32 v18, v20, v18
	v_div_fixup_f32 v17, v18, v13, 1.0

; __device__ __forceinline__ float sigmoidf_(float x) { return 1.f / (1.f + __expf(-x)); }
; __device__ __forceinline__ void rwkv_lin_ph(const int WID_, const bf16* __restrict__ proj, const float* __restrict__ mu, bf16* __restrict__ lin, const int row_lo, const int row_hi) {
;     ...
;             for (int e = 0; e < 4; ++e) { float t = c[e] + (q[e] - c[e]) * mm[e];
;                 if (lane < 16) t = 1.f - 2.f / (1.f + __expf(2.f * t));
;                 else if (lane >= 32) t = sigmoidf_(t);
.LBB0_509:
	s_or_b64 exec, exec, s[62:63]
	v_and_b32_e32 v13, 0xffff0000, v10
	v_sub_f32_e32 v10, v12, v13
	v_fma_f32 v18, v1, v10, v13
	s_and_saveexec_b64 s[10:11], s[0:1]
	s_xor_b64 s[62:63], exec, s[10:11]
	s_cbranch_execz .LBB0_513
	s_and_saveexec_b64 s[68:69], s[2:3]
	s_cbranch_execz .LBB0_512
	v_mul_f32_e32 v10, 0xbfb8aa3b, v18
	v_exp_f32_e32 v10, v10
	s_nop 0
	v_add_f32_e32 v10, 1.0, v10
	v_rcp_f32_e32 v18, v10
	s_nop 0
	v_fma_f32 v20, -v10, v18, 1.0
	v_fmac_f32_e32 v18, v20, v18
	v_div_fixup_f32 v18, v18, v10, 1.0

; __device__ __forceinline__ float sigmoidf_(float x) { return 1.f / (1.f + __expf(-x)); }
; __device__ __forceinline__ void rwkv_lin_ph(const int WID_, const bf16* __restrict__ proj, const float* __restrict__ mu, bf16* __restrict__ lin, const int row_lo, const int row_hi) {
;     ...
;             for (int e = 0; e < 4; ++e) { float t = c[e] + (q[e] - c[e]) * mm[e];
;                 if (lane < 16) t = 1.f - 2.f / (1.f + __expf(2.f * t));
;                 else if (lane >= 32) t = sigmoidf_(t);
.LBB0_515:
	s_or_b64 exec, exec, s[62:63]
	v_lshlrev_b32_e32 v12, 16, v11
	v_sub_f32_e32 v10, v14, v12
	v_fma_f32 v14, v2, v10, v12
	s_and_saveexec_b64 s[10:11], s[0:1]
	s_xor_b64 s[62:63], exec, s[10:11]
	s_cbranch_execz .LBB0_519
	s_and_saveexec_b64 s[68:69], s[2:3]
	s_cbranch_execz .LBB0_518
	v_mul_f32_e32 v10, 0xbfb8aa3b, v14
	v_exp_f32_e32 v10, v10
	s_nop 0
	v_add_f32_e32 v10, 1.0, v10
	v_rcp_f32_e32 v19, v10
	s_nop 0
	v_fma_f32 v21, -v10, v19, 1.0
	v_fmac_f32_e32 v19, v21, v19
	v_div_fixup_f32 v14, v19, v10, 1.0

; __device__ __forceinline__ float sigmoidf_(float x) { return 1.f / (1.f + __expf(-x)); }
; __device__ __forceinline__ void rwkv_lin_ph(const int WID_, const bf16* __restrict__ proj, const float* __restrict__ mu, bf16* __restrict__ lin, const int row_lo, const int row_hi) {
;     ...
;             for (int e = 0; e < 4; ++e) { float t = c[e] + (q[e] - c[e]) * mm[e];
;                 if (lane < 16) t = 1.f - 2.f / (1.f + __expf(2.f * t));
;                 else if (lane >= 32) t = sigmoidf_(t);
.LBB0_521:
	s_or_b64 exec, exec, s[62:63]
	v_and_b32_e32 v10, 0xffff0000, v11
	v_sub_f32_e32 v11, v16, v10
	v_fma_f32 v11, v3, v11, v10
	s_and_saveexec_b64 s[10:11], s[0:1]
	s_xor_b64 s[62:63], exec, s[10:11]
	s_cbranch_execz .LBB0_525
	s_and_saveexec_b64 s[68:69], s[2:3]
	s_cbranch_execz .LBB0_524
	v_mul_f32_e32 v11, 0xbfb8aa3b, v11
	v_exp_f32_e32 v11, v11
	s_nop 0
	v_add_f32_e32 v11, 1.0, v11
	v_rcp_f32_e32 v19, v11
	s_nop 0
	v_fma_f32 v21, -v11, v19, 1.0
	v_fmac_f32_e32 v19, v21, v19
	v_div_fixup_f32 v11, v19, v11, 1.0

; __device__ __forceinline__ unsigned pk2(float lo, float hi) { const f32x2h v = {lo, hi}; const bf16x2h b = __builtin_convertvector(v, bf16x2h); return __builtin_bit_cast(unsigned, b); }
; __device__ __forceinline__ float sigmoidf_(float x) { return 1.f / (1.f + __expf(-x)); }
; __device__ __forceinline__ void rwkv_lin_ph(const int WID_, const bf16* __restrict__ proj, const float* __restrict__ mu, bf16* __restrict__ lin, const int row_lo, const int row_hi) {
;     ...
;             for (int e = 0; e < 4; ++e) { float t = c[e] + (q[e] - c[e]) * mm[e];
;                 if (lane < 16) t = 1.f - 2.f / (1.f + __expf(2.f * t));
;                 else if (lane >= 32) t = sigmoidf_(t);
;                 c[e] = t; }
;             uint2 o; o.x = pk2(c[0], c[1]); o.y = pk2(c[2], c[3]);
;             *(uint2*)(lin + (size_t)(m0 + i) * 256 + 4 * lane) = o;
.LBB0_527:
	s_or_b64 exec, exec, s[62:63]
	v_cvt_pk_bf16_f32 v16, v17, v18
	v_cvt_pk_bf16_f32 v17, v14, v11
	v_lshl_add_u64 v[18:19], s[44:45], 0, v[4:5]
	v_lshlrev_b32_e32 v11, 16, v8
	v_add_co_u32_e32 v18, vcc, 0x23000000, v18
	v_sub_f32_e32 v14, v15, v11
	s_nop 0
	v_addc_co_u32_e32 v19, vcc, 0, v19, vcc
	v_fmac_f32_e32 v11, v0, v14
	global_store_dwordx2 v[18:19], v[16:17], off
	s_and_saveexec_b64 s[10:11], s[0:1]
	s_xor_b64 s[62:63], exec, s[10:11]
	s_cbranch_execz .LBB0_531
	s_and_saveexec_b64 s[68:69], s[2:3]
	s_cbranch_execz .LBB0_530
	v_mul_f32_e32 v11, 0xbfb8aa3b, v11
	v_exp_f32_e32 v11, v11
	s_nop 0
	v_add_f32_e32 v11, 1.0, v11
	v_rcp_f32_e32 v15, v11
	s_nop 0
	v_fma_f32 v17, -v11, v15, 1.0
	v_fmac_f32_e32 v15, v17, v15
	v_div_fixup_f32 v11, v15, v11, 1.0

; __device__ __forceinline__ float sigmoidf_(float x) { return 1.f / (1.f + __expf(-x)); }
; __device__ __forceinline__ void rwkv_lin_ph(const int WID_, const bf16* __restrict__ proj, const float* __restrict__ mu, bf16* __restrict__ lin, const int row_lo, const int row_hi) {
;     ...
;             for (int e = 0; e < 4; ++e) { float t = c[e] + (q[e] - c[e]) * mm[e];
;                 if (lane < 16) t = 1.f - 2.f / (1.f + __expf(2.f * t));
;                 else if (lane >= 32) t = sigmoidf_(t);
.LBB0_533:
	s_or_b64 exec, exec, s[62:63]
	v_and_b32_e32 v8, 0xffff0000, v8
	v_sub_f32_e32 v13, v13, v8
	v_fmac_f32_e32 v8, v1, v13
	s_and_saveexec_b64 s[10:11], s[0:1]
	s_xor_b64 s[62:63], exec, s[10:11]
	s_cbranch_execz .LBB0_537
	s_and_saveexec_b64 s[68:69], s[2:3]
	s_cbranch_execz .LBB0_536
	v_mul_f32_e32 v8, 0xbfb8aa3b, v8
	v_exp_f32_e32 v8, v8
	s_nop 0
	v_add_f32_e32 v8, 1.0, v8
	v_rcp_f32_e32 v14, v8
	s_nop 0
	v_fma_f32 v16, -v8, v14, 1.0
	v_fmac_f32_e32 v14, v16, v14
	v_div_fixup_f32 v8, v14, v8, 1.0

; __device__ __forceinline__ float sigmoidf_(float x) { return 1.f / (1.f + __expf(-x)); }
; __device__ __forceinline__ void rwkv_lin_ph(const int WID_, const bf16* __restrict__ proj, const float* __restrict__ mu, bf16* __restrict__ lin, const int row_lo, const int row_hi) {
;     ...
;             for (int e = 0; e < 4; ++e) { float t = c[e] + (q[e] - c[e]) * mm[e];
;                 if (lane < 16) t = 1.f - 2.f / (1.f + __expf(2.f * t));
;                 else if (lane >= 32) t = sigmoidf_(t);
.LBB0_539:
	s_or_b64 exec, exec, s[62:63]
	v_lshlrev_b32_e32 v13, 16, v9
	v_sub_f32_e32 v12, v12, v13
	v_fmac_f32_e32 v13, v2, v12
	s_and_saveexec_b64 s[10:11], s[0:1]
	s_xor_b64 s[62:63], exec, s[10:11]
	s_cbranch_execz .LBB0_543
	s_and_saveexec_b64 s[68:69], s[2:3]
	s_cbranch_execz .LBB0_542
	v_mul_f32_e32 v12, 0xbfb8aa3b, v13
	v_exp_f32_e32 v12, v12
	s_nop 0
	v_add_f32_e32 v12, 1.0, v12
	v_rcp_f32_e32 v14, v12
	s_nop 0
	v_fma_f32 v16, -v12, v14, 1.0
	v_fmac_f32_e32 v14, v16, v14
	v_div_fixup_f32 v13, v14, v12, 1.0

; __device__ __forceinline__ float sigmoidf_(float x) { return 1.f / (1.f + __expf(-x)); }
; __device__ __forceinline__ void rwkv_lin_ph(const int WID_, const bf16* __restrict__ proj, const float* __restrict__ mu, bf16* __restrict__ lin, const int row_lo, const int row_hi) {
;     ...
;             for (int e = 0; e < 4; ++e) { float t = c[e] + (q[e] - c[e]) * mm[e];
;                 if (lane < 16) t = 1.f - 2.f / (1.f + __expf(2.f * t));
;                 else if (lane >= 32) t = sigmoidf_(t);
.LBB0_545:
	s_or_b64 exec, exec, s[62:63]
	v_and_b32_e32 v9, 0xffff0000, v9
	v_sub_f32_e32 v10, v10, v9
	v_fmac_f32_e32 v9, v3, v10
	s_and_saveexec_b64 s[10:11], s[0:1]
	s_xor_b64 s[62:63], exec, s[10:11]
	s_cbranch_execz .LBB0_549
	s_and_saveexec_b64 s[68:69], s[2:3]
	s_cbranch_execz .LBB0_548
	v_mul_f32_e32 v9, 0xbfb8aa3b, v9
	v_exp_f32_e32 v9, v9
	s_nop 0
	v_add_f32_e32 v9, 1.0, v9
	v_rcp_f32_e32 v12, v9
	s_nop 0
	v_fma_f32 v15, -v9, v12, 1.0
	v_fmac_f32_e32 v12, v15, v12
	v_div_fixup_f32 v9, v12, v9, 1.0

; __device__ __forceinline__ float sigmoidf_(float x) { return 1.f / (1.f + __expf(-x)); }
;     __device__ __forceinline__ void operator()(const f32x4 (&acc)[2][2][4][2], const Unit& u, int wr, int wc, int fr, int fq) const {
;     ...
;                     const f32x4 v0 = acc[ai][bj][m][0] + b0, v1 = acc[ai][bj][m][1] + b1; float o[8];
; #pragma unroll
;                     for (int e = 0; e < 8; ++e) { float x = (e < 4) ? v0[e & 3] : v1[e & 3];
;                         if (kind == 0) x = -0.6065306597126334f * sigmoidf_(x);
;                         else if (kind == 1) x = sigmoidf_(x);
;                         o[e] = x; }
.LBB0_573:
	v_cndmask_b32_e64 v157, 0, 1, s[0:1]
	s_waitcnt vmcnt(0)
	v_add_f32_e32 v132, v132, v88
	s_mov_b64 s[2:3], -1
	s_and_b64 vcc, exec, s[78:79]
	v_cmp_ne_u32_e64 s[0:1], 1, v157
	s_cbranch_vccz .LBB0_577
	s_and_b64 vcc, exec, s[0:1]
	v_mov_b32_e32 v157, v132
	s_cbranch_vccnz .LBB0_576
	v_mul_f32_e32 v157, 0xbfb8aa3b, v132
	v_exp_f32_e32 v157, v157
	s_nop 0
	v_add_f32_e32 v157, 1.0, v157
	v_rcp_f32_e32 v159, v157
	s_nop 0
	v_fma_f32 v161, -v157, v159, 1.0
	v_fmac_f32_e32 v159, v161, v159
	v_div_fixup_f32 v157, v159, v157, 1.0

; __device__ __forceinline__ float sigmoidf_(float x) { return 1.f / (1.f + __expf(-x)); }
;     __device__ __forceinline__ void operator()(const f32x4 (&acc)[2][2][4][2], const Unit& u, int wr, int wc, int fr, int fq) const {
;     ...
;                     const f32x4 v0 = acc[ai][bj][m][0] + b0, v1 = acc[ai][bj][m][1] + b1; float o[8];
; #pragma unroll
;                     for (int e = 0; e < 8; ++e) { float x = (e < 4) ? v0[e & 3] : v1[e & 3];
;                         if (kind == 0) x = -0.6065306597126334f * sigmoidf_(x);
;                         else if (kind == 1) x = sigmoidf_(x);
;                         o[e] = x; }
.LBB0_577:
	s_andn2_b64 vcc, exec, s[2:3]
	s_cbranch_vccnz .LBB0_579
	v_mul_f32_e32 v132, 0xbfb8aa3b, v132
	v_exp_f32_e32 v132, v132
	s_nop 0
	v_add_f32_e32 v132, 1.0, v132
	v_rcp_f32_e32 v158, v132
	s_nop 0
	v_fma_f32 v160, -v132, v158, 1.0
	v_fmac_f32_e32 v158, v160, v158
	v_div_fixup_f32 v132, v158, v132, 1.0
	v_mul_f32_e32 v157, 0xbf1b4598, v132
.LBB0_579:
	v_add_f32_e32 v132, v133, v89
	v_cndmask_b32_e64 v133, 0, 1, s[78:79]
	v_cmp_ne_u32_e64 s[2:3], 1, v133
	s_andn2_b64 vcc, exec, s[78:79]
	s_mov_b64 s[78:79], -1
	s_cbranch_vccnz .LBB0_583
	s_and_b64 vcc, exec, s[0:1]
	v_mov_b32_e32 v158, v132
	s_cbranch_vccnz .LBB0_582
	v_mul_f32_e32 v133, 0xbfb8aa3b, v132
	v_exp_f32_e32 v133, v133
	s_nop 0
	v_add_f32_e32 v133, 1.0, v133
	v_rcp_f32_e32 v159, v133
	s_nop 0
	v_fma_f32 v161, -v133, v159, 1.0
	v_fmac_f32_e32 v159, v161, v159
	v_div_fixup_f32 v158, v159, v133, 1.0

; __device__ __forceinline__ float sigmoidf_(float x) { return 1.f / (1.f + __expf(-x)); }
;     __device__ __forceinline__ void operator()(const f32x4 (&acc)[2][2][4][2], const Unit& u, int wr, int wc, int fr, int fq) const {
;     ...
;                     const f32x4 v0 = acc[ai][bj][m][0] + b0, v1 = acc[ai][bj][m][1] + b1; float o[8];
; #pragma unroll
;                     for (int e = 0; e < 8; ++e) { float x = (e < 4) ? v0[e & 3] : v1[e & 3];
;                         if (kind == 0) x = -0.6065306597126334f * sigmoidf_(x);
;                         else if (kind == 1) x = sigmoidf_(x);
;                         o[e] = x; }
.LBB0_584:
	v_mul_f32_e32 v132, 0xbfb8aa3b, v132
	v_exp_f32_e32 v132, v132
	s_nop 0
	v_add_f32_e32 v132, 1.0, v132
	v_rcp_f32_e32 v158, v132
	s_nop 0
	v_fma_f32 v160, -v132, v158, 1.0
	v_fmac_f32_e32 v158, v160, v158
	v_div_fixup_f32 v132, v158, v132, 1.0
	v_mul_f32_e32 v158, 0xbf1b4598, v132
.LBB0_585:
	v_add_f32_e32 v132, v134, v90
	s_and_b64 vcc, exec, s[2:3]
	s_mov_b64 s[78:79], -1
	s_cbranch_vccnz .LBB0_589
	s_and_b64 vcc, exec, s[0:1]
	v_mov_b32_e32 v134, v132
	s_cbranch_vccnz .LBB0_588
	v_mul_f32_e32 v133, 0xbfb8aa3b, v132
	v_exp_f32_e32 v133, v133
	s_nop 0
	v_add_f32_e32 v133, 1.0, v133
	v_rcp_f32_e32 v159, v133
	s_nop 0
	v_fma_f32 v161, -v133, v159, 1.0
	v_fmac_f32_e32 v159, v161, v159
	v_div_fixup_f32 v134, v159, v133, 1.0

; __device__ __forceinline__ unsigned cvt_pk_bf16(float lo, float hi) { const f32x2c v = {lo, hi}; const bf16x2c b = __builtin_convertvector(v, bf16x2c); return __builtin_bit_cast(unsigned, b); }
; __device__ __forceinline__ float sigmoidf_(float x) { return 1.f / (1.f + __expf(-x)); }
;     __device__ __forceinline__ void operator()(const f32x4 (&acc)[2][2][4][2], const Unit& u, int wr, int wc, int fr, int fq) const {
;     ...
;         for (int bj = 0; bj < 2; ++bj) { const int col = (col0 + bj * HALF) & 511;
;             f32x4 b0 = (f32x4){0.f, 0.f, 0.f, 0.f}, b1 = b0;
;             if (kind == 0) { b0 = *(const f32x4*)(w0 + col); b1 = *(const f32x4*)(w0 + col + 4); }
;             else if (kind == 1) { b0 = *(const f32x4*)(a0 + col); b1 = *(const f32x4*)(a0 + col + 4); }
; #pragma unroll
;             for (int ai = 0; ai < 2; ++ai)
; #pragma unroll
;                 for (int m = 0; m < 4; ++m) { const size_t row = (size_t)(row0 + ai * HALF + m * 16);
;                     const f32x4 v0 = acc[ai][bj][m][0] + b0, v1 = acc[ai][bj][m][1] + b1; float o[8];
; #pragma unroll
;                     for (int e = 0; e < 8; ++e) { float x = (e < 4) ? v0[e & 3] : v1[e & 3];
;                         if (kind == 0) x = -0.6065306597126334f * sigmoidf_(x);
;                         else if (kind == 1) x = sigmoidf_(x);
;                         o[e] = x; }
;                     u32x4 w; w.x = cvt_pk_bf16(o[0], o[1]); w.y = cvt_pk_bf16(o[2], o[3]); w.z = cvt_pk_bf16(o[4], o[5]); w.w = cvt_pk_bf16(o[6], o[7]);
;                     *(u32x4*)(O + row * 512 + col) = w; } }
.LBB0_590:
	v_mul_f32_e32 v132, 0xbfb8aa3b, v132
	v_exp_f32_e32 v132, v132
	s_nop 0
	v_add_f32_e32 v132, 1.0, v132
	v_rcp_f32_e32 v134, v132
	s_nop 0
	v_fma_f32 v160, -v132, v134, 1.0
	v_fmac_f32_e32 v134, v160, v134
	v_div_fixup_f32 v132, v134, v132, 1.0
	v_mul_f32_e32 v134, 0xbf1b4598, v132
.LBB0_591:
	v_add_f32_e32 v132, v135, v91
	s_and_b64 vcc, exec, s[2:3]
	s_mov_b64 s[78:79], -1
	s_cbranch_vccnz .LBB0_595
	s_and_b64 vcc, exec, s[0:1]
	v_mov_b32_e32 v135, v132
	s_cbranch_vccnz .LBB0_594
	v_mul_f32_e32 v133, 0xbfb8aa3b, v132
	v_exp_f32_e32 v133, v133
	s_nop 0
	v_add_f32_e32 v133, 1.0, v133
	v_rcp_f32_e32 v159, v133
	s_nop 0
	v_fma_f32 v161, -v133, v159, 1.0
	v_fmac_f32_e32 v159, v161, v159
	v_div_fixup_f32 v135, v159, v133, 1.0

; __device__ __forceinline__ unsigned cvt_pk_bf16(float lo, float hi) { const f32x2c v = {lo, hi}; const bf16x2c b = __builtin_convertvector(v, bf16x2c); return __builtin_bit_cast(unsigned, b); }
; __device__ __forceinline__ float sigmoidf_(float x) { return 1.f / (1.f + __expf(-x)); }
;     __device__ __forceinline__ void operator()(const f32x4 (&acc)[2][2][4][2], const Unit& u, int wr, int wc, int fr, int fq) const {
;     ...
;         for (int bj = 0; bj < 2; ++bj) { const int col = (col0 + bj * HALF) & 511;
;             f32x4 b0 = (f32x4){0.f, 0.f, 0.f, 0.f}, b1 = b0;
;             if (kind == 0) { b0 = *(const f32x4*)(w0 + col); b1 = *(const f32x4*)(w0 + col + 4); }
;             else if (kind == 1) { b0 = *(const f32x4*)(a0 + col); b1 = *(const f32x4*)(a0 + col + 4); }
; #pragma unroll
;             for (int ai = 0; ai < 2; ++ai)
; #pragma unroll
;                 for (int m = 0; m < 4; ++m) { const size_t row = (size_t)(row0 + ai * HALF + m * 16);
;                     const f32x4 v0 = acc[ai][bj][m][0] + b0, v1 = acc[ai][bj][m][1] + b1; float o[8];
; #pragma unroll
;                     for (int e = 0; e < 8; ++e) { float x = (e < 4) ? v0[e & 3] : v1[e & 3];
;                         if (kind == 0) x = -0.6065306597126334f * sigmoidf_(x);
;                         else if (kind == 1) x = sigmoidf_(x);
;                         o[e] = x; }
;                     u32x4 w; w.x = cvt_pk_bf16(o[0], o[1]); w.y = cvt_pk_bf16(o[2], o[3]); w.z = cvt_pk_bf16(o[4], o[5]); w.w = cvt_pk_bf16(o[6], o[7]);
;                     *(u32x4*)(O + row * 512 + col) = w; } }
.LBB0_596:
	v_mul_f32_e32 v132, 0xbfb8aa3b, v132
	v_exp_f32_e32 v132, v132
	s_nop 0
	v_add_f32_e32 v132, 1.0, v132
	v_rcp_f32_e32 v135, v132
	s_nop 0
	v_fma_f32 v160, -v132, v135, 1.0
	v_fmac_f32_e32 v135, v160, v135
	v_div_fixup_f32 v132, v135, v132, 1.0
	v_mul_f32_e32 v135, 0xbf1b4598, v132
.LBB0_597:
	v_add_f32_e32 v132, v128, v80
	s_and_b64 vcc, exec, s[2:3]
	s_mov_b64 s[78:79], -1
	s_cbranch_vccnz .LBB0_601
	s_and_b64 vcc, exec, s[0:1]
	v_mov_b32_e32 v128, v132
	s_cbranch_vccnz .LBB0_600
	v_mul_f32_e32 v128, 0xbfb8aa3b, v132
	v_exp_f32_e32 v128, v128
	s_nop 0
	v_add_f32_e32 v128, 1.0, v128
	v_rcp_f32_e32 v159, v128
	s_nop 0
	v_fma_f32 v161, -v128, v159, 1.0
	v_fmac_f32_e32 v159, v161, v159
	v_div_fixup_f32 v128, v159, v128, 1.0

; __device__ __forceinline__ unsigned cvt_pk_bf16(float lo, float hi) { const f32x2c v = {lo, hi}; const bf16x2c b = __builtin_convertvector(v, bf16x2c); return __builtin_bit_cast(unsigned, b); }
; __device__ __forceinline__ float sigmoidf_(float x) { return 1.f / (1.f + __expf(-x)); }
;     __device__ __forceinline__ void operator()(const f32x4 (&acc)[2][2][4][2], const Unit& u, int wr, int wc, int fr, int fq) const {
;     ...
;         for (int bj = 0; bj < 2; ++bj) { const int col = (col0 + bj * HALF) & 511;
;             f32x4 b0 = (f32x4){0.f, 0.f, 0.f, 0.f}, b1 = b0;
;             if (kind == 0) { b0 = *(const f32x4*)(w0 + col); b1 = *(const f32x4*)(w0 + col + 4); }
;             else if (kind == 1) { b0 = *(const f32x4*)(a0 + col); b1 = *(const f32x4*)(a0 + col + 4); }
; #pragma unroll
;             for (int ai = 0; ai < 2; ++ai)
; #pragma unroll
;                 for (int m = 0; m < 4; ++m) { const size_t row = (size_t)(row0 + ai * HALF + m * 16);
;                     const f32x4 v0 = acc[ai][bj][m][0] + b0, v1 = acc[ai][bj][m][1] + b1; float o[8];
; #pragma unroll
;                     for (int e = 0; e < 8; ++e) { float x = (e < 4) ? v0[e & 3] : v1[e & 3];
;                         if (kind == 0) x = -0.6065306597126334f * sigmoidf_(x);
;                         else if (kind == 1) x = sigmoidf_(x);
;                         o[e] = x; }
;                     u32x4 w; w.x = cvt_pk_bf16(o[0], o[1]); w.y = cvt_pk_bf16(o[2], o[3]); w.z = cvt_pk_bf16(o[4], o[5]); w.w = cvt_pk_bf16(o[6], o[7]);
;                     *(u32x4*)(O + row * 512 + col) = w; } }
.LBB0_602:
	v_mul_f32_e32 v128, 0xbfb8aa3b, v132
	v_exp_f32_e32 v128, v128
	s_nop 0
	v_add_f32_e32 v128, 1.0, v128
	v_rcp_f32_e32 v133, v128
	s_nop 0
	v_fma_f32 v160, -v128, v133, 1.0
	v_fmac_f32_e32 v133, v160, v133
	v_div_fixup_f32 v128, v133, v128, 1.0
	v_mul_f32_e32 v128, 0xbf1b4598, v128
.LBB0_603:
	v_add_f32_e32 v132, v129, v81
	s_and_b64 vcc, exec, s[2:3]
	s_mov_b64 s[78:79], -1
	s_cbranch_vccnz .LBB0_607
	s_and_b64 vcc, exec, s[0:1]
	v_mov_b32_e32 v129, v132
	s_cbranch_vccnz .LBB0_606
	v_mul_f32_e32 v129, 0xbfb8aa3b, v132
	v_exp_f32_e32 v129, v129
	s_nop 0
	v_add_f32_e32 v129, 1.0, v129
	v_rcp_f32_e32 v159, v129
	s_nop 0
	v_fma_f32 v161, -v129, v159, 1.0
	v_fmac_f32_e32 v159, v161, v159
	v_div_fixup_f32 v129, v159, v129, 1.0

; __device__ __forceinline__ unsigned cvt_pk_bf16(float lo, float hi) { const f32x2c v = {lo, hi}; const bf16x2c b = __builtin_convertvector(v, bf16x2c); return __builtin_bit_cast(unsigned, b); }
; __device__ __forceinline__ float sigmoidf_(float x) { return 1.f / (1.f + __expf(-x)); }
;     __device__ __forceinline__ void operator()(const f32x4 (&acc)[2][2][4][2], const Unit& u, int wr, int wc, int fr, int fq) const {
;     ...
;         for (int bj = 0; bj < 2; ++bj) { const int col = (col0 + bj * HALF) & 511;
;             f32x4 b0 = (f32x4){0.f, 0.f, 0.f, 0.f}, b1 = b0;
;             if (kind == 0) { b0 = *(const f32x4*)(w0 + col); b1 = *(const f32x4*)(w0 + col + 4); }
;             else if (kind == 1) { b0 = *(const f32x4*)(a0 + col); b1 = *(const f32x4*)(a0 + col + 4); }
; #pragma unroll
;             for (int ai = 0; ai < 2; ++ai)
; #pragma unroll
;                 for (int m = 0; m < 4; ++m) { const size_t row = (size_t)(row0 + ai * HALF + m * 16);
;                     const f32x4 v0 = acc[ai][bj][m][0] + b0, v1 = acc[ai][bj][m][1] + b1; float o[8];
; #pragma unroll
;                     for (int e = 0; e < 8; ++e) { float x = (e < 4) ? v0[e & 3] : v1[e & 3];
;                         if (kind == 0) x = -0.6065306597126334f * sigmoidf_(x);
;                         else if (kind == 1) x = sigmoidf_(x);
;                         o[e] = x; }
;                     u32x4 w; w.x = cvt_pk_bf16(o[0], o[1]); w.y = cvt_pk_bf16(o[2], o[3]); w.z = cvt_pk_bf16(o[4], o[5]); w.w = cvt_pk_bf16(o[6], o[7]);
;                     *(u32x4*)(O + row * 512 + col) = w; } }
.LBB0_608:
	v_mul_f32_e32 v129, 0xbfb8aa3b, v132
	v_exp_f32_e32 v129, v129
	s_nop 0
	v_add_f32_e32 v129, 1.0, v129
	v_rcp_f32_e32 v133, v129
	s_nop 0
	v_fma_f32 v160, -v129, v133, 1.0
	v_fmac_f32_e32 v133, v160, v133
	v_div_fixup_f32 v129, v133, v129, 1.0
	v_mul_f32_e32 v129, 0xbf1b4598, v129
.LBB0_609:
	v_add_f32_e32 v130, v130, v82
	s_and_b64 vcc, exec, s[2:3]
	s_mov_b64 s[78:79], -1
	s_cbranch_vccnz .LBB0_613
	s_and_b64 vcc, exec, s[0:1]
	v_mov_b32_e32 v159, v130
	s_cbranch_vccnz .LBB0_612
	v_mul_f32_e32 v132, 0xbfb8aa3b, v130
	v_exp_f32_e32 v132, v132
	s_nop 0
	v_add_f32_e32 v132, 1.0, v132
	v_rcp_f32_e32 v159, v132
	s_nop 0
	v_fma_f32 v161, -v132, v159, 1.0
	v_fmac_f32_e32 v159, v161, v159
	v_div_fixup_f32 v159, v159, v132, 1.0

; __device__ __forceinline__ unsigned cvt_pk_bf16(float lo, float hi) { const f32x2c v = {lo, hi}; const bf16x2c b = __builtin_convertvector(v, bf16x2c); return __builtin_bit_cast(unsigned, b); }
; __device__ __forceinline__ float sigmoidf_(float x) { return 1.f / (1.f + __expf(-x)); }
;     __device__ __forceinline__ void operator()(const f32x4 (&acc)[2][2][4][2], const Unit& u, int wr, int wc, int fr, int fq) const {
;     ...
;         for (int bj = 0; bj < 2; ++bj) { const int col = (col0 + bj * HALF) & 511;
;             f32x4 b0 = (f32x4){0.f, 0.f, 0.f, 0.f}, b1 = b0;
;             if (kind == 0) { b0 = *(const f32x4*)(w0 + col); b1 = *(const f32x4*)(w0 + col + 4); }
;             else if (kind == 1) { b0 = *(const f32x4*)(a0 + col); b1 = *(const f32x4*)(a0 + col + 4); }
; #pragma unroll
;             for (int ai = 0; ai < 2; ++ai)
; #pragma unroll
;                 for (int m = 0; m < 4; ++m) { const size_t row = (size_t)(row0 + ai * HALF + m * 16);
;                     const f32x4 v0 = acc[ai][bj][m][0] + b0, v1 = acc[ai][bj][m][1] + b1; float o[8];
; #pragma unroll
;                     for (int e = 0; e < 8; ++e) { float x = (e < 4) ? v0[e & 3] : v1[e & 3];
;                         if (kind == 0) x = -0.6065306597126334f * sigmoidf_(x);
;                         else if (kind == 1) x = sigmoidf_(x);
;                         o[e] = x; }
;                     u32x4 w; w.x = cvt_pk_bf16(o[0], o[1]); w.y = cvt_pk_bf16(o[2], o[3]); w.z = cvt_pk_bf16(o[4], o[5]); w.w = cvt_pk_bf16(o[6], o[7]);
;                     *(u32x4*)(O + row * 512 + col) = w; } }
.LBB0_614:
	v_mul_f32_e32 v130, 0xbfb8aa3b, v130
	v_exp_f32_e32 v130, v130
	s_nop 0
	v_add_f32_e32 v130, 1.0, v130
	v_rcp_f32_e32 v133, v130
	s_nop 0
	v_fma_f32 v160, -v130, v133, 1.0
	v_fmac_f32_e32 v133, v160, v133
	v_div_fixup_f32 v130, v133, v130, 1.0
	v_mul_f32_e32 v159, 0xbf1b4598, v130
.LBB0_615:
	v_add_f32_e32 v130, v131, v83
	s_and_b64 vcc, exec, s[2:3]
	s_mov_b64 s[78:79], -1
	s_cbranch_vccnz .LBB0_619
	s_and_b64 vcc, exec, s[0:1]
	v_mov_b32_e32 v160, v130
	s_cbranch_vccnz .LBB0_618
	v_mul_f32_e32 v131, 0xbfb8aa3b, v130
	v_exp_f32_e32 v131, v131
	s_nop 0
	v_add_f32_e32 v131, 1.0, v131
	v_rcp_f32_e32 v133, v131
	s_nop 0
	v_fma_f32 v161, -v131, v133, 1.0
	v_fmac_f32_e32 v133, v161, v133
	v_div_fixup_f32 v160, v133, v131, 1.0

; __device__ __forceinline__ unsigned cvt_pk_bf16(float lo, float hi) { const f32x2c v = {lo, hi}; const bf16x2c b = __builtin_convertvector(v, bf16x2c); return __builtin_bit_cast(unsigned, b); }
; __device__ __forceinline__ float sigmoidf_(float x) { return 1.f / (1.f + __expf(-x)); }
;     __device__ __forceinline__ void operator()(const f32x4 (&acc)[2][2][4][2], const Unit& u, int wr, int wc, int fr, int fq) const {
;     ...
;         for (int bj = 0; bj < 2; ++bj) { const int col = (col0 + bj * HALF) & 511;
;             f32x4 b0 = (f32x4){0.f, 0.f, 0.f, 0.f}, b1 = b0;
;             if (kind == 0) { b0 = *(const f32x4*)(w0 + col); b1 = *(const f32x4*)(w0 + col + 4); }
;             else if (kind == 1) { b0 = *(const f32x4*)(a0 + col); b1 = *(const f32x4*)(a0 + col + 4); }
; #pragma unroll
;             for (int ai = 0; ai < 2; ++ai)
; #pragma unroll
;                 for (int m = 0; m < 4; ++m) { const size_t row = (size_t)(row0 + ai * HALF + m * 16);
;                     const f32x4 v0 = acc[ai][bj][m][0] + b0, v1 = acc[ai][bj][m][1] + b1; float o[8];
; #pragma unroll
;                     for (int e = 0; e < 8; ++e) { float x = (e < 4) ? v0[e & 3] : v1[e & 3];
;                         if (kind == 0) x = -0.6065306597126334f * sigmoidf_(x);
;                         else if (kind == 1) x = sigmoidf_(x);
;                         o[e] = x; }
;                     u32x4 w; w.x = cvt_pk_bf16(o[0], o[1]); w.y = cvt_pk_bf16(o[2], o[3]); w.z = cvt_pk_bf16(o[4], o[5]); w.w = cvt_pk_bf16(o[6], o[7]);
;                     *(u32x4*)(O + row * 512 + col) = w; } }
.LBB0_620:
	v_mul_f32_e32 v130, 0xbfb8aa3b, v130
	v_exp_f32_e32 v130, v130
	s_nop 0
	v_add_f32_e32 v130, 1.0, v130
	v_rcp_f32_e32 v132, v130
	s_nop 0
	v_fma_f32 v160, -v130, v132, 1.0
	v_fmac_f32_e32 v132, v160, v132
	v_div_fixup_f32 v130, v132, v130, 1.0
	v_mul_f32_e32 v160, 0xbf1b4598, v130
.LBB0_621:
	s_ashr_i32 s77, s76, 31
	s_lshl_b64 s[76:77], s[76:77], 26
	s_add_u32 s76, s28, s76
	v_lshl_add_u32 v132, s68, 8, v152
	s_addc_u32 s77, s29, s77
	v_lshlrev_b32_e32 v136, 1, v136
	v_ashrrev_i32_e32 v133, 31, v132
	v_lshl_add_u64 v[130:131], s[76:77], 0, v[136:137]
	v_cvt_pk_bf16_f32 v164, v128, v129
	v_lshlrev_b64 v[128:129], 10, v[132:133]
	v_cvt_pk_bf16_f32 v162, v157, v158
	v_cvt_pk_bf16_f32 v163, v134, v135
	v_cvt_pk_bf16_f32 v165, v159, v160
	v_lshl_add_u64 v[128:129], v[130:131], 0, v[128:129]
	v_add_f32_e32 v134, v124, v88
	s_and_b64 vcc, exec, s[2:3]
	s_mov_b64 s[68:69], -1
	global_store_dwordx4 v[128:129], v[162:165], off
	s_cbranch_vccnz .LBB0_625
	s_and_b64 vcc, exec, s[0:1]
	v_mov_b32_e32 v124, v134
	s_cbranch_vccnz .LBB0_624
	v_mul_f32_e32 v124, 0xbfb8aa3b, v134
	v_exp_f32_e32 v124, v124
	s_nop 0
	v_add_f32_e32 v124, 1.0, v124
	v_rcp_f32_e32 v136, v124
	s_nop 0
	v_fma_f32 v158, -v124, v136, 1.0
	v_fmac_f32_e32 v136, v158, v136
	v_div_fixup_f32 v124, v136, v124, 1.0

; __device__ __forceinline__ unsigned cvt_pk_bf16(float lo, float hi) { const f32x2c v = {lo, hi}; const bf16x2c b = __builtin_convertvector(v, bf16x2c); return __builtin_bit_cast(unsigned, b); }
; __device__ __forceinline__ float sigmoidf_(float x) { return 1.f / (1.f + __expf(-x)); }
;     __device__ __forceinline__ void operator()(const f32x4 (&acc)[2][2][4][2], const Unit& u, int wr, int wc, int fr, int fq) const {
;     ...
;         for (int bj = 0; bj < 2; ++bj) { const int col = (col0 + bj * HALF) & 511;
;             f32x4 b0 = (f32x4){0.f, 0.f, 0.f, 0.f}, b1 = b0;
;             if (kind == 0) { b0 = *(const f32x4*)(w0 + col); b1 = *(const f32x4*)(w0 + col + 4); }
;             else if (kind == 1) { b0 = *(const f32x4*)(a0 + col); b1 = *(const f32x4*)(a0 + col + 4); }
; #pragma unroll
;             for (int ai = 0; ai < 2; ++ai)
; #pragma unroll
;                 for (int m = 0; m < 4; ++m) { const size_t row = (size_t)(row0 + ai * HALF + m * 16);
;                     const f32x4 v0 = acc[ai][bj][m][0] + b0, v1 = acc[ai][bj][m][1] + b1; float o[8];
; #pragma unroll
;                     for (int e = 0; e < 8; ++e) { float x = (e < 4) ? v0[e & 3] : v1[e & 3];
;                         if (kind == 0) x = -0.6065306597126334f * sigmoidf_(x);
;                         else if (kind == 1) x = sigmoidf_(x);
;                         o[e] = x; }
;                     u32x4 w; w.x = cvt_pk_bf16(o[0], o[1]); w.y = cvt_pk_bf16(o[2], o[3]); w.z = cvt_pk_bf16(o[4], o[5]); w.w = cvt_pk_bf16(o[6], o[7]);
;                     *(u32x4*)(O + row * 512 + col) = w; } }
.LBB0_626:
	v_mul_f32_e32 v124, 0xbfb8aa3b, v134
	v_exp_f32_e32 v124, v124
	s_nop 0
	v_add_f32_e32 v124, 1.0, v124
	v_rcp_f32_e32 v135, v124
	s_nop 0
	v_fma_f32 v157, -v124, v135, 1.0
	v_fmac_f32_e32 v135, v157, v135
	v_div_fixup_f32 v124, v135, v124, 1.0
	v_mul_f32_e32 v124, 0xbf1b4598, v124
.LBB0_627:
	v_add_f32_e32 v134, v125, v89
	s_and_b64 vcc, exec, s[2:3]
	s_mov_b64 s[68:69], -1
	s_cbranch_vccnz .LBB0_631
	s_and_b64 vcc, exec, s[0:1]
	v_mov_b32_e32 v125, v134
	s_cbranch_vccnz .LBB0_630
	v_mul_f32_e32 v125, 0xbfb8aa3b, v134
	v_exp_f32_e32 v125, v125
	s_nop 0
	v_add_f32_e32 v125, 1.0, v125
	v_rcp_f32_e32 v136, v125
	s_nop 0
	v_fma_f32 v158, -v125, v136, 1.0
	v_fmac_f32_e32 v136, v158, v136
	v_div_fixup_f32 v125, v136, v125, 1.0

; __device__ __forceinline__ unsigned cvt_pk_bf16(float lo, float hi) { const f32x2c v = {lo, hi}; const bf16x2c b = __builtin_convertvector(v, bf16x2c); return __builtin_bit_cast(unsigned, b); }
; __device__ __forceinline__ float sigmoidf_(float x) { return 1.f / (1.f + __expf(-x)); }
;     __device__ __forceinline__ void operator()(const f32x4 (&acc)[2][2][4][2], const Unit& u, int wr, int wc, int fr, int fq) const {
;     ...
;         for (int bj = 0; bj < 2; ++bj) { const int col = (col0 + bj * HALF) & 511;
;             f32x4 b0 = (f32x4){0.f, 0.f, 0.f, 0.f}, b1 = b0;
;             if (kind == 0) { b0 = *(const f32x4*)(w0 + col); b1 = *(const f32x4*)(w0 + col + 4); }
;             else if (kind == 1) { b0 = *(const f32x4*)(a0 + col); b1 = *(const f32x4*)(a0 + col + 4); }
; #pragma unroll
;             for (int ai = 0; ai < 2; ++ai)
; #pragma unroll
;                 for (int m = 0; m < 4; ++m) { const size_t row = (size_t)(row0 + ai * HALF + m * 16);
;                     const f32x4 v0 = acc[ai][bj][m][0] + b0, v1 = acc[ai][bj][m][1] + b1; float o[8];
; #pragma unroll
;                     for (int e = 0; e < 8; ++e) { float x = (e < 4) ? v0[e & 3] : v1[e & 3];
;                         if (kind == 0) x = -0.6065306597126334f * sigmoidf_(x);
;                         else if (kind == 1) x = sigmoidf_(x);
;                         o[e] = x; }
;                     u32x4 w; w.x = cvt_pk_bf16(o[0], o[1]); w.y = cvt_pk_bf16(o[2], o[3]); w.z = cvt_pk_bf16(o[4], o[5]); w.w = cvt_pk_bf16(o[6], o[7]);
;                     *(u32x4*)(O + row * 512 + col) = w; } }
.LBB0_632:
	v_mul_f32_e32 v125, 0xbfb8aa3b, v134
	v_exp_f32_e32 v125, v125
	s_nop 0
	v_add_f32_e32 v125, 1.0, v125
	v_rcp_f32_e32 v135, v125
	s_nop 0
	v_fma_f32 v157, -v125, v135, 1.0
	v_fmac_f32_e32 v135, v157, v135
	v_div_fixup_f32 v125, v135, v125, 1.0
	v_mul_f32_e32 v125, 0xbf1b4598, v125
.LBB0_633:
	v_add_f32_e32 v134, v126, v90
	s_and_b64 vcc, exec, s[2:3]
	s_mov_b64 s[68:69], -1
	s_cbranch_vccnz .LBB0_637
	s_and_b64 vcc, exec, s[0:1]
	v_mov_b32_e32 v126, v134
	s_cbranch_vccnz .LBB0_636
	v_mul_f32_e32 v126, 0xbfb8aa3b, v134
	v_exp_f32_e32 v126, v126
	s_nop 0
	v_add_f32_e32 v126, 1.0, v126
	v_rcp_f32_e32 v136, v126
	s_nop 0
	v_fma_f32 v158, -v126, v136, 1.0
	v_fmac_f32_e32 v136, v158, v136
	v_div_fixup_f32 v126, v136, v126, 1.0

; __device__ __forceinline__ unsigned cvt_pk_bf16(float lo, float hi) { const f32x2c v = {lo, hi}; const bf16x2c b = __builtin_convertvector(v, bf16x2c); return __builtin_bit_cast(unsigned, b); }
; __device__ __forceinline__ float sigmoidf_(float x) { return 1.f / (1.f + __expf(-x)); }
;     __device__ __forceinline__ void operator()(const f32x4 (&acc)[2][2][4][2], const Unit& u, int wr, int wc, int fr, int fq) const {
;     ...
;         for (int bj = 0; bj < 2; ++bj) { const int col = (col0 + bj * HALF) & 511;
;             f32x4 b0 = (f32x4){0.f, 0.f, 0.f, 0.f}, b1 = b0;
;             if (kind == 0) { b0 = *(const f32x4*)(w0 + col); b1 = *(const f32x4*)(w0 + col + 4); }
;             else if (kind == 1) { b0 = *(const f32x4*)(a0 + col); b1 = *(const f32x4*)(a0 + col + 4); }
; #pragma unroll
;             for (int ai = 0; ai < 2; ++ai)
; #pragma unroll
;                 for (int m = 0; m < 4; ++m) { const size_t row = (size_t)(row0 + ai * HALF + m * 16);
;                     const f32x4 v0 = acc[ai][bj][m][0] + b0, v1 = acc[ai][bj][m][1] + b1; float o[8];
; #pragma unroll
;                     for (int e = 0; e < 8; ++e) { float x = (e < 4) ? v0[e & 3] : v1[e & 3];
;                         if (kind == 0) x = -0.6065306597126334f * sigmoidf_(x);
;                         else if (kind == 1) x = sigmoidf_(x);
;                         o[e] = x; }
;                     u32x4 w; w.x = cvt_pk_bf16(o[0], o[1]); w.y = cvt_pk_bf16(o[2], o[3]); w.z = cvt_pk_bf16(o[4], o[5]); w.w = cvt_pk_bf16(o[6], o[7]);
;                     *(u32x4*)(O + row * 512 + col) = w; } }
.LBB0_638:
	v_mul_f32_e32 v126, 0xbfb8aa3b, v134
	v_exp_f32_e32 v126, v126
	s_nop 0
	v_add_f32_e32 v126, 1.0, v126
	v_rcp_f32_e32 v135, v126
	s_nop 0
	v_fma_f32 v157, -v126, v135, 1.0
	v_fmac_f32_e32 v135, v157, v135
	v_div_fixup_f32 v126, v135, v126, 1.0
	v_mul_f32_e32 v126, 0xbf1b4598, v126
.LBB0_639:
	v_add_f32_e32 v134, v127, v91
	s_and_b64 vcc, exec, s[2:3]
	s_mov_b64 s[68:69], -1
	s_cbranch_vccnz .LBB0_643
	s_and_b64 vcc, exec, s[0:1]
	v_mov_b32_e32 v127, v134
	s_cbranch_vccnz .LBB0_642
	v_mul_f32_e32 v127, 0xbfb8aa3b, v134
	v_exp_f32_e32 v127, v127
	s_nop 0
	v_add_f32_e32 v127, 1.0, v127
	v_rcp_f32_e32 v136, v127
	s_nop 0
	v_fma_f32 v158, -v127, v136, 1.0
	v_fmac_f32_e32 v136, v158, v136
	v_div_fixup_f32 v127, v136, v127, 1.0

; __device__ __forceinline__ unsigned cvt_pk_bf16(float lo, float hi) { const f32x2c v = {lo, hi}; const bf16x2c b = __builtin_convertvector(v, bf16x2c); return __builtin_bit_cast(unsigned, b); }
; __device__ __forceinline__ float sigmoidf_(float x) { return 1.f / (1.f + __expf(-x)); }
;     __device__ __forceinline__ void operator()(const f32x4 (&acc)[2][2][4][2], const Unit& u, int wr, int wc, int fr, int fq) const {
;     ...
;         for (int bj = 0; bj < 2; ++bj) { const int col = (col0 + bj * HALF) & 511;
;             f32x4 b0 = (f32x4){0.f, 0.f, 0.f, 0.f}, b1 = b0;
;             if (kind == 0) { b0 = *(const f32x4*)(w0 + col); b1 = *(const f32x4*)(w0 + col + 4); }
;             else if (kind == 1) { b0 = *(const f32x4*)(a0 + col); b1 = *(const f32x4*)(a0 + col + 4); }
; #pragma unroll
;             for (int ai = 0; ai < 2; ++ai)
; #pragma unroll
;                 for (int m = 0; m < 4; ++m) { const size_t row = (size_t)(row0 + ai * HALF + m * 16);
;                     const f32x4 v0 = acc[ai][bj][m][0] + b0, v1 = acc[ai][bj][m][1] + b1; float o[8];
; #pragma unroll
;                     for (int e = 0; e < 8; ++e) { float x = (e < 4) ? v0[e & 3] : v1[e & 3];
;                         if (kind == 0) x = -0.6065306597126334f * sigmoidf_(x);
;                         else if (kind == 1) x = sigmoidf_(x);
;                         o[e] = x; }
;                     u32x4 w; w.x = cvt_pk_bf16(o[0], o[1]); w.y = cvt_pk_bf16(o[2], o[3]); w.z = cvt_pk_bf16(o[4], o[5]); w.w = cvt_pk_bf16(o[6], o[7]);
;                     *(u32x4*)(O + row * 512 + col) = w; } }
.LBB0_644:
	v_mul_f32_e32 v127, 0xbfb8aa3b, v134
	v_exp_f32_e32 v127, v127
	s_nop 0
	v_add_f32_e32 v127, 1.0, v127
	v_rcp_f32_e32 v135, v127
	s_nop 0
	v_fma_f32 v157, -v127, v135, 1.0
	v_fmac_f32_e32 v135, v157, v135
	v_div_fixup_f32 v127, v135, v127, 1.0
	v_mul_f32_e32 v127, 0xbf1b4598, v127
.LBB0_645:
	v_add_f32_e32 v134, v120, v80
	s_and_b64 vcc, exec, s[2:3]
	s_mov_b64 s[68:69], -1
	s_cbranch_vccnz .LBB0_649
	s_and_b64 vcc, exec, s[0:1]
	v_mov_b32_e32 v120, v134
	s_cbranch_vccnz .LBB0_648
	v_mul_f32_e32 v120, 0xbfb8aa3b, v134
	v_exp_f32_e32 v120, v120
	s_nop 0
	v_add_f32_e32 v120, 1.0, v120
	v_rcp_f32_e32 v136, v120
	s_nop 0
	v_fma_f32 v158, -v120, v136, 1.0
	v_fmac_f32_e32 v136, v158, v136
	v_div_fixup_f32 v120, v136, v120, 1.0

; __device__ __forceinline__ unsigned cvt_pk_bf16(float lo, float hi) { const f32x2c v = {lo, hi}; const bf16x2c b = __builtin_convertvector(v, bf16x2c); return __builtin_bit_cast(unsigned, b); }
; __device__ __forceinline__ float sigmoidf_(float x) { return 1.f / (1.f + __expf(-x)); }
;     __device__ __forceinline__ void operator()(const f32x4 (&acc)[2][2][4][2], const Unit& u, int wr, int wc, int fr, int fq) const {
;     ...
;         for (int bj = 0; bj < 2; ++bj) { const int col = (col0 + bj * HALF) & 511;
;             f32x4 b0 = (f32x4){0.f, 0.f, 0.f, 0.f}, b1 = b0;
;             if (kind == 0) { b0 = *(const f32x4*)(w0 + col); b1 = *(const f32x4*)(w0 + col + 4); }
;             else if (kind == 1) { b0 = *(const f32x4*)(a0 + col); b1 = *(const f32x4*)(a0 + col + 4); }
; #pragma unroll
;             for (int ai = 0; ai < 2; ++ai)
; #pragma unroll
;                 for (int m = 0; m < 4; ++m) { const size_t row = (size_t)(row0 + ai * HALF + m * 16);
;                     const f32x4 v0 = acc[ai][bj][m][0] + b0, v1 = acc[ai][bj][m][1] + b1; float o[8];
; #pragma unroll
;                     for (int e = 0; e < 8; ++e) { float x = (e < 4) ? v0[e & 3] : v1[e & 3];
;                         if (kind == 0) x = -0.6065306597126334f * sigmoidf_(x);
;                         else if (kind == 1) x = sigmoidf_(x);
;                         o[e] = x; }
;                     u32x4 w; w.x = cvt_pk_bf16(o[0], o[1]); w.y = cvt_pk_bf16(o[2], o[3]); w.z = cvt_pk_bf16(o[4], o[5]); w.w = cvt_pk_bf16(o[6], o[7]);
;                     *(u32x4*)(O + row * 512 + col) = w; } }
.LBB0_650:
	v_mul_f32_e32 v120, 0xbfb8aa3b, v134
	v_exp_f32_e32 v120, v120
	s_nop 0
	v_add_f32_e32 v120, 1.0, v120
	v_rcp_f32_e32 v135, v120
	s_nop 0
	v_fma_f32 v157, -v120, v135, 1.0
	v_fmac_f32_e32 v135, v157, v135
	v_div_fixup_f32 v120, v135, v120, 1.0
	v_mul_f32_e32 v120, 0xbf1b4598, v120
.LBB0_651:
	v_add_f32_e32 v134, v121, v81
	s_and_b64 vcc, exec, s[2:3]
	s_mov_b64 s[68:69], -1
	s_cbranch_vccnz .LBB0_655
	s_and_b64 vcc, exec, s[0:1]
	v_mov_b32_e32 v121, v134
	s_cbranch_vccnz .LBB0_654
	v_mul_f32_e32 v121, 0xbfb8aa3b, v134
	v_exp_f32_e32 v121, v121
	s_nop 0
	v_add_f32_e32 v121, 1.0, v121
	v_rcp_f32_e32 v136, v121
	s_nop 0
	v_fma_f32 v158, -v121, v136, 1.0
	v_fmac_f32_e32 v136, v158, v136
	v_div_fixup_f32 v121, v136, v121, 1.0

; __device__ __forceinline__ unsigned cvt_pk_bf16(float lo, float hi) { const f32x2c v = {lo, hi}; const bf16x2c b = __builtin_convertvector(v, bf16x2c); return __builtin_bit_cast(unsigned, b); }
; __device__ __forceinline__ float sigmoidf_(float x) { return 1.f / (1.f + __expf(-x)); }
;     __device__ __forceinline__ void operator()(const f32x4 (&acc)[2][2][4][2], const Unit& u, int wr, int wc, int fr, int fq) const {
;     ...
;         for (int bj = 0; bj < 2; ++bj) { const int col = (col0 + bj * HALF) & 511;
;             f32x4 b0 = (f32x4){0.f, 0.f, 0.f, 0.f}, b1 = b0;
;             if (kind == 0) { b0 = *(const f32x4*)(w0 + col); b1 = *(const f32x4*)(w0 + col + 4); }
;             else if (kind == 1) { b0 = *(const f32x4*)(a0 + col); b1 = *(const f32x4*)(a0 + col + 4); }
; #pragma unroll
;             for (int ai = 0; ai < 2; ++ai)
; #pragma unroll
;                 for (int m = 0; m < 4; ++m) { const size_t row = (size_t)(row0 + ai * HALF + m * 16);
;                     const f32x4 v0 = acc[ai][bj][m][0] + b0, v1 = acc[ai][bj][m][1] + b1; float o[8];
; #pragma unroll
;                     for (int e = 0; e < 8; ++e) { float x = (e < 4) ? v0[e & 3] : v1[e & 3];
;                         if (kind == 0) x = -0.6065306597126334f * sigmoidf_(x);
;                         else if (kind == 1) x = sigmoidf_(x);
;                         o[e] = x; }
;                     u32x4 w; w.x = cvt_pk_bf16(o[0], o[1]); w.y = cvt_pk_bf16(o[2], o[3]); w.z = cvt_pk_bf16(o[4], o[5]); w.w = cvt_pk_bf16(o[6], o[7]);
;                     *(u32x4*)(O + row * 512 + col) = w; } }
.LBB0_656:
	v_mul_f32_e32 v121, 0xbfb8aa3b, v134
	v_exp_f32_e32 v121, v121
	s_nop 0
	v_add_f32_e32 v121, 1.0, v121
	v_rcp_f32_e32 v135, v121
	s_nop 0
	v_fma_f32 v157, -v121, v135, 1.0
	v_fmac_f32_e32 v135, v157, v135
	v_div_fixup_f32 v121, v135, v121, 1.0
	v_mul_f32_e32 v121, 0xbf1b4598, v121
.LBB0_657:
	v_add_f32_e32 v134, v122, v82
	s_and_b64 vcc, exec, s[2:3]
	s_mov_b64 s[68:69], -1
	s_cbranch_vccnz .LBB0_661
	s_and_b64 vcc, exec, s[0:1]
	v_mov_b32_e32 v122, v134
	s_cbranch_vccnz .LBB0_660
	v_mul_f32_e32 v122, 0xbfb8aa3b, v134
	v_exp_f32_e32 v122, v122
	s_nop 0
	v_add_f32_e32 v122, 1.0, v122
	v_rcp_f32_e32 v136, v122
	s_nop 0
	v_fma_f32 v158, -v122, v136, 1.0
	v_fmac_f32_e32 v136, v158, v136
	v_div_fixup_f32 v122, v136, v122, 1.0

; __device__ __forceinline__ unsigned cvt_pk_bf16(float lo, float hi) { const f32x2c v = {lo, hi}; const bf16x2c b = __builtin_convertvector(v, bf16x2c); return __builtin_bit_cast(unsigned, b); }
; __device__ __forceinline__ float sigmoidf_(float x) { return 1.f / (1.f + __expf(-x)); }
;     __device__ __forceinline__ void operator()(const f32x4 (&acc)[2][2][4][2], const Unit& u, int wr, int wc, int fr, int fq) const {
;     ...
;         for (int bj = 0; bj < 2; ++bj) { const int col = (col0 + bj * HALF) & 511;
;             f32x4 b0 = (f32x4){0.f, 0.f, 0.f, 0.f}, b1 = b0;
;             if (kind == 0) { b0 = *(const f32x4*)(w0 + col); b1 = *(const f32x4*)(w0 + col + 4); }
;             else if (kind == 1) { b0 = *(const f32x4*)(a0 + col); b1 = *(const f32x4*)(a0 + col + 4); }
; #pragma unroll
;             for (int ai = 0; ai < 2; ++ai)
; #pragma unroll
;                 for (int m = 0; m < 4; ++m) { const size_t row = (size_t)(row0 + ai * HALF + m * 16);
;                     const f32x4 v0 = acc[ai][bj][m][0] + b0, v1 = acc[ai][bj][m][1] + b1; float o[8];
; #pragma unroll
;                     for (int e = 0; e < 8; ++e) { float x = (e < 4) ? v0[e & 3] : v1[e & 3];
;                         if (kind == 0) x = -0.6065306597126334f * sigmoidf_(x);
;                         else if (kind == 1) x = sigmoidf_(x);
;                         o[e] = x; }
;                     u32x4 w; w.x = cvt_pk_bf16(o[0], o[1]); w.y = cvt_pk_bf16(o[2], o[3]); w.z = cvt_pk_bf16(o[4], o[5]); w.w = cvt_pk_bf16(o[6], o[7]);
;                     *(u32x4*)(O + row * 512 + col) = w; } }
.LBB0_662:
	v_mul_f32_e32 v122, 0xbfb8aa3b, v134
	v_exp_f32_e32 v122, v122
	s_nop 0
	v_add_f32_e32 v122, 1.0, v122
	v_rcp_f32_e32 v135, v122
	s_nop 0
	v_fma_f32 v157, -v122, v135, 1.0
	v_fmac_f32_e32 v135, v157, v135
	v_div_fixup_f32 v122, v135, v122, 1.0
	v_mul_f32_e32 v122, 0xbf1b4598, v122
.LBB0_663:
	v_add_f32_e32 v123, v123, v83
	s_and_b64 vcc, exec, s[2:3]
	s_mov_b64 s[68:69], -1
	s_cbranch_vccnz .LBB0_667
	s_and_b64 vcc, exec, s[0:1]
	v_mov_b32_e32 v134, v123
	s_cbranch_vccnz .LBB0_666
	v_mul_f32_e32 v134, 0xbfb8aa3b, v123
	v_exp_f32_e32 v134, v134
	s_nop 0
	v_add_f32_e32 v134, 1.0, v134
	v_rcp_f32_e32 v136, v134
	s_nop 0
	v_fma_f32 v158, -v134, v136, 1.0
	v_fmac_f32_e32 v136, v158, v136
	v_div_fixup_f32 v134, v136, v134, 1.0

; __device__ __forceinline__ unsigned cvt_pk_bf16(float lo, float hi) { const f32x2c v = {lo, hi}; const bf16x2c b = __builtin_convertvector(v, bf16x2c); return __builtin_bit_cast(unsigned, b); }
; __device__ __forceinline__ float sigmoidf_(float x) { return 1.f / (1.f + __expf(-x)); }
;     __device__ __forceinline__ void operator()(const f32x4 (&acc)[2][2][4][2], const Unit& u, int wr, int wc, int fr, int fq) const {
;     ...
;         for (int bj = 0; bj < 2; ++bj) { const int col = (col0 + bj * HALF) & 511;
;             f32x4 b0 = (f32x4){0.f, 0.f, 0.f, 0.f}, b1 = b0;
;             if (kind == 0) { b0 = *(const f32x4*)(w0 + col); b1 = *(const f32x4*)(w0 + col + 4); }
;             else if (kind == 1) { b0 = *(const f32x4*)(a0 + col); b1 = *(const f32x4*)(a0 + col + 4); }
; #pragma unroll
;             for (int ai = 0; ai < 2; ++ai)
; #pragma unroll
;                 for (int m = 0; m < 4; ++m) { const size_t row = (size_t)(row0 + ai * HALF + m * 16);
;                     const f32x4 v0 = acc[ai][bj][m][0] + b0, v1 = acc[ai][bj][m][1] + b1; float o[8];
; #pragma unroll
;                     for (int e = 0; e < 8; ++e) { float x = (e < 4) ? v0[e & 3] : v1[e & 3];
;                         if (kind == 0) x = -0.6065306597126334f * sigmoidf_(x);
;                         else if (kind == 1) x = sigmoidf_(x);
;                         o[e] = x; }
;                     u32x4 w; w.x = cvt_pk_bf16(o[0], o[1]); w.y = cvt_pk_bf16(o[2], o[3]); w.z = cvt_pk_bf16(o[4], o[5]); w.w = cvt_pk_bf16(o[6], o[7]);
;                     *(u32x4*)(O + row * 512 + col) = w; } }
.LBB0_668:
	v_mul_f32_e32 v123, 0xbfb8aa3b, v123
	v_exp_f32_e32 v123, v123
	s_nop 0
	v_add_f32_e32 v123, 1.0, v123
	v_rcp_f32_e32 v135, v123
	s_nop 0
	v_fma_f32 v157, -v123, v135, 1.0
	v_fmac_f32_e32 v135, v157, v135
	v_div_fixup_f32 v123, v135, v123, 1.0
	v_mul_f32_e32 v134, 0xbf1b4598, v123
.LBB0_669:
	v_or_b32_e32 v158, 16, v132
	v_ashrrev_i32_e32 v159, 31, v158
	v_cvt_pk_bf16_f32 v124, v124, v125
	v_cvt_pk_bf16_f32 v125, v126, v127
	v_cvt_pk_bf16_f32 v126, v120, v121
	v_lshlrev_b64 v[120:121], 10, v[158:159]
	v_cvt_pk_bf16_f32 v127, v122, v134
	v_lshl_add_u64 v[120:121], v[130:131], 0, v[120:121]
	v_add_f32_e32 v122, v116, v88
	s_and_b64 vcc, exec, s[2:3]
	s_mov_b64 s[68:69], -1
	global_store_dwordx4 v[120:121], v[124:127], off
	s_cbranch_vccnz .LBB0_673
	s_and_b64 vcc, exec, s[0:1]
	v_mov_b32_e32 v116, v122
	s_cbranch_vccnz .LBB0_672
	v_mul_f32_e32 v116, 0xbfb8aa3b, v122
	v_exp_f32_e32 v116, v116
	s_nop 0
	v_add_f32_e32 v116, 1.0, v116
	v_rcp_f32_e32 v124, v116
	s_nop 0
	v_fma_f32 v126, -v116, v124, 1.0
	v_fmac_f32_e32 v124, v126, v124
	v_div_fixup_f32 v116, v124, v116, 1.0

; __device__ __forceinline__ unsigned cvt_pk_bf16(float lo, float hi) { const f32x2c v = {lo, hi}; const bf16x2c b = __builtin_convertvector(v, bf16x2c); return __builtin_bit_cast(unsigned, b); }
; __device__ __forceinline__ float sigmoidf_(float x) { return 1.f / (1.f + __expf(-x)); }
;     __device__ __forceinline__ void operator()(const f32x4 (&acc)[2][2][4][2], const Unit& u, int wr, int wc, int fr, int fq) const {
;     ...
;         for (int bj = 0; bj < 2; ++bj) { const int col = (col0 + bj * HALF) & 511;
;             f32x4 b0 = (f32x4){0.f, 0.f, 0.f, 0.f}, b1 = b0;
;             if (kind == 0) { b0 = *(const f32x4*)(w0 + col); b1 = *(const f32x4*)(w0 + col + 4); }
;             else if (kind == 1) { b0 = *(const f32x4*)(a0 + col); b1 = *(const f32x4*)(a0 + col + 4); }
; #pragma unroll
;             for (int ai = 0; ai < 2; ++ai)
; #pragma unroll
;                 for (int m = 0; m < 4; ++m) { const size_t row = (size_t)(row0 + ai * HALF + m * 16);
;                     const f32x4 v0 = acc[ai][bj][m][0] + b0, v1 = acc[ai][bj][m][1] + b1; float o[8];
; #pragma unroll
;                     for (int e = 0; e < 8; ++e) { float x = (e < 4) ? v0[e & 3] : v1[e & 3];
;                         if (kind == 0) x = -0.6065306597126334f * sigmoidf_(x);
;                         else if (kind == 1) x = sigmoidf_(x);
;                         o[e] = x; }
;                     u32x4 w; w.x = cvt_pk_bf16(o[0], o[1]); w.y = cvt_pk_bf16(o[2], o[3]); w.z = cvt_pk_bf16(o[4], o[5]); w.w = cvt_pk_bf16(o[6], o[7]);
;                     *(u32x4*)(O + row * 512 + col) = w; } }
.LBB0_674:
	v_mul_f32_e32 v116, 0xbfb8aa3b, v122
	v_exp_f32_e32 v116, v116
	s_nop 0
	v_add_f32_e32 v116, 1.0, v116
	v_rcp_f32_e32 v123, v116
	s_nop 0
	v_fma_f32 v125, -v116, v123, 1.0
	v_fmac_f32_e32 v123, v125, v123
	v_div_fixup_f32 v116, v123, v116, 1.0
	v_mul_f32_e32 v116, 0xbf1b4598, v116
.LBB0_675:
	v_add_f32_e32 v122, v117, v89
	s_and_b64 vcc, exec, s[2:3]
	s_mov_b64 s[68:69], -1
	s_cbranch_vccnz .LBB0_679
	s_and_b64 vcc, exec, s[0:1]
	v_mov_b32_e32 v117, v122
	s_cbranch_vccnz .LBB0_678
	v_mul_f32_e32 v117, 0xbfb8aa3b, v122
	v_exp_f32_e32 v117, v117
	s_nop 0
	v_add_f32_e32 v117, 1.0, v117
	v_rcp_f32_e32 v124, v117
	s_nop 0
	v_fma_f32 v126, -v117, v124, 1.0
	v_fmac_f32_e32 v124, v126, v124
	v_div_fixup_f32 v117, v124, v117, 1.0

; __device__ __forceinline__ unsigned cvt_pk_bf16(float lo, float hi) { const f32x2c v = {lo, hi}; const bf16x2c b = __builtin_convertvector(v, bf16x2c); return __builtin_bit_cast(unsigned, b); }
; __device__ __forceinline__ float sigmoidf_(float x) { return 1.f / (1.f + __expf(-x)); }
;     __device__ __forceinline__ void operator()(const f32x4 (&acc)[2][2][4][2], const Unit& u, int wr, int wc, int fr, int fq) const {
;     ...
;         for (int bj = 0; bj < 2; ++bj) { const int col = (col0 + bj * HALF) & 511;
;             f32x4 b0 = (f32x4){0.f, 0.f, 0.f, 0.f}, b1 = b0;
;             if (kind == 0) { b0 = *(const f32x4*)(w0 + col); b1 = *(const f32x4*)(w0 + col + 4); }
;             else if (kind == 1) { b0 = *(const f32x4*)(a0 + col); b1 = *(const f32x4*)(a0 + col + 4); }
; #pragma unroll
;             for (int ai = 0; ai < 2; ++ai)
; #pragma unroll
;                 for (int m = 0; m < 4; ++m) { const size_t row = (size_t)(row0 + ai * HALF + m * 16);
;                     const f32x4 v0 = acc[ai][bj][m][0] + b0, v1 = acc[ai][bj][m][1] + b1; float o[8];
; #pragma unroll
;                     for (int e = 0; e < 8; ++e) { float x = (e < 4) ? v0[e & 3] : v1[e & 3];
;                         if (kind == 0) x = -0.6065306597126334f * sigmoidf_(x);
;                         else if (kind == 1) x = sigmoidf_(x);
;                         o[e] = x; }
;                     u32x4 w; w.x = cvt_pk_bf16(o[0], o[1]); w.y = cvt_pk_bf16(o[2], o[3]); w.z = cvt_pk_bf16(o[4], o[5]); w.w = cvt_pk_bf16(o[6], o[7]);
;                     *(u32x4*)(O + row * 512 + col) = w; } }
.LBB0_680:
	v_mul_f32_e32 v117, 0xbfb8aa3b, v122
	v_exp_f32_e32 v117, v117
	s_nop 0
	v_add_f32_e32 v117, 1.0, v117
	v_rcp_f32_e32 v123, v117
	s_nop 0
	v_fma_f32 v125, -v117, v123, 1.0
	v_fmac_f32_e32 v123, v125, v123
	v_div_fixup_f32 v117, v123, v117, 1.0
	v_mul_f32_e32 v117, 0xbf1b4598, v117
.LBB0_681:
	v_add_f32_e32 v122, v118, v90
	s_and_b64 vcc, exec, s[2:3]
	s_mov_b64 s[68:69], -1
	s_cbranch_vccnz .LBB0_685
	s_and_b64 vcc, exec, s[0:1]
	v_mov_b32_e32 v118, v122
	s_cbranch_vccnz .LBB0_684
	v_mul_f32_e32 v118, 0xbfb8aa3b, v122
	v_exp_f32_e32 v118, v118
	s_nop 0
	v_add_f32_e32 v118, 1.0, v118
	v_rcp_f32_e32 v124, v118
	s_nop 0
	v_fma_f32 v126, -v118, v124, 1.0
	v_fmac_f32_e32 v124, v126, v124
	v_div_fixup_f32 v118, v124, v118, 1.0

; __device__ __forceinline__ unsigned cvt_pk_bf16(float lo, float hi) { const f32x2c v = {lo, hi}; const bf16x2c b = __builtin_convertvector(v, bf16x2c); return __builtin_bit_cast(unsigned, b); }
; __device__ __forceinline__ float sigmoidf_(float x) { return 1.f / (1.f + __expf(-x)); }
;     __device__ __forceinline__ void operator()(const f32x4 (&acc)[2][2][4][2], const Unit& u, int wr, int wc, int fr, int fq) const {
;     ...
;         for (int bj = 0; bj < 2; ++bj) { const int col = (col0 + bj * HALF) & 511;
;             f32x4 b0 = (f32x4){0.f, 0.f, 0.f, 0.f}, b1 = b0;
;             if (kind == 0) { b0 = *(const f32x4*)(w0 + col); b1 = *(const f32x4*)(w0 + col + 4); }
;             else if (kind == 1) { b0 = *(const f32x4*)(a0 + col); b1 = *(const f32x4*)(a0 + col + 4); }
; #pragma unroll
;             for (int ai = 0; ai < 2; ++ai)
; #pragma unroll
;                 for (int m = 0; m < 4; ++m) { const size_t row = (size_t)(row0 + ai * HALF + m * 16);
;                     const f32x4 v0 = acc[ai][bj][m][0] + b0, v1 = acc[ai][bj][m][1] + b1; float o[8];
; #pragma unroll
;                     for (int e = 0; e < 8; ++e) { float x = (e < 4) ? v0[e & 3] : v1[e & 3];
;                         if (kind == 0) x = -0.6065306597126334f * sigmoidf_(x);
;                         else if (kind == 1) x = sigmoidf_(x);
;                         o[e] = x; }
;                     u32x4 w; w.x = cvt_pk_bf16(o[0], o[1]); w.y = cvt_pk_bf16(o[2], o[3]); w.z = cvt_pk_bf16(o[4], o[5]); w.w = cvt_pk_bf16(o[6], o[7]);
;                     *(u32x4*)(O + row * 512 + col) = w; } }
.LBB0_686:
	v_mul_f32_e32 v118, 0xbfb8aa3b, v122
	v_exp_f32_e32 v118, v118
	s_nop 0
	v_add_f32_e32 v118, 1.0, v118
	v_rcp_f32_e32 v123, v118
	s_nop 0
	v_fma_f32 v125, -v118, v123, 1.0
	v_fmac_f32_e32 v123, v125, v123
	v_div_fixup_f32 v118, v123, v118, 1.0
	v_mul_f32_e32 v118, 0xbf1b4598, v118
.LBB0_687:
	v_add_f32_e32 v122, v119, v91
	s_and_b64 vcc, exec, s[2:3]
	s_mov_b64 s[68:69], -1
	s_cbranch_vccnz .LBB0_691
	s_and_b64 vcc, exec, s[0:1]
	v_mov_b32_e32 v119, v122
	s_cbranch_vccnz .LBB0_690
	v_mul_f32_e32 v119, 0xbfb8aa3b, v122
	v_exp_f32_e32 v119, v119
	s_nop 0
	v_add_f32_e32 v119, 1.0, v119
	v_rcp_f32_e32 v124, v119
	s_nop 0
	v_fma_f32 v126, -v119, v124, 1.0
	v_fmac_f32_e32 v124, v126, v124
	v_div_fixup_f32 v119, v124, v119, 1.0

; __device__ __forceinline__ unsigned cvt_pk_bf16(float lo, float hi) { const f32x2c v = {lo, hi}; const bf16x2c b = __builtin_convertvector(v, bf16x2c); return __builtin_bit_cast(unsigned, b); }
; __device__ __forceinline__ float sigmoidf_(float x) { return 1.f / (1.f + __expf(-x)); }
;     __device__ __forceinline__ void operator()(const f32x4 (&acc)[2][2][4][2], const Unit& u, int wr, int wc, int fr, int fq) const {
;     ...
;         for (int bj = 0; bj < 2; ++bj) { const int col = (col0 + bj * HALF) & 511;
;             f32x4 b0 = (f32x4){0.f, 0.f, 0.f, 0.f}, b1 = b0;
;             if (kind == 0) { b0 = *(const f32x4*)(w0 + col); b1 = *(const f32x4*)(w0 + col + 4); }
;             else if (kind == 1) { b0 = *(const f32x4*)(a0 + col); b1 = *(const f32x4*)(a0 + col + 4); }
; #pragma unroll
;             for (int ai = 0; ai < 2; ++ai)
; #pragma unroll
;                 for (int m = 0; m < 4; ++m) { const size_t row = (size_t)(row0 + ai * HALF + m * 16);
;                     const f32x4 v0 = acc[ai][bj][m][0] + b0, v1 = acc[ai][bj][m][1] + b1; float o[8];
; #pragma unroll
;                     for (int e = 0; e < 8; ++e) { float x = (e < 4) ? v0[e & 3] : v1[e & 3];
;                         if (kind == 0) x = -0.6065306597126334f * sigmoidf_(x);
;                         else if (kind == 1) x = sigmoidf_(x);
;                         o[e] = x; }
;                     u32x4 w; w.x = cvt_pk_bf16(o[0], o[1]); w.y = cvt_pk_bf16(o[2], o[3]); w.z = cvt_pk_bf16(o[4], o[5]); w.w = cvt_pk_bf16(o[6], o[7]);
;                     *(u32x4*)(O + row * 512 + col) = w; } }
.LBB0_692:
	v_mul_f32_e32 v119, 0xbfb8aa3b, v122
	v_exp_f32_e32 v119, v119
	s_nop 0
	v_add_f32_e32 v119, 1.0, v119
	v_rcp_f32_e32 v123, v119
	s_nop 0
	v_fma_f32 v125, -v119, v123, 1.0
	v_fmac_f32_e32 v123, v125, v123
	v_div_fixup_f32 v119, v123, v119, 1.0
	v_mul_f32_e32 v119, 0xbf1b4598, v119
.LBB0_693:
	v_add_f32_e32 v122, v112, v80
	s_and_b64 vcc, exec, s[2:3]
	s_mov_b64 s[68:69], -1
	s_cbranch_vccnz .LBB0_697
	s_and_b64 vcc, exec, s[0:1]
	v_mov_b32_e32 v112, v122
	s_cbranch_vccnz .LBB0_696
	v_mul_f32_e32 v112, 0xbfb8aa3b, v122
	v_exp_f32_e32 v112, v112
	s_nop 0
	v_add_f32_e32 v112, 1.0, v112
	v_rcp_f32_e32 v124, v112
	s_nop 0
	v_fma_f32 v126, -v112, v124, 1.0
	v_fmac_f32_e32 v124, v126, v124
	v_div_fixup_f32 v112, v124, v112, 1.0

; __device__ __forceinline__ unsigned cvt_pk_bf16(float lo, float hi) { const f32x2c v = {lo, hi}; const bf16x2c b = __builtin_convertvector(v, bf16x2c); return __builtin_bit_cast(unsigned, b); }
; __device__ __forceinline__ float sigmoidf_(float x) { return 1.f / (1.f + __expf(-x)); }
;     __device__ __forceinline__ void operator()(const f32x4 (&acc)[2][2][4][2], const Unit& u, int wr, int wc, int fr, int fq) const {
;     ...
;         for (int bj = 0; bj < 2; ++bj) { const int col = (col0 + bj * HALF) & 511;
;             f32x4 b0 = (f32x4){0.f, 0.f, 0.f, 0.f}, b1 = b0;
;             if (kind == 0) { b0 = *(const f32x4*)(w0 + col); b1 = *(const f32x4*)(w0 + col + 4); }
;             else if (kind == 1) { b0 = *(const f32x4*)(a0 + col); b1 = *(const f32x4*)(a0 + col + 4); }
; #pragma unroll
;             for (int ai = 0; ai < 2; ++ai)
; #pragma unroll
;                 for (int m = 0; m < 4; ++m) { const size_t row = (size_t)(row0 + ai * HALF + m * 16);
;                     const f32x4 v0 = acc[ai][bj][m][0] + b0, v1 = acc[ai][bj][m][1] + b1; float o[8];
; #pragma unroll
;                     for (int e = 0; e < 8; ++e) { float x = (e < 4) ? v0[e & 3] : v1[e & 3];
;                         if (kind == 0) x = -0.6065306597126334f * sigmoidf_(x);
;                         else if (kind == 1) x = sigmoidf_(x);
;                         o[e] = x; }
;                     u32x4 w; w.x = cvt_pk_bf16(o[0], o[1]); w.y = cvt_pk_bf16(o[2], o[3]); w.z = cvt_pk_bf16(o[4], o[5]); w.w = cvt_pk_bf16(o[6], o[7]);
;                     *(u32x4*)(O + row * 512 + col) = w; } }
.LBB0_698:
	v_mul_f32_e32 v112, 0xbfb8aa3b, v122
	v_exp_f32_e32 v112, v112
	s_nop 0
	v_add_f32_e32 v112, 1.0, v112
	v_rcp_f32_e32 v123, v112
	s_nop 0
	v_fma_f32 v125, -v112, v123, 1.0
	v_fmac_f32_e32 v123, v125, v123
	v_div_fixup_f32 v112, v123, v112, 1.0
	v_mul_f32_e32 v112, 0xbf1b4598, v112
.LBB0_699:
	v_add_f32_e32 v122, v113, v81
	s_and_b64 vcc, exec, s[2:3]
	s_mov_b64 s[68:69], -1
	s_cbranch_vccnz .LBB0_703
	s_and_b64 vcc, exec, s[0:1]
	v_mov_b32_e32 v113, v122
	s_cbranch_vccnz .LBB0_702
	v_mul_f32_e32 v113, 0xbfb8aa3b, v122
	v_exp_f32_e32 v113, v113
	s_nop 0
	v_add_f32_e32 v113, 1.0, v113
	v_rcp_f32_e32 v124, v113
	s_nop 0
	v_fma_f32 v126, -v113, v124, 1.0
	v_fmac_f32_e32 v124, v126, v124
	v_div_fixup_f32 v113, v124, v113, 1.0

; __device__ __forceinline__ unsigned cvt_pk_bf16(float lo, float hi) { const f32x2c v = {lo, hi}; const bf16x2c b = __builtin_convertvector(v, bf16x2c); return __builtin_bit_cast(unsigned, b); }
; __device__ __forceinline__ float sigmoidf_(float x) { return 1.f / (1.f + __expf(-x)); }
;     __device__ __forceinline__ void operator()(const f32x4 (&acc)[2][2][4][2], const Unit& u, int wr, int wc, int fr, int fq) const {
;     ...
;         for (int bj = 0; bj < 2; ++bj) { const int col = (col0 + bj * HALF) & 511;
;             f32x4 b0 = (f32x4){0.f, 0.f, 0.f, 0.f}, b1 = b0;
;             if (kind == 0) { b0 = *(const f32x4*)(w0 + col); b1 = *(const f32x4*)(w0 + col + 4); }
;             else if (kind == 1) { b0 = *(const f32x4*)(a0 + col); b1 = *(const f32x4*)(a0 + col + 4); }
; #pragma unroll
;             for (int ai = 0; ai < 2; ++ai)
; #pragma unroll
;                 for (int m = 0; m < 4; ++m) { const size_t row = (size_t)(row0 + ai * HALF + m * 16);
;                     const f32x4 v0 = acc[ai][bj][m][0] + b0, v1 = acc[ai][bj][m][1] + b1; float o[8];
; #pragma unroll
;                     for (int e = 0; e < 8; ++e) { float x = (e < 4) ? v0[e & 3] : v1[e & 3];
;                         if (kind == 0) x = -0.6065306597126334f * sigmoidf_(x);
;                         else if (kind == 1) x = sigmoidf_(x);
;                         o[e] = x; }
;                     u32x4 w; w.x = cvt_pk_bf16(o[0], o[1]); w.y = cvt_pk_bf16(o[2], o[3]); w.z = cvt_pk_bf16(o[4], o[5]); w.w = cvt_pk_bf16(o[6], o[7]);
;                     *(u32x4*)(O + row * 512 + col) = w; } }
.LBB0_704:
	v_mul_f32_e32 v113, 0xbfb8aa3b, v122
	v_exp_f32_e32 v113, v113
	s_nop 0
	v_add_f32_e32 v113, 1.0, v113
	v_rcp_f32_e32 v123, v113
	s_nop 0
	v_fma_f32 v125, -v113, v123, 1.0
	v_fmac_f32_e32 v123, v125, v123
	v_div_fixup_f32 v113, v123, v113, 1.0
	v_mul_f32_e32 v113, 0xbf1b4598, v113
.LBB0_705:
	v_add_f32_e32 v122, v114, v82
	s_and_b64 vcc, exec, s[2:3]
	s_mov_b64 s[68:69], -1
	s_cbranch_vccnz .LBB0_709
	s_and_b64 vcc, exec, s[0:1]
	v_mov_b32_e32 v114, v122
	s_cbranch_vccnz .LBB0_708
	v_mul_f32_e32 v114, 0xbfb8aa3b, v122
	v_exp_f32_e32 v114, v114
	s_nop 0
	v_add_f32_e32 v114, 1.0, v114
	v_rcp_f32_e32 v124, v114
	s_nop 0
	v_fma_f32 v126, -v114, v124, 1.0
	v_fmac_f32_e32 v124, v126, v124
	v_div_fixup_f32 v114, v124, v114, 1.0

; __device__ __forceinline__ unsigned cvt_pk_bf16(float lo, float hi) { const f32x2c v = {lo, hi}; const bf16x2c b = __builtin_convertvector(v, bf16x2c); return __builtin_bit_cast(unsigned, b); }
; __device__ __forceinline__ float sigmoidf_(float x) { return 1.f / (1.f + __expf(-x)); }
;     __device__ __forceinline__ void operator()(const f32x4 (&acc)[2][2][4][2], const Unit& u, int wr, int wc, int fr, int fq) const {
;     ...
;         for (int bj = 0; bj < 2; ++bj) { const int col = (col0 + bj * HALF) & 511;
;             f32x4 b0 = (f32x4){0.f, 0.f, 0.f, 0.f}, b1 = b0;
;             if (kind == 0) { b0 = *(const f32x4*)(w0 + col); b1 = *(const f32x4*)(w0 + col + 4); }
;             else if (kind == 1) { b0 = *(const f32x4*)(a0 + col); b1 = *(const f32x4*)(a0 + col + 4); }
; #pragma unroll
;             for (int ai = 0; ai < 2; ++ai)
; #pragma unroll
;                 for (int m = 0; m < 4; ++m) { const size_t row = (size_t)(row0 + ai * HALF + m * 16);
;                     const f32x4 v0 = acc[ai][bj][m][0] + b0, v1 = acc[ai][bj][m][1] + b1; float o[8];
; #pragma unroll
;                     for (int e = 0; e < 8; ++e) { float x = (e < 4) ? v0[e & 3] : v1[e & 3];
;                         if (kind == 0) x = -0.6065306597126334f * sigmoidf_(x);
;                         else if (kind == 1) x = sigmoidf_(x);
;                         o[e] = x; }
;                     u32x4 w; w.x = cvt_pk_bf16(o[0], o[1]); w.y = cvt_pk_bf16(o[2], o[3]); w.z = cvt_pk_bf16(o[4], o[5]); w.w = cvt_pk_bf16(o[6], o[7]);
;                     *(u32x4*)(O + row * 512 + col) = w; } }
.LBB0_710:
	v_mul_f32_e32 v114, 0xbfb8aa3b, v122
	v_exp_f32_e32 v114, v114
	s_nop 0
	v_add_f32_e32 v114, 1.0, v114
	v_rcp_f32_e32 v123, v114
	s_nop 0
	v_fma_f32 v125, -v114, v123, 1.0
	v_fmac_f32_e32 v123, v125, v123
	v_div_fixup_f32 v114, v123, v114, 1.0
	v_mul_f32_e32 v114, 0xbf1b4598, v114
.LBB0_711:
	v_add_f32_e32 v115, v115, v83
	s_and_b64 vcc, exec, s[2:3]
	s_mov_b64 s[68:69], -1
	s_cbranch_vccnz .LBB0_715
	s_and_b64 vcc, exec, s[0:1]
	v_mov_b32_e32 v122, v115
	s_cbranch_vccnz .LBB0_714
	v_mul_f32_e32 v122, 0xbfb8aa3b, v115
	v_exp_f32_e32 v122, v122
	s_nop 0
	v_add_f32_e32 v122, 1.0, v122
	v_rcp_f32_e32 v124, v122
	s_nop 0
	v_fma_f32 v126, -v122, v124, 1.0
	v_fmac_f32_e32 v124, v126, v124
	v_div_fixup_f32 v122, v124, v122, 1.0

; __device__ __forceinline__ unsigned cvt_pk_bf16(float lo, float hi) { const f32x2c v = {lo, hi}; const bf16x2c b = __builtin_convertvector(v, bf16x2c); return __builtin_bit_cast(unsigned, b); }
; __device__ __forceinline__ float sigmoidf_(float x) { return 1.f / (1.f + __expf(-x)); }
;     __device__ __forceinline__ void operator()(const f32x4 (&acc)[2][2][4][2], const Unit& u, int wr, int wc, int fr, int fq) const {
;     ...
;         for (int bj = 0; bj < 2; ++bj) { const int col = (col0 + bj * HALF) & 511;
;             f32x4 b0 = (f32x4){0.f, 0.f, 0.f, 0.f}, b1 = b0;
;             if (kind == 0) { b0 = *(const f32x4*)(w0 + col); b1 = *(const f32x4*)(w0 + col + 4); }
;             else if (kind == 1) { b0 = *(const f32x4*)(a0 + col); b1 = *(const f32x4*)(a0 + col + 4); }
; #pragma unroll
;             for (int ai = 0; ai < 2; ++ai)
; #pragma unroll
;                 for (int m = 0; m < 4; ++m) { const size_t row = (size_t)(row0 + ai * HALF + m * 16);
;                     const f32x4 v0 = acc[ai][bj][m][0] + b0, v1 = acc[ai][bj][m][1] + b1; float o[8];
; #pragma unroll
;                     for (int e = 0; e < 8; ++e) { float x = (e < 4) ? v0[e & 3] : v1[e & 3];
;                         if (kind == 0) x = -0.6065306597126334f * sigmoidf_(x);
;                         else if (kind == 1) x = sigmoidf_(x);
;                         o[e] = x; }
;                     u32x4 w; w.x = cvt_pk_bf16(o[0], o[1]); w.y = cvt_pk_bf16(o[2], o[3]); w.z = cvt_pk_bf16(o[4], o[5]); w.w = cvt_pk_bf16(o[6], o[7]);
;                     *(u32x4*)(O + row * 512 + col) = w; } }
.LBB0_716:
	v_mul_f32_e32 v115, 0xbfb8aa3b, v115
	v_exp_f32_e32 v115, v115
	s_nop 0
	v_add_f32_e32 v115, 1.0, v115
	v_rcp_f32_e32 v123, v115
	s_nop 0
	v_fma_f32 v125, -v115, v123, 1.0
	v_fmac_f32_e32 v123, v125, v123
	v_div_fixup_f32 v115, v123, v115, 1.0
	v_mul_f32_e32 v122, 0xbf1b4598, v115
.LBB0_717:
	v_or_b32_e32 v124, 32, v132
	v_ashrrev_i32_e32 v125, 31, v124
	v_cvt_pk_bf16_f32 v116, v116, v117
	v_cvt_pk_bf16_f32 v117, v118, v119
	v_cvt_pk_bf16_f32 v118, v112, v113
	v_lshlrev_b64 v[112:113], 10, v[124:125]
	v_cvt_pk_bf16_f32 v119, v114, v122
	v_lshl_add_u64 v[112:113], v[130:131], 0, v[112:113]
	v_add_f32_e32 v114, v108, v88
	s_and_b64 vcc, exec, s[2:3]
	s_mov_b64 s[68:69], -1
	global_store_dwordx4 v[112:113], v[116:119], off
	s_cbranch_vccnz .LBB0_721
	s_and_b64 vcc, exec, s[0:1]
	v_mov_b32_e32 v108, v114
	s_cbranch_vccnz .LBB0_720
	v_mul_f32_e32 v108, 0xbfb8aa3b, v114
	v_exp_f32_e32 v108, v108
	s_nop 0
	v_add_f32_e32 v108, 1.0, v108
	v_rcp_f32_e32 v116, v108
	s_nop 0
	v_fma_f32 v118, -v108, v116, 1.0
	v_fmac_f32_e32 v116, v118, v116
	v_div_fixup_f32 v108, v116, v108, 1.0

; __device__ __forceinline__ unsigned cvt_pk_bf16(float lo, float hi) { const f32x2c v = {lo, hi}; const bf16x2c b = __builtin_convertvector(v, bf16x2c); return __builtin_bit_cast(unsigned, b); }
; __device__ __forceinline__ float sigmoidf_(float x) { return 1.f / (1.f + __expf(-x)); }
;     __device__ __forceinline__ void operator()(const f32x4 (&acc)[2][2][4][2], const Unit& u, int wr, int wc, int fr, int fq) const {
;     ...
;         for (int bj = 0; bj < 2; ++bj) { const int col = (col0 + bj * HALF) & 511;
;             f32x4 b0 = (f32x4){0.f, 0.f, 0.f, 0.f}, b1 = b0;
;             if (kind == 0) { b0 = *(const f32x4*)(w0 + col); b1 = *(const f32x4*)(w0 + col + 4); }
;             else if (kind == 1) { b0 = *(const f32x4*)(a0 + col); b1 = *(const f32x4*)(a0 + col + 4); }
; #pragma unroll
;             for (int ai = 0; ai < 2; ++ai)
; #pragma unroll
;                 for (int m = 0; m < 4; ++m) { const size_t row = (size_t)(row0 + ai * HALF + m * 16);
;                     const f32x4 v0 = acc[ai][bj][m][0] + b0, v1 = acc[ai][bj][m][1] + b1; float o[8];
; #pragma unroll
;                     for (int e = 0; e < 8; ++e) { float x = (e < 4) ? v0[e & 3] : v1[e & 3];
;                         if (kind == 0) x = -0.6065306597126334f * sigmoidf_(x);
;                         else if (kind == 1) x = sigmoidf_(x);
;                         o[e] = x; }
;                     u32x4 w; w.x = cvt_pk_bf16(o[0], o[1]); w.y = cvt_pk_bf16(o[2], o[3]); w.z = cvt_pk_bf16(o[4], o[5]); w.w = cvt_pk_bf16(o[6], o[7]);
;                     *(u32x4*)(O + row * 512 + col) = w; } }
.LBB0_722:
	v_mul_f32_e32 v108, 0xbfb8aa3b, v114
	v_exp_f32_e32 v108, v108
	s_nop 0
	v_add_f32_e32 v108, 1.0, v108
	v_rcp_f32_e32 v115, v108
	s_nop 0
	v_fma_f32 v117, -v108, v115, 1.0
	v_fmac_f32_e32 v115, v117, v115
	v_div_fixup_f32 v108, v115, v108, 1.0
	v_mul_f32_e32 v108, 0xbf1b4598, v108
.LBB0_723:
	v_add_f32_e32 v114, v109, v89
	s_and_b64 vcc, exec, s[2:3]
	s_mov_b64 s[68:69], -1
	s_cbranch_vccnz .LBB0_727
	s_and_b64 vcc, exec, s[0:1]
	v_mov_b32_e32 v109, v114
	s_cbranch_vccnz .LBB0_726
	v_mul_f32_e32 v109, 0xbfb8aa3b, v114
	v_exp_f32_e32 v109, v109
	s_nop 0
	v_add_f32_e32 v109, 1.0, v109
	v_rcp_f32_e32 v116, v109
	s_nop 0
	v_fma_f32 v118, -v109, v116, 1.0
	v_fmac_f32_e32 v116, v118, v116
	v_div_fixup_f32 v109, v116, v109, 1.0

; __device__ __forceinline__ unsigned cvt_pk_bf16(float lo, float hi) { const f32x2c v = {lo, hi}; const bf16x2c b = __builtin_convertvector(v, bf16x2c); return __builtin_bit_cast(unsigned, b); }
; __device__ __forceinline__ float sigmoidf_(float x) { return 1.f / (1.f + __expf(-x)); }
;     __device__ __forceinline__ void operator()(const f32x4 (&acc)[2][2][4][2], const Unit& u, int wr, int wc, int fr, int fq) const {
;     ...
;         for (int bj = 0; bj < 2; ++bj) { const int col = (col0 + bj * HALF) & 511;
;             f32x4 b0 = (f32x4){0.f, 0.f, 0.f, 0.f}, b1 = b0;
;             if (kind == 0) { b0 = *(const f32x4*)(w0 + col); b1 = *(const f32x4*)(w0 + col + 4); }
;             else if (kind == 1) { b0 = *(const f32x4*)(a0 + col); b1 = *(const f32x4*)(a0 + col + 4); }
; #pragma unroll
;             for (int ai = 0; ai < 2; ++ai)
; #pragma unroll
;                 for (int m = 0; m < 4; ++m) { const size_t row = (size_t)(row0 + ai * HALF + m * 16);
;                     const f32x4 v0 = acc[ai][bj][m][0] + b0, v1 = acc[ai][bj][m][1] + b1; float o[8];
; #pragma unroll
;                     for (int e = 0; e < 8; ++e) { float x = (e < 4) ? v0[e & 3] : v1[e & 3];
;                         if (kind == 0) x = -0.6065306597126334f * sigmoidf_(x);
;                         else if (kind == 1) x = sigmoidf_(x);
;                         o[e] = x; }
;                     u32x4 w; w.x = cvt_pk_bf16(o[0], o[1]); w.y = cvt_pk_bf16(o[2], o[3]); w.z = cvt_pk_bf16(o[4], o[5]); w.w = cvt_pk_bf16(o[6], o[7]);
;                     *(u32x4*)(O + row * 512 + col) = w; } }
.LBB0_728:
	v_mul_f32_e32 v109, 0xbfb8aa3b, v114
	v_exp_f32_e32 v109, v109
	s_nop 0
	v_add_f32_e32 v109, 1.0, v109
	v_rcp_f32_e32 v115, v109
	s_nop 0
	v_fma_f32 v117, -v109, v115, 1.0
	v_fmac_f32_e32 v115, v117, v115
	v_div_fixup_f32 v109, v115, v109, 1.0
	v_mul_f32_e32 v109, 0xbf1b4598, v109
.LBB0_729:
	v_add_f32_e32 v114, v110, v90
	s_and_b64 vcc, exec, s[2:3]
	s_mov_b64 s[68:69], -1
	s_cbranch_vccnz .LBB0_733
	s_and_b64 vcc, exec, s[0:1]
	v_mov_b32_e32 v110, v114
	s_cbranch_vccnz .LBB0_732
	v_mul_f32_e32 v110, 0xbfb8aa3b, v114
	v_exp_f32_e32 v110, v110
	s_nop 0
	v_add_f32_e32 v110, 1.0, v110
	v_rcp_f32_e32 v116, v110
	s_nop 0
	v_fma_f32 v118, -v110, v116, 1.0
	v_fmac_f32_e32 v116, v118, v116
	v_div_fixup_f32 v110, v116, v110, 1.0

; __device__ __forceinline__ unsigned cvt_pk_bf16(float lo, float hi) { const f32x2c v = {lo, hi}; const bf16x2c b = __builtin_convertvector(v, bf16x2c); return __builtin_bit_cast(unsigned, b); }
; __device__ __forceinline__ float sigmoidf_(float x) { return 1.f / (1.f + __expf(-x)); }
;     __device__ __forceinline__ void operator()(const f32x4 (&acc)[2][2][4][2], const Unit& u, int wr, int wc, int fr, int fq) const {
;     ...
;         for (int bj = 0; bj < 2; ++bj) { const int col = (col0 + bj * HALF) & 511;
;             f32x4 b0 = (f32x4){0.f, 0.f, 0.f, 0.f}, b1 = b0;
;             if (kind == 0) { b0 = *(const f32x4*)(w0 + col); b1 = *(const f32x4*)(w0 + col + 4); }
;             else if (kind == 1) { b0 = *(const f32x4*)(a0 + col); b1 = *(const f32x4*)(a0 + col + 4); }
; #pragma unroll
;             for (int ai = 0; ai < 2; ++ai)
; #pragma unroll
;                 for (int m = 0; m < 4; ++m) { const size_t row = (size_t)(row0 + ai * HALF + m * 16);
;                     const f32x4 v0 = acc[ai][bj][m][0] + b0, v1 = acc[ai][bj][m][1] + b1; float o[8];
; #pragma unroll
;                     for (int e = 0; e < 8; ++e) { float x = (e < 4) ? v0[e & 3] : v1[e & 3];
;                         if (kind == 0) x = -0.6065306597126334f * sigmoidf_(x);
;                         else if (kind == 1) x = sigmoidf_(x);
;                         o[e] = x; }
;                     u32x4 w; w.x = cvt_pk_bf16(o[0], o[1]); w.y = cvt_pk_bf16(o[2], o[3]); w.z = cvt_pk_bf16(o[4], o[5]); w.w = cvt_pk_bf16(o[6], o[7]);
;                     *(u32x4*)(O + row * 512 + col) = w; } }
.LBB0_734:
	v_mul_f32_e32 v110, 0xbfb8aa3b, v114
	v_exp_f32_e32 v110, v110
	s_nop 0
	v_add_f32_e32 v110, 1.0, v110
	v_rcp_f32_e32 v115, v110
	s_nop 0
	v_fma_f32 v117, -v110, v115, 1.0
	v_fmac_f32_e32 v115, v117, v115
	v_div_fixup_f32 v110, v115, v110, 1.0
	v_mul_f32_e32 v110, 0xbf1b4598, v110
.LBB0_735:
	v_add_f32_e32 v114, v111, v91
	s_and_b64 vcc, exec, s[2:3]
	s_mov_b64 s[68:69], -1
	s_cbranch_vccnz .LBB0_739
	s_and_b64 vcc, exec, s[0:1]
	v_mov_b32_e32 v111, v114
	s_cbranch_vccnz .LBB0_738
	v_mul_f32_e32 v111, 0xbfb8aa3b, v114
	v_exp_f32_e32 v111, v111
	s_nop 0
	v_add_f32_e32 v111, 1.0, v111
	v_rcp_f32_e32 v116, v111
	s_nop 0
	v_fma_f32 v118, -v111, v116, 1.0
	v_fmac_f32_e32 v116, v118, v116
	v_div_fixup_f32 v111, v116, v111, 1.0

; __device__ __forceinline__ unsigned cvt_pk_bf16(float lo, float hi) { const f32x2c v = {lo, hi}; const bf16x2c b = __builtin_convertvector(v, bf16x2c); return __builtin_bit_cast(unsigned, b); }
; __device__ __forceinline__ float sigmoidf_(float x) { return 1.f / (1.f + __expf(-x)); }
;     __device__ __forceinline__ void operator()(const f32x4 (&acc)[2][2][4][2], const Unit& u, int wr, int wc, int fr, int fq) const {
;     ...
;         for (int bj = 0; bj < 2; ++bj) { const int col = (col0 + bj * HALF) & 511;
;             f32x4 b0 = (f32x4){0.f, 0.f, 0.f, 0.f}, b1 = b0;
;             if (kind == 0) { b0 = *(const f32x4*)(w0 + col); b1 = *(const f32x4*)(w0 + col + 4); }
;             else if (kind == 1) { b0 = *(const f32x4*)(a0 + col); b1 = *(const f32x4*)(a0 + col + 4); }
; #pragma unroll
;             for (int ai = 0; ai < 2; ++ai)
; #pragma unroll
;                 for (int m = 0; m < 4; ++m) { const size_t row = (size_t)(row0 + ai * HALF + m * 16);
;                     const f32x4 v0 = acc[ai][bj][m][0] + b0, v1 = acc[ai][bj][m][1] + b1; float o[8];
; #pragma unroll
;                     for (int e = 0; e < 8; ++e) { float x = (e < 4) ? v0[e & 3] : v1[e & 3];
;                         if (kind == 0) x = -0.6065306597126334f * sigmoidf_(x);
;                         else if (kind == 1) x = sigmoidf_(x);
;                         o[e] = x; }
;                     u32x4 w; w.x = cvt_pk_bf16(o[0], o[1]); w.y = cvt_pk_bf16(o[2], o[3]); w.z = cvt_pk_bf16(o[4], o[5]); w.w = cvt_pk_bf16(o[6], o[7]);
;                     *(u32x4*)(O + row * 512 + col) = w; } }
.LBB0_740:
	v_mul_f32_e32 v111, 0xbfb8aa3b, v114
	v_exp_f32_e32 v111, v111
	s_nop 0
	v_add_f32_e32 v111, 1.0, v111
	v_rcp_f32_e32 v115, v111
	s_nop 0
	v_fma_f32 v117, -v111, v115, 1.0
	v_fmac_f32_e32 v115, v117, v115
	v_div_fixup_f32 v111, v115, v111, 1.0
	v_mul_f32_e32 v111, 0xbf1b4598, v111
.LBB0_741:
	v_add_f32_e32 v114, v104, v80
	s_and_b64 vcc, exec, s[2:3]
	s_mov_b64 s[68:69], -1
	s_cbranch_vccnz .LBB0_745
	s_and_b64 vcc, exec, s[0:1]
	v_mov_b32_e32 v104, v114
	s_cbranch_vccnz .LBB0_744
	v_mul_f32_e32 v104, 0xbfb8aa3b, v114
	v_exp_f32_e32 v104, v104
	s_nop 0
	v_add_f32_e32 v104, 1.0, v104
	v_rcp_f32_e32 v116, v104
	s_nop 0
	v_fma_f32 v118, -v104, v116, 1.0
	v_fmac_f32_e32 v116, v118, v116
	v_div_fixup_f32 v104, v116, v104, 1.0

; __device__ __forceinline__ unsigned cvt_pk_bf16(float lo, float hi) { const f32x2c v = {lo, hi}; const bf16x2c b = __builtin_convertvector(v, bf16x2c); return __builtin_bit_cast(unsigned, b); }
; __device__ __forceinline__ float sigmoidf_(float x) { return 1.f / (1.f + __expf(-x)); }
;     __device__ __forceinline__ void operator()(const f32x4 (&acc)[2][2][4][2], const Unit& u, int wr, int wc, int fr, int fq) const {
;     ...
;         for (int bj = 0; bj < 2; ++bj) { const int col = (col0 + bj * HALF) & 511;
;             f32x4 b0 = (f32x4){0.f, 0.f, 0.f, 0.f}, b1 = b0;
;             if (kind == 0) { b0 = *(const f32x4*)(w0 + col); b1 = *(const f32x4*)(w0 + col + 4); }
;             else if (kind == 1) { b0 = *(const f32x4*)(a0 + col); b1 = *(const f32x4*)(a0 + col + 4); }
; #pragma unroll
;             for (int ai = 0; ai < 2; ++ai)
; #pragma unroll
;                 for (int m = 0; m < 4; ++m) { const size_t row = (size_t)(row0 + ai * HALF + m * 16);
;                     const f32x4 v0 = acc[ai][bj][m][0] + b0, v1 = acc[ai][bj][m][1] + b1; float o[8];
; #pragma unroll
;                     for (int e = 0; e < 8; ++e) { float x = (e < 4) ? v0[e & 3] : v1[e & 3];
;                         if (kind == 0) x = -0.6065306597126334f * sigmoidf_(x);
;                         else if (kind == 1) x = sigmoidf_(x);
;                         o[e] = x; }
;                     u32x4 w; w.x = cvt_pk_bf16(o[0], o[1]); w.y = cvt_pk_bf16(o[2], o[3]); w.z = cvt_pk_bf16(o[4], o[5]); w.w = cvt_pk_bf16(o[6], o[7]);
;                     *(u32x4*)(O + row * 512 + col) = w; } }
.LBB0_746:
	v_mul_f32_e32 v104, 0xbfb8aa3b, v114
	v_exp_f32_e32 v104, v104
	s_nop 0
	v_add_f32_e32 v104, 1.0, v104
	v_rcp_f32_e32 v115, v104
	s_nop 0
	v_fma_f32 v117, -v104, v115, 1.0
	v_fmac_f32_e32 v115, v117, v115
	v_div_fixup_f32 v104, v115, v104, 1.0
	v_mul_f32_e32 v104, 0xbf1b4598, v104
.LBB0_747:
	v_add_f32_e32 v114, v105, v81
	s_and_b64 vcc, exec, s[2:3]
	s_mov_b64 s[68:69], -1
	s_cbranch_vccnz .LBB0_751
	s_and_b64 vcc, exec, s[0:1]
	v_mov_b32_e32 v105, v114
	s_cbranch_vccnz .LBB0_750
	v_mul_f32_e32 v105, 0xbfb8aa3b, v114
	v_exp_f32_e32 v105, v105
	s_nop 0
	v_add_f32_e32 v105, 1.0, v105
	v_rcp_f32_e32 v116, v105
	s_nop 0
	v_fma_f32 v118, -v105, v116, 1.0
	v_fmac_f32_e32 v116, v118, v116
	v_div_fixup_f32 v105, v116, v105, 1.0

; __device__ __forceinline__ unsigned cvt_pk_bf16(float lo, float hi) { const f32x2c v = {lo, hi}; const bf16x2c b = __builtin_convertvector(v, bf16x2c); return __builtin_bit_cast(unsigned, b); }
; __device__ __forceinline__ float sigmoidf_(float x) { return 1.f / (1.f + __expf(-x)); }
;     __device__ __forceinline__ void operator()(const f32x4 (&acc)[2][2][4][2], const Unit& u, int wr, int wc, int fr, int fq) const {
;     ...
;         for (int bj = 0; bj < 2; ++bj) { const int col = (col0 + bj * HALF) & 511;
;             f32x4 b0 = (f32x4){0.f, 0.f, 0.f, 0.f}, b1 = b0;
;             if (kind == 0) { b0 = *(const f32x4*)(w0 + col); b1 = *(const f32x4*)(w0 + col + 4); }
;             else if (kind == 1) { b0 = *(const f32x4*)(a0 + col); b1 = *(const f32x4*)(a0 + col + 4); }
; #pragma unroll
;             for (int ai = 0; ai < 2; ++ai)
; #pragma unroll
;                 for (int m = 0; m < 4; ++m) { const size_t row = (size_t)(row0 + ai * HALF + m * 16);
;                     const f32x4 v0 = acc[ai][bj][m][0] + b0, v1 = acc[ai][bj][m][1] + b1; float o[8];
; #pragma unroll
;                     for (int e = 0; e < 8; ++e) { float x = (e < 4) ? v0[e & 3] : v1[e & 3];
;                         if (kind == 0) x = -0.6065306597126334f * sigmoidf_(x);
;                         else if (kind == 1) x = sigmoidf_(x);
;                         o[e] = x; }
;                     u32x4 w; w.x = cvt_pk_bf16(o[0], o[1]); w.y = cvt_pk_bf16(o[2], o[3]); w.z = cvt_pk_bf16(o[4], o[5]); w.w = cvt_pk_bf16(o[6], o[7]);
;                     *(u32x4*)(O + row * 512 + col) = w; } }
.LBB0_752:
	v_mul_f32_e32 v105, 0xbfb8aa3b, v114
	v_exp_f32_e32 v105, v105
	s_nop 0
	v_add_f32_e32 v105, 1.0, v105
	v_rcp_f32_e32 v115, v105
	s_nop 0
	v_fma_f32 v117, -v105, v115, 1.0
	v_fmac_f32_e32 v115, v117, v115
	v_div_fixup_f32 v105, v115, v105, 1.0
	v_mul_f32_e32 v105, 0xbf1b4598, v105
.LBB0_753:
	v_add_f32_e32 v114, v106, v82
	s_and_b64 vcc, exec, s[2:3]
	s_mov_b64 s[68:69], -1
	s_cbranch_vccnz .LBB0_757
	s_and_b64 vcc, exec, s[0:1]
	v_mov_b32_e32 v106, v114
	s_cbranch_vccnz .LBB0_756
	v_mul_f32_e32 v106, 0xbfb8aa3b, v114
	v_exp_f32_e32 v106, v106
	s_nop 0
	v_add_f32_e32 v106, 1.0, v106
	v_rcp_f32_e32 v116, v106
	s_nop 0
	v_fma_f32 v118, -v106, v116, 1.0
	v_fmac_f32_e32 v116, v118, v116
	v_div_fixup_f32 v106, v116, v106, 1.0

; __device__ __forceinline__ unsigned cvt_pk_bf16(float lo, float hi) { const f32x2c v = {lo, hi}; const bf16x2c b = __builtin_convertvector(v, bf16x2c); return __builtin_bit_cast(unsigned, b); }
; __device__ __forceinline__ float sigmoidf_(float x) { return 1.f / (1.f + __expf(-x)); }
;     __device__ __forceinline__ void operator()(const f32x4 (&acc)[2][2][4][2], const Unit& u, int wr, int wc, int fr, int fq) const {
;     ...
;         for (int bj = 0; bj < 2; ++bj) { const int col = (col0 + bj * HALF) & 511;
;             f32x4 b0 = (f32x4){0.f, 0.f, 0.f, 0.f}, b1 = b0;
;             if (kind == 0) { b0 = *(const f32x4*)(w0 + col); b1 = *(const f32x4*)(w0 + col + 4); }
;             else if (kind == 1) { b0 = *(const f32x4*)(a0 + col); b1 = *(const f32x4*)(a0 + col + 4); }
; #pragma unroll
;             for (int ai = 0; ai < 2; ++ai)
; #pragma unroll
;                 for (int m = 0; m < 4; ++m) { const size_t row = (size_t)(row0 + ai * HALF + m * 16);
;                     const f32x4 v0 = acc[ai][bj][m][0] + b0, v1 = acc[ai][bj][m][1] + b1; float o[8];
; #pragma unroll
;                     for (int e = 0; e < 8; ++e) { float x = (e < 4) ? v0[e & 3] : v1[e & 3];
;                         if (kind == 0) x = -0.6065306597126334f * sigmoidf_(x);
;                         else if (kind == 1) x = sigmoidf_(x);
;                         o[e] = x; }
;                     u32x4 w; w.x = cvt_pk_bf16(o[0], o[1]); w.y = cvt_pk_bf16(o[2], o[3]); w.z = cvt_pk_bf16(o[4], o[5]); w.w = cvt_pk_bf16(o[6], o[7]);
;                     *(u32x4*)(O + row * 512 + col) = w; } }
.LBB0_758:
	v_mul_f32_e32 v106, 0xbfb8aa3b, v114
	v_exp_f32_e32 v106, v106
	s_nop 0
	v_add_f32_e32 v106, 1.0, v106
	v_rcp_f32_e32 v115, v106
	s_nop 0
	v_fma_f32 v117, -v106, v115, 1.0
	v_fmac_f32_e32 v115, v117, v115
	v_div_fixup_f32 v106, v115, v106, 1.0
	v_mul_f32_e32 v106, 0xbf1b4598, v106
.LBB0_759:
	v_add_f32_e32 v107, v107, v83
	s_and_b64 vcc, exec, s[2:3]
	s_mov_b64 s[68:69], -1
	s_cbranch_vccnz .LBB0_763
	s_and_b64 vcc, exec, s[0:1]
	v_mov_b32_e32 v114, v107
	s_cbranch_vccnz .LBB0_762
	v_mul_f32_e32 v114, 0xbfb8aa3b, v107
	v_exp_f32_e32 v114, v114
	s_nop 0
	v_add_f32_e32 v114, 1.0, v114
	v_rcp_f32_e32 v116, v114
	s_nop 0
	v_fma_f32 v118, -v114, v116, 1.0
	v_fmac_f32_e32 v116, v118, v116
	v_div_fixup_f32 v114, v116, v114, 1.0

; __device__ __forceinline__ unsigned cvt_pk_bf16(float lo, float hi) { const f32x2c v = {lo, hi}; const bf16x2c b = __builtin_convertvector(v, bf16x2c); return __builtin_bit_cast(unsigned, b); }
; __device__ __forceinline__ float sigmoidf_(float x) { return 1.f / (1.f + __expf(-x)); }
;     __device__ __forceinline__ void operator()(const f32x4 (&acc)[2][2][4][2], const Unit& u, int wr, int wc, int fr, int fq) const {
;     ...
;         for (int bj = 0; bj < 2; ++bj) { const int col = (col0 + bj * HALF) & 511;
;             f32x4 b0 = (f32x4){0.f, 0.f, 0.f, 0.f}, b1 = b0;
;             if (kind == 0) { b0 = *(const f32x4*)(w0 + col); b1 = *(const f32x4*)(w0 + col + 4); }
;             else if (kind == 1) { b0 = *(const f32x4*)(a0 + col); b1 = *(const f32x4*)(a0 + col + 4); }
; #pragma unroll
;             for (int ai = 0; ai < 2; ++ai)
; #pragma unroll
;                 for (int m = 0; m < 4; ++m) { const size_t row = (size_t)(row0 + ai * HALF + m * 16);
;                     const f32x4 v0 = acc[ai][bj][m][0] + b0, v1 = acc[ai][bj][m][1] + b1; float o[8];
; #pragma unroll
;                     for (int e = 0; e < 8; ++e) { float x = (e < 4) ? v0[e & 3] : v1[e & 3];
;                         if (kind == 0) x = -0.6065306597126334f * sigmoidf_(x);
;                         else if (kind == 1) x = sigmoidf_(x);
;                         o[e] = x; }
;                     u32x4 w; w.x = cvt_pk_bf16(o[0], o[1]); w.y = cvt_pk_bf16(o[2], o[3]); w.z = cvt_pk_bf16(o[4], o[5]); w.w = cvt_pk_bf16(o[6], o[7]);
;                     *(u32x4*)(O + row * 512 + col) = w; } }
.LBB0_764:
	v_mul_f32_e32 v107, 0xbfb8aa3b, v107
	v_exp_f32_e32 v107, v107
	s_nop 0
	v_add_f32_e32 v107, 1.0, v107
	v_rcp_f32_e32 v115, v107
	s_nop 0
	v_fma_f32 v117, -v107, v115, 1.0
	v_fmac_f32_e32 v115, v117, v115
	v_div_fixup_f32 v107, v115, v107, 1.0
	v_mul_f32_e32 v114, 0xbf1b4598, v107
.LBB0_765:
	v_or_b32_e32 v116, 48, v132
	v_ashrrev_i32_e32 v117, 31, v116
	v_cvt_pk_bf16_f32 v108, v108, v109
	v_cvt_pk_bf16_f32 v109, v110, v111
	v_cvt_pk_bf16_f32 v110, v104, v105
	v_lshlrev_b64 v[104:105], 10, v[116:117]
	v_cvt_pk_bf16_f32 v111, v106, v114
	v_lshl_add_u64 v[104:105], v[130:131], 0, v[104:105]
	v_add_f32_e32 v106, v100, v88
	s_and_b64 vcc, exec, s[2:3]
	s_mov_b64 s[68:69], -1
	global_store_dwordx4 v[104:105], v[108:111], off
	s_cbranch_vccnz .LBB0_769
	s_and_b64 vcc, exec, s[0:1]
	v_mov_b32_e32 v100, v106
	s_cbranch_vccnz .LBB0_768
	v_mul_f32_e32 v100, 0xbfb8aa3b, v106
	v_exp_f32_e32 v100, v100
	s_nop 0
	v_add_f32_e32 v100, 1.0, v100
	v_rcp_f32_e32 v108, v100
	s_nop 0
	v_fma_f32 v110, -v100, v108, 1.0
	v_fmac_f32_e32 v108, v110, v108
	v_div_fixup_f32 v100, v108, v100, 1.0

; __device__ __forceinline__ unsigned cvt_pk_bf16(float lo, float hi) { const f32x2c v = {lo, hi}; const bf16x2c b = __builtin_convertvector(v, bf16x2c); return __builtin_bit_cast(unsigned, b); }
; __device__ __forceinline__ float sigmoidf_(float x) { return 1.f / (1.f + __expf(-x)); }
;     __device__ __forceinline__ void operator()(const f32x4 (&acc)[2][2][4][2], const Unit& u, int wr, int wc, int fr, int fq) const {
;     ...
;         for (int bj = 0; bj < 2; ++bj) { const int col = (col0 + bj * HALF) & 511;
;             f32x4 b0 = (f32x4){0.f, 0.f, 0.f, 0.f}, b1 = b0;
;             if (kind == 0) { b0 = *(const f32x4*)(w0 + col); b1 = *(const f32x4*)(w0 + col + 4); }
;             else if (kind == 1) { b0 = *(const f32x4*)(a0 + col); b1 = *(const f32x4*)(a0 + col + 4); }
; #pragma unroll
;             for (int ai = 0; ai < 2; ++ai)
; #pragma unroll
;                 for (int m = 0; m < 4; ++m) { const size_t row = (size_t)(row0 + ai * HALF + m * 16);
;                     const f32x4 v0 = acc[ai][bj][m][0] + b0, v1 = acc[ai][bj][m][1] + b1; float o[8];
; #pragma unroll
;                     for (int e = 0; e < 8; ++e) { float x = (e < 4) ? v0[e & 3] : v1[e & 3];
;                         if (kind == 0) x = -0.6065306597126334f * sigmoidf_(x);
;                         else if (kind == 1) x = sigmoidf_(x);
;                         o[e] = x; }
;                     u32x4 w; w.x = cvt_pk_bf16(o[0], o[1]); w.y = cvt_pk_bf16(o[2], o[3]); w.z = cvt_pk_bf16(o[4], o[5]); w.w = cvt_pk_bf16(o[6], o[7]);
;                     *(u32x4*)(O + row * 512 + col) = w; } }
.LBB0_770:
	v_mul_f32_e32 v100, 0xbfb8aa3b, v106
	v_exp_f32_e32 v100, v100
	s_nop 0
	v_add_f32_e32 v100, 1.0, v100
	v_rcp_f32_e32 v107, v100
	s_nop 0
	v_fma_f32 v109, -v100, v107, 1.0
	v_fmac_f32_e32 v107, v109, v107
	v_div_fixup_f32 v100, v107, v100, 1.0
	v_mul_f32_e32 v100, 0xbf1b4598, v100
.LBB0_771:
	v_add_f32_e32 v106, v101, v89
	s_and_b64 vcc, exec, s[2:3]
	s_mov_b64 s[68:69], -1
	s_cbranch_vccnz .LBB0_775
	s_and_b64 vcc, exec, s[0:1]
	v_mov_b32_e32 v101, v106
	s_cbranch_vccnz .LBB0_774
	v_mul_f32_e32 v101, 0xbfb8aa3b, v106
	v_exp_f32_e32 v101, v101
	s_nop 0
	v_add_f32_e32 v101, 1.0, v101
	v_rcp_f32_e32 v108, v101
	s_nop 0
	v_fma_f32 v110, -v101, v108, 1.0
	v_fmac_f32_e32 v108, v110, v108
	v_div_fixup_f32 v101, v108, v101, 1.0

; __device__ __forceinline__ unsigned cvt_pk_bf16(float lo, float hi) { const f32x2c v = {lo, hi}; const bf16x2c b = __builtin_convertvector(v, bf16x2c); return __builtin_bit_cast(unsigned, b); }
; __device__ __forceinline__ float sigmoidf_(float x) { return 1.f / (1.f + __expf(-x)); }
;     __device__ __forceinline__ void operator()(const f32x4 (&acc)[2][2][4][2], const Unit& u, int wr, int wc, int fr, int fq) const {
;     ...
;         for (int bj = 0; bj < 2; ++bj) { const int col = (col0 + bj * HALF) & 511;
;             f32x4 b0 = (f32x4){0.f, 0.f, 0.f, 0.f}, b1 = b0;
;             if (kind == 0) { b0 = *(const f32x4*)(w0 + col); b1 = *(const f32x4*)(w0 + col + 4); }
;             else if (kind == 1) { b0 = *(const f32x4*)(a0 + col); b1 = *(const f32x4*)(a0 + col + 4); }
; #pragma unroll
;             for (int ai = 0; ai < 2; ++ai)
; #pragma unroll
;                 for (int m = 0; m < 4; ++m) { const size_t row = (size_t)(row0 + ai * HALF + m * 16);
;                     const f32x4 v0 = acc[ai][bj][m][0] + b0, v1 = acc[ai][bj][m][1] + b1; float o[8];
; #pragma unroll
;                     for (int e = 0; e < 8; ++e) { float x = (e < 4) ? v0[e & 3] : v1[e & 3];
;                         if (kind == 0) x = -0.6065306597126334f * sigmoidf_(x);
;                         else if (kind == 1) x = sigmoidf_(x);
;                         o[e] = x; }
;                     u32x4 w; w.x = cvt_pk_bf16(o[0], o[1]); w.y = cvt_pk_bf16(o[2], o[3]); w.z = cvt_pk_bf16(o[4], o[5]); w.w = cvt_pk_bf16(o[6], o[7]);
;                     *(u32x4*)(O + row * 512 + col) = w; } }
.LBB0_776:
	v_mul_f32_e32 v101, 0xbfb8aa3b, v106
	v_exp_f32_e32 v101, v101
	s_nop 0
	v_add_f32_e32 v101, 1.0, v101
	v_rcp_f32_e32 v107, v101
	s_nop 0
	v_fma_f32 v109, -v101, v107, 1.0
	v_fmac_f32_e32 v107, v109, v107
	v_div_fixup_f32 v101, v107, v101, 1.0
	v_mul_f32_e32 v101, 0xbf1b4598, v101
.LBB0_777:
	v_add_f32_e32 v106, v102, v90
	s_and_b64 vcc, exec, s[2:3]
	s_mov_b64 s[68:69], -1
	s_cbranch_vccnz .LBB0_781
	s_and_b64 vcc, exec, s[0:1]
	v_mov_b32_e32 v102, v106
	s_cbranch_vccnz .LBB0_780
	v_mul_f32_e32 v102, 0xbfb8aa3b, v106
	v_exp_f32_e32 v102, v102
	s_nop 0
	v_add_f32_e32 v102, 1.0, v102
	v_rcp_f32_e32 v108, v102
	s_nop 0
	v_fma_f32 v110, -v102, v108, 1.0
	v_fmac_f32_e32 v108, v110, v108
	v_div_fixup_f32 v102, v108, v102, 1.0

; __device__ __forceinline__ unsigned cvt_pk_bf16(float lo, float hi) { const f32x2c v = {lo, hi}; const bf16x2c b = __builtin_convertvector(v, bf16x2c); return __builtin_bit_cast(unsigned, b); }
; __device__ __forceinline__ float sigmoidf_(float x) { return 1.f / (1.f + __expf(-x)); }
;     __device__ __forceinline__ void operator()(const f32x4 (&acc)[2][2][4][2], const Unit& u, int wr, int wc, int fr, int fq) const {
;     ...
;         for (int bj = 0; bj < 2; ++bj) { const int col = (col0 + bj * HALF) & 511;
;             f32x4 b0 = (f32x4){0.f, 0.f, 0.f, 0.f}, b1 = b0;
;             if (kind == 0) { b0 = *(const f32x4*)(w0 + col); b1 = *(const f32x4*)(w0 + col + 4); }
;             else if (kind == 1) { b0 = *(const f32x4*)(a0 + col); b1 = *(const f32x4*)(a0 + col + 4); }
; #pragma unroll
;             for (int ai = 0; ai < 2; ++ai)
; #pragma unroll
;                 for (int m = 0; m < 4; ++m) { const size_t row = (size_t)(row0 + ai * HALF + m * 16);
;                     const f32x4 v0 = acc[ai][bj][m][0] + b0, v1 = acc[ai][bj][m][1] + b1; float o[8];
; #pragma unroll
;                     for (int e = 0; e < 8; ++e) { float x = (e < 4) ? v0[e & 3] : v1[e & 3];
;                         if (kind == 0) x = -0.6065306597126334f * sigmoidf_(x);
;                         else if (kind == 1) x = sigmoidf_(x);
;                         o[e] = x; }
;                     u32x4 w; w.x = cvt_pk_bf16(o[0], o[1]); w.y = cvt_pk_bf16(o[2], o[3]); w.z = cvt_pk_bf16(o[4], o[5]); w.w = cvt_pk_bf16(o[6], o[7]);
;                     *(u32x4*)(O + row * 512 + col) = w; } }
.LBB0_782:
	v_mul_f32_e32 v102, 0xbfb8aa3b, v106
	v_exp_f32_e32 v102, v102
	s_nop 0
	v_add_f32_e32 v102, 1.0, v102
	v_rcp_f32_e32 v107, v102
	s_nop 0
	v_fma_f32 v109, -v102, v107, 1.0
	v_fmac_f32_e32 v107, v109, v107
	v_div_fixup_f32 v102, v107, v102, 1.0
	v_mul_f32_e32 v102, 0xbf1b4598, v102
.LBB0_783:
	v_add_f32_e32 v106, v103, v91
	s_and_b64 vcc, exec, s[2:3]
	s_mov_b64 s[68:69], -1
	s_cbranch_vccnz .LBB0_787
	s_and_b64 vcc, exec, s[0:1]
	v_mov_b32_e32 v103, v106
	s_cbranch_vccnz .LBB0_786
	v_mul_f32_e32 v103, 0xbfb8aa3b, v106
	v_exp_f32_e32 v103, v103
	s_nop 0
	v_add_f32_e32 v103, 1.0, v103
	v_rcp_f32_e32 v108, v103
	s_nop 0
	v_fma_f32 v110, -v103, v108, 1.0
	v_fmac_f32_e32 v108, v110, v108
	v_div_fixup_f32 v103, v108, v103, 1.0

; __device__ __forceinline__ unsigned cvt_pk_bf16(float lo, float hi) { const f32x2c v = {lo, hi}; const bf16x2c b = __builtin_convertvector(v, bf16x2c); return __builtin_bit_cast(unsigned, b); }
; __device__ __forceinline__ float sigmoidf_(float x) { return 1.f / (1.f + __expf(-x)); }
;     __device__ __forceinline__ void operator()(const f32x4 (&acc)[2][2][4][2], const Unit& u, int wr, int wc, int fr, int fq) const {
;     ...
;         for (int bj = 0; bj < 2; ++bj) { const int col = (col0 + bj * HALF) & 511;
;             f32x4 b0 = (f32x4){0.f, 0.f, 0.f, 0.f}, b1 = b0;
;             if (kind == 0) { b0 = *(const f32x4*)(w0 + col); b1 = *(const f32x4*)(w0 + col + 4); }
;             else if (kind == 1) { b0 = *(const f32x4*)(a0 + col); b1 = *(const f32x4*)(a0 + col + 4); }
; #pragma unroll
;             for (int ai = 0; ai < 2; ++ai)
; #pragma unroll
;                 for (int m = 0; m < 4; ++m) { const size_t row = (size_t)(row0 + ai * HALF + m * 16);
;                     const f32x4 v0 = acc[ai][bj][m][0] + b0, v1 = acc[ai][bj][m][1] + b1; float o[8];
; #pragma unroll
;                     for (int e = 0; e < 8; ++e) { float x = (e < 4) ? v0[e & 3] : v1[e & 3];
;                         if (kind == 0) x = -0.6065306597126334f * sigmoidf_(x);
;                         else if (kind == 1) x = sigmoidf_(x);
;                         o[e] = x; }
;                     u32x4 w; w.x = cvt_pk_bf16(o[0], o[1]); w.y = cvt_pk_bf16(o[2], o[3]); w.z = cvt_pk_bf16(o[4], o[5]); w.w = cvt_pk_bf16(o[6], o[7]);
;                     *(u32x4*)(O + row * 512 + col) = w; } }
.LBB0_788:
	v_mul_f32_e32 v103, 0xbfb8aa3b, v106
	v_exp_f32_e32 v103, v103
	s_nop 0
	v_add_f32_e32 v103, 1.0, v103
	v_rcp_f32_e32 v107, v103
	s_nop 0
	v_fma_f32 v109, -v103, v107, 1.0
	v_fmac_f32_e32 v107, v109, v107
	v_div_fixup_f32 v103, v107, v103, 1.0
	v_mul_f32_e32 v103, 0xbf1b4598, v103
.LBB0_789:
	v_add_f32_e32 v106, v96, v80
	s_and_b64 vcc, exec, s[2:3]
	s_mov_b64 s[68:69], -1
	s_cbranch_vccnz .LBB0_793
	s_and_b64 vcc, exec, s[0:1]
	v_mov_b32_e32 v96, v106
	s_cbranch_vccnz .LBB0_792
	v_mul_f32_e32 v96, 0xbfb8aa3b, v106
	v_exp_f32_e32 v96, v96
	s_nop 0
	v_add_f32_e32 v96, 1.0, v96
	v_rcp_f32_e32 v108, v96
	s_nop 0
	v_fma_f32 v110, -v96, v108, 1.0
	v_fmac_f32_e32 v108, v110, v108
	v_div_fixup_f32 v96, v108, v96, 1.0

; __device__ __forceinline__ unsigned cvt_pk_bf16(float lo, float hi) { const f32x2c v = {lo, hi}; const bf16x2c b = __builtin_convertvector(v, bf16x2c); return __builtin_bit_cast(unsigned, b); }
; __device__ __forceinline__ float sigmoidf_(float x) { return 1.f / (1.f + __expf(-x)); }
;     __device__ __forceinline__ void operator()(const f32x4 (&acc)[2][2][4][2], const Unit& u, int wr, int wc, int fr, int fq) const {
;     ...
;         for (int bj = 0; bj < 2; ++bj) { const int col = (col0 + bj * HALF) & 511;
;             f32x4 b0 = (f32x4){0.f, 0.f, 0.f, 0.f}, b1 = b0;
;             if (kind == 0) { b0 = *(const f32x4*)(w0 + col); b1 = *(const f32x4*)(w0 + col + 4); }
;             else if (kind == 1) { b0 = *(const f32x4*)(a0 + col); b1 = *(const f32x4*)(a0 + col + 4); }
; #pragma unroll
;             for (int ai = 0; ai < 2; ++ai)
; #pragma unroll
;                 for (int m = 0; m < 4; ++m) { const size_t row = (size_t)(row0 + ai * HALF + m * 16);
;                     const f32x4 v0 = acc[ai][bj][m][0] + b0, v1 = acc[ai][bj][m][1] + b1; float o[8];
; #pragma unroll
;                     for (int e = 0; e < 8; ++e) { float x = (e < 4) ? v0[e & 3] : v1[e & 3];
;                         if (kind == 0) x = -0.6065306597126334f * sigmoidf_(x);
;                         else if (kind == 1) x = sigmoidf_(x);
;                         o[e] = x; }
;                     u32x4 w; w.x = cvt_pk_bf16(o[0], o[1]); w.y = cvt_pk_bf16(o[2], o[3]); w.z = cvt_pk_bf16(o[4], o[5]); w.w = cvt_pk_bf16(o[6], o[7]);
;                     *(u32x4*)(O + row * 512 + col) = w; } }
.LBB0_794:
	v_mul_f32_e32 v96, 0xbfb8aa3b, v106
	v_exp_f32_e32 v96, v96
	s_nop 0
	v_add_f32_e32 v96, 1.0, v96
	v_rcp_f32_e32 v107, v96
	s_nop 0
	v_fma_f32 v109, -v96, v107, 1.0
	v_fmac_f32_e32 v107, v109, v107
	v_div_fixup_f32 v96, v107, v96, 1.0
	v_mul_f32_e32 v96, 0xbf1b4598, v96
.LBB0_795:
	v_add_f32_e32 v106, v97, v81
	s_and_b64 vcc, exec, s[2:3]
	s_mov_b64 s[68:69], -1
	s_cbranch_vccnz .LBB0_799
	s_and_b64 vcc, exec, s[0:1]
	v_mov_b32_e32 v97, v106
	s_cbranch_vccnz .LBB0_798
	v_mul_f32_e32 v97, 0xbfb8aa3b, v106
	v_exp_f32_e32 v97, v97
	s_nop 0
	v_add_f32_e32 v97, 1.0, v97
	v_rcp_f32_e32 v108, v97
	s_nop 0
	v_fma_f32 v110, -v97, v108, 1.0
	v_fmac_f32_e32 v108, v110, v108
	v_div_fixup_f32 v97, v108, v97, 1.0

; __device__ __forceinline__ unsigned cvt_pk_bf16(float lo, float hi) { const f32x2c v = {lo, hi}; const bf16x2c b = __builtin_convertvector(v, bf16x2c); return __builtin_bit_cast(unsigned, b); }
; __device__ __forceinline__ float sigmoidf_(float x) { return 1.f / (1.f + __expf(-x)); }
;     __device__ __forceinline__ void operator()(const f32x4 (&acc)[2][2][4][2], const Unit& u, int wr, int wc, int fr, int fq) const {
;     ...
;         for (int bj = 0; bj < 2; ++bj) { const int col = (col0 + bj * HALF) & 511;
;             f32x4 b0 = (f32x4){0.f, 0.f, 0.f, 0.f}, b1 = b0;
;             if (kind == 0) { b0 = *(const f32x4*)(w0 + col); b1 = *(const f32x4*)(w0 + col + 4); }
;             else if (kind == 1) { b0 = *(const f32x4*)(a0 + col); b1 = *(const f32x4*)(a0 + col + 4); }
; #pragma unroll
;             for (int ai = 0; ai < 2; ++ai)
; #pragma unroll
;                 for (int m = 0; m < 4; ++m) { const size_t row = (size_t)(row0 + ai * HALF + m * 16);
;                     const f32x4 v0 = acc[ai][bj][m][0] + b0, v1 = acc[ai][bj][m][1] + b1; float o[8];
; #pragma unroll
;                     for (int e = 0; e < 8; ++e) { float x = (e < 4) ? v0[e & 3] : v1[e & 3];
;                         if (kind == 0) x = -0.6065306597126334f * sigmoidf_(x);
;                         else if (kind == 1) x = sigmoidf_(x);
;                         o[e] = x; }
;                     u32x4 w; w.x = cvt_pk_bf16(o[0], o[1]); w.y = cvt_pk_bf16(o[2], o[3]); w.z = cvt_pk_bf16(o[4], o[5]); w.w = cvt_pk_bf16(o[6], o[7]);
;                     *(u32x4*)(O + row * 512 + col) = w; } }
.LBB0_800:
	v_mul_f32_e32 v97, 0xbfb8aa3b, v106
	v_exp_f32_e32 v97, v97
	s_nop 0
	v_add_f32_e32 v97, 1.0, v97
	v_rcp_f32_e32 v107, v97
	s_nop 0
	v_fma_f32 v109, -v97, v107, 1.0
	v_fmac_f32_e32 v107, v109, v107
	v_div_fixup_f32 v97, v107, v97, 1.0
	v_mul_f32_e32 v97, 0xbf1b4598, v97
.LBB0_801:
	v_add_f32_e32 v106, v98, v82
	s_and_b64 vcc, exec, s[2:3]
	s_mov_b64 s[68:69], -1
	s_cbranch_vccnz .LBB0_805
	s_and_b64 vcc, exec, s[0:1]
	v_mov_b32_e32 v98, v106
	s_cbranch_vccnz .LBB0_804
	v_mul_f32_e32 v98, 0xbfb8aa3b, v106
	v_exp_f32_e32 v98, v98
	s_nop 0
	v_add_f32_e32 v98, 1.0, v98
	v_rcp_f32_e32 v108, v98
	s_nop 0
	v_fma_f32 v110, -v98, v108, 1.0
	v_fmac_f32_e32 v108, v110, v108
	v_div_fixup_f32 v98, v108, v98, 1.0

; __device__ __forceinline__ unsigned cvt_pk_bf16(float lo, float hi) { const f32x2c v = {lo, hi}; const bf16x2c b = __builtin_convertvector(v, bf16x2c); return __builtin_bit_cast(unsigned, b); }
; __device__ __forceinline__ float sigmoidf_(float x) { return 1.f / (1.f + __expf(-x)); }
;     __device__ __forceinline__ void operator()(const f32x4 (&acc)[2][2][4][2], const Unit& u, int wr, int wc, int fr, int fq) const {
;     ...
;         for (int bj = 0; bj < 2; ++bj) { const int col = (col0 + bj * HALF) & 511;
;             f32x4 b0 = (f32x4){0.f, 0.f, 0.f, 0.f}, b1 = b0;
;             if (kind == 0) { b0 = *(const f32x4*)(w0 + col); b1 = *(const f32x4*)(w0 + col + 4); }
;             else if (kind == 1) { b0 = *(const f32x4*)(a0 + col); b1 = *(const f32x4*)(a0 + col + 4); }
; #pragma unroll
;             for (int ai = 0; ai < 2; ++ai)
; #pragma unroll
;                 for (int m = 0; m < 4; ++m) { const size_t row = (size_t)(row0 + ai * HALF + m * 16);
;                     const f32x4 v0 = acc[ai][bj][m][0] + b0, v1 = acc[ai][bj][m][1] + b1; float o[8];
; #pragma unroll
;                     for (int e = 0; e < 8; ++e) { float x = (e < 4) ? v0[e & 3] : v1[e & 3];
;                         if (kind == 0) x = -0.6065306597126334f * sigmoidf_(x);
;                         else if (kind == 1) x = sigmoidf_(x);
;                         o[e] = x; }
;                     u32x4 w; w.x = cvt_pk_bf16(o[0], o[1]); w.y = cvt_pk_bf16(o[2], o[3]); w.z = cvt_pk_bf16(o[4], o[5]); w.w = cvt_pk_bf16(o[6], o[7]);
;                     *(u32x4*)(O + row * 512 + col) = w; } }
.LBB0_806:
	v_mul_f32_e32 v98, 0xbfb8aa3b, v106
	v_exp_f32_e32 v98, v98
	s_nop 0
	v_add_f32_e32 v98, 1.0, v98
	v_rcp_f32_e32 v107, v98
	s_nop 0
	v_fma_f32 v109, -v98, v107, 1.0
	v_fmac_f32_e32 v107, v109, v107
	v_div_fixup_f32 v98, v107, v98, 1.0
	v_mul_f32_e32 v98, 0xbf1b4598, v98
.LBB0_807:
	v_add_f32_e32 v99, v99, v83
	s_and_b64 vcc, exec, s[2:3]
	s_mov_b64 s[68:69], -1
	s_cbranch_vccnz .LBB0_811
	s_and_b64 vcc, exec, s[0:1]
	v_mov_b32_e32 v106, v99
	s_cbranch_vccnz .LBB0_810
	v_mul_f32_e32 v106, 0xbfb8aa3b, v99
	v_exp_f32_e32 v106, v106
	s_nop 0
	v_add_f32_e32 v106, 1.0, v106
	v_rcp_f32_e32 v108, v106
	s_nop 0
	v_fma_f32 v110, -v106, v108, 1.0
	v_fmac_f32_e32 v108, v110, v108
	v_div_fixup_f32 v106, v108, v106, 1.0

; __device__ __forceinline__ unsigned cvt_pk_bf16(float lo, float hi) { const f32x2c v = {lo, hi}; const bf16x2c b = __builtin_convertvector(v, bf16x2c); return __builtin_bit_cast(unsigned, b); }
; __device__ __forceinline__ float sigmoidf_(float x) { return 1.f / (1.f + __expf(-x)); }
;     __device__ __forceinline__ void operator()(const f32x4 (&acc)[2][2][4][2], const Unit& u, int wr, int wc, int fr, int fq) const {
;     ...
;         for (int bj = 0; bj < 2; ++bj) { const int col = (col0 + bj * HALF) & 511;
;             f32x4 b0 = (f32x4){0.f, 0.f, 0.f, 0.f}, b1 = b0;
;             if (kind == 0) { b0 = *(const f32x4*)(w0 + col); b1 = *(const f32x4*)(w0 + col + 4); }
;             else if (kind == 1) { b0 = *(const f32x4*)(a0 + col); b1 = *(const f32x4*)(a0 + col + 4); }
; #pragma unroll
;             for (int ai = 0; ai < 2; ++ai)
; #pragma unroll
;                 for (int m = 0; m < 4; ++m) { const size_t row = (size_t)(row0 + ai * HALF + m * 16);
;                     const f32x4 v0 = acc[ai][bj][m][0] + b0, v1 = acc[ai][bj][m][1] + b1; float o[8];
; #pragma unroll
;                     for (int e = 0; e < 8; ++e) { float x = (e < 4) ? v0[e & 3] : v1[e & 3];
;                         if (kind == 0) x = -0.6065306597126334f * sigmoidf_(x);
;                         else if (kind == 1) x = sigmoidf_(x);
;                         o[e] = x; }
;                     u32x4 w; w.x = cvt_pk_bf16(o[0], o[1]); w.y = cvt_pk_bf16(o[2], o[3]); w.z = cvt_pk_bf16(o[4], o[5]); w.w = cvt_pk_bf16(o[6], o[7]);
;                     *(u32x4*)(O + row * 512 + col) = w; } }
.LBB0_812:
	v_mul_f32_e32 v99, 0xbfb8aa3b, v99
	v_exp_f32_e32 v99, v99
	s_nop 0
	v_add_f32_e32 v99, 1.0, v99
	v_rcp_f32_e32 v107, v99
	s_nop 0
	v_fma_f32 v109, -v99, v107, 1.0
	v_fmac_f32_e32 v107, v109, v107
	v_div_fixup_f32 v99, v107, v99, 1.0
	v_mul_f32_e32 v106, 0xbf1b4598, v99
.LBB0_813:
	v_lshlrev_b64 v[108:109], 10, v[132:133]
	v_cvt_pk_bf16_f32 v100, v100, v101
	v_cvt_pk_bf16_f32 v101, v102, v103
	v_cvt_pk_bf16_f32 v102, v96, v97
	v_lshl_add_u64 v[96:97], v[130:131], 0, v[108:109]
	v_cvt_pk_bf16_f32 v103, v98, v106
	v_add_co_u32_e32 v98, vcc, 0x20000, v96
	s_mov_b64 s[68:69], -1
	s_nop 0
	v_addc_co_u32_e32 v99, vcc, 0, v97, vcc
	global_store_dwordx4 v[98:99], v[100:103], off
	v_add_f32_e32 v98, v92, v88
	s_and_b64 vcc, exec, s[2:3]
	s_cbranch_vccnz .LBB0_817
	s_and_b64 vcc, exec, s[0:1]
	v_mov_b32_e32 v92, v98
	s_cbranch_vccnz .LBB0_816
	v_mul_f32_e32 v92, 0xbfb8aa3b, v98
	v_exp_f32_e32 v92, v92
	s_nop 0
	v_add_f32_e32 v92, 1.0, v92
	v_rcp_f32_e32 v100, v92
	s_nop 0
	v_fma_f32 v102, -v92, v100, 1.0
	v_fmac_f32_e32 v100, v102, v100
	v_div_fixup_f32 v92, v100, v92, 1.0

; __device__ __forceinline__ unsigned cvt_pk_bf16(float lo, float hi) { const f32x2c v = {lo, hi}; const bf16x2c b = __builtin_convertvector(v, bf16x2c); return __builtin_bit_cast(unsigned, b); }
; __device__ __forceinline__ float sigmoidf_(float x) { return 1.f / (1.f + __expf(-x)); }
;     __device__ __forceinline__ void operator()(const f32x4 (&acc)[2][2][4][2], const Unit& u, int wr, int wc, int fr, int fq) const {
;     ...
;         for (int bj = 0; bj < 2; ++bj) { const int col = (col0 + bj * HALF) & 511;
;             f32x4 b0 = (f32x4){0.f, 0.f, 0.f, 0.f}, b1 = b0;
;             if (kind == 0) { b0 = *(const f32x4*)(w0 + col); b1 = *(const f32x4*)(w0 + col + 4); }
;             else if (kind == 1) { b0 = *(const f32x4*)(a0 + col); b1 = *(const f32x4*)(a0 + col + 4); }
; #pragma unroll
;             for (int ai = 0; ai < 2; ++ai)
; #pragma unroll
;                 for (int m = 0; m < 4; ++m) { const size_t row = (size_t)(row0 + ai * HALF + m * 16);
;                     const f32x4 v0 = acc[ai][bj][m][0] + b0, v1 = acc[ai][bj][m][1] + b1; float o[8];
; #pragma unroll
;                     for (int e = 0; e < 8; ++e) { float x = (e < 4) ? v0[e & 3] : v1[e & 3];
;                         if (kind == 0) x = -0.6065306597126334f * sigmoidf_(x);
;                         else if (kind == 1) x = sigmoidf_(x);
;                         o[e] = x; }
;                     u32x4 w; w.x = cvt_pk_bf16(o[0], o[1]); w.y = cvt_pk_bf16(o[2], o[3]); w.z = cvt_pk_bf16(o[4], o[5]); w.w = cvt_pk_bf16(o[6], o[7]);
;                     *(u32x4*)(O + row * 512 + col) = w; } }
.LBB0_818:
	v_mul_f32_e32 v92, 0xbfb8aa3b, v98
	v_exp_f32_e32 v92, v92
	s_nop 0
	v_add_f32_e32 v92, 1.0, v92
	v_rcp_f32_e32 v99, v92
	s_nop 0
	v_fma_f32 v101, -v92, v99, 1.0
	v_fmac_f32_e32 v99, v101, v99
	v_div_fixup_f32 v92, v99, v92, 1.0
	v_mul_f32_e32 v92, 0xbf1b4598, v92
.LBB0_819:
	v_add_f32_e32 v98, v93, v89
	s_and_b64 vcc, exec, s[2:3]
	s_mov_b64 s[68:69], -1
	s_cbranch_vccnz .LBB0_823
	s_and_b64 vcc, exec, s[0:1]
	v_mov_b32_e32 v93, v98
	s_cbranch_vccnz .LBB0_822
	v_mul_f32_e32 v93, 0xbfb8aa3b, v98
	v_exp_f32_e32 v93, v93
	s_nop 0
	v_add_f32_e32 v93, 1.0, v93
	v_rcp_f32_e32 v100, v93
	s_nop 0
	v_fma_f32 v102, -v93, v100, 1.0
	v_fmac_f32_e32 v100, v102, v100
	v_div_fixup_f32 v93, v100, v93, 1.0

; __device__ __forceinline__ unsigned cvt_pk_bf16(float lo, float hi) { const f32x2c v = {lo, hi}; const bf16x2c b = __builtin_convertvector(v, bf16x2c); return __builtin_bit_cast(unsigned, b); }
; __device__ __forceinline__ float sigmoidf_(float x) { return 1.f / (1.f + __expf(-x)); }
;     __device__ __forceinline__ void operator()(const f32x4 (&acc)[2][2][4][2], const Unit& u, int wr, int wc, int fr, int fq) const {
;     ...
;         for (int bj = 0; bj < 2; ++bj) { const int col = (col0 + bj * HALF) & 511;
;             f32x4 b0 = (f32x4){0.f, 0.f, 0.f, 0.f}, b1 = b0;
;             if (kind == 0) { b0 = *(const f32x4*)(w0 + col); b1 = *(const f32x4*)(w0 + col + 4); }
;             else if (kind == 1) { b0 = *(const f32x4*)(a0 + col); b1 = *(const f32x4*)(a0 + col + 4); }
; #pragma unroll
;             for (int ai = 0; ai < 2; ++ai)
; #pragma unroll
;                 for (int m = 0; m < 4; ++m) { const size_t row = (size_t)(row0 + ai * HALF + m * 16);
;                     const f32x4 v0 = acc[ai][bj][m][0] + b0, v1 = acc[ai][bj][m][1] + b1; float o[8];
; #pragma unroll
;                     for (int e = 0; e < 8; ++e) { float x = (e < 4) ? v0[e & 3] : v1[e & 3];
;                         if (kind == 0) x = -0.6065306597126334f * sigmoidf_(x);
;                         else if (kind == 1) x = sigmoidf_(x);
;                         o[e] = x; }
;                     u32x4 w; w.x = cvt_pk_bf16(o[0], o[1]); w.y = cvt_pk_bf16(o[2], o[3]); w.z = cvt_pk_bf16(o[4], o[5]); w.w = cvt_pk_bf16(o[6], o[7]);
;                     *(u32x4*)(O + row * 512 + col) = w; } }
.LBB0_824:
	v_mul_f32_e32 v93, 0xbfb8aa3b, v98
	v_exp_f32_e32 v93, v93
	s_nop 0
	v_add_f32_e32 v93, 1.0, v93
	v_rcp_f32_e32 v99, v93
	s_nop 0
	v_fma_f32 v101, -v93, v99, 1.0
	v_fmac_f32_e32 v99, v101, v99
	v_div_fixup_f32 v93, v99, v93, 1.0
	v_mul_f32_e32 v93, 0xbf1b4598, v93
.LBB0_825:
	v_add_f32_e32 v98, v94, v90
	s_and_b64 vcc, exec, s[2:3]
	s_mov_b64 s[68:69], -1
	s_cbranch_vccnz .LBB0_829
	s_and_b64 vcc, exec, s[0:1]
	v_mov_b32_e32 v94, v98
	s_cbranch_vccnz .LBB0_828
	v_mul_f32_e32 v94, 0xbfb8aa3b, v98
	v_exp_f32_e32 v94, v94
	s_nop 0
	v_add_f32_e32 v94, 1.0, v94
	v_rcp_f32_e32 v100, v94
	s_nop 0
	v_fma_f32 v102, -v94, v100, 1.0
	v_fmac_f32_e32 v100, v102, v100
	v_div_fixup_f32 v94, v100, v94, 1.0

; __device__ __forceinline__ unsigned cvt_pk_bf16(float lo, float hi) { const f32x2c v = {lo, hi}; const bf16x2c b = __builtin_convertvector(v, bf16x2c); return __builtin_bit_cast(unsigned, b); }
; __device__ __forceinline__ float sigmoidf_(float x) { return 1.f / (1.f + __expf(-x)); }
;     __device__ __forceinline__ void operator()(const f32x4 (&acc)[2][2][4][2], const Unit& u, int wr, int wc, int fr, int fq) const {
;     ...
;         for (int bj = 0; bj < 2; ++bj) { const int col = (col0 + bj * HALF) & 511;
;             f32x4 b0 = (f32x4){0.f, 0.f, 0.f, 0.f}, b1 = b0;
;             if (kind == 0) { b0 = *(const f32x4*)(w0 + col); b1 = *(const f32x4*)(w0 + col + 4); }
;             else if (kind == 1) { b0 = *(const f32x4*)(a0 + col); b1 = *(const f32x4*)(a0 + col + 4); }
; #pragma unroll
;             for (int ai = 0; ai < 2; ++ai)
; #pragma unroll
;                 for (int m = 0; m < 4; ++m) { const size_t row = (size_t)(row0 + ai * HALF + m * 16);
;                     const f32x4 v0 = acc[ai][bj][m][0] + b0, v1 = acc[ai][bj][m][1] + b1; float o[8];
; #pragma unroll
;                     for (int e = 0; e < 8; ++e) { float x = (e < 4) ? v0[e & 3] : v1[e & 3];
;                         if (kind == 0) x = -0.6065306597126334f * sigmoidf_(x);
;                         else if (kind == 1) x = sigmoidf_(x);
;                         o[e] = x; }
;                     u32x4 w; w.x = cvt_pk_bf16(o[0], o[1]); w.y = cvt_pk_bf16(o[2], o[3]); w.z = cvt_pk_bf16(o[4], o[5]); w.w = cvt_pk_bf16(o[6], o[7]);
;                     *(u32x4*)(O + row * 512 + col) = w; } }
.LBB0_830:
	v_mul_f32_e32 v94, 0xbfb8aa3b, v98
	v_exp_f32_e32 v94, v94
	s_nop 0
	v_add_f32_e32 v94, 1.0, v94
	v_rcp_f32_e32 v99, v94
	s_nop 0
	v_fma_f32 v101, -v94, v99, 1.0
	v_fmac_f32_e32 v99, v101, v99
	v_div_fixup_f32 v94, v99, v94, 1.0
	v_mul_f32_e32 v94, 0xbf1b4598, v94
.LBB0_831:
	v_add_f32_e32 v98, v95, v91
	s_and_b64 vcc, exec, s[2:3]
	s_mov_b64 s[68:69], -1
	s_cbranch_vccnz .LBB0_835
	s_and_b64 vcc, exec, s[0:1]
	v_mov_b32_e32 v95, v98
	s_cbranch_vccnz .LBB0_834
	v_mul_f32_e32 v95, 0xbfb8aa3b, v98
	v_exp_f32_e32 v95, v95
	s_nop 0
	v_add_f32_e32 v95, 1.0, v95
	v_rcp_f32_e32 v100, v95
	s_nop 0
	v_fma_f32 v102, -v95, v100, 1.0
	v_fmac_f32_e32 v100, v102, v100
	v_div_fixup_f32 v95, v100, v95, 1.0

; __device__ __forceinline__ unsigned cvt_pk_bf16(float lo, float hi) { const f32x2c v = {lo, hi}; const bf16x2c b = __builtin_convertvector(v, bf16x2c); return __builtin_bit_cast(unsigned, b); }
; __device__ __forceinline__ float sigmoidf_(float x) { return 1.f / (1.f + __expf(-x)); }
;     __device__ __forceinline__ void operator()(const f32x4 (&acc)[2][2][4][2], const Unit& u, int wr, int wc, int fr, int fq) const {
;     ...
;         for (int bj = 0; bj < 2; ++bj) { const int col = (col0 + bj * HALF) & 511;
;             f32x4 b0 = (f32x4){0.f, 0.f, 0.f, 0.f}, b1 = b0;
;             if (kind == 0) { b0 = *(const f32x4*)(w0 + col); b1 = *(const f32x4*)(w0 + col + 4); }
;             else if (kind == 1) { b0 = *(const f32x4*)(a0 + col); b1 = *(const f32x4*)(a0 + col + 4); }
; #pragma unroll
;             for (int ai = 0; ai < 2; ++ai)
; #pragma unroll
;                 for (int m = 0; m < 4; ++m) { const size_t row = (size_t)(row0 + ai * HALF + m * 16);
;                     const f32x4 v0 = acc[ai][bj][m][0] + b0, v1 = acc[ai][bj][m][1] + b1; float o[8];
; #pragma unroll
;                     for (int e = 0; e < 8; ++e) { float x = (e < 4) ? v0[e & 3] : v1[e & 3];
;                         if (kind == 0) x = -0.6065306597126334f * sigmoidf_(x);
;                         else if (kind == 1) x = sigmoidf_(x);
;                         o[e] = x; }
;                     u32x4 w; w.x = cvt_pk_bf16(o[0], o[1]); w.y = cvt_pk_bf16(o[2], o[3]); w.z = cvt_pk_bf16(o[4], o[5]); w.w = cvt_pk_bf16(o[6], o[7]);
;                     *(u32x4*)(O + row * 512 + col) = w; } }
.LBB0_836:
	v_mul_f32_e32 v95, 0xbfb8aa3b, v98
	v_exp_f32_e32 v95, v95
	s_nop 0
	v_add_f32_e32 v95, 1.0, v95
	v_rcp_f32_e32 v99, v95
	s_nop 0
	v_fma_f32 v101, -v95, v99, 1.0
	v_fmac_f32_e32 v99, v101, v99
	v_div_fixup_f32 v95, v99, v95, 1.0
	v_mul_f32_e32 v95, 0xbf1b4598, v95
.LBB0_837:
	v_add_f32_e32 v98, v84, v80
	s_and_b64 vcc, exec, s[2:3]
	s_mov_b64 s[68:69], -1
	s_cbranch_vccnz .LBB0_841
	s_and_b64 vcc, exec, s[0:1]
	v_mov_b32_e32 v84, v98
	s_cbranch_vccnz .LBB0_840
	v_mul_f32_e32 v84, 0xbfb8aa3b, v98
	v_exp_f32_e32 v84, v84
	s_nop 0
	v_add_f32_e32 v84, 1.0, v84
	v_rcp_f32_e32 v100, v84
	s_nop 0
	v_fma_f32 v102, -v84, v100, 1.0
	v_fmac_f32_e32 v100, v102, v100
	v_div_fixup_f32 v84, v100, v84, 1.0

; __device__ __forceinline__ unsigned cvt_pk_bf16(float lo, float hi) { const f32x2c v = {lo, hi}; const bf16x2c b = __builtin_convertvector(v, bf16x2c); return __builtin_bit_cast(unsigned, b); }
; __device__ __forceinline__ float sigmoidf_(float x) { return 1.f / (1.f + __expf(-x)); }
;     __device__ __forceinline__ void operator()(const f32x4 (&acc)[2][2][4][2], const Unit& u, int wr, int wc, int fr, int fq) const {
;     ...
;         for (int bj = 0; bj < 2; ++bj) { const int col = (col0 + bj * HALF) & 511;
;             f32x4 b0 = (f32x4){0.f, 0.f, 0.f, 0.f}, b1 = b0;
;             if (kind == 0) { b0 = *(const f32x4*)(w0 + col); b1 = *(const f32x4*)(w0 + col + 4); }
;             else if (kind == 1) { b0 = *(const f32x4*)(a0 + col); b1 = *(const f32x4*)(a0 + col + 4); }
; #pragma unroll
;             for (int ai = 0; ai < 2; ++ai)
; #pragma unroll
;                 for (int m = 0; m < 4; ++m) { const size_t row = (size_t)(row0 + ai * HALF + m * 16);
;                     const f32x4 v0 = acc[ai][bj][m][0] + b0, v1 = acc[ai][bj][m][1] + b1; float o[8];
; #pragma unroll
;                     for (int e = 0; e < 8; ++e) { float x = (e < 4) ? v0[e & 3] : v1[e & 3];
;                         if (kind == 0) x = -0.6065306597126334f * sigmoidf_(x);
;                         else if (kind == 1) x = sigmoidf_(x);
;                         o[e] = x; }
;                     u32x4 w; w.x = cvt_pk_bf16(o[0], o[1]); w.y = cvt_pk_bf16(o[2], o[3]); w.z = cvt_pk_bf16(o[4], o[5]); w.w = cvt_pk_bf16(o[6], o[7]);
;                     *(u32x4*)(O + row * 512 + col) = w; } }
.LBB0_842:
	v_mul_f32_e32 v84, 0xbfb8aa3b, v98
	v_exp_f32_e32 v84, v84
	s_nop 0
	v_add_f32_e32 v84, 1.0, v84
	v_rcp_f32_e32 v99, v84
	s_nop 0
	v_fma_f32 v101, -v84, v99, 1.0
	v_fmac_f32_e32 v99, v101, v99
	v_div_fixup_f32 v84, v99, v84, 1.0
	v_mul_f32_e32 v84, 0xbf1b4598, v84
.LBB0_843:
	v_add_f32_e32 v98, v85, v81
	s_and_b64 vcc, exec, s[2:3]
	s_mov_b64 s[68:69], -1
	s_cbranch_vccnz .LBB0_847
	s_and_b64 vcc, exec, s[0:1]
	v_mov_b32_e32 v85, v98
	s_cbranch_vccnz .LBB0_846
	v_mul_f32_e32 v85, 0xbfb8aa3b, v98
	v_exp_f32_e32 v85, v85
	s_nop 0
	v_add_f32_e32 v85, 1.0, v85
	v_rcp_f32_e32 v100, v85
	s_nop 0
	v_fma_f32 v102, -v85, v100, 1.0
	v_fmac_f32_e32 v100, v102, v100
	v_div_fixup_f32 v85, v100, v85, 1.0

; __device__ __forceinline__ unsigned cvt_pk_bf16(float lo, float hi) { const f32x2c v = {lo, hi}; const bf16x2c b = __builtin_convertvector(v, bf16x2c); return __builtin_bit_cast(unsigned, b); }
; __device__ __forceinline__ float sigmoidf_(float x) { return 1.f / (1.f + __expf(-x)); }
;     __device__ __forceinline__ void operator()(const f32x4 (&acc)[2][2][4][2], const Unit& u, int wr, int wc, int fr, int fq) const {
;     ...
;         for (int bj = 0; bj < 2; ++bj) { const int col = (col0 + bj * HALF) & 511;
;             f32x4 b0 = (f32x4){0.f, 0.f, 0.f, 0.f}, b1 = b0;
;             if (kind == 0) { b0 = *(const f32x4*)(w0 + col); b1 = *(const f32x4*)(w0 + col + 4); }
;             else if (kind == 1) { b0 = *(const f32x4*)(a0 + col); b1 = *(const f32x4*)(a0 + col + 4); }
; #pragma unroll
;             for (int ai = 0; ai < 2; ++ai)
; #pragma unroll
;                 for (int m = 0; m < 4; ++m) { const size_t row = (size_t)(row0 + ai * HALF + m * 16);
;                     const f32x4 v0 = acc[ai][bj][m][0] + b0, v1 = acc[ai][bj][m][1] + b1; float o[8];
; #pragma unroll
;                     for (int e = 0; e < 8; ++e) { float x = (e < 4) ? v0[e & 3] : v1[e & 3];
;                         if (kind == 0) x = -0.6065306597126334f * sigmoidf_(x);
;                         else if (kind == 1) x = sigmoidf_(x);
;                         o[e] = x; }
;                     u32x4 w; w.x = cvt_pk_bf16(o[0], o[1]); w.y = cvt_pk_bf16(o[2], o[3]); w.z = cvt_pk_bf16(o[4], o[5]); w.w = cvt_pk_bf16(o[6], o[7]);
;                     *(u32x4*)(O + row * 512 + col) = w; } }
.LBB0_848:
	v_mul_f32_e32 v85, 0xbfb8aa3b, v98
	v_exp_f32_e32 v85, v85
	s_nop 0
	v_add_f32_e32 v85, 1.0, v85
	v_rcp_f32_e32 v99, v85
	s_nop 0
	v_fma_f32 v101, -v85, v99, 1.0
	v_fmac_f32_e32 v99, v101, v99
	v_div_fixup_f32 v85, v99, v85, 1.0
	v_mul_f32_e32 v85, 0xbf1b4598, v85
.LBB0_849:
	v_add_f32_e32 v98, v86, v82
	s_and_b64 vcc, exec, s[2:3]
	s_mov_b64 s[68:69], -1
	s_cbranch_vccnz .LBB0_853
	s_and_b64 vcc, exec, s[0:1]
	v_mov_b32_e32 v86, v98
	s_cbranch_vccnz .LBB0_852
	v_mul_f32_e32 v86, 0xbfb8aa3b, v98
	v_exp_f32_e32 v86, v86
	s_nop 0
	v_add_f32_e32 v86, 1.0, v86
	v_rcp_f32_e32 v100, v86
	s_nop 0
	v_fma_f32 v102, -v86, v100, 1.0
	v_fmac_f32_e32 v100, v102, v100
	v_div_fixup_f32 v86, v100, v86, 1.0

; __device__ __forceinline__ unsigned cvt_pk_bf16(float lo, float hi) { const f32x2c v = {lo, hi}; const bf16x2c b = __builtin_convertvector(v, bf16x2c); return __builtin_bit_cast(unsigned, b); }
; __device__ __forceinline__ float sigmoidf_(float x) { return 1.f / (1.f + __expf(-x)); }
;     __device__ __forceinline__ void operator()(const f32x4 (&acc)[2][2][4][2], const Unit& u, int wr, int wc, int fr, int fq) const {
;     ...
;         for (int bj = 0; bj < 2; ++bj) { const int col = (col0 + bj * HALF) & 511;
;             f32x4 b0 = (f32x4){0.f, 0.f, 0.f, 0.f}, b1 = b0;
;             if (kind == 0) { b0 = *(const f32x4*)(w0 + col); b1 = *(const f32x4*)(w0 + col + 4); }
;             else if (kind == 1) { b0 = *(const f32x4*)(a0 + col); b1 = *(const f32x4*)(a0 + col + 4); }
; #pragma unroll
;             for (int ai = 0; ai < 2; ++ai)
; #pragma unroll
;                 for (int m = 0; m < 4; ++m) { const size_t row = (size_t)(row0 + ai * HALF + m * 16);
;                     const f32x4 v0 = acc[ai][bj][m][0] + b0, v1 = acc[ai][bj][m][1] + b1; float o[8];
; #pragma unroll
;                     for (int e = 0; e < 8; ++e) { float x = (e < 4) ? v0[e & 3] : v1[e & 3];
;                         if (kind == 0) x = -0.6065306597126334f * sigmoidf_(x);
;                         else if (kind == 1) x = sigmoidf_(x);
;                         o[e] = x; }
;                     u32x4 w; w.x = cvt_pk_bf16(o[0], o[1]); w.y = cvt_pk_bf16(o[2], o[3]); w.z = cvt_pk_bf16(o[4], o[5]); w.w = cvt_pk_bf16(o[6], o[7]);
;                     *(u32x4*)(O + row * 512 + col) = w; } }
.LBB0_854:
	v_mul_f32_e32 v86, 0xbfb8aa3b, v98
	v_exp_f32_e32 v86, v86
	s_nop 0
	v_add_f32_e32 v86, 1.0, v86
	v_rcp_f32_e32 v99, v86
	s_nop 0
	v_fma_f32 v101, -v86, v99, 1.0
	v_fmac_f32_e32 v99, v101, v99
	v_div_fixup_f32 v86, v99, v86, 1.0
	v_mul_f32_e32 v86, 0xbf1b4598, v86
.LBB0_855:
	v_add_f32_e32 v87, v87, v83
	s_and_b64 vcc, exec, s[2:3]
	s_mov_b64 s[68:69], -1
	s_cbranch_vccnz .LBB0_859
	s_and_b64 vcc, exec, s[0:1]
	v_mov_b32_e32 v98, v87
	s_cbranch_vccnz .LBB0_858
	v_mul_f32_e32 v98, 0xbfb8aa3b, v87
	v_exp_f32_e32 v98, v98
	s_nop 0
	v_add_f32_e32 v98, 1.0, v98
	v_rcp_f32_e32 v100, v98
	s_nop 0
	v_fma_f32 v102, -v98, v100, 1.0
	v_fmac_f32_e32 v100, v102, v100
	v_div_fixup_f32 v98, v100, v98, 1.0

; __device__ __forceinline__ unsigned cvt_pk_bf16(float lo, float hi) { const f32x2c v = {lo, hi}; const bf16x2c b = __builtin_convertvector(v, bf16x2c); return __builtin_bit_cast(unsigned, b); }
; __device__ __forceinline__ float sigmoidf_(float x) { return 1.f / (1.f + __expf(-x)); }
;     __device__ __forceinline__ void operator()(const f32x4 (&acc)[2][2][4][2], const Unit& u, int wr, int wc, int fr, int fq) const {
;     ...
;         for (int bj = 0; bj < 2; ++bj) { const int col = (col0 + bj * HALF) & 511;
;             f32x4 b0 = (f32x4){0.f, 0.f, 0.f, 0.f}, b1 = b0;
;             if (kind == 0) { b0 = *(const f32x4*)(w0 + col); b1 = *(const f32x4*)(w0 + col + 4); }
;             else if (kind == 1) { b0 = *(const f32x4*)(a0 + col); b1 = *(const f32x4*)(a0 + col + 4); }
; #pragma unroll
;             for (int ai = 0; ai < 2; ++ai)
; #pragma unroll
;                 for (int m = 0; m < 4; ++m) { const size_t row = (size_t)(row0 + ai * HALF + m * 16);
;                     const f32x4 v0 = acc[ai][bj][m][0] + b0, v1 = acc[ai][bj][m][1] + b1; float o[8];
; #pragma unroll
;                     for (int e = 0; e < 8; ++e) { float x = (e < 4) ? v0[e & 3] : v1[e & 3];
;                         if (kind == 0) x = -0.6065306597126334f * sigmoidf_(x);
;                         else if (kind == 1) x = sigmoidf_(x);
;                         o[e] = x; }
;                     u32x4 w; w.x = cvt_pk_bf16(o[0], o[1]); w.y = cvt_pk_bf16(o[2], o[3]); w.z = cvt_pk_bf16(o[4], o[5]); w.w = cvt_pk_bf16(o[6], o[7]);
;                     *(u32x4*)(O + row * 512 + col) = w; } }
.LBB0_860:
	v_mul_f32_e32 v87, 0xbfb8aa3b, v87
	v_exp_f32_e32 v87, v87
	s_nop 0
	v_add_f32_e32 v87, 1.0, v87
	v_rcp_f32_e32 v99, v87
	s_nop 0
	v_fma_f32 v101, -v87, v99, 1.0
	v_fmac_f32_e32 v99, v101, v99
	v_div_fixup_f32 v87, v99, v87, 1.0
	v_mul_f32_e32 v98, 0xbf1b4598, v87
.LBB0_861:
	v_lshlrev_b64 v[100:101], 10, v[132:133]
	v_cvt_pk_bf16_f32 v92, v92, v93
	v_cvt_pk_bf16_f32 v93, v94, v95
	v_cvt_pk_bf16_f32 v94, v84, v85
	v_lshl_add_u64 v[84:85], v[130:131], 0, v[100:101]
	v_cvt_pk_bf16_f32 v95, v86, v98
	v_add_co_u32_e32 v86, vcc, 0x24000, v84
	s_mov_b64 s[68:69], -1
	s_nop 0
	v_addc_co_u32_e32 v87, vcc, 0, v85, vcc
	global_store_dwordx4 v[86:87], v[92:95], off
	v_add_f32_e32 v86, v76, v88
	s_and_b64 vcc, exec, s[2:3]
	s_cbranch_vccnz .LBB0_865
	s_and_b64 vcc, exec, s[0:1]
	v_mov_b32_e32 v76, v86
	s_cbranch_vccnz .LBB0_864
	v_mul_f32_e32 v76, 0xbfb8aa3b, v86
	v_exp_f32_e32 v76, v76
	s_nop 0
	v_add_f32_e32 v76, 1.0, v76
	v_rcp_f32_e32 v92, v76
	s_nop 0
	v_fma_f32 v94, -v76, v92, 1.0
	v_fmac_f32_e32 v92, v94, v92
	v_div_fixup_f32 v76, v92, v76, 1.0

; __device__ __forceinline__ unsigned cvt_pk_bf16(float lo, float hi) { const f32x2c v = {lo, hi}; const bf16x2c b = __builtin_convertvector(v, bf16x2c); return __builtin_bit_cast(unsigned, b); }
; __device__ __forceinline__ float sigmoidf_(float x) { return 1.f / (1.f + __expf(-x)); }
;     __device__ __forceinline__ void operator()(const f32x4 (&acc)[2][2][4][2], const Unit& u, int wr, int wc, int fr, int fq) const {
;     ...
;         for (int bj = 0; bj < 2; ++bj) { const int col = (col0 + bj * HALF) & 511;
;             f32x4 b0 = (f32x4){0.f, 0.f, 0.f, 0.f}, b1 = b0;
;             if (kind == 0) { b0 = *(const f32x4*)(w0 + col); b1 = *(const f32x4*)(w0 + col + 4); }
;             else if (kind == 1) { b0 = *(const f32x4*)(a0 + col); b1 = *(const f32x4*)(a0 + col + 4); }
; #pragma unroll
;             for (int ai = 0; ai < 2; ++ai)
; #pragma unroll
;                 for (int m = 0; m < 4; ++m) { const size_t row = (size_t)(row0 + ai * HALF + m * 16);
;                     const f32x4 v0 = acc[ai][bj][m][0] + b0, v1 = acc[ai][bj][m][1] + b1; float o[8];
; #pragma unroll
;                     for (int e = 0; e < 8; ++e) { float x = (e < 4) ? v0[e & 3] : v1[e & 3];
;                         if (kind == 0) x = -0.6065306597126334f * sigmoidf_(x);
;                         else if (kind == 1) x = sigmoidf_(x);
;                         o[e] = x; }
;                     u32x4 w; w.x = cvt_pk_bf16(o[0], o[1]); w.y = cvt_pk_bf16(o[2], o[3]); w.z = cvt_pk_bf16(o[4], o[5]); w.w = cvt_pk_bf16(o[6], o[7]);
;                     *(u32x4*)(O + row * 512 + col) = w; } }
.LBB0_866:
	v_mul_f32_e32 v76, 0xbfb8aa3b, v86
	v_exp_f32_e32 v76, v76
	s_nop 0
	v_add_f32_e32 v76, 1.0, v76
	v_rcp_f32_e32 v87, v76
	s_nop 0
	v_fma_f32 v93, -v76, v87, 1.0
	v_fmac_f32_e32 v87, v93, v87
	v_div_fixup_f32 v76, v87, v76, 1.0
	v_mul_f32_e32 v76, 0xbf1b4598, v76
.LBB0_867:
	v_add_f32_e32 v86, v77, v89
	s_and_b64 vcc, exec, s[2:3]
	s_mov_b64 s[68:69], -1
	s_cbranch_vccnz .LBB0_871
	s_and_b64 vcc, exec, s[0:1]
	v_mov_b32_e32 v77, v86
	s_cbranch_vccnz .LBB0_870
	v_mul_f32_e32 v77, 0xbfb8aa3b, v86
	v_exp_f32_e32 v77, v77
	s_nop 0
	v_add_f32_e32 v77, 1.0, v77
	v_rcp_f32_e32 v92, v77
	s_nop 0
	v_fma_f32 v94, -v77, v92, 1.0
	v_fmac_f32_e32 v92, v94, v92
	v_div_fixup_f32 v77, v92, v77, 1.0

; __device__ __forceinline__ unsigned cvt_pk_bf16(float lo, float hi) { const f32x2c v = {lo, hi}; const bf16x2c b = __builtin_convertvector(v, bf16x2c); return __builtin_bit_cast(unsigned, b); }
; __device__ __forceinline__ float sigmoidf_(float x) { return 1.f / (1.f + __expf(-x)); }
;     __device__ __forceinline__ void operator()(const f32x4 (&acc)[2][2][4][2], const Unit& u, int wr, int wc, int fr, int fq) const {
;     ...
;         for (int bj = 0; bj < 2; ++bj) { const int col = (col0 + bj * HALF) & 511;
;             f32x4 b0 = (f32x4){0.f, 0.f, 0.f, 0.f}, b1 = b0;
;             if (kind == 0) { b0 = *(const f32x4*)(w0 + col); b1 = *(const f32x4*)(w0 + col + 4); }
;             else if (kind == 1) { b0 = *(const f32x4*)(a0 + col); b1 = *(const f32x4*)(a0 + col + 4); }
; #pragma unroll
;             for (int ai = 0; ai < 2; ++ai)
; #pragma unroll
;                 for (int m = 0; m < 4; ++m) { const size_t row = (size_t)(row0 + ai * HALF + m * 16);
;                     const f32x4 v0 = acc[ai][bj][m][0] + b0, v1 = acc[ai][bj][m][1] + b1; float o[8];
; #pragma unroll
;                     for (int e = 0; e < 8; ++e) { float x = (e < 4) ? v0[e & 3] : v1[e & 3];
;                         if (kind == 0) x = -0.6065306597126334f * sigmoidf_(x);
;                         else if (kind == 1) x = sigmoidf_(x);
;                         o[e] = x; }
;                     u32x4 w; w.x = cvt_pk_bf16(o[0], o[1]); w.y = cvt_pk_bf16(o[2], o[3]); w.z = cvt_pk_bf16(o[4], o[5]); w.w = cvt_pk_bf16(o[6], o[7]);
;                     *(u32x4*)(O + row * 512 + col) = w; } }
.LBB0_872:
	v_mul_f32_e32 v77, 0xbfb8aa3b, v86
	v_exp_f32_e32 v77, v77
	s_nop 0
	v_add_f32_e32 v77, 1.0, v77
	v_rcp_f32_e32 v87, v77
	s_nop 0
	v_fma_f32 v93, -v77, v87, 1.0
	v_fmac_f32_e32 v87, v93, v87
	v_div_fixup_f32 v77, v87, v77, 1.0
	v_mul_f32_e32 v77, 0xbf1b4598, v77
.LBB0_873:
	v_add_f32_e32 v86, v78, v90
	s_and_b64 vcc, exec, s[2:3]
	s_mov_b64 s[68:69], -1
	s_cbranch_vccnz .LBB0_877
	s_and_b64 vcc, exec, s[0:1]
	v_mov_b32_e32 v78, v86
	s_cbranch_vccnz .LBB0_876
	v_mul_f32_e32 v78, 0xbfb8aa3b, v86
	v_exp_f32_e32 v78, v78
	s_nop 0
	v_add_f32_e32 v78, 1.0, v78
	v_rcp_f32_e32 v92, v78
	s_nop 0
	v_fma_f32 v94, -v78, v92, 1.0
	v_fmac_f32_e32 v92, v94, v92
	v_div_fixup_f32 v78, v92, v78, 1.0

; __device__ __forceinline__ unsigned cvt_pk_bf16(float lo, float hi) { const f32x2c v = {lo, hi}; const bf16x2c b = __builtin_convertvector(v, bf16x2c); return __builtin_bit_cast(unsigned, b); }
; __device__ __forceinline__ float sigmoidf_(float x) { return 1.f / (1.f + __expf(-x)); }
;     __device__ __forceinline__ void operator()(const f32x4 (&acc)[2][2][4][2], const Unit& u, int wr, int wc, int fr, int fq) const {
;     ...
;         for (int bj = 0; bj < 2; ++bj) { const int col = (col0 + bj * HALF) & 511;
;             f32x4 b0 = (f32x4){0.f, 0.f, 0.f, 0.f}, b1 = b0;
;             if (kind == 0) { b0 = *(const f32x4*)(w0 + col); b1 = *(const f32x4*)(w0 + col + 4); }
;             else if (kind == 1) { b0 = *(const f32x4*)(a0 + col); b1 = *(const f32x4*)(a0 + col + 4); }
; #pragma unroll
;             for (int ai = 0; ai < 2; ++ai)
; #pragma unroll
;                 for (int m = 0; m < 4; ++m) { const size_t row = (size_t)(row0 + ai * HALF + m * 16);
;                     const f32x4 v0 = acc[ai][bj][m][0] + b0, v1 = acc[ai][bj][m][1] + b1; float o[8];
; #pragma unroll
;                     for (int e = 0; e < 8; ++e) { float x = (e < 4) ? v0[e & 3] : v1[e & 3];
;                         if (kind == 0) x = -0.6065306597126334f * sigmoidf_(x);
;                         else if (kind == 1) x = sigmoidf_(x);
;                         o[e] = x; }
;                     u32x4 w; w.x = cvt_pk_bf16(o[0], o[1]); w.y = cvt_pk_bf16(o[2], o[3]); w.z = cvt_pk_bf16(o[4], o[5]); w.w = cvt_pk_bf16(o[6], o[7]);
;                     *(u32x4*)(O + row * 512 + col) = w; } }
.LBB0_878:
	v_mul_f32_e32 v78, 0xbfb8aa3b, v86
	v_exp_f32_e32 v78, v78
	s_nop 0
	v_add_f32_e32 v78, 1.0, v78
	v_rcp_f32_e32 v87, v78
	s_nop 0
	v_fma_f32 v93, -v78, v87, 1.0
	v_fmac_f32_e32 v87, v93, v87
	v_div_fixup_f32 v78, v87, v78, 1.0
	v_mul_f32_e32 v78, 0xbf1b4598, v78
.LBB0_879:
	v_add_f32_e32 v86, v79, v91
	s_and_b64 vcc, exec, s[2:3]
	s_mov_b64 s[68:69], -1
	s_cbranch_vccnz .LBB0_883
	s_and_b64 vcc, exec, s[0:1]
	v_mov_b32_e32 v79, v86
	s_cbranch_vccnz .LBB0_882
	v_mul_f32_e32 v79, 0xbfb8aa3b, v86
	v_exp_f32_e32 v79, v79
	s_nop 0
	v_add_f32_e32 v79, 1.0, v79
	v_rcp_f32_e32 v92, v79
	s_nop 0
	v_fma_f32 v94, -v79, v92, 1.0
	v_fmac_f32_e32 v92, v94, v92
	v_div_fixup_f32 v79, v92, v79, 1.0

; __device__ __forceinline__ unsigned cvt_pk_bf16(float lo, float hi) { const f32x2c v = {lo, hi}; const bf16x2c b = __builtin_convertvector(v, bf16x2c); return __builtin_bit_cast(unsigned, b); }
; __device__ __forceinline__ float sigmoidf_(float x) { return 1.f / (1.f + __expf(-x)); }
;     __device__ __forceinline__ void operator()(const f32x4 (&acc)[2][2][4][2], const Unit& u, int wr, int wc, int fr, int fq) const {
;     ...
;         for (int bj = 0; bj < 2; ++bj) { const int col = (col0 + bj * HALF) & 511;
;             f32x4 b0 = (f32x4){0.f, 0.f, 0.f, 0.f}, b1 = b0;
;             if (kind == 0) { b0 = *(const f32x4*)(w0 + col); b1 = *(const f32x4*)(w0 + col + 4); }
;             else if (kind == 1) { b0 = *(const f32x4*)(a0 + col); b1 = *(const f32x4*)(a0 + col + 4); }
; #pragma unroll
;             for (int ai = 0; ai < 2; ++ai)
; #pragma unroll
;                 for (int m = 0; m < 4; ++m) { const size_t row = (size_t)(row0 + ai * HALF + m * 16);
;                     const f32x4 v0 = acc[ai][bj][m][0] + b0, v1 = acc[ai][bj][m][1] + b1; float o[8];
; #pragma unroll
;                     for (int e = 0; e < 8; ++e) { float x = (e < 4) ? v0[e & 3] : v1[e & 3];
;                         if (kind == 0) x = -0.6065306597126334f * sigmoidf_(x);
;                         else if (kind == 1) x = sigmoidf_(x);
;                         o[e] = x; }
;                     u32x4 w; w.x = cvt_pk_bf16(o[0], o[1]); w.y = cvt_pk_bf16(o[2], o[3]); w.z = cvt_pk_bf16(o[4], o[5]); w.w = cvt_pk_bf16(o[6], o[7]);
;                     *(u32x4*)(O + row * 512 + col) = w; } }
.LBB0_884:
	v_mul_f32_e32 v79, 0xbfb8aa3b, v86
	v_exp_f32_e32 v79, v79
	s_nop 0
	v_add_f32_e32 v79, 1.0, v79
	v_rcp_f32_e32 v87, v79
	s_nop 0
	v_fma_f32 v93, -v79, v87, 1.0
	v_fmac_f32_e32 v87, v93, v87
	v_div_fixup_f32 v79, v87, v79, 1.0
	v_mul_f32_e32 v79, 0xbf1b4598, v79
.LBB0_885:
	v_add_f32_e32 v86, v72, v80
	s_and_b64 vcc, exec, s[2:3]
	s_mov_b64 s[68:69], -1
	s_cbranch_vccnz .LBB0_889
	s_and_b64 vcc, exec, s[0:1]
	v_mov_b32_e32 v72, v86
	s_cbranch_vccnz .LBB0_888
	v_mul_f32_e32 v72, 0xbfb8aa3b, v86
	v_exp_f32_e32 v72, v72
	s_nop 0
	v_add_f32_e32 v72, 1.0, v72
	v_rcp_f32_e32 v92, v72
	s_nop 0
	v_fma_f32 v94, -v72, v92, 1.0
	v_fmac_f32_e32 v92, v94, v92
	v_div_fixup_f32 v72, v92, v72, 1.0

; __device__ __forceinline__ unsigned cvt_pk_bf16(float lo, float hi) { const f32x2c v = {lo, hi}; const bf16x2c b = __builtin_convertvector(v, bf16x2c); return __builtin_bit_cast(unsigned, b); }
; __device__ __forceinline__ float sigmoidf_(float x) { return 1.f / (1.f + __expf(-x)); }
;     __device__ __forceinline__ void operator()(const f32x4 (&acc)[2][2][4][2], const Unit& u, int wr, int wc, int fr, int fq) const {
;     ...
;         for (int bj = 0; bj < 2; ++bj) { const int col = (col0 + bj * HALF) & 511;
;             f32x4 b0 = (f32x4){0.f, 0.f, 0.f, 0.f}, b1 = b0;
;             if (kind == 0) { b0 = *(const f32x4*)(w0 + col); b1 = *(const f32x4*)(w0 + col + 4); }
;             else if (kind == 1) { b0 = *(const f32x4*)(a0 + col); b1 = *(const f32x4*)(a0 + col + 4); }
; #pragma unroll
;             for (int ai = 0; ai < 2; ++ai)
; #pragma unroll
;                 for (int m = 0; m < 4; ++m) { const size_t row = (size_t)(row0 + ai * HALF + m * 16);
;                     const f32x4 v0 = acc[ai][bj][m][0] + b0, v1 = acc[ai][bj][m][1] + b1; float o[8];
; #pragma unroll
;                     for (int e = 0; e < 8; ++e) { float x = (e < 4) ? v0[e & 3] : v1[e & 3];
;                         if (kind == 0) x = -0.6065306597126334f * sigmoidf_(x);
;                         else if (kind == 1) x = sigmoidf_(x);
;                         o[e] = x; }
;                     u32x4 w; w.x = cvt_pk_bf16(o[0], o[1]); w.y = cvt_pk_bf16(o[2], o[3]); w.z = cvt_pk_bf16(o[4], o[5]); w.w = cvt_pk_bf16(o[6], o[7]);
;                     *(u32x4*)(O + row * 512 + col) = w; } }
.LBB0_890:
	v_mul_f32_e32 v72, 0xbfb8aa3b, v86
	v_exp_f32_e32 v72, v72
	s_nop 0
	v_add_f32_e32 v72, 1.0, v72
	v_rcp_f32_e32 v87, v72
	s_nop 0
	v_fma_f32 v93, -v72, v87, 1.0
	v_fmac_f32_e32 v87, v93, v87
	v_div_fixup_f32 v72, v87, v72, 1.0
	v_mul_f32_e32 v72, 0xbf1b4598, v72
.LBB0_891:
	v_add_f32_e32 v86, v73, v81
	s_and_b64 vcc, exec, s[2:3]
	s_mov_b64 s[68:69], -1
	s_cbranch_vccnz .LBB0_895
	s_and_b64 vcc, exec, s[0:1]
	v_mov_b32_e32 v73, v86
	s_cbranch_vccnz .LBB0_894
	v_mul_f32_e32 v73, 0xbfb8aa3b, v86
	v_exp_f32_e32 v73, v73
	s_nop 0
	v_add_f32_e32 v73, 1.0, v73
	v_rcp_f32_e32 v92, v73
	s_nop 0
	v_fma_f32 v94, -v73, v92, 1.0
	v_fmac_f32_e32 v92, v94, v92
	v_div_fixup_f32 v73, v92, v73, 1.0

; __device__ __forceinline__ unsigned cvt_pk_bf16(float lo, float hi) { const f32x2c v = {lo, hi}; const bf16x2c b = __builtin_convertvector(v, bf16x2c); return __builtin_bit_cast(unsigned, b); }
; __device__ __forceinline__ float sigmoidf_(float x) { return 1.f / (1.f + __expf(-x)); }
;     __device__ __forceinline__ void operator()(const f32x4 (&acc)[2][2][4][2], const Unit& u, int wr, int wc, int fr, int fq) const {
;     ...
;         for (int bj = 0; bj < 2; ++bj) { const int col = (col0 + bj * HALF) & 511;
;             f32x4 b0 = (f32x4){0.f, 0.f, 0.f, 0.f}, b1 = b0;
;             if (kind == 0) { b0 = *(const f32x4*)(w0 + col); b1 = *(const f32x4*)(w0 + col + 4); }
;             else if (kind == 1) { b0 = *(const f32x4*)(a0 + col); b1 = *(const f32x4*)(a0 + col + 4); }
; #pragma unroll
;             for (int ai = 0; ai < 2; ++ai)
; #pragma unroll
;                 for (int m = 0; m < 4; ++m) { const size_t row = (size_t)(row0 + ai * HALF + m * 16);
;                     const f32x4 v0 = acc[ai][bj][m][0] + b0, v1 = acc[ai][bj][m][1] + b1; float o[8];
; #pragma unroll
;                     for (int e = 0; e < 8; ++e) { float x = (e < 4) ? v0[e & 3] : v1[e & 3];
;                         if (kind == 0) x = -0.6065306597126334f * sigmoidf_(x);
;                         else if (kind == 1) x = sigmoidf_(x);
;                         o[e] = x; }
;                     u32x4 w; w.x = cvt_pk_bf16(o[0], o[1]); w.y = cvt_pk_bf16(o[2], o[3]); w.z = cvt_pk_bf16(o[4], o[5]); w.w = cvt_pk_bf16(o[6], o[7]);
;                     *(u32x4*)(O + row * 512 + col) = w; } }
.LBB0_896:
	v_mul_f32_e32 v73, 0xbfb8aa3b, v86
	v_exp_f32_e32 v73, v73
	s_nop 0
	v_add_f32_e32 v73, 1.0, v73
	v_rcp_f32_e32 v87, v73
	s_nop 0
	v_fma_f32 v93, -v73, v87, 1.0
	v_fmac_f32_e32 v87, v93, v87
	v_div_fixup_f32 v73, v87, v73, 1.0
	v_mul_f32_e32 v73, 0xbf1b4598, v73
.LBB0_897:
	v_add_f32_e32 v86, v74, v82
	s_and_b64 vcc, exec, s[2:3]
	s_mov_b64 s[68:69], -1
	s_cbranch_vccnz .LBB0_901
	s_and_b64 vcc, exec, s[0:1]
	v_mov_b32_e32 v74, v86
	s_cbranch_vccnz .LBB0_900
	v_mul_f32_e32 v74, 0xbfb8aa3b, v86
	v_exp_f32_e32 v74, v74
	s_nop 0
	v_add_f32_e32 v74, 1.0, v74
	v_rcp_f32_e32 v92, v74
	s_nop 0
	v_fma_f32 v94, -v74, v92, 1.0
	v_fmac_f32_e32 v92, v94, v92
	v_div_fixup_f32 v74, v92, v74, 1.0

; __device__ __forceinline__ unsigned cvt_pk_bf16(float lo, float hi) { const f32x2c v = {lo, hi}; const bf16x2c b = __builtin_convertvector(v, bf16x2c); return __builtin_bit_cast(unsigned, b); }
; __device__ __forceinline__ float sigmoidf_(float x) { return 1.f / (1.f + __expf(-x)); }
;     __device__ __forceinline__ void operator()(const f32x4 (&acc)[2][2][4][2], const Unit& u, int wr, int wc, int fr, int fq) const {
;     ...
;         for (int bj = 0; bj < 2; ++bj) { const int col = (col0 + bj * HALF) & 511;
;             f32x4 b0 = (f32x4){0.f, 0.f, 0.f, 0.f}, b1 = b0;
;             if (kind == 0) { b0 = *(const f32x4*)(w0 + col); b1 = *(const f32x4*)(w0 + col + 4); }
;             else if (kind == 1) { b0 = *(const f32x4*)(a0 + col); b1 = *(const f32x4*)(a0 + col + 4); }
; #pragma unroll
;             for (int ai = 0; ai < 2; ++ai)
; #pragma unroll
;                 for (int m = 0; m < 4; ++m) { const size_t row = (size_t)(row0 + ai * HALF + m * 16);
;                     const f32x4 v0 = acc[ai][bj][m][0] + b0, v1 = acc[ai][bj][m][1] + b1; float o[8];
; #pragma unroll
;                     for (int e = 0; e < 8; ++e) { float x = (e < 4) ? v0[e & 3] : v1[e & 3];
;                         if (kind == 0) x = -0.6065306597126334f * sigmoidf_(x);
;                         else if (kind == 1) x = sigmoidf_(x);
;                         o[e] = x; }
;                     u32x4 w; w.x = cvt_pk_bf16(o[0], o[1]); w.y = cvt_pk_bf16(o[2], o[3]); w.z = cvt_pk_bf16(o[4], o[5]); w.w = cvt_pk_bf16(o[6], o[7]);
;                     *(u32x4*)(O + row * 512 + col) = w; } }
.LBB0_902:
	v_mul_f32_e32 v74, 0xbfb8aa3b, v86
	v_exp_f32_e32 v74, v74
	s_nop 0
	v_add_f32_e32 v74, 1.0, v74
	v_rcp_f32_e32 v87, v74
	s_nop 0
	v_fma_f32 v93, -v74, v87, 1.0
	v_fmac_f32_e32 v87, v93, v87
	v_div_fixup_f32 v74, v87, v74, 1.0
	v_mul_f32_e32 v74, 0xbf1b4598, v74
.LBB0_903:
	v_add_f32_e32 v75, v75, v83
	s_and_b64 vcc, exec, s[2:3]
	s_mov_b64 s[68:69], -1
	s_cbranch_vccnz .LBB0_907
	s_and_b64 vcc, exec, s[0:1]
	v_mov_b32_e32 v86, v75
	s_cbranch_vccnz .LBB0_906
	v_mul_f32_e32 v86, 0xbfb8aa3b, v75
	v_exp_f32_e32 v86, v86
	s_nop 0
	v_add_f32_e32 v86, 1.0, v86
	v_rcp_f32_e32 v92, v86
	s_nop 0
	v_fma_f32 v94, -v86, v92, 1.0
	v_fmac_f32_e32 v92, v94, v92
	v_div_fixup_f32 v86, v92, v86, 1.0

; __device__ __forceinline__ unsigned cvt_pk_bf16(float lo, float hi) { const f32x2c v = {lo, hi}; const bf16x2c b = __builtin_convertvector(v, bf16x2c); return __builtin_bit_cast(unsigned, b); }
; __device__ __forceinline__ float sigmoidf_(float x) { return 1.f / (1.f + __expf(-x)); }
;     __device__ __forceinline__ void operator()(const f32x4 (&acc)[2][2][4][2], const Unit& u, int wr, int wc, int fr, int fq) const {
;     ...
;         for (int bj = 0; bj < 2; ++bj) { const int col = (col0 + bj * HALF) & 511;
;             f32x4 b0 = (f32x4){0.f, 0.f, 0.f, 0.f}, b1 = b0;
;             if (kind == 0) { b0 = *(const f32x4*)(w0 + col); b1 = *(const f32x4*)(w0 + col + 4); }
;             else if (kind == 1) { b0 = *(const f32x4*)(a0 + col); b1 = *(const f32x4*)(a0 + col + 4); }
; #pragma unroll
;             for (int ai = 0; ai < 2; ++ai)
; #pragma unroll
;                 for (int m = 0; m < 4; ++m) { const size_t row = (size_t)(row0 + ai * HALF + m * 16);
;                     const f32x4 v0 = acc[ai][bj][m][0] + b0, v1 = acc[ai][bj][m][1] + b1; float o[8];
; #pragma unroll
;                     for (int e = 0; e < 8; ++e) { float x = (e < 4) ? v0[e & 3] : v1[e & 3];
;                         if (kind == 0) x = -0.6065306597126334f * sigmoidf_(x);
;                         else if (kind == 1) x = sigmoidf_(x);
;                         o[e] = x; }
;                     u32x4 w; w.x = cvt_pk_bf16(o[0], o[1]); w.y = cvt_pk_bf16(o[2], o[3]); w.z = cvt_pk_bf16(o[4], o[5]); w.w = cvt_pk_bf16(o[6], o[7]);
;                     *(u32x4*)(O + row * 512 + col) = w; } }
.LBB0_908:
	v_mul_f32_e32 v75, 0xbfb8aa3b, v75
	v_exp_f32_e32 v75, v75
	s_nop 0
	v_add_f32_e32 v75, 1.0, v75
	v_rcp_f32_e32 v87, v75
	s_nop 0
	v_fma_f32 v93, -v75, v87, 1.0
	v_fmac_f32_e32 v87, v93, v87
	v_div_fixup_f32 v75, v87, v75, 1.0
	v_mul_f32_e32 v86, 0xbf1b4598, v75
.LBB0_909:
	v_lshlrev_b64 v[92:93], 10, v[132:133]
	v_cvt_pk_bf16_f32 v76, v76, v77
	v_cvt_pk_bf16_f32 v77, v78, v79
	v_cvt_pk_bf16_f32 v78, v72, v73
	v_lshl_add_u64 v[72:73], v[130:131], 0, v[92:93]
	v_cvt_pk_bf16_f32 v79, v74, v86
	v_add_co_u32_e32 v74, vcc, 0x28000, v72
	s_mov_b64 s[68:69], -1
	s_nop 0
	v_addc_co_u32_e32 v75, vcc, 0, v73, vcc
	global_store_dwordx4 v[74:75], v[76:79], off
	v_add_f32_e32 v74, v68, v88
	s_and_b64 vcc, exec, s[2:3]
	s_cbranch_vccnz .LBB0_913
	s_and_b64 vcc, exec, s[0:1]
	v_mov_b32_e32 v68, v74
	s_cbranch_vccnz .LBB0_912
	v_mul_f32_e32 v68, 0xbfb8aa3b, v74
	v_exp_f32_e32 v68, v68
	s_nop 0
	v_add_f32_e32 v68, 1.0, v68
	v_rcp_f32_e32 v76, v68
	s_nop 0
	v_fma_f32 v78, -v68, v76, 1.0
	v_fmac_f32_e32 v76, v78, v76
	v_div_fixup_f32 v68, v76, v68, 1.0

; __device__ __forceinline__ unsigned cvt_pk_bf16(float lo, float hi) { const f32x2c v = {lo, hi}; const bf16x2c b = __builtin_convertvector(v, bf16x2c); return __builtin_bit_cast(unsigned, b); }
; __device__ __forceinline__ float sigmoidf_(float x) { return 1.f / (1.f + __expf(-x)); }
;     __device__ __forceinline__ void operator()(const f32x4 (&acc)[2][2][4][2], const Unit& u, int wr, int wc, int fr, int fq) const {
;     ...
;         for (int bj = 0; bj < 2; ++bj) { const int col = (col0 + bj * HALF) & 511;
;             f32x4 b0 = (f32x4){0.f, 0.f, 0.f, 0.f}, b1 = b0;
;             if (kind == 0) { b0 = *(const f32x4*)(w0 + col); b1 = *(const f32x4*)(w0 + col + 4); }
;             else if (kind == 1) { b0 = *(const f32x4*)(a0 + col); b1 = *(const f32x4*)(a0 + col + 4); }
; #pragma unroll
;             for (int ai = 0; ai < 2; ++ai)
; #pragma unroll
;                 for (int m = 0; m < 4; ++m) { const size_t row = (size_t)(row0 + ai * HALF + m * 16);
;                     const f32x4 v0 = acc[ai][bj][m][0] + b0, v1 = acc[ai][bj][m][1] + b1; float o[8];
; #pragma unroll
;                     for (int e = 0; e < 8; ++e) { float x = (e < 4) ? v0[e & 3] : v1[e & 3];
;                         if (kind == 0) x = -0.6065306597126334f * sigmoidf_(x);
;                         else if (kind == 1) x = sigmoidf_(x);
;                         o[e] = x; }
;                     u32x4 w; w.x = cvt_pk_bf16(o[0], o[1]); w.y = cvt_pk_bf16(o[2], o[3]); w.z = cvt_pk_bf16(o[4], o[5]); w.w = cvt_pk_bf16(o[6], o[7]);
;                     *(u32x4*)(O + row * 512 + col) = w; } }
.LBB0_914:
	v_mul_f32_e32 v68, 0xbfb8aa3b, v74
	v_exp_f32_e32 v68, v68
	s_nop 0
	v_add_f32_e32 v68, 1.0, v68
	v_rcp_f32_e32 v75, v68
	s_nop 0
	v_fma_f32 v77, -v68, v75, 1.0
	v_fmac_f32_e32 v75, v77, v75
	v_div_fixup_f32 v68, v75, v68, 1.0
	v_mul_f32_e32 v68, 0xbf1b4598, v68
.LBB0_915:
	v_add_f32_e32 v74, v69, v89
	s_and_b64 vcc, exec, s[2:3]
	s_mov_b64 s[68:69], -1
	s_cbranch_vccnz .LBB0_919
	s_and_b64 vcc, exec, s[0:1]
	v_mov_b32_e32 v69, v74
	s_cbranch_vccnz .LBB0_918
	v_mul_f32_e32 v69, 0xbfb8aa3b, v74
	v_exp_f32_e32 v69, v69
	s_nop 0
	v_add_f32_e32 v69, 1.0, v69
	v_rcp_f32_e32 v76, v69
	s_nop 0
	v_fma_f32 v78, -v69, v76, 1.0
	v_fmac_f32_e32 v76, v78, v76
	v_div_fixup_f32 v69, v76, v69, 1.0

; __device__ __forceinline__ unsigned cvt_pk_bf16(float lo, float hi) { const f32x2c v = {lo, hi}; const bf16x2c b = __builtin_convertvector(v, bf16x2c); return __builtin_bit_cast(unsigned, b); }
; __device__ __forceinline__ float sigmoidf_(float x) { return 1.f / (1.f + __expf(-x)); }
;     __device__ __forceinline__ void operator()(const f32x4 (&acc)[2][2][4][2], const Unit& u, int wr, int wc, int fr, int fq) const {
;     ...
;         for (int bj = 0; bj < 2; ++bj) { const int col = (col0 + bj * HALF) & 511;
;             f32x4 b0 = (f32x4){0.f, 0.f, 0.f, 0.f}, b1 = b0;
;             if (kind == 0) { b0 = *(const f32x4*)(w0 + col); b1 = *(const f32x4*)(w0 + col + 4); }
;             else if (kind == 1) { b0 = *(const f32x4*)(a0 + col); b1 = *(const f32x4*)(a0 + col + 4); }
; #pragma unroll
;             for (int ai = 0; ai < 2; ++ai)
; #pragma unroll
;                 for (int m = 0; m < 4; ++m) { const size_t row = (size_t)(row0 + ai * HALF + m * 16);
;                     const f32x4 v0 = acc[ai][bj][m][0] + b0, v1 = acc[ai][bj][m][1] + b1; float o[8];
; #pragma unroll
;                     for (int e = 0; e < 8; ++e) { float x = (e < 4) ? v0[e & 3] : v1[e & 3];
;                         if (kind == 0) x = -0.6065306597126334f * sigmoidf_(x);
;                         else if (kind == 1) x = sigmoidf_(x);
;                         o[e] = x; }
;                     u32x4 w; w.x = cvt_pk_bf16(o[0], o[1]); w.y = cvt_pk_bf16(o[2], o[3]); w.z = cvt_pk_bf16(o[4], o[5]); w.w = cvt_pk_bf16(o[6], o[7]);
;                     *(u32x4*)(O + row * 512 + col) = w; } }
.LBB0_920:
	v_mul_f32_e32 v69, 0xbfb8aa3b, v74
	v_exp_f32_e32 v69, v69
	s_nop 0
	v_add_f32_e32 v69, 1.0, v69
	v_rcp_f32_e32 v75, v69
	s_nop 0
	v_fma_f32 v77, -v69, v75, 1.0
	v_fmac_f32_e32 v75, v77, v75
	v_div_fixup_f32 v69, v75, v69, 1.0
	v_mul_f32_e32 v69, 0xbf1b4598, v69
.LBB0_921:
	v_add_f32_e32 v74, v70, v90
	s_and_b64 vcc, exec, s[2:3]
	s_mov_b64 s[68:69], -1
	s_cbranch_vccnz .LBB0_925
	s_and_b64 vcc, exec, s[0:1]
	v_mov_b32_e32 v70, v74
	s_cbranch_vccnz .LBB0_924
	v_mul_f32_e32 v70, 0xbfb8aa3b, v74
	v_exp_f32_e32 v70, v70
	s_nop 0
	v_add_f32_e32 v70, 1.0, v70
	v_rcp_f32_e32 v76, v70
	s_nop 0
	v_fma_f32 v78, -v70, v76, 1.0
	v_fmac_f32_e32 v76, v78, v76
	v_div_fixup_f32 v70, v76, v70, 1.0

; __device__ __forceinline__ unsigned cvt_pk_bf16(float lo, float hi) { const f32x2c v = {lo, hi}; const bf16x2c b = __builtin_convertvector(v, bf16x2c); return __builtin_bit_cast(unsigned, b); }
; __device__ __forceinline__ float sigmoidf_(float x) { return 1.f / (1.f + __expf(-x)); }
;     __device__ __forceinline__ void operator()(const f32x4 (&acc)[2][2][4][2], const Unit& u, int wr, int wc, int fr, int fq) const {
;     ...
;         for (int bj = 0; bj < 2; ++bj) { const int col = (col0 + bj * HALF) & 511;
;             f32x4 b0 = (f32x4){0.f, 0.f, 0.f, 0.f}, b1 = b0;
;             if (kind == 0) { b0 = *(const f32x4*)(w0 + col); b1 = *(const f32x4*)(w0 + col + 4); }
;             else if (kind == 1) { b0 = *(const f32x4*)(a0 + col); b1 = *(const f32x4*)(a0 + col + 4); }
; #pragma unroll
;             for (int ai = 0; ai < 2; ++ai)
; #pragma unroll
;                 for (int m = 0; m < 4; ++m) { const size_t row = (size_t)(row0 + ai * HALF + m * 16);
;                     const f32x4 v0 = acc[ai][bj][m][0] + b0, v1 = acc[ai][bj][m][1] + b1; float o[8];
; #pragma unroll
;                     for (int e = 0; e < 8; ++e) { float x = (e < 4) ? v0[e & 3] : v1[e & 3];
;                         if (kind == 0) x = -0.6065306597126334f * sigmoidf_(x);
;                         else if (kind == 1) x = sigmoidf_(x);
;                         o[e] = x; }
;                     u32x4 w; w.x = cvt_pk_bf16(o[0], o[1]); w.y = cvt_pk_bf16(o[2], o[3]); w.z = cvt_pk_bf16(o[4], o[5]); w.w = cvt_pk_bf16(o[6], o[7]);
;                     *(u32x4*)(O + row * 512 + col) = w; } }
.LBB0_926:
	v_mul_f32_e32 v70, 0xbfb8aa3b, v74
	v_exp_f32_e32 v70, v70
	s_nop 0
	v_add_f32_e32 v70, 1.0, v70
	v_rcp_f32_e32 v75, v70
	s_nop 0
	v_fma_f32 v77, -v70, v75, 1.0
	v_fmac_f32_e32 v75, v77, v75
	v_div_fixup_f32 v70, v75, v70, 1.0
	v_mul_f32_e32 v70, 0xbf1b4598, v70
.LBB0_927:
	v_add_f32_e32 v74, v71, v91
	s_and_b64 vcc, exec, s[2:3]
	s_mov_b64 s[68:69], -1
	s_cbranch_vccnz .LBB0_931
	s_and_b64 vcc, exec, s[0:1]
	v_mov_b32_e32 v71, v74
	s_cbranch_vccnz .LBB0_930
	v_mul_f32_e32 v71, 0xbfb8aa3b, v74
	v_exp_f32_e32 v71, v71
	s_nop 0
	v_add_f32_e32 v71, 1.0, v71
	v_rcp_f32_e32 v76, v71
	s_nop 0
	v_fma_f32 v78, -v71, v76, 1.0
	v_fmac_f32_e32 v76, v78, v76
	v_div_fixup_f32 v71, v76, v71, 1.0

; __device__ __forceinline__ unsigned cvt_pk_bf16(float lo, float hi) { const f32x2c v = {lo, hi}; const bf16x2c b = __builtin_convertvector(v, bf16x2c); return __builtin_bit_cast(unsigned, b); }
; __device__ __forceinline__ float sigmoidf_(float x) { return 1.f / (1.f + __expf(-x)); }
;     __device__ __forceinline__ void operator()(const f32x4 (&acc)[2][2][4][2], const Unit& u, int wr, int wc, int fr, int fq) const {
;     ...
;         for (int bj = 0; bj < 2; ++bj) { const int col = (col0 + bj * HALF) & 511;
;             f32x4 b0 = (f32x4){0.f, 0.f, 0.f, 0.f}, b1 = b0;
;             if (kind == 0) { b0 = *(const f32x4*)(w0 + col); b1 = *(const f32x4*)(w0 + col + 4); }
;             else if (kind == 1) { b0 = *(const f32x4*)(a0 + col); b1 = *(const f32x4*)(a0 + col + 4); }
; #pragma unroll
;             for (int ai = 0; ai < 2; ++ai)
; #pragma unroll
;                 for (int m = 0; m < 4; ++m) { const size_t row = (size_t)(row0 + ai * HALF + m * 16);
;                     const f32x4 v0 = acc[ai][bj][m][0] + b0, v1 = acc[ai][bj][m][1] + b1; float o[8];
; #pragma unroll
;                     for (int e = 0; e < 8; ++e) { float x = (e < 4) ? v0[e & 3] : v1[e & 3];
;                         if (kind == 0) x = -0.6065306597126334f * sigmoidf_(x);
;                         else if (kind == 1) x = sigmoidf_(x);
;                         o[e] = x; }
;                     u32x4 w; w.x = cvt_pk_bf16(o[0], o[1]); w.y = cvt_pk_bf16(o[2], o[3]); w.z = cvt_pk_bf16(o[4], o[5]); w.w = cvt_pk_bf16(o[6], o[7]);
;                     *(u32x4*)(O + row * 512 + col) = w; } }
.LBB0_932:
	v_mul_f32_e32 v71, 0xbfb8aa3b, v74
	v_exp_f32_e32 v71, v71
	s_nop 0
	v_add_f32_e32 v71, 1.0, v71
	v_rcp_f32_e32 v75, v71
	s_nop 0
	v_fma_f32 v77, -v71, v75, 1.0
	v_fmac_f32_e32 v75, v77, v75
	v_div_fixup_f32 v71, v75, v71, 1.0
	v_mul_f32_e32 v71, 0xbf1b4598, v71
.LBB0_933:
	v_add_f32_e32 v74, v64, v80
	s_and_b64 vcc, exec, s[2:3]
	s_mov_b64 s[68:69], -1
	s_cbranch_vccnz .LBB0_937
	s_and_b64 vcc, exec, s[0:1]
	v_mov_b32_e32 v64, v74
	s_cbranch_vccnz .LBB0_936
	v_mul_f32_e32 v64, 0xbfb8aa3b, v74
	v_exp_f32_e32 v64, v64
	s_nop 0
	v_add_f32_e32 v64, 1.0, v64
	v_rcp_f32_e32 v76, v64
	s_nop 0
	v_fma_f32 v78, -v64, v76, 1.0
	v_fmac_f32_e32 v76, v78, v76
	v_div_fixup_f32 v64, v76, v64, 1.0

; __device__ __forceinline__ unsigned cvt_pk_bf16(float lo, float hi) { const f32x2c v = {lo, hi}; const bf16x2c b = __builtin_convertvector(v, bf16x2c); return __builtin_bit_cast(unsigned, b); }
; __device__ __forceinline__ float sigmoidf_(float x) { return 1.f / (1.f + __expf(-x)); }
;     __device__ __forceinline__ void operator()(const f32x4 (&acc)[2][2][4][2], const Unit& u, int wr, int wc, int fr, int fq) const {
;     ...
;         for (int bj = 0; bj < 2; ++bj) { const int col = (col0 + bj * HALF) & 511;
;             f32x4 b0 = (f32x4){0.f, 0.f, 0.f, 0.f}, b1 = b0;
;             if (kind == 0) { b0 = *(const f32x4*)(w0 + col); b1 = *(const f32x4*)(w0 + col + 4); }
;             else if (kind == 1) { b0 = *(const f32x4*)(a0 + col); b1 = *(const f32x4*)(a0 + col + 4); }
; #pragma unroll
;             for (int ai = 0; ai < 2; ++ai)
; #pragma unroll
;                 for (int m = 0; m < 4; ++m) { const size_t row = (size_t)(row0 + ai * HALF + m * 16);
;                     const f32x4 v0 = acc[ai][bj][m][0] + b0, v1 = acc[ai][bj][m][1] + b1; float o[8];
; #pragma unroll
;                     for (int e = 0; e < 8; ++e) { float x = (e < 4) ? v0[e & 3] : v1[e & 3];
;                         if (kind == 0) x = -0.6065306597126334f * sigmoidf_(x);
;                         else if (kind == 1) x = sigmoidf_(x);
;                         o[e] = x; }
;                     u32x4 w; w.x = cvt_pk_bf16(o[0], o[1]); w.y = cvt_pk_bf16(o[2], o[3]); w.z = cvt_pk_bf16(o[4], o[5]); w.w = cvt_pk_bf16(o[6], o[7]);
;                     *(u32x4*)(O + row * 512 + col) = w; } }
.LBB0_938:
	v_mul_f32_e32 v64, 0xbfb8aa3b, v74
	v_exp_f32_e32 v64, v64
	s_nop 0
	v_add_f32_e32 v64, 1.0, v64
	v_rcp_f32_e32 v75, v64
	s_nop 0
	v_fma_f32 v77, -v64, v75, 1.0
	v_fmac_f32_e32 v75, v77, v75
	v_div_fixup_f32 v64, v75, v64, 1.0
	v_mul_f32_e32 v64, 0xbf1b4598, v64
.LBB0_939:
	v_add_f32_e32 v74, v65, v81
	s_and_b64 vcc, exec, s[2:3]
	s_mov_b64 s[68:69], -1
	s_cbranch_vccnz .LBB0_943
	s_and_b64 vcc, exec, s[0:1]
	v_mov_b32_e32 v65, v74
	s_cbranch_vccnz .LBB0_942
	v_mul_f32_e32 v65, 0xbfb8aa3b, v74
	v_exp_f32_e32 v65, v65
	s_nop 0
	v_add_f32_e32 v65, 1.0, v65
	v_rcp_f32_e32 v76, v65
	s_nop 0
	v_fma_f32 v78, -v65, v76, 1.0
	v_fmac_f32_e32 v76, v78, v76
	v_div_fixup_f32 v65, v76, v65, 1.0

; __device__ __forceinline__ unsigned cvt_pk_bf16(float lo, float hi) { const f32x2c v = {lo, hi}; const bf16x2c b = __builtin_convertvector(v, bf16x2c); return __builtin_bit_cast(unsigned, b); }
; __device__ __forceinline__ float sigmoidf_(float x) { return 1.f / (1.f + __expf(-x)); }
;     __device__ __forceinline__ void operator()(const f32x4 (&acc)[2][2][4][2], const Unit& u, int wr, int wc, int fr, int fq) const {
;     ...
;         for (int bj = 0; bj < 2; ++bj) { const int col = (col0 + bj * HALF) & 511;
;             f32x4 b0 = (f32x4){0.f, 0.f, 0.f, 0.f}, b1 = b0;
;             if (kind == 0) { b0 = *(const f32x4*)(w0 + col); b1 = *(const f32x4*)(w0 + col + 4); }
;             else if (kind == 1) { b0 = *(const f32x4*)(a0 + col); b1 = *(const f32x4*)(a0 + col + 4); }
; #pragma unroll
;             for (int ai = 0; ai < 2; ++ai)
; #pragma unroll
;                 for (int m = 0; m < 4; ++m) { const size_t row = (size_t)(row0 + ai * HALF + m * 16);
;                     const f32x4 v0 = acc[ai][bj][m][0] + b0, v1 = acc[ai][bj][m][1] + b1; float o[8];
; #pragma unroll
;                     for (int e = 0; e < 8; ++e) { float x = (e < 4) ? v0[e & 3] : v1[e & 3];
;                         if (kind == 0) x = -0.6065306597126334f * sigmoidf_(x);
;                         else if (kind == 1) x = sigmoidf_(x);
;                         o[e] = x; }
;                     u32x4 w; w.x = cvt_pk_bf16(o[0], o[1]); w.y = cvt_pk_bf16(o[2], o[3]); w.z = cvt_pk_bf16(o[4], o[5]); w.w = cvt_pk_bf16(o[6], o[7]);
;                     *(u32x4*)(O + row * 512 + col) = w; } }
.LBB0_944:
	v_mul_f32_e32 v65, 0xbfb8aa3b, v74
	v_exp_f32_e32 v65, v65
	s_nop 0
	v_add_f32_e32 v65, 1.0, v65
	v_rcp_f32_e32 v75, v65
	s_nop 0
	v_fma_f32 v77, -v65, v75, 1.0
	v_fmac_f32_e32 v75, v77, v75
	v_div_fixup_f32 v65, v75, v65, 1.0
	v_mul_f32_e32 v65, 0xbf1b4598, v65
.LBB0_945:
	v_add_f32_e32 v74, v66, v82
	s_and_b64 vcc, exec, s[2:3]
	s_mov_b64 s[68:69], -1
	s_cbranch_vccnz .LBB0_949
	s_and_b64 vcc, exec, s[0:1]
	v_mov_b32_e32 v66, v74
	s_cbranch_vccnz .LBB0_948
	v_mul_f32_e32 v66, 0xbfb8aa3b, v74
	v_exp_f32_e32 v66, v66
	s_nop 0
	v_add_f32_e32 v66, 1.0, v66
	v_rcp_f32_e32 v76, v66
	s_nop 0
	v_fma_f32 v78, -v66, v76, 1.0
	v_fmac_f32_e32 v76, v78, v76
	v_div_fixup_f32 v66, v76, v66, 1.0

; __device__ __forceinline__ float sigmoidf_(float x) { return 1.f / (1.f + __expf(-x)); }
;     __device__ __forceinline__ void operator()(const f32x4 (&acc)[2][2][4][2], const Unit& u, int wr, int wc, int fr, int fq) const {
;     ...
;                     const f32x4 v0 = acc[ai][bj][m][0] + b0, v1 = acc[ai][bj][m][1] + b1; float o[8];
; #pragma unroll
;                     for (int e = 0; e < 8; ++e) { float x = (e < 4) ? v0[e & 3] : v1[e & 3];
;                         if (kind == 0) x = -0.6065306597126334f * sigmoidf_(x);
;                         else if (kind == 1) x = sigmoidf_(x);
;                         o[e] = x; }
.LBB0_950:
	v_mul_f32_e32 v66, 0xbfb8aa3b, v74
	v_exp_f32_e32 v66, v66
	s_nop 0
	v_add_f32_e32 v66, 1.0, v66
	v_rcp_f32_e32 v75, v66
	s_nop 0
	v_fma_f32 v77, -v66, v75, 1.0
	v_fmac_f32_e32 v75, v77, v75
	v_div_fixup_f32 v66, v75, v66, 1.0
	v_mul_f32_e32 v66, 0xbf1b4598, v66
.LBB0_951:
	v_add_f32_e32 v67, v67, v83
	s_and_b64 vcc, exec, s[2:3]
	s_mov_b64 s[68:69], -1
	s_cbranch_vccnz .LBB0_955
	s_and_b64 vcc, exec, s[0:1]
	v_mov_b32_e32 v74, v67
	s_cbranch_vccnz .LBB0_954
	v_mul_f32_e32 v74, 0xbfb8aa3b, v67
	v_exp_f32_e32 v74, v74
	s_nop 0
	v_add_f32_e32 v74, 1.0, v74
	v_rcp_f32_e32 v76, v74
	s_nop 0
	v_fma_f32 v78, -v74, v76, 1.0
	v_fmac_f32_e32 v76, v78, v76
	v_div_fixup_f32 v74, v76, v74, 1.0

; __device__ __forceinline__ float sigmoidf_(float x) { return 1.f / (1.f + __expf(-x)); }
;     __device__ __forceinline__ void operator()(const f32x4 (&acc)[2][2][4][2], const Unit& u, int wr, int wc, int fr, int fq) const {
;     ...
;                     for (int e = 0; e < 8; ++e) { float x = (e < 4) ? v0[e & 3] : v1[e & 3];
;                         if (kind == 0) x = -0.6065306597126334f * sigmoidf_(x);
;                         else if (kind == 1) x = sigmoidf_(x);
;                         o[e] = x; }
.LBB0_956:
	v_mul_f32_e32 v67, 0xbfb8aa3b, v67
	v_exp_f32_e32 v67, v67
	s_nop 0
	v_add_f32_e32 v67, 1.0, v67
	v_rcp_f32_e32 v75, v67
	s_nop 0
	v_fma_f32 v77, -v67, v75, 1.0
	v_fmac_f32_e32 v75, v77, v75
	v_div_fixup_f32 v67, v75, v67, 1.0
	v_mul_f32_e32 v74, 0xbf1b4598, v67

; __device__ __forceinline__ float sigmoidf_(float x) { return 1.f / (1.f + __expf(-x)); }
;     __device__ __forceinline__ void operator()(const f32x4 (&acc)[2][2][4][2], const Unit& u, int wr, int wc, int fr, int fq) const {
;     ...
;                     const f32x4 v0 = acc[ai][bj][m][0] + b0, v1 = acc[ai][bj][m][1] + b1; float o[8];
; #pragma unroll
;                     for (int e = 0; e < 8; ++e) { float x = (e < 4) ? v0[e & 3] : v1[e & 3];
;                         if (kind == 0) x = -0.6065306597126334f * sigmoidf_(x);
;                         else if (kind == 1) x = sigmoidf_(x);
;                         o[e] = x; }
.LBB0_959:
	s_waitcnt vmcnt(0)
	v_add_f32_e32 v76, v60, v68
	s_and_b64 vcc, exec, s[2:3]
	s_mov_b64 s[4:5], -1
	s_cbranch_vccnz .LBB0_963
	s_and_b64 vcc, exec, s[0:1]
	v_mov_b32_e32 v60, v76
	s_cbranch_vccnz .LBB0_962
	v_mul_f32_e32 v60, 0xbfb8aa3b, v76
	v_exp_f32_e32 v60, v60
	s_nop 0
	v_add_f32_e32 v60, 1.0, v60
	v_rcp_f32_e32 v78, v60
	s_nop 0
	v_fma_f32 v80, -v60, v78, 1.0
	v_fmac_f32_e32 v78, v80, v78
	v_div_fixup_f32 v60, v78, v60, 1.0

; __device__ __forceinline__ float sigmoidf_(float x) { return 1.f / (1.f + __expf(-x)); }
;     __device__ __forceinline__ void operator()(const f32x4 (&acc)[2][2][4][2], const Unit& u, int wr, int wc, int fr, int fq) const {
;     ...
;                     for (int e = 0; e < 8; ++e) { float x = (e < 4) ? v0[e & 3] : v1[e & 3];
;                         if (kind == 0) x = -0.6065306597126334f * sigmoidf_(x);
;                         else if (kind == 1) x = sigmoidf_(x);
;                         o[e] = x; }
.LBB0_964:
	v_mul_f32_e32 v60, 0xbfb8aa3b, v76
	v_exp_f32_e32 v60, v60
	s_nop 0
	v_add_f32_e32 v60, 1.0, v60
	v_rcp_f32_e32 v77, v60
	s_nop 0
	v_fma_f32 v79, -v60, v77, 1.0
	v_fmac_f32_e32 v77, v79, v77
	v_div_fixup_f32 v60, v77, v60, 1.0
	v_mul_f32_e32 v60, 0xbf1b4598, v60
.LBB0_965:
	v_add_f32_e32 v76, v61, v69
	s_and_b64 vcc, exec, s[2:3]
	s_mov_b64 s[4:5], -1
	s_cbranch_vccnz .LBB0_969
	s_and_b64 vcc, exec, s[0:1]
	v_mov_b32_e32 v61, v76
	s_cbranch_vccnz .LBB0_968
	v_mul_f32_e32 v61, 0xbfb8aa3b, v76
	v_exp_f32_e32 v61, v61
	s_nop 0
	v_add_f32_e32 v61, 1.0, v61
	v_rcp_f32_e32 v78, v61
	s_nop 0
	v_fma_f32 v80, -v61, v78, 1.0
	v_fmac_f32_e32 v78, v80, v78
	v_div_fixup_f32 v61, v78, v61, 1.0

; __device__ __forceinline__ float sigmoidf_(float x) { return 1.f / (1.f + __expf(-x)); }
;     __device__ __forceinline__ void operator()(const f32x4 (&acc)[2][2][4][2], const Unit& u, int wr, int wc, int fr, int fq) const {
;     ...
;                     for (int e = 0; e < 8; ++e) { float x = (e < 4) ? v0[e & 3] : v1[e & 3];
;                         if (kind == 0) x = -0.6065306597126334f * sigmoidf_(x);
;                         else if (kind == 1) x = sigmoidf_(x);
;                         o[e] = x; }
.LBB0_970:
	v_mul_f32_e32 v61, 0xbfb8aa3b, v76
	v_exp_f32_e32 v61, v61
	s_nop 0
	v_add_f32_e32 v61, 1.0, v61
	v_rcp_f32_e32 v77, v61
	s_nop 0
	v_fma_f32 v79, -v61, v77, 1.0
	v_fmac_f32_e32 v77, v79, v77
	v_div_fixup_f32 v61, v77, v61, 1.0
	v_mul_f32_e32 v61, 0xbf1b4598, v61
.LBB0_971:
	v_add_f32_e32 v76, v62, v70
	s_and_b64 vcc, exec, s[2:3]
	s_mov_b64 s[4:5], -1
	s_cbranch_vccnz .LBB0_975
	s_and_b64 vcc, exec, s[0:1]
	v_mov_b32_e32 v62, v76
	s_cbranch_vccnz .LBB0_974
	v_mul_f32_e32 v62, 0xbfb8aa3b, v76
	v_exp_f32_e32 v62, v62
	s_nop 0
	v_add_f32_e32 v62, 1.0, v62
	v_rcp_f32_e32 v78, v62
	s_nop 0
	v_fma_f32 v80, -v62, v78, 1.0
	v_fmac_f32_e32 v78, v80, v78
	v_div_fixup_f32 v62, v78, v62, 1.0

; __device__ __forceinline__ float sigmoidf_(float x) { return 1.f / (1.f + __expf(-x)); }
;     __device__ __forceinline__ void operator()(const f32x4 (&acc)[2][2][4][2], const Unit& u, int wr, int wc, int fr, int fq) const {
;     ...
;                     for (int e = 0; e < 8; ++e) { float x = (e < 4) ? v0[e & 3] : v1[e & 3];
;                         if (kind == 0) x = -0.6065306597126334f * sigmoidf_(x);
;                         else if (kind == 1) x = sigmoidf_(x);
;                         o[e] = x; }
.LBB0_976:
	v_mul_f32_e32 v62, 0xbfb8aa3b, v76
	v_exp_f32_e32 v62, v62
	s_nop 0
	v_add_f32_e32 v62, 1.0, v62
	v_rcp_f32_e32 v77, v62
	s_nop 0
	v_fma_f32 v79, -v62, v77, 1.0
	v_fmac_f32_e32 v77, v79, v77
	v_div_fixup_f32 v62, v77, v62, 1.0
	v_mul_f32_e32 v62, 0xbf1b4598, v62
.LBB0_977:
	v_add_f32_e32 v76, v63, v71
	s_and_b64 vcc, exec, s[2:3]
	s_mov_b64 s[4:5], -1
	s_cbranch_vccnz .LBB0_981
	s_and_b64 vcc, exec, s[0:1]
	v_mov_b32_e32 v63, v76
	s_cbranch_vccnz .LBB0_980
	v_mul_f32_e32 v63, 0xbfb8aa3b, v76
	v_exp_f32_e32 v63, v63
	s_nop 0
	v_add_f32_e32 v63, 1.0, v63
	v_rcp_f32_e32 v78, v63
	s_nop 0
	v_fma_f32 v80, -v63, v78, 1.0
	v_fmac_f32_e32 v78, v80, v78
	v_div_fixup_f32 v63, v78, v63, 1.0

; __device__ __forceinline__ float sigmoidf_(float x) { return 1.f / (1.f + __expf(-x)); }
;     __device__ __forceinline__ void operator()(const f32x4 (&acc)[2][2][4][2], const Unit& u, int wr, int wc, int fr, int fq) const {
;     ...
;                     for (int e = 0; e < 8; ++e) { float x = (e < 4) ? v0[e & 3] : v1[e & 3];
;                         if (kind == 0) x = -0.6065306597126334f * sigmoidf_(x);
;                         else if (kind == 1) x = sigmoidf_(x);
;                         o[e] = x; }
.LBB0_982:
	v_mul_f32_e32 v63, 0xbfb8aa3b, v76
	v_exp_f32_e32 v63, v63
	s_nop 0
	v_add_f32_e32 v63, 1.0, v63
	v_rcp_f32_e32 v77, v63
	s_nop 0
	v_fma_f32 v79, -v63, v77, 1.0
	v_fmac_f32_e32 v77, v79, v77
	v_div_fixup_f32 v63, v77, v63, 1.0
	v_mul_f32_e32 v63, 0xbf1b4598, v63
.LBB0_983:
	v_add_f32_e32 v76, v56, v64
	s_and_b64 vcc, exec, s[2:3]
	s_mov_b64 s[4:5], -1
	s_cbranch_vccnz .LBB0_987
	s_and_b64 vcc, exec, s[0:1]
	v_mov_b32_e32 v56, v76
	s_cbranch_vccnz .LBB0_986
	v_mul_f32_e32 v56, 0xbfb8aa3b, v76
	v_exp_f32_e32 v56, v56
	s_nop 0
	v_add_f32_e32 v56, 1.0, v56
	v_rcp_f32_e32 v78, v56
	s_nop 0
	v_fma_f32 v80, -v56, v78, 1.0
	v_fmac_f32_e32 v78, v80, v78
	v_div_fixup_f32 v56, v78, v56, 1.0

; __device__ __forceinline__ float sigmoidf_(float x) { return 1.f / (1.f + __expf(-x)); }
;     __device__ __forceinline__ void operator()(const f32x4 (&acc)[2][2][4][2], const Unit& u, int wr, int wc, int fr, int fq) const {
;     ...
;                     for (int e = 0; e < 8; ++e) { float x = (e < 4) ? v0[e & 3] : v1[e & 3];
;                         if (kind == 0) x = -0.6065306597126334f * sigmoidf_(x);
;                         else if (kind == 1) x = sigmoidf_(x);
;                         o[e] = x; }
.LBB0_988:
	v_mul_f32_e32 v56, 0xbfb8aa3b, v76
	v_exp_f32_e32 v56, v56
	s_nop 0
	v_add_f32_e32 v56, 1.0, v56
	v_rcp_f32_e32 v77, v56
	s_nop 0
	v_fma_f32 v79, -v56, v77, 1.0
	v_fmac_f32_e32 v77, v79, v77
	v_div_fixup_f32 v56, v77, v56, 1.0
	v_mul_f32_e32 v56, 0xbf1b4598, v56
.LBB0_989:
	v_add_f32_e32 v76, v57, v65
	s_and_b64 vcc, exec, s[2:3]
	s_mov_b64 s[4:5], -1
	s_cbranch_vccnz .LBB0_993
	s_and_b64 vcc, exec, s[0:1]
	v_mov_b32_e32 v57, v76
	s_cbranch_vccnz .LBB0_992
	v_mul_f32_e32 v57, 0xbfb8aa3b, v76
	v_exp_f32_e32 v57, v57
	s_nop 0
	v_add_f32_e32 v57, 1.0, v57
	v_rcp_f32_e32 v78, v57
	s_nop 0
	v_fma_f32 v80, -v57, v78, 1.0
	v_fmac_f32_e32 v78, v80, v78
	v_div_fixup_f32 v57, v78, v57, 1.0

; __device__ __forceinline__ float sigmoidf_(float x) { return 1.f / (1.f + __expf(-x)); }
;     __device__ __forceinline__ void operator()(const f32x4 (&acc)[2][2][4][2], const Unit& u, int wr, int wc, int fr, int fq) const {
;     ...
;                     for (int e = 0; e < 8; ++e) { float x = (e < 4) ? v0[e & 3] : v1[e & 3];
;                         if (kind == 0) x = -0.6065306597126334f * sigmoidf_(x);
;                         else if (kind == 1) x = sigmoidf_(x);
;                         o[e] = x; }
.LBB0_994:
	v_mul_f32_e32 v57, 0xbfb8aa3b, v76
	v_exp_f32_e32 v57, v57
	s_nop 0
	v_add_f32_e32 v57, 1.0, v57
	v_rcp_f32_e32 v77, v57
	s_nop 0
	v_fma_f32 v79, -v57, v77, 1.0
	v_fmac_f32_e32 v77, v79, v77
	v_div_fixup_f32 v57, v77, v57, 1.0
	v_mul_f32_e32 v57, 0xbf1b4598, v57
.LBB0_995:
	v_add_f32_e32 v76, v58, v66
	s_and_b64 vcc, exec, s[2:3]
	s_mov_b64 s[4:5], -1
	s_cbranch_vccnz .LBB0_999
	s_and_b64 vcc, exec, s[0:1]
	v_mov_b32_e32 v58, v76
	s_cbranch_vccnz .LBB0_998
	v_mul_f32_e32 v58, 0xbfb8aa3b, v76
	v_exp_f32_e32 v58, v58
	s_nop 0
	v_add_f32_e32 v58, 1.0, v58
	v_rcp_f32_e32 v78, v58
	s_nop 0
	v_fma_f32 v80, -v58, v78, 1.0
	v_fmac_f32_e32 v78, v80, v78
	v_div_fixup_f32 v58, v78, v58, 1.0

; __device__ __forceinline__ float sigmoidf_(float x) { return 1.f / (1.f + __expf(-x)); }
;     __device__ __forceinline__ void operator()(const f32x4 (&acc)[2][2][4][2], const Unit& u, int wr, int wc, int fr, int fq) const {
;     ...
;                     for (int e = 0; e < 8; ++e) { float x = (e < 4) ? v0[e & 3] : v1[e & 3];
;                         if (kind == 0) x = -0.6065306597126334f * sigmoidf_(x);
;                         else if (kind == 1) x = sigmoidf_(x);
;                         o[e] = x; }
.LBB0_1000:
	v_mul_f32_e32 v58, 0xbfb8aa3b, v76
	v_exp_f32_e32 v58, v58
	s_nop 0
	v_add_f32_e32 v58, 1.0, v58
	v_rcp_f32_e32 v77, v58
	s_nop 0
	v_fma_f32 v79, -v58, v77, 1.0
	v_fmac_f32_e32 v77, v79, v77
	v_div_fixup_f32 v58, v77, v58, 1.0
	v_mul_f32_e32 v58, 0xbf1b4598, v58
.LBB0_1001:
	v_add_f32_e32 v59, v59, v67
	s_and_b64 vcc, exec, s[2:3]
	s_mov_b64 s[4:5], -1
	s_cbranch_vccnz .LBB0_1005
	s_and_b64 vcc, exec, s[0:1]
	v_mov_b32_e32 v76, v59
	s_cbranch_vccnz .LBB0_1004
	v_mul_f32_e32 v76, 0xbfb8aa3b, v59
	v_exp_f32_e32 v76, v76
	s_nop 0
	v_add_f32_e32 v76, 1.0, v76
	v_rcp_f32_e32 v78, v76
	s_nop 0
	v_fma_f32 v80, -v76, v78, 1.0
	v_fmac_f32_e32 v78, v80, v78
	v_div_fixup_f32 v76, v78, v76, 1.0

; __device__ __forceinline__ unsigned cvt_pk_bf16(float lo, float hi) { const f32x2c v = {lo, hi}; const bf16x2c b = __builtin_convertvector(v, bf16x2c); return __builtin_bit_cast(unsigned, b); }
; __device__ __forceinline__ float sigmoidf_(float x) { return 1.f / (1.f + __expf(-x)); }
;     __device__ __forceinline__ void operator()(const f32x4 (&acc)[2][2][4][2], const Unit& u, int wr, int wc, int fr, int fq) const {
;     ...
;                     const f32x4 v0 = acc[ai][bj][m][0] + b0, v1 = acc[ai][bj][m][1] + b1; float o[8];
; #pragma unroll
;                     for (int e = 0; e < 8; ++e) { float x = (e < 4) ? v0[e & 3] : v1[e & 3];
;                         if (kind == 0) x = -0.6065306597126334f * sigmoidf_(x);
;                         else if (kind == 1) x = sigmoidf_(x);
;                         o[e] = x; }
;                     u32x4 w; w.x = cvt_pk_bf16(o[0], o[1]); w.y = cvt_pk_bf16(o[2], o[3]); w.z = cvt_pk_bf16(o[4], o[5]); w.w = cvt_pk_bf16(o[6], o[7]);
;                     *(u32x4*)(O + row * 512 + col) = w; } }
.LBB0_1006:
	v_mul_f32_e32 v59, 0xbfb8aa3b, v59
	v_exp_f32_e32 v59, v59
	s_nop 0
	v_add_f32_e32 v59, 1.0, v59
	v_rcp_f32_e32 v77, v59
	s_nop 0
	v_fma_f32 v79, -v59, v77, 1.0
	v_fmac_f32_e32 v77, v79, v77
	v_div_fixup_f32 v59, v77, v59, 1.0
	v_mul_f32_e32 v76, 0xbf1b4598, v59
.LBB0_1007:
	v_cvt_pk_bf16_f32 v60, v60, v61
	v_cvt_pk_bf16_f32 v61, v62, v63
	v_cvt_pk_bf16_f32 v62, v56, v57
	v_cvt_pk_bf16_f32 v63, v58, v76
	v_add_f32_e32 v56, v52, v68
	s_and_b64 vcc, exec, s[2:3]
	s_mov_b64 s[4:5], -1
	global_store_dwordx4 v[128:129], v[60:63], off offset:256
	s_cbranch_vccnz .LBB0_1011
	s_and_b64 vcc, exec, s[0:1]
	v_mov_b32_e32 v52, v56
	s_cbranch_vccnz .LBB0_1010
	v_mul_f32_e32 v52, 0xbfb8aa3b, v56
	v_exp_f32_e32 v52, v52
	s_nop 0
	v_add_f32_e32 v52, 1.0, v52
	v_rcp_f32_e32 v58, v52
	s_nop 0
	v_fma_f32 v60, -v52, v58, 1.0
	v_fmac_f32_e32 v58, v60, v58
	v_div_fixup_f32 v52, v58, v52, 1.0

; __device__ __forceinline__ float sigmoidf_(float x) { return 1.f / (1.f + __expf(-x)); }
;     __device__ __forceinline__ void operator()(const f32x4 (&acc)[2][2][4][2], const Unit& u, int wr, int wc, int fr, int fq) const {
;     ...
;                     for (int e = 0; e < 8; ++e) { float x = (e < 4) ? v0[e & 3] : v1[e & 3];
;                         if (kind == 0) x = -0.6065306597126334f * sigmoidf_(x);
;                         else if (kind == 1) x = sigmoidf_(x);
;                         o[e] = x; }
.LBB0_1012:
	v_mul_f32_e32 v52, 0xbfb8aa3b, v56
	v_exp_f32_e32 v52, v52
	s_nop 0
	v_add_f32_e32 v52, 1.0, v52
	v_rcp_f32_e32 v57, v52
	s_nop 0
	v_fma_f32 v59, -v52, v57, 1.0
	v_fmac_f32_e32 v57, v59, v57
	v_div_fixup_f32 v52, v57, v52, 1.0
	v_mul_f32_e32 v52, 0xbf1b4598, v52
.LBB0_1013:
	v_add_f32_e32 v56, v53, v69
	s_and_b64 vcc, exec, s[2:3]
	s_mov_b64 s[4:5], -1
	s_cbranch_vccnz .LBB0_1017
	s_and_b64 vcc, exec, s[0:1]
	v_mov_b32_e32 v53, v56
	s_cbranch_vccnz .LBB0_1016
	v_mul_f32_e32 v53, 0xbfb8aa3b, v56
	v_exp_f32_e32 v53, v53
	s_nop 0
	v_add_f32_e32 v53, 1.0, v53
	v_rcp_f32_e32 v58, v53
	s_nop 0
	v_fma_f32 v60, -v53, v58, 1.0
	v_fmac_f32_e32 v58, v60, v58
	v_div_fixup_f32 v53, v58, v53, 1.0

; __device__ __forceinline__ float sigmoidf_(float x) { return 1.f / (1.f + __expf(-x)); }
;     __device__ __forceinline__ void operator()(const f32x4 (&acc)[2][2][4][2], const Unit& u, int wr, int wc, int fr, int fq) const {
;     ...
;                     for (int e = 0; e < 8; ++e) { float x = (e < 4) ? v0[e & 3] : v1[e & 3];
;                         if (kind == 0) x = -0.6065306597126334f * sigmoidf_(x);
;                         else if (kind == 1) x = sigmoidf_(x);
;                         o[e] = x; }
.LBB0_1018:
	v_mul_f32_e32 v53, 0xbfb8aa3b, v56
	v_exp_f32_e32 v53, v53
	s_nop 0
	v_add_f32_e32 v53, 1.0, v53
	v_rcp_f32_e32 v57, v53
	s_nop 0
	v_fma_f32 v59, -v53, v57, 1.0
	v_fmac_f32_e32 v57, v59, v57
	v_div_fixup_f32 v53, v57, v53, 1.0
	v_mul_f32_e32 v53, 0xbf1b4598, v53
.LBB0_1019:
	v_add_f32_e32 v56, v54, v70
	s_and_b64 vcc, exec, s[2:3]
	s_mov_b64 s[4:5], -1
	s_cbranch_vccnz .LBB0_1023
	s_and_b64 vcc, exec, s[0:1]
	v_mov_b32_e32 v54, v56
	s_cbranch_vccnz .LBB0_1022
	v_mul_f32_e32 v54, 0xbfb8aa3b, v56
	v_exp_f32_e32 v54, v54
	s_nop 0
	v_add_f32_e32 v54, 1.0, v54
	v_rcp_f32_e32 v58, v54
	s_nop 0
	v_fma_f32 v60, -v54, v58, 1.0
	v_fmac_f32_e32 v58, v60, v58
	v_div_fixup_f32 v54, v58, v54, 1.0

; __device__ __forceinline__ float sigmoidf_(float x) { return 1.f / (1.f + __expf(-x)); }
;     __device__ __forceinline__ void operator()(const f32x4 (&acc)[2][2][4][2], const Unit& u, int wr, int wc, int fr, int fq) const {
;     ...
;                     for (int e = 0; e < 8; ++e) { float x = (e < 4) ? v0[e & 3] : v1[e & 3];
;                         if (kind == 0) x = -0.6065306597126334f * sigmoidf_(x);
;                         else if (kind == 1) x = sigmoidf_(x);
;                         o[e] = x; }
.LBB0_1024:
	v_mul_f32_e32 v54, 0xbfb8aa3b, v56
	v_exp_f32_e32 v54, v54
	s_nop 0
	v_add_f32_e32 v54, 1.0, v54
	v_rcp_f32_e32 v57, v54
	s_nop 0
	v_fma_f32 v59, -v54, v57, 1.0
	v_fmac_f32_e32 v57, v59, v57
	v_div_fixup_f32 v54, v57, v54, 1.0
	v_mul_f32_e32 v54, 0xbf1b4598, v54
.LBB0_1025:
	v_add_f32_e32 v56, v55, v71
	s_and_b64 vcc, exec, s[2:3]
	s_mov_b64 s[4:5], -1
	s_cbranch_vccnz .LBB0_1029
	s_and_b64 vcc, exec, s[0:1]
	v_mov_b32_e32 v55, v56
	s_cbranch_vccnz .LBB0_1028
	v_mul_f32_e32 v55, 0xbfb8aa3b, v56
	v_exp_f32_e32 v55, v55
	s_nop 0
	v_add_f32_e32 v55, 1.0, v55
	v_rcp_f32_e32 v58, v55
	s_nop 0
	v_fma_f32 v60, -v55, v58, 1.0
	v_fmac_f32_e32 v58, v60, v58
	v_div_fixup_f32 v55, v58, v55, 1.0

; __device__ __forceinline__ float sigmoidf_(float x) { return 1.f / (1.f + __expf(-x)); }
;     __device__ __forceinline__ void operator()(const f32x4 (&acc)[2][2][4][2], const Unit& u, int wr, int wc, int fr, int fq) const {
;     ...
;                     for (int e = 0; e < 8; ++e) { float x = (e < 4) ? v0[e & 3] : v1[e & 3];
;                         if (kind == 0) x = -0.6065306597126334f * sigmoidf_(x);
;                         else if (kind == 1) x = sigmoidf_(x);
;                         o[e] = x; }
.LBB0_1030:
	v_mul_f32_e32 v55, 0xbfb8aa3b, v56
	v_exp_f32_e32 v55, v55
	s_nop 0
	v_add_f32_e32 v55, 1.0, v55
	v_rcp_f32_e32 v57, v55
	s_nop 0
	v_fma_f32 v59, -v55, v57, 1.0
	v_fmac_f32_e32 v57, v59, v57
	v_div_fixup_f32 v55, v57, v55, 1.0
	v_mul_f32_e32 v55, 0xbf1b4598, v55
.LBB0_1031:
	v_add_f32_e32 v56, v48, v64
	s_and_b64 vcc, exec, s[2:3]
	s_mov_b64 s[4:5], -1
	s_cbranch_vccnz .LBB0_1035
	s_and_b64 vcc, exec, s[0:1]
	v_mov_b32_e32 v48, v56
	s_cbranch_vccnz .LBB0_1034
	v_mul_f32_e32 v48, 0xbfb8aa3b, v56
	v_exp_f32_e32 v48, v48
	s_nop 0
	v_add_f32_e32 v48, 1.0, v48
	v_rcp_f32_e32 v58, v48
	s_nop 0
	v_fma_f32 v60, -v48, v58, 1.0
	v_fmac_f32_e32 v58, v60, v58
	v_div_fixup_f32 v48, v58, v48, 1.0

; __device__ __forceinline__ float sigmoidf_(float x) { return 1.f / (1.f + __expf(-x)); }
;     __device__ __forceinline__ void operator()(const f32x4 (&acc)[2][2][4][2], const Unit& u, int wr, int wc, int fr, int fq) const {
;     ...
;                     for (int e = 0; e < 8; ++e) { float x = (e < 4) ? v0[e & 3] : v1[e & 3];
;                         if (kind == 0) x = -0.6065306597126334f * sigmoidf_(x);
;                         else if (kind == 1) x = sigmoidf_(x);
;                         o[e] = x; }
.LBB0_1036:
	v_mul_f32_e32 v48, 0xbfb8aa3b, v56
	v_exp_f32_e32 v48, v48
	s_nop 0
	v_add_f32_e32 v48, 1.0, v48
	v_rcp_f32_e32 v57, v48
	s_nop 0
	v_fma_f32 v59, -v48, v57, 1.0
	v_fmac_f32_e32 v57, v59, v57
	v_div_fixup_f32 v48, v57, v48, 1.0
	v_mul_f32_e32 v48, 0xbf1b4598, v48
.LBB0_1037:
	v_add_f32_e32 v56, v49, v65
	s_and_b64 vcc, exec, s[2:3]
	s_mov_b64 s[4:5], -1
	s_cbranch_vccnz .LBB0_1041
	s_and_b64 vcc, exec, s[0:1]
	v_mov_b32_e32 v49, v56
	s_cbranch_vccnz .LBB0_1040
	v_mul_f32_e32 v49, 0xbfb8aa3b, v56
	v_exp_f32_e32 v49, v49
	s_nop 0
	v_add_f32_e32 v49, 1.0, v49
	v_rcp_f32_e32 v58, v49
	s_nop 0
	v_fma_f32 v60, -v49, v58, 1.0
	v_fmac_f32_e32 v58, v60, v58
	v_div_fixup_f32 v49, v58, v49, 1.0

; __device__ __forceinline__ float sigmoidf_(float x) { return 1.f / (1.f + __expf(-x)); }
;     __device__ __forceinline__ void operator()(const f32x4 (&acc)[2][2][4][2], const Unit& u, int wr, int wc, int fr, int fq) const {
;     ...
;                     for (int e = 0; e < 8; ++e) { float x = (e < 4) ? v0[e & 3] : v1[e & 3];
;                         if (kind == 0) x = -0.6065306597126334f * sigmoidf_(x);
;                         else if (kind == 1) x = sigmoidf_(x);
;                         o[e] = x; }
.LBB0_1042:
	v_mul_f32_e32 v49, 0xbfb8aa3b, v56
	v_exp_f32_e32 v49, v49
	s_nop 0
	v_add_f32_e32 v49, 1.0, v49
	v_rcp_f32_e32 v57, v49
	s_nop 0
	v_fma_f32 v59, -v49, v57, 1.0
	v_fmac_f32_e32 v57, v59, v57
	v_div_fixup_f32 v49, v57, v49, 1.0
	v_mul_f32_e32 v49, 0xbf1b4598, v49
.LBB0_1043:
	v_add_f32_e32 v56, v50, v66
	s_and_b64 vcc, exec, s[2:3]
	s_mov_b64 s[4:5], -1
	s_cbranch_vccnz .LBB0_1047
	s_and_b64 vcc, exec, s[0:1]
	v_mov_b32_e32 v50, v56
	s_cbranch_vccnz .LBB0_1046
	v_mul_f32_e32 v50, 0xbfb8aa3b, v56
	v_exp_f32_e32 v50, v50
	s_nop 0
	v_add_f32_e32 v50, 1.0, v50
	v_rcp_f32_e32 v58, v50
	s_nop 0
	v_fma_f32 v60, -v50, v58, 1.0
	v_fmac_f32_e32 v58, v60, v58
	v_div_fixup_f32 v50, v58, v50, 1.0

; __device__ __forceinline__ float sigmoidf_(float x) { return 1.f / (1.f + __expf(-x)); }
;     __device__ __forceinline__ void operator()(const f32x4 (&acc)[2][2][4][2], const Unit& u, int wr, int wc, int fr, int fq) const {
;     ...
;                     for (int e = 0; e < 8; ++e) { float x = (e < 4) ? v0[e & 3] : v1[e & 3];
;                         if (kind == 0) x = -0.6065306597126334f * sigmoidf_(x);
;                         else if (kind == 1) x = sigmoidf_(x);
;                         o[e] = x; }
.LBB0_1048:
	v_mul_f32_e32 v50, 0xbfb8aa3b, v56
	v_exp_f32_e32 v50, v50
	s_nop 0
	v_add_f32_e32 v50, 1.0, v50
	v_rcp_f32_e32 v57, v50
	s_nop 0
	v_fma_f32 v59, -v50, v57, 1.0
	v_fmac_f32_e32 v57, v59, v57
	v_div_fixup_f32 v50, v57, v50, 1.0
	v_mul_f32_e32 v50, 0xbf1b4598, v50
.LBB0_1049:
	v_add_f32_e32 v51, v51, v67
	s_and_b64 vcc, exec, s[2:3]
	s_mov_b64 s[4:5], -1
	s_cbranch_vccnz .LBB0_1053
	s_and_b64 vcc, exec, s[0:1]
	v_mov_b32_e32 v56, v51
	s_cbranch_vccnz .LBB0_1052
	v_mul_f32_e32 v56, 0xbfb8aa3b, v51
	v_exp_f32_e32 v56, v56
	s_nop 0
	v_add_f32_e32 v56, 1.0, v56
	v_rcp_f32_e32 v58, v56
	s_nop 0
	v_fma_f32 v60, -v56, v58, 1.0
	v_fmac_f32_e32 v58, v60, v58
	v_div_fixup_f32 v56, v58, v56, 1.0

; __device__ __forceinline__ unsigned cvt_pk_bf16(float lo, float hi) { const f32x2c v = {lo, hi}; const bf16x2c b = __builtin_convertvector(v, bf16x2c); return __builtin_bit_cast(unsigned, b); }
; __device__ __forceinline__ float sigmoidf_(float x) { return 1.f / (1.f + __expf(-x)); }
;     __device__ __forceinline__ void operator()(const f32x4 (&acc)[2][2][4][2], const Unit& u, int wr, int wc, int fr, int fq) const {
;     ...
;                     const f32x4 v0 = acc[ai][bj][m][0] + b0, v1 = acc[ai][bj][m][1] + b1; float o[8];
; #pragma unroll
;                     for (int e = 0; e < 8; ++e) { float x = (e < 4) ? v0[e & 3] : v1[e & 3];
;                         if (kind == 0) x = -0.6065306597126334f * sigmoidf_(x);
;                         else if (kind == 1) x = sigmoidf_(x);
;                         o[e] = x; }
;                     u32x4 w; w.x = cvt_pk_bf16(o[0], o[1]); w.y = cvt_pk_bf16(o[2], o[3]); w.z = cvt_pk_bf16(o[4], o[5]); w.w = cvt_pk_bf16(o[6], o[7]);
;                     *(u32x4*)(O + row * 512 + col) = w; } }
.LBB0_1054:
	v_mul_f32_e32 v51, 0xbfb8aa3b, v51
	v_exp_f32_e32 v51, v51
	s_nop 0
	v_add_f32_e32 v51, 1.0, v51
	v_rcp_f32_e32 v57, v51
	s_nop 0
	v_fma_f32 v59, -v51, v57, 1.0
	v_fmac_f32_e32 v57, v59, v57
	v_div_fixup_f32 v51, v57, v51, 1.0
	v_mul_f32_e32 v56, 0xbf1b4598, v51
.LBB0_1055:
	v_cvt_pk_bf16_f32 v52, v52, v53
	v_cvt_pk_bf16_f32 v53, v54, v55
	v_cvt_pk_bf16_f32 v54, v48, v49
	v_cvt_pk_bf16_f32 v55, v50, v56
	v_add_f32_e32 v48, v44, v68
	s_and_b64 vcc, exec, s[2:3]
	s_mov_b64 s[4:5], -1
	global_store_dwordx4 v[120:121], v[52:55], off offset:256
	s_cbranch_vccnz .LBB0_1059
	s_and_b64 vcc, exec, s[0:1]
	v_mov_b32_e32 v44, v48
	s_cbranch_vccnz .LBB0_1058
	v_mul_f32_e32 v44, 0xbfb8aa3b, v48
	v_exp_f32_e32 v44, v44
	s_nop 0
	v_add_f32_e32 v44, 1.0, v44
	v_rcp_f32_e32 v50, v44
	s_nop 0
	v_fma_f32 v52, -v44, v50, 1.0
	v_fmac_f32_e32 v50, v52, v50
	v_div_fixup_f32 v44, v50, v44, 1.0

; __device__ __forceinline__ float sigmoidf_(float x) { return 1.f / (1.f + __expf(-x)); }
;     __device__ __forceinline__ void operator()(const f32x4 (&acc)[2][2][4][2], const Unit& u, int wr, int wc, int fr, int fq) const {
;     ...
;                     for (int e = 0; e < 8; ++e) { float x = (e < 4) ? v0[e & 3] : v1[e & 3];
;                         if (kind == 0) x = -0.6065306597126334f * sigmoidf_(x);
;                         else if (kind == 1) x = sigmoidf_(x);
;                         o[e] = x; }
.LBB0_1060:
	v_mul_f32_e32 v44, 0xbfb8aa3b, v48
	v_exp_f32_e32 v44, v44
	s_nop 0
	v_add_f32_e32 v44, 1.0, v44
	v_rcp_f32_e32 v49, v44
	s_nop 0
	v_fma_f32 v51, -v44, v49, 1.0
	v_fmac_f32_e32 v49, v51, v49
	v_div_fixup_f32 v44, v49, v44, 1.0
	v_mul_f32_e32 v44, 0xbf1b4598, v44
.LBB0_1061:
	v_add_f32_e32 v48, v45, v69
	s_and_b64 vcc, exec, s[2:3]
	s_mov_b64 s[4:5], -1
	s_cbranch_vccnz .LBB0_1065
	s_and_b64 vcc, exec, s[0:1]
	v_mov_b32_e32 v45, v48
	s_cbranch_vccnz .LBB0_1064
	v_mul_f32_e32 v45, 0xbfb8aa3b, v48
	v_exp_f32_e32 v45, v45
	s_nop 0
	v_add_f32_e32 v45, 1.0, v45
	v_rcp_f32_e32 v50, v45
	s_nop 0
	v_fma_f32 v52, -v45, v50, 1.0
	v_fmac_f32_e32 v50, v52, v50
	v_div_fixup_f32 v45, v50, v45, 1.0

; __device__ __forceinline__ float sigmoidf_(float x) { return 1.f / (1.f + __expf(-x)); }
;     __device__ __forceinline__ void operator()(const f32x4 (&acc)[2][2][4][2], const Unit& u, int wr, int wc, int fr, int fq) const {
;     ...
;                     for (int e = 0; e < 8; ++e) { float x = (e < 4) ? v0[e & 3] : v1[e & 3];
;                         if (kind == 0) x = -0.6065306597126334f * sigmoidf_(x);
;                         else if (kind == 1) x = sigmoidf_(x);
;                         o[e] = x; }
.LBB0_1066:
	v_mul_f32_e32 v45, 0xbfb8aa3b, v48
	v_exp_f32_e32 v45, v45
	s_nop 0
	v_add_f32_e32 v45, 1.0, v45
	v_rcp_f32_e32 v49, v45
	s_nop 0
	v_fma_f32 v51, -v45, v49, 1.0
	v_fmac_f32_e32 v49, v51, v49
	v_div_fixup_f32 v45, v49, v45, 1.0
	v_mul_f32_e32 v45, 0xbf1b4598, v45
.LBB0_1067:
	v_add_f32_e32 v48, v46, v70
	s_and_b64 vcc, exec, s[2:3]
	s_mov_b64 s[4:5], -1
	s_cbranch_vccnz .LBB0_1071
	s_and_b64 vcc, exec, s[0:1]
	v_mov_b32_e32 v46, v48
	s_cbranch_vccnz .LBB0_1070
	v_mul_f32_e32 v46, 0xbfb8aa3b, v48
	v_exp_f32_e32 v46, v46
	s_nop 0
	v_add_f32_e32 v46, 1.0, v46
	v_rcp_f32_e32 v50, v46
	s_nop 0
	v_fma_f32 v52, -v46, v50, 1.0
	v_fmac_f32_e32 v50, v52, v50
	v_div_fixup_f32 v46, v50, v46, 1.0

; __device__ __forceinline__ float sigmoidf_(float x) { return 1.f / (1.f + __expf(-x)); }
;     __device__ __forceinline__ void operator()(const f32x4 (&acc)[2][2][4][2], const Unit& u, int wr, int wc, int fr, int fq) const {
;     ...
;                     for (int e = 0; e < 8; ++e) { float x = (e < 4) ? v0[e & 3] : v1[e & 3];
;                         if (kind == 0) x = -0.6065306597126334f * sigmoidf_(x);
;                         else if (kind == 1) x = sigmoidf_(x);
;                         o[e] = x; }
.LBB0_1072:
	v_mul_f32_e32 v46, 0xbfb8aa3b, v48
	v_exp_f32_e32 v46, v46
	s_nop 0
	v_add_f32_e32 v46, 1.0, v46
	v_rcp_f32_e32 v49, v46
	s_nop 0
	v_fma_f32 v51, -v46, v49, 1.0
	v_fmac_f32_e32 v49, v51, v49
	v_div_fixup_f32 v46, v49, v46, 1.0
	v_mul_f32_e32 v46, 0xbf1b4598, v46
.LBB0_1073:
	v_add_f32_e32 v48, v47, v71
	s_and_b64 vcc, exec, s[2:3]
	s_mov_b64 s[4:5], -1
	s_cbranch_vccnz .LBB0_1077
	s_and_b64 vcc, exec, s[0:1]
	v_mov_b32_e32 v47, v48
	s_cbranch_vccnz .LBB0_1076
	v_mul_f32_e32 v47, 0xbfb8aa3b, v48
	v_exp_f32_e32 v47, v47
	s_nop 0
	v_add_f32_e32 v47, 1.0, v47
	v_rcp_f32_e32 v50, v47
	s_nop 0
	v_fma_f32 v52, -v47, v50, 1.0
	v_fmac_f32_e32 v50, v52, v50
	v_div_fixup_f32 v47, v50, v47, 1.0

; __device__ __forceinline__ float sigmoidf_(float x) { return 1.f / (1.f + __expf(-x)); }
;     __device__ __forceinline__ void operator()(const f32x4 (&acc)[2][2][4][2], const Unit& u, int wr, int wc, int fr, int fq) const {
;     ...
;                     for (int e = 0; e < 8; ++e) { float x = (e < 4) ? v0[e & 3] : v1[e & 3];
;                         if (kind == 0) x = -0.6065306597126334f * sigmoidf_(x);
;                         else if (kind == 1) x = sigmoidf_(x);
;                         o[e] = x; }
.LBB0_1078:
	v_mul_f32_e32 v47, 0xbfb8aa3b, v48
	v_exp_f32_e32 v47, v47
	s_nop 0
	v_add_f32_e32 v47, 1.0, v47
	v_rcp_f32_e32 v49, v47
	s_nop 0
	v_fma_f32 v51, -v47, v49, 1.0
	v_fmac_f32_e32 v49, v51, v49
	v_div_fixup_f32 v47, v49, v47, 1.0
	v_mul_f32_e32 v47, 0xbf1b4598, v47
.LBB0_1079:
	v_add_f32_e32 v48, v40, v64
	s_and_b64 vcc, exec, s[2:3]
	s_mov_b64 s[4:5], -1
	s_cbranch_vccnz .LBB0_1083
	s_and_b64 vcc, exec, s[0:1]
	v_mov_b32_e32 v40, v48
	s_cbranch_vccnz .LBB0_1082
	v_mul_f32_e32 v40, 0xbfb8aa3b, v48
	v_exp_f32_e32 v40, v40
	s_nop 0
	v_add_f32_e32 v40, 1.0, v40
	v_rcp_f32_e32 v50, v40
	s_nop 0
	v_fma_f32 v52, -v40, v50, 1.0
	v_fmac_f32_e32 v50, v52, v50
	v_div_fixup_f32 v40, v50, v40, 1.0

; __device__ __forceinline__ float sigmoidf_(float x) { return 1.f / (1.f + __expf(-x)); }
;     __device__ __forceinline__ void operator()(const f32x4 (&acc)[2][2][4][2], const Unit& u, int wr, int wc, int fr, int fq) const {
;     ...
;                     for (int e = 0; e < 8; ++e) { float x = (e < 4) ? v0[e & 3] : v1[e & 3];
;                         if (kind == 0) x = -0.6065306597126334f * sigmoidf_(x);
;                         else if (kind == 1) x = sigmoidf_(x);
;                         o[e] = x; }
.LBB0_1084:
	v_mul_f32_e32 v40, 0xbfb8aa3b, v48
	v_exp_f32_e32 v40, v40
	s_nop 0
	v_add_f32_e32 v40, 1.0, v40
	v_rcp_f32_e32 v49, v40
	s_nop 0
	v_fma_f32 v51, -v40, v49, 1.0
	v_fmac_f32_e32 v49, v51, v49
	v_div_fixup_f32 v40, v49, v40, 1.0
	v_mul_f32_e32 v40, 0xbf1b4598, v40
.LBB0_1085:
	v_add_f32_e32 v48, v41, v65
	s_and_b64 vcc, exec, s[2:3]
	s_mov_b64 s[4:5], -1
	s_cbranch_vccnz .LBB0_1089
	s_and_b64 vcc, exec, s[0:1]
	v_mov_b32_e32 v41, v48
	s_cbranch_vccnz .LBB0_1088
	v_mul_f32_e32 v41, 0xbfb8aa3b, v48
	v_exp_f32_e32 v41, v41
	s_nop 0
	v_add_f32_e32 v41, 1.0, v41
	v_rcp_f32_e32 v50, v41
	s_nop 0
	v_fma_f32 v52, -v41, v50, 1.0
	v_fmac_f32_e32 v50, v52, v50
	v_div_fixup_f32 v41, v50, v41, 1.0

; __device__ __forceinline__ float sigmoidf_(float x) { return 1.f / (1.f + __expf(-x)); }
;     __device__ __forceinline__ void operator()(const f32x4 (&acc)[2][2][4][2], const Unit& u, int wr, int wc, int fr, int fq) const {
;     ...
;                     for (int e = 0; e < 8; ++e) { float x = (e < 4) ? v0[e & 3] : v1[e & 3];
;                         if (kind == 0) x = -0.6065306597126334f * sigmoidf_(x);
;                         else if (kind == 1) x = sigmoidf_(x);
;                         o[e] = x; }
.LBB0_1090:
	v_mul_f32_e32 v41, 0xbfb8aa3b, v48
	v_exp_f32_e32 v41, v41
	s_nop 0
	v_add_f32_e32 v41, 1.0, v41
	v_rcp_f32_e32 v49, v41
	s_nop 0
	v_fma_f32 v51, -v41, v49, 1.0
	v_fmac_f32_e32 v49, v51, v49
	v_div_fixup_f32 v41, v49, v41, 1.0
	v_mul_f32_e32 v41, 0xbf1b4598, v41
.LBB0_1091:
	v_add_f32_e32 v48, v42, v66
	s_and_b64 vcc, exec, s[2:3]
	s_mov_b64 s[4:5], -1
	s_cbranch_vccnz .LBB0_1095
	s_and_b64 vcc, exec, s[0:1]
	v_mov_b32_e32 v42, v48
	s_cbranch_vccnz .LBB0_1094
	v_mul_f32_e32 v42, 0xbfb8aa3b, v48
	v_exp_f32_e32 v42, v42
	s_nop 0
	v_add_f32_e32 v42, 1.0, v42
	v_rcp_f32_e32 v50, v42
	s_nop 0
	v_fma_f32 v52, -v42, v50, 1.0
	v_fmac_f32_e32 v50, v52, v50
	v_div_fixup_f32 v42, v50, v42, 1.0

; __device__ __forceinline__ float sigmoidf_(float x) { return 1.f / (1.f + __expf(-x)); }
;     __device__ __forceinline__ void operator()(const f32x4 (&acc)[2][2][4][2], const Unit& u, int wr, int wc, int fr, int fq) const {
;     ...
;                     for (int e = 0; e < 8; ++e) { float x = (e < 4) ? v0[e & 3] : v1[e & 3];
;                         if (kind == 0) x = -0.6065306597126334f * sigmoidf_(x);
;                         else if (kind == 1) x = sigmoidf_(x);
;                         o[e] = x; }
.LBB0_1096:
	v_mul_f32_e32 v42, 0xbfb8aa3b, v48
	v_exp_f32_e32 v42, v42
	s_nop 0
	v_add_f32_e32 v42, 1.0, v42
	v_rcp_f32_e32 v49, v42
	s_nop 0
	v_fma_f32 v51, -v42, v49, 1.0
	v_fmac_f32_e32 v49, v51, v49
	v_div_fixup_f32 v42, v49, v42, 1.0
	v_mul_f32_e32 v42, 0xbf1b4598, v42
.LBB0_1097:
	v_add_f32_e32 v43, v43, v67
	s_and_b64 vcc, exec, s[2:3]
	s_mov_b64 s[4:5], -1
	s_cbranch_vccnz .LBB0_1101
	s_and_b64 vcc, exec, s[0:1]
	v_mov_b32_e32 v48, v43
	s_cbranch_vccnz .LBB0_1100
	v_mul_f32_e32 v48, 0xbfb8aa3b, v43
	v_exp_f32_e32 v48, v48
	s_nop 0
	v_add_f32_e32 v48, 1.0, v48
	v_rcp_f32_e32 v50, v48
	s_nop 0
	v_fma_f32 v52, -v48, v50, 1.0
	v_fmac_f32_e32 v50, v52, v50
	v_div_fixup_f32 v48, v50, v48, 1.0

; __device__ __forceinline__ unsigned cvt_pk_bf16(float lo, float hi) { const f32x2c v = {lo, hi}; const bf16x2c b = __builtin_convertvector(v, bf16x2c); return __builtin_bit_cast(unsigned, b); }
; __device__ __forceinline__ float sigmoidf_(float x) { return 1.f / (1.f + __expf(-x)); }
;     __device__ __forceinline__ void operator()(const f32x4 (&acc)[2][2][4][2], const Unit& u, int wr, int wc, int fr, int fq) const {
;     ...
;                     const f32x4 v0 = acc[ai][bj][m][0] + b0, v1 = acc[ai][bj][m][1] + b1; float o[8];
; #pragma unroll
;                     for (int e = 0; e < 8; ++e) { float x = (e < 4) ? v0[e & 3] : v1[e & 3];
;                         if (kind == 0) x = -0.6065306597126334f * sigmoidf_(x);
;                         else if (kind == 1) x = sigmoidf_(x);
;                         o[e] = x; }
;                     u32x4 w; w.x = cvt_pk_bf16(o[0], o[1]); w.y = cvt_pk_bf16(o[2], o[3]); w.z = cvt_pk_bf16(o[4], o[5]); w.w = cvt_pk_bf16(o[6], o[7]);
;                     *(u32x4*)(O + row * 512 + col) = w; } }
.LBB0_1102:
	v_mul_f32_e32 v43, 0xbfb8aa3b, v43
	v_exp_f32_e32 v43, v43
	s_nop 0
	v_add_f32_e32 v43, 1.0, v43
	v_rcp_f32_e32 v49, v43
	s_nop 0
	v_fma_f32 v51, -v43, v49, 1.0
	v_fmac_f32_e32 v49, v51, v49
	v_div_fixup_f32 v43, v49, v43, 1.0
	v_mul_f32_e32 v48, 0xbf1b4598, v43
.LBB0_1103:
	v_cvt_pk_bf16_f32 v44, v44, v45
	v_cvt_pk_bf16_f32 v45, v46, v47
	v_cvt_pk_bf16_f32 v46, v40, v41
	v_cvt_pk_bf16_f32 v47, v42, v48
	v_add_f32_e32 v40, v36, v68
	s_and_b64 vcc, exec, s[2:3]
	s_mov_b64 s[4:5], -1
	global_store_dwordx4 v[112:113], v[44:47], off offset:256
	s_cbranch_vccnz .LBB0_1107
	s_and_b64 vcc, exec, s[0:1]
	v_mov_b32_e32 v36, v40
	s_cbranch_vccnz .LBB0_1106
	v_mul_f32_e32 v36, 0xbfb8aa3b, v40
	v_exp_f32_e32 v36, v36
	s_nop 0
	v_add_f32_e32 v36, 1.0, v36
	v_rcp_f32_e32 v42, v36
	s_nop 0
	v_fma_f32 v44, -v36, v42, 1.0
	v_fmac_f32_e32 v42, v44, v42
	v_div_fixup_f32 v36, v42, v36, 1.0

; __device__ __forceinline__ float sigmoidf_(float x) { return 1.f / (1.f + __expf(-x)); }
;     __device__ __forceinline__ void operator()(const f32x4 (&acc)[2][2][4][2], const Unit& u, int wr, int wc, int fr, int fq) const {
;     ...
;                     for (int e = 0; e < 8; ++e) { float x = (e < 4) ? v0[e & 3] : v1[e & 3];
;                         if (kind == 0) x = -0.6065306597126334f * sigmoidf_(x);
;                         else if (kind == 1) x = sigmoidf_(x);
;                         o[e] = x; }
.LBB0_1108:
	v_mul_f32_e32 v36, 0xbfb8aa3b, v40
	v_exp_f32_e32 v36, v36
	s_nop 0
	v_add_f32_e32 v36, 1.0, v36
	v_rcp_f32_e32 v41, v36
	s_nop 0
	v_fma_f32 v43, -v36, v41, 1.0
	v_fmac_f32_e32 v41, v43, v41
	v_div_fixup_f32 v36, v41, v36, 1.0
	v_mul_f32_e32 v36, 0xbf1b4598, v36
.LBB0_1109:
	v_add_f32_e32 v40, v37, v69
	s_and_b64 vcc, exec, s[2:3]
	s_mov_b64 s[4:5], -1
	s_cbranch_vccnz .LBB0_1113
	s_and_b64 vcc, exec, s[0:1]
	v_mov_b32_e32 v37, v40
	s_cbranch_vccnz .LBB0_1112
	v_mul_f32_e32 v37, 0xbfb8aa3b, v40
	v_exp_f32_e32 v37, v37
	s_nop 0
	v_add_f32_e32 v37, 1.0, v37
	v_rcp_f32_e32 v42, v37
	s_nop 0
	v_fma_f32 v44, -v37, v42, 1.0
	v_fmac_f32_e32 v42, v44, v42
	v_div_fixup_f32 v37, v42, v37, 1.0

; __device__ __forceinline__ float sigmoidf_(float x) { return 1.f / (1.f + __expf(-x)); }
;     __device__ __forceinline__ void operator()(const f32x4 (&acc)[2][2][4][2], const Unit& u, int wr, int wc, int fr, int fq) const {
;     ...
;                     for (int e = 0; e < 8; ++e) { float x = (e < 4) ? v0[e & 3] : v1[e & 3];
;                         if (kind == 0) x = -0.6065306597126334f * sigmoidf_(x);
;                         else if (kind == 1) x = sigmoidf_(x);
;                         o[e] = x; }
.LBB0_1114:
	v_mul_f32_e32 v37, 0xbfb8aa3b, v40
	v_exp_f32_e32 v37, v37
	s_nop 0
	v_add_f32_e32 v37, 1.0, v37
	v_rcp_f32_e32 v41, v37
	s_nop 0
	v_fma_f32 v43, -v37, v41, 1.0
	v_fmac_f32_e32 v41, v43, v41
	v_div_fixup_f32 v37, v41, v37, 1.0
	v_mul_f32_e32 v37, 0xbf1b4598, v37
.LBB0_1115:
	v_add_f32_e32 v40, v38, v70
	s_and_b64 vcc, exec, s[2:3]
	s_mov_b64 s[4:5], -1
	s_cbranch_vccnz .LBB0_1119
	s_and_b64 vcc, exec, s[0:1]
	v_mov_b32_e32 v38, v40
	s_cbranch_vccnz .LBB0_1118
	v_mul_f32_e32 v38, 0xbfb8aa3b, v40
	v_exp_f32_e32 v38, v38
	s_nop 0
	v_add_f32_e32 v38, 1.0, v38
	v_rcp_f32_e32 v42, v38
	s_nop 0
	v_fma_f32 v44, -v38, v42, 1.0
	v_fmac_f32_e32 v42, v44, v42
	v_div_fixup_f32 v38, v42, v38, 1.0

; __device__ __forceinline__ float sigmoidf_(float x) { return 1.f / (1.f + __expf(-x)); }
;     __device__ __forceinline__ void operator()(const f32x4 (&acc)[2][2][4][2], const Unit& u, int wr, int wc, int fr, int fq) const {
;     ...
;                     for (int e = 0; e < 8; ++e) { float x = (e < 4) ? v0[e & 3] : v1[e & 3];
;                         if (kind == 0) x = -0.6065306597126334f * sigmoidf_(x);
;                         else if (kind == 1) x = sigmoidf_(x);
;                         o[e] = x; }
.LBB0_1120:
	v_mul_f32_e32 v38, 0xbfb8aa3b, v40
	v_exp_f32_e32 v38, v38
	s_nop 0
	v_add_f32_e32 v38, 1.0, v38
	v_rcp_f32_e32 v41, v38
	s_nop 0
	v_fma_f32 v43, -v38, v41, 1.0
	v_fmac_f32_e32 v41, v43, v41
	v_div_fixup_f32 v38, v41, v38, 1.0
	v_mul_f32_e32 v38, 0xbf1b4598, v38
.LBB0_1121:
	v_add_f32_e32 v40, v39, v71
	s_and_b64 vcc, exec, s[2:3]
	s_mov_b64 s[4:5], -1
	s_cbranch_vccnz .LBB0_1125
	s_and_b64 vcc, exec, s[0:1]
	v_mov_b32_e32 v39, v40
	s_cbranch_vccnz .LBB0_1124
	v_mul_f32_e32 v39, 0xbfb8aa3b, v40
	v_exp_f32_e32 v39, v39
	s_nop 0
	v_add_f32_e32 v39, 1.0, v39
	v_rcp_f32_e32 v42, v39
	s_nop 0
	v_fma_f32 v44, -v39, v42, 1.0
	v_fmac_f32_e32 v42, v44, v42
	v_div_fixup_f32 v39, v42, v39, 1.0

; __device__ __forceinline__ float sigmoidf_(float x) { return 1.f / (1.f + __expf(-x)); }
;     __device__ __forceinline__ void operator()(const f32x4 (&acc)[2][2][4][2], const Unit& u, int wr, int wc, int fr, int fq) const {
;     ...
;                     for (int e = 0; e < 8; ++e) { float x = (e < 4) ? v0[e & 3] : v1[e & 3];
;                         if (kind == 0) x = -0.6065306597126334f * sigmoidf_(x);
;                         else if (kind == 1) x = sigmoidf_(x);
;                         o[e] = x; }
.LBB0_1126:
	v_mul_f32_e32 v39, 0xbfb8aa3b, v40
	v_exp_f32_e32 v39, v39
	s_nop 0
	v_add_f32_e32 v39, 1.0, v39
	v_rcp_f32_e32 v41, v39
	s_nop 0
	v_fma_f32 v43, -v39, v41, 1.0
	v_fmac_f32_e32 v41, v43, v41
	v_div_fixup_f32 v39, v41, v39, 1.0
	v_mul_f32_e32 v39, 0xbf1b4598, v39
.LBB0_1127:
	v_add_f32_e32 v40, v32, v64
	s_and_b64 vcc, exec, s[2:3]
	s_mov_b64 s[4:5], -1
	s_cbranch_vccnz .LBB0_1131
	s_and_b64 vcc, exec, s[0:1]
	v_mov_b32_e32 v32, v40
	s_cbranch_vccnz .LBB0_1130
	v_mul_f32_e32 v32, 0xbfb8aa3b, v40
	v_exp_f32_e32 v32, v32
	s_nop 0
	v_add_f32_e32 v32, 1.0, v32
	v_rcp_f32_e32 v42, v32
	s_nop 0
	v_fma_f32 v44, -v32, v42, 1.0
	v_fmac_f32_e32 v42, v44, v42
	v_div_fixup_f32 v32, v42, v32, 1.0

; __device__ __forceinline__ float sigmoidf_(float x) { return 1.f / (1.f + __expf(-x)); }
;     __device__ __forceinline__ void operator()(const f32x4 (&acc)[2][2][4][2], const Unit& u, int wr, int wc, int fr, int fq) const {
;     ...
;                     for (int e = 0; e < 8; ++e) { float x = (e < 4) ? v0[e & 3] : v1[e & 3];
;                         if (kind == 0) x = -0.6065306597126334f * sigmoidf_(x);
;                         else if (kind == 1) x = sigmoidf_(x);
;                         o[e] = x; }
.LBB0_1132:
	v_mul_f32_e32 v32, 0xbfb8aa3b, v40
	v_exp_f32_e32 v32, v32
	s_nop 0
	v_add_f32_e32 v32, 1.0, v32
	v_rcp_f32_e32 v41, v32
	s_nop 0
	v_fma_f32 v43, -v32, v41, 1.0
	v_fmac_f32_e32 v41, v43, v41
	v_div_fixup_f32 v32, v41, v32, 1.0
	v_mul_f32_e32 v32, 0xbf1b4598, v32
.LBB0_1133:
	v_add_f32_e32 v40, v33, v65
	s_and_b64 vcc, exec, s[2:3]
	s_mov_b64 s[4:5], -1
	s_cbranch_vccnz .LBB0_1137
	s_and_b64 vcc, exec, s[0:1]
	v_mov_b32_e32 v33, v40
	s_cbranch_vccnz .LBB0_1136
	v_mul_f32_e32 v33, 0xbfb8aa3b, v40
	v_exp_f32_e32 v33, v33
	s_nop 0
	v_add_f32_e32 v33, 1.0, v33
	v_rcp_f32_e32 v42, v33
	s_nop 0
	v_fma_f32 v44, -v33, v42, 1.0
	v_fmac_f32_e32 v42, v44, v42
	v_div_fixup_f32 v33, v42, v33, 1.0

; __device__ __forceinline__ float sigmoidf_(float x) { return 1.f / (1.f + __expf(-x)); }
;     __device__ __forceinline__ void operator()(const f32x4 (&acc)[2][2][4][2], const Unit& u, int wr, int wc, int fr, int fq) const {
;     ...
;                     for (int e = 0; e < 8; ++e) { float x = (e < 4) ? v0[e & 3] : v1[e & 3];
;                         if (kind == 0) x = -0.6065306597126334f * sigmoidf_(x);
;                         else if (kind == 1) x = sigmoidf_(x);
;                         o[e] = x; }
.LBB0_1138:
	v_mul_f32_e32 v33, 0xbfb8aa3b, v40
	v_exp_f32_e32 v33, v33
	s_nop 0
	v_add_f32_e32 v33, 1.0, v33
	v_rcp_f32_e32 v41, v33
	s_nop 0
	v_fma_f32 v43, -v33, v41, 1.0
	v_fmac_f32_e32 v41, v43, v41
	v_div_fixup_f32 v33, v41, v33, 1.0
	v_mul_f32_e32 v33, 0xbf1b4598, v33
.LBB0_1139:
	v_add_f32_e32 v40, v34, v66
	s_and_b64 vcc, exec, s[2:3]
	s_mov_b64 s[4:5], -1
	s_cbranch_vccnz .LBB0_1143
	s_and_b64 vcc, exec, s[0:1]
	v_mov_b32_e32 v34, v40
	s_cbranch_vccnz .LBB0_1142
	v_mul_f32_e32 v34, 0xbfb8aa3b, v40
	v_exp_f32_e32 v34, v34
	s_nop 0
	v_add_f32_e32 v34, 1.0, v34
	v_rcp_f32_e32 v42, v34
	s_nop 0
	v_fma_f32 v44, -v34, v42, 1.0
	v_fmac_f32_e32 v42, v44, v42
	v_div_fixup_f32 v34, v42, v34, 1.0

; __device__ __forceinline__ float sigmoidf_(float x) { return 1.f / (1.f + __expf(-x)); }
;     __device__ __forceinline__ void operator()(const f32x4 (&acc)[2][2][4][2], const Unit& u, int wr, int wc, int fr, int fq) const {
;     ...
;                     for (int e = 0; e < 8; ++e) { float x = (e < 4) ? v0[e & 3] : v1[e & 3];
;                         if (kind == 0) x = -0.6065306597126334f * sigmoidf_(x);
;                         else if (kind == 1) x = sigmoidf_(x);
;                         o[e] = x; }
.LBB0_1144:
	v_mul_f32_e32 v34, 0xbfb8aa3b, v40
	v_exp_f32_e32 v34, v34
	s_nop 0
	v_add_f32_e32 v34, 1.0, v34
	v_rcp_f32_e32 v41, v34
	s_nop 0
	v_fma_f32 v43, -v34, v41, 1.0
	v_fmac_f32_e32 v41, v43, v41
	v_div_fixup_f32 v34, v41, v34, 1.0
	v_mul_f32_e32 v34, 0xbf1b4598, v34
.LBB0_1145:
	v_add_f32_e32 v35, v35, v67
	s_and_b64 vcc, exec, s[2:3]
	s_mov_b64 s[4:5], -1
	s_cbranch_vccnz .LBB0_1149
	s_and_b64 vcc, exec, s[0:1]
	v_mov_b32_e32 v40, v35
	s_cbranch_vccnz .LBB0_1148
	v_mul_f32_e32 v40, 0xbfb8aa3b, v35
	v_exp_f32_e32 v40, v40
	s_nop 0
	v_add_f32_e32 v40, 1.0, v40
	v_rcp_f32_e32 v42, v40
	s_nop 0
	v_fma_f32 v44, -v40, v42, 1.0
	v_fmac_f32_e32 v42, v44, v42
	v_div_fixup_f32 v40, v42, v40, 1.0

; __device__ __forceinline__ unsigned cvt_pk_bf16(float lo, float hi) { const f32x2c v = {lo, hi}; const bf16x2c b = __builtin_convertvector(v, bf16x2c); return __builtin_bit_cast(unsigned, b); }
; __device__ __forceinline__ float sigmoidf_(float x) { return 1.f / (1.f + __expf(-x)); }
;     __device__ __forceinline__ void operator()(const f32x4 (&acc)[2][2][4][2], const Unit& u, int wr, int wc, int fr, int fq) const {
;     ...
;                     const f32x4 v0 = acc[ai][bj][m][0] + b0, v1 = acc[ai][bj][m][1] + b1; float o[8];
; #pragma unroll
;                     for (int e = 0; e < 8; ++e) { float x = (e < 4) ? v0[e & 3] : v1[e & 3];
;                         if (kind == 0) x = -0.6065306597126334f * sigmoidf_(x);
;                         else if (kind == 1) x = sigmoidf_(x);
;                         o[e] = x; }
;                     u32x4 w; w.x = cvt_pk_bf16(o[0], o[1]); w.y = cvt_pk_bf16(o[2], o[3]); w.z = cvt_pk_bf16(o[4], o[5]); w.w = cvt_pk_bf16(o[6], o[7]);
;                     *(u32x4*)(O + row * 512 + col) = w; } }
.LBB0_1150:
	v_mul_f32_e32 v35, 0xbfb8aa3b, v35
	v_exp_f32_e32 v35, v35
	s_nop 0
	v_add_f32_e32 v35, 1.0, v35
	v_rcp_f32_e32 v41, v35
	s_nop 0
	v_fma_f32 v43, -v35, v41, 1.0
	v_fmac_f32_e32 v41, v43, v41
	v_div_fixup_f32 v35, v41, v35, 1.0
	v_mul_f32_e32 v40, 0xbf1b4598, v35
.LBB0_1151:
	v_cvt_pk_bf16_f32 v36, v36, v37
	v_cvt_pk_bf16_f32 v37, v38, v39
	v_cvt_pk_bf16_f32 v38, v32, v33
	v_cvt_pk_bf16_f32 v39, v34, v40
	v_add_f32_e32 v32, v28, v68
	s_and_b64 vcc, exec, s[2:3]
	s_mov_b64 s[4:5], -1
	global_store_dwordx4 v[104:105], v[36:39], off offset:256
	s_cbranch_vccnz .LBB0_1155
	s_and_b64 vcc, exec, s[0:1]
	v_mov_b32_e32 v28, v32
	s_cbranch_vccnz .LBB0_1154
	v_mul_f32_e32 v28, 0xbfb8aa3b, v32
	v_exp_f32_e32 v28, v28
	s_nop 0
	v_add_f32_e32 v28, 1.0, v28
	v_rcp_f32_e32 v34, v28
	s_nop 0
	v_fma_f32 v36, -v28, v34, 1.0
	v_fmac_f32_e32 v34, v36, v34
	v_div_fixup_f32 v28, v34, v28, 1.0

; __device__ __forceinline__ float sigmoidf_(float x) { return 1.f / (1.f + __expf(-x)); }
;     __device__ __forceinline__ void operator()(const f32x4 (&acc)[2][2][4][2], const Unit& u, int wr, int wc, int fr, int fq) const {
;     ...
;                     for (int e = 0; e < 8; ++e) { float x = (e < 4) ? v0[e & 3] : v1[e & 3];
;                         if (kind == 0) x = -0.6065306597126334f * sigmoidf_(x);
;                         else if (kind == 1) x = sigmoidf_(x);
;                         o[e] = x; }
.LBB0_1156:
	v_mul_f32_e32 v28, 0xbfb8aa3b, v32
	v_exp_f32_e32 v28, v28
	s_nop 0
	v_add_f32_e32 v28, 1.0, v28
	v_rcp_f32_e32 v33, v28
	s_nop 0
	v_fma_f32 v35, -v28, v33, 1.0
	v_fmac_f32_e32 v33, v35, v33
	v_div_fixup_f32 v28, v33, v28, 1.0
	v_mul_f32_e32 v28, 0xbf1b4598, v28
.LBB0_1157:
	v_add_f32_e32 v32, v29, v69
	s_and_b64 vcc, exec, s[2:3]
	s_mov_b64 s[4:5], -1
	s_cbranch_vccnz .LBB0_1161
	s_and_b64 vcc, exec, s[0:1]
	v_mov_b32_e32 v29, v32
	s_cbranch_vccnz .LBB0_1160
	v_mul_f32_e32 v29, 0xbfb8aa3b, v32
	v_exp_f32_e32 v29, v29
	s_nop 0
	v_add_f32_e32 v29, 1.0, v29
	v_rcp_f32_e32 v34, v29
	s_nop 0
	v_fma_f32 v36, -v29, v34, 1.0
	v_fmac_f32_e32 v34, v36, v34
	v_div_fixup_f32 v29, v34, v29, 1.0

; __device__ __forceinline__ float sigmoidf_(float x) { return 1.f / (1.f + __expf(-x)); }
;     __device__ __forceinline__ void operator()(const f32x4 (&acc)[2][2][4][2], const Unit& u, int wr, int wc, int fr, int fq) const {
;     ...
;                     for (int e = 0; e < 8; ++e) { float x = (e < 4) ? v0[e & 3] : v1[e & 3];
;                         if (kind == 0) x = -0.6065306597126334f * sigmoidf_(x);
;                         else if (kind == 1) x = sigmoidf_(x);
;                         o[e] = x; }
.LBB0_1162:
	v_mul_f32_e32 v29, 0xbfb8aa3b, v32
	v_exp_f32_e32 v29, v29
	s_nop 0
	v_add_f32_e32 v29, 1.0, v29
	v_rcp_f32_e32 v33, v29
	s_nop 0
	v_fma_f32 v35, -v29, v33, 1.0
	v_fmac_f32_e32 v33, v35, v33
	v_div_fixup_f32 v29, v33, v29, 1.0
	v_mul_f32_e32 v29, 0xbf1b4598, v29
.LBB0_1163:
	v_add_f32_e32 v32, v30, v70
	s_and_b64 vcc, exec, s[2:3]
	s_mov_b64 s[4:5], -1
	s_cbranch_vccnz .LBB0_1167
	s_and_b64 vcc, exec, s[0:1]
	v_mov_b32_e32 v30, v32
	s_cbranch_vccnz .LBB0_1166
	v_mul_f32_e32 v30, 0xbfb8aa3b, v32
	v_exp_f32_e32 v30, v30
	s_nop 0
	v_add_f32_e32 v30, 1.0, v30
	v_rcp_f32_e32 v34, v30
	s_nop 0
	v_fma_f32 v36, -v30, v34, 1.0
	v_fmac_f32_e32 v34, v36, v34
	v_div_fixup_f32 v30, v34, v30, 1.0

; __device__ __forceinline__ float sigmoidf_(float x) { return 1.f / (1.f + __expf(-x)); }
;     __device__ __forceinline__ void operator()(const f32x4 (&acc)[2][2][4][2], const Unit& u, int wr, int wc, int fr, int fq) const {
;     ...
;                     for (int e = 0; e < 8; ++e) { float x = (e < 4) ? v0[e & 3] : v1[e & 3];
;                         if (kind == 0) x = -0.6065306597126334f * sigmoidf_(x);
;                         else if (kind == 1) x = sigmoidf_(x);
;                         o[e] = x; }
.LBB0_1168:
	v_mul_f32_e32 v30, 0xbfb8aa3b, v32
	v_exp_f32_e32 v30, v30
	s_nop 0
	v_add_f32_e32 v30, 1.0, v30
	v_rcp_f32_e32 v33, v30
	s_nop 0
	v_fma_f32 v35, -v30, v33, 1.0
	v_fmac_f32_e32 v33, v35, v33
	v_div_fixup_f32 v30, v33, v30, 1.0
	v_mul_f32_e32 v30, 0xbf1b4598, v30
.LBB0_1169:
	v_add_f32_e32 v32, v31, v71
	s_and_b64 vcc, exec, s[2:3]
	s_mov_b64 s[4:5], -1
	s_cbranch_vccnz .LBB0_1173
	s_and_b64 vcc, exec, s[0:1]
	v_mov_b32_e32 v31, v32
	s_cbranch_vccnz .LBB0_1172
	v_mul_f32_e32 v31, 0xbfb8aa3b, v32
	v_exp_f32_e32 v31, v31
	s_nop 0
	v_add_f32_e32 v31, 1.0, v31
	v_rcp_f32_e32 v34, v31
	s_nop 0
	v_fma_f32 v36, -v31, v34, 1.0
	v_fmac_f32_e32 v34, v36, v34
	v_div_fixup_f32 v31, v34, v31, 1.0

; __device__ __forceinline__ float sigmoidf_(float x) { return 1.f / (1.f + __expf(-x)); }
;     __device__ __forceinline__ void operator()(const f32x4 (&acc)[2][2][4][2], const Unit& u, int wr, int wc, int fr, int fq) const {
;     ...
;                     for (int e = 0; e < 8; ++e) { float x = (e < 4) ? v0[e & 3] : v1[e & 3];
;                         if (kind == 0) x = -0.6065306597126334f * sigmoidf_(x);
;                         else if (kind == 1) x = sigmoidf_(x);
;                         o[e] = x; }
.LBB0_1174:
	v_mul_f32_e32 v31, 0xbfb8aa3b, v32
	v_exp_f32_e32 v31, v31
	s_nop 0
	v_add_f32_e32 v31, 1.0, v31
	v_rcp_f32_e32 v33, v31
	s_nop 0
	v_fma_f32 v35, -v31, v33, 1.0
	v_fmac_f32_e32 v33, v35, v33
	v_div_fixup_f32 v31, v33, v31, 1.0
	v_mul_f32_e32 v31, 0xbf1b4598, v31
.LBB0_1175:
	v_add_f32_e32 v32, v24, v64
	s_and_b64 vcc, exec, s[2:3]
	s_mov_b64 s[4:5], -1
	s_cbranch_vccnz .LBB0_1179
	s_and_b64 vcc, exec, s[0:1]
	v_mov_b32_e32 v24, v32
	s_cbranch_vccnz .LBB0_1178
	v_mul_f32_e32 v24, 0xbfb8aa3b, v32
	v_exp_f32_e32 v24, v24
	s_nop 0
	v_add_f32_e32 v24, 1.0, v24
	v_rcp_f32_e32 v34, v24
	s_nop 0
	v_fma_f32 v36, -v24, v34, 1.0
	v_fmac_f32_e32 v34, v36, v34
	v_div_fixup_f32 v24, v34, v24, 1.0

; __device__ __forceinline__ float sigmoidf_(float x) { return 1.f / (1.f + __expf(-x)); }
;     __device__ __forceinline__ void operator()(const f32x4 (&acc)[2][2][4][2], const Unit& u, int wr, int wc, int fr, int fq) const {
;     ...
;                     for (int e = 0; e < 8; ++e) { float x = (e < 4) ? v0[e & 3] : v1[e & 3];
;                         if (kind == 0) x = -0.6065306597126334f * sigmoidf_(x);
;                         else if (kind == 1) x = sigmoidf_(x);
;                         o[e] = x; }
.LBB0_1180:
	v_mul_f32_e32 v24, 0xbfb8aa3b, v32
	v_exp_f32_e32 v24, v24
	s_nop 0
	v_add_f32_e32 v24, 1.0, v24
	v_rcp_f32_e32 v33, v24
	s_nop 0
	v_fma_f32 v35, -v24, v33, 1.0
	v_fmac_f32_e32 v33, v35, v33
	v_div_fixup_f32 v24, v33, v24, 1.0
	v_mul_f32_e32 v24, 0xbf1b4598, v24
.LBB0_1181:
	v_add_f32_e32 v32, v25, v65
	s_and_b64 vcc, exec, s[2:3]
	s_mov_b64 s[4:5], -1
	s_cbranch_vccnz .LBB0_1185
	s_and_b64 vcc, exec, s[0:1]
	v_mov_b32_e32 v25, v32
	s_cbranch_vccnz .LBB0_1184
	v_mul_f32_e32 v25, 0xbfb8aa3b, v32
	v_exp_f32_e32 v25, v25
	s_nop 0
	v_add_f32_e32 v25, 1.0, v25
	v_rcp_f32_e32 v34, v25
	s_nop 0
	v_fma_f32 v36, -v25, v34, 1.0
	v_fmac_f32_e32 v34, v36, v34
	v_div_fixup_f32 v25, v34, v25, 1.0

; __device__ __forceinline__ float sigmoidf_(float x) { return 1.f / (1.f + __expf(-x)); }
;     __device__ __forceinline__ void operator()(const f32x4 (&acc)[2][2][4][2], const Unit& u, int wr, int wc, int fr, int fq) const {
;     ...
;                     for (int e = 0; e < 8; ++e) { float x = (e < 4) ? v0[e & 3] : v1[e & 3];
;                         if (kind == 0) x = -0.6065306597126334f * sigmoidf_(x);
;                         else if (kind == 1) x = sigmoidf_(x);
;                         o[e] = x; }
.LBB0_1186:
	v_mul_f32_e32 v25, 0xbfb8aa3b, v32
	v_exp_f32_e32 v25, v25
	s_nop 0
	v_add_f32_e32 v25, 1.0, v25
	v_rcp_f32_e32 v33, v25
	s_nop 0
	v_fma_f32 v35, -v25, v33, 1.0
	v_fmac_f32_e32 v33, v35, v33
	v_div_fixup_f32 v25, v33, v25, 1.0
	v_mul_f32_e32 v25, 0xbf1b4598, v25
.LBB0_1187:
	v_add_f32_e32 v32, v26, v66
	s_and_b64 vcc, exec, s[2:3]
	s_mov_b64 s[4:5], -1
	s_cbranch_vccnz .LBB0_1191
	s_and_b64 vcc, exec, s[0:1]
	v_mov_b32_e32 v26, v32
	s_cbranch_vccnz .LBB0_1190
	v_mul_f32_e32 v26, 0xbfb8aa3b, v32
	v_exp_f32_e32 v26, v26
	s_nop 0
	v_add_f32_e32 v26, 1.0, v26
	v_rcp_f32_e32 v34, v26
	s_nop 0
	v_fma_f32 v36, -v26, v34, 1.0
	v_fmac_f32_e32 v34, v36, v34
	v_div_fixup_f32 v26, v34, v26, 1.0

; __device__ __forceinline__ float sigmoidf_(float x) { return 1.f / (1.f + __expf(-x)); }
;     __device__ __forceinline__ void operator()(const f32x4 (&acc)[2][2][4][2], const Unit& u, int wr, int wc, int fr, int fq) const {
;     ...
;                     for (int e = 0; e < 8; ++e) { float x = (e < 4) ? v0[e & 3] : v1[e & 3];
;                         if (kind == 0) x = -0.6065306597126334f * sigmoidf_(x);
;                         else if (kind == 1) x = sigmoidf_(x);
;                         o[e] = x; }
.LBB0_1192:
	v_mul_f32_e32 v26, 0xbfb8aa3b, v32
	v_exp_f32_e32 v26, v26
	s_nop 0
	v_add_f32_e32 v26, 1.0, v26
	v_rcp_f32_e32 v33, v26
	s_nop 0
	v_fma_f32 v35, -v26, v33, 1.0
	v_fmac_f32_e32 v33, v35, v33
	v_div_fixup_f32 v26, v33, v26, 1.0
	v_mul_f32_e32 v26, 0xbf1b4598, v26
.LBB0_1193:
	v_add_f32_e32 v27, v27, v67
	s_and_b64 vcc, exec, s[2:3]
	s_mov_b64 s[4:5], -1
	s_cbranch_vccnz .LBB0_1197
	s_and_b64 vcc, exec, s[0:1]
	v_mov_b32_e32 v32, v27
	s_cbranch_vccnz .LBB0_1196
	v_mul_f32_e32 v32, 0xbfb8aa3b, v27
	v_exp_f32_e32 v32, v32
	s_nop 0
	v_add_f32_e32 v32, 1.0, v32
	v_rcp_f32_e32 v34, v32
	s_nop 0
	v_fma_f32 v36, -v32, v34, 1.0
	v_fmac_f32_e32 v34, v36, v34
	v_div_fixup_f32 v32, v34, v32, 1.0

; __device__ __forceinline__ unsigned cvt_pk_bf16(float lo, float hi) { const f32x2c v = {lo, hi}; const bf16x2c b = __builtin_convertvector(v, bf16x2c); return __builtin_bit_cast(unsigned, b); }
; __device__ __forceinline__ float sigmoidf_(float x) { return 1.f / (1.f + __expf(-x)); }
;     __device__ __forceinline__ void operator()(const f32x4 (&acc)[2][2][4][2], const Unit& u, int wr, int wc, int fr, int fq) const {
;     ...
;                     const f32x4 v0 = acc[ai][bj][m][0] + b0, v1 = acc[ai][bj][m][1] + b1; float o[8];
; #pragma unroll
;                     for (int e = 0; e < 8; ++e) { float x = (e < 4) ? v0[e & 3] : v1[e & 3];
;                         if (kind == 0) x = -0.6065306597126334f * sigmoidf_(x);
;                         else if (kind == 1) x = sigmoidf_(x);
;                         o[e] = x; }
;                     u32x4 w; w.x = cvt_pk_bf16(o[0], o[1]); w.y = cvt_pk_bf16(o[2], o[3]); w.z = cvt_pk_bf16(o[4], o[5]); w.w = cvt_pk_bf16(o[6], o[7]);
;                     *(u32x4*)(O + row * 512 + col) = w; } }
.LBB0_1198:
	v_mul_f32_e32 v27, 0xbfb8aa3b, v27
	v_exp_f32_e32 v27, v27
	s_nop 0
	v_add_f32_e32 v27, 1.0, v27
	v_rcp_f32_e32 v33, v27
	s_nop 0
	v_fma_f32 v35, -v27, v33, 1.0
	v_fmac_f32_e32 v33, v35, v33
	v_div_fixup_f32 v27, v33, v27, 1.0
	v_mul_f32_e32 v32, 0xbf1b4598, v27
.LBB0_1199:
	s_mov_b64 s[4:5], 0x20000
	v_lshl_add_u64 v[34:35], v[96:97], 0, s[4:5]
	v_cvt_pk_bf16_f32 v28, v28, v29
	v_cvt_pk_bf16_f32 v29, v30, v31
	v_cvt_pk_bf16_f32 v30, v24, v25
	v_cvt_pk_bf16_f32 v31, v26, v32
	v_add_f32_e32 v24, v20, v68
	s_and_b64 vcc, exec, s[2:3]
	s_mov_b64 s[4:5], -1
	global_store_dwordx4 v[34:35], v[28:31], off offset:256
	s_cbranch_vccnz .LBB0_1203
	s_and_b64 vcc, exec, s[0:1]
	v_mov_b32_e32 v20, v24
	s_cbranch_vccnz .LBB0_1202
	v_mul_f32_e32 v20, 0xbfb8aa3b, v24
	v_exp_f32_e32 v20, v20
	s_nop 0
	v_add_f32_e32 v20, 1.0, v20
	v_rcp_f32_e32 v26, v20
	s_nop 0
	v_fma_f32 v28, -v20, v26, 1.0
	v_fmac_f32_e32 v26, v28, v26
	v_div_fixup_f32 v20, v26, v20, 1.0

; __device__ __forceinline__ float sigmoidf_(float x) { return 1.f / (1.f + __expf(-x)); }
;     __device__ __forceinline__ void operator()(const f32x4 (&acc)[2][2][4][2], const Unit& u, int wr, int wc, int fr, int fq) const {
;     ...
;                     for (int e = 0; e < 8; ++e) { float x = (e < 4) ? v0[e & 3] : v1[e & 3];
;                         if (kind == 0) x = -0.6065306597126334f * sigmoidf_(x);
;                         else if (kind == 1) x = sigmoidf_(x);
;                         o[e] = x; }
.LBB0_1204:
	v_mul_f32_e32 v20, 0xbfb8aa3b, v24
	v_exp_f32_e32 v20, v20
	s_nop 0
	v_add_f32_e32 v20, 1.0, v20
	v_rcp_f32_e32 v25, v20
	s_nop 0
	v_fma_f32 v27, -v20, v25, 1.0
	v_fmac_f32_e32 v25, v27, v25
	v_div_fixup_f32 v20, v25, v20, 1.0
	v_mul_f32_e32 v20, 0xbf1b4598, v20
.LBB0_1205:
	v_add_f32_e32 v24, v21, v69
	s_and_b64 vcc, exec, s[2:3]
	s_mov_b64 s[4:5], -1
	s_cbranch_vccnz .LBB0_1209
	s_and_b64 vcc, exec, s[0:1]
	v_mov_b32_e32 v21, v24
	s_cbranch_vccnz .LBB0_1208
	v_mul_f32_e32 v21, 0xbfb8aa3b, v24
	v_exp_f32_e32 v21, v21
	s_nop 0
	v_add_f32_e32 v21, 1.0, v21
	v_rcp_f32_e32 v26, v21
	s_nop 0
	v_fma_f32 v28, -v21, v26, 1.0
	v_fmac_f32_e32 v26, v28, v26
	v_div_fixup_f32 v21, v26, v21, 1.0

; __device__ __forceinline__ float sigmoidf_(float x) { return 1.f / (1.f + __expf(-x)); }
;     __device__ __forceinline__ void operator()(const f32x4 (&acc)[2][2][4][2], const Unit& u, int wr, int wc, int fr, int fq) const {
;     ...
;                     for (int e = 0; e < 8; ++e) { float x = (e < 4) ? v0[e & 3] : v1[e & 3];
;                         if (kind == 0) x = -0.6065306597126334f * sigmoidf_(x);
;                         else if (kind == 1) x = sigmoidf_(x);
;                         o[e] = x; }
.LBB0_1210:
	v_mul_f32_e32 v21, 0xbfb8aa3b, v24
	v_exp_f32_e32 v21, v21
	s_nop 0
	v_add_f32_e32 v21, 1.0, v21
	v_rcp_f32_e32 v25, v21
	s_nop 0
	v_fma_f32 v27, -v21, v25, 1.0
	v_fmac_f32_e32 v25, v27, v25
	v_div_fixup_f32 v21, v25, v21, 1.0
	v_mul_f32_e32 v21, 0xbf1b4598, v21
.LBB0_1211:
	v_add_f32_e32 v24, v22, v70
	s_and_b64 vcc, exec, s[2:3]
	s_mov_b64 s[4:5], -1
	s_cbranch_vccnz .LBB0_1215
	s_and_b64 vcc, exec, s[0:1]
	v_mov_b32_e32 v22, v24
	s_cbranch_vccnz .LBB0_1214
	v_mul_f32_e32 v22, 0xbfb8aa3b, v24
	v_exp_f32_e32 v22, v22
	s_nop 0
	v_add_f32_e32 v22, 1.0, v22
	v_rcp_f32_e32 v26, v22
	s_nop 0
	v_fma_f32 v28, -v22, v26, 1.0
	v_fmac_f32_e32 v26, v28, v26
	v_div_fixup_f32 v22, v26, v22, 1.0

; __device__ __forceinline__ float sigmoidf_(float x) { return 1.f / (1.f + __expf(-x)); }
;     __device__ __forceinline__ void operator()(const f32x4 (&acc)[2][2][4][2], const Unit& u, int wr, int wc, int fr, int fq) const {
;     ...
;                     for (int e = 0; e < 8; ++e) { float x = (e < 4) ? v0[e & 3] : v1[e & 3];
;                         if (kind == 0) x = -0.6065306597126334f * sigmoidf_(x);
;                         else if (kind == 1) x = sigmoidf_(x);
;                         o[e] = x; }
.LBB0_1216:
	v_mul_f32_e32 v22, 0xbfb8aa3b, v24
	v_exp_f32_e32 v22, v22
	s_nop 0
	v_add_f32_e32 v22, 1.0, v22
	v_rcp_f32_e32 v25, v22
	s_nop 0
	v_fma_f32 v27, -v22, v25, 1.0
	v_fmac_f32_e32 v25, v27, v25
	v_div_fixup_f32 v22, v25, v22, 1.0
	v_mul_f32_e32 v22, 0xbf1b4598, v22
.LBB0_1217:
	v_add_f32_e32 v24, v23, v71
	s_and_b64 vcc, exec, s[2:3]
	s_mov_b64 s[4:5], -1
	s_cbranch_vccnz .LBB0_1221
	s_and_b64 vcc, exec, s[0:1]
	v_mov_b32_e32 v23, v24
	s_cbranch_vccnz .LBB0_1220
	v_mul_f32_e32 v23, 0xbfb8aa3b, v24
	v_exp_f32_e32 v23, v23
	s_nop 0
	v_add_f32_e32 v23, 1.0, v23
	v_rcp_f32_e32 v26, v23
	s_nop 0
	v_fma_f32 v28, -v23, v26, 1.0
	v_fmac_f32_e32 v26, v28, v26
	v_div_fixup_f32 v23, v26, v23, 1.0

; __device__ __forceinline__ float sigmoidf_(float x) { return 1.f / (1.f + __expf(-x)); }
;     __device__ __forceinline__ void operator()(const f32x4 (&acc)[2][2][4][2], const Unit& u, int wr, int wc, int fr, int fq) const {
;     ...
;                     for (int e = 0; e < 8; ++e) { float x = (e < 4) ? v0[e & 3] : v1[e & 3];
;                         if (kind == 0) x = -0.6065306597126334f * sigmoidf_(x);
;                         else if (kind == 1) x = sigmoidf_(x);
;                         o[e] = x; }
.LBB0_1222:
	v_mul_f32_e32 v23, 0xbfb8aa3b, v24
	v_exp_f32_e32 v23, v23
	s_nop 0
	v_add_f32_e32 v23, 1.0, v23
	v_rcp_f32_e32 v25, v23
	s_nop 0
	v_fma_f32 v27, -v23, v25, 1.0
	v_fmac_f32_e32 v25, v27, v25
	v_div_fixup_f32 v23, v25, v23, 1.0
	v_mul_f32_e32 v23, 0xbf1b4598, v23
.LBB0_1223:
	v_add_f32_e32 v24, v16, v64
	s_and_b64 vcc, exec, s[2:3]
	s_mov_b64 s[4:5], -1
	s_cbranch_vccnz .LBB0_1227
	s_and_b64 vcc, exec, s[0:1]
	v_mov_b32_e32 v16, v24
	s_cbranch_vccnz .LBB0_1226
	v_mul_f32_e32 v16, 0xbfb8aa3b, v24
	v_exp_f32_e32 v16, v16
	s_nop 0
	v_add_f32_e32 v16, 1.0, v16
	v_rcp_f32_e32 v26, v16
	s_nop 0
	v_fma_f32 v28, -v16, v26, 1.0
	v_fmac_f32_e32 v26, v28, v26
	v_div_fixup_f32 v16, v26, v16, 1.0

; __device__ __forceinline__ float sigmoidf_(float x) { return 1.f / (1.f + __expf(-x)); }
;     __device__ __forceinline__ void operator()(const f32x4 (&acc)[2][2][4][2], const Unit& u, int wr, int wc, int fr, int fq) const {
;     ...
;                     for (int e = 0; e < 8; ++e) { float x = (e < 4) ? v0[e & 3] : v1[e & 3];
;                         if (kind == 0) x = -0.6065306597126334f * sigmoidf_(x);
;                         else if (kind == 1) x = sigmoidf_(x);
;                         o[e] = x; }
.LBB0_1228:
	v_mul_f32_e32 v16, 0xbfb8aa3b, v24
	v_exp_f32_e32 v16, v16
	s_nop 0
	v_add_f32_e32 v16, 1.0, v16
	v_rcp_f32_e32 v25, v16
	s_nop 0
	v_fma_f32 v27, -v16, v25, 1.0
	v_fmac_f32_e32 v25, v27, v25
	v_div_fixup_f32 v16, v25, v16, 1.0
	v_mul_f32_e32 v16, 0xbf1b4598, v16
.LBB0_1229:
	v_add_f32_e32 v24, v17, v65
	s_and_b64 vcc, exec, s[2:3]
	s_mov_b64 s[4:5], -1
	s_cbranch_vccnz .LBB0_1233
	s_and_b64 vcc, exec, s[0:1]
	v_mov_b32_e32 v17, v24
	s_cbranch_vccnz .LBB0_1232
	v_mul_f32_e32 v17, 0xbfb8aa3b, v24
	v_exp_f32_e32 v17, v17
	s_nop 0
	v_add_f32_e32 v17, 1.0, v17
	v_rcp_f32_e32 v26, v17
	s_nop 0
	v_fma_f32 v28, -v17, v26, 1.0
	v_fmac_f32_e32 v26, v28, v26
	v_div_fixup_f32 v17, v26, v17, 1.0

; __device__ __forceinline__ float sigmoidf_(float x) { return 1.f / (1.f + __expf(-x)); }
;     __device__ __forceinline__ void operator()(const f32x4 (&acc)[2][2][4][2], const Unit& u, int wr, int wc, int fr, int fq) const {
;     ...
;                     for (int e = 0; e < 8; ++e) { float x = (e < 4) ? v0[e & 3] : v1[e & 3];
;                         if (kind == 0) x = -0.6065306597126334f * sigmoidf_(x);
;                         else if (kind == 1) x = sigmoidf_(x);
;                         o[e] = x; }
.LBB0_1234:
	v_mul_f32_e32 v17, 0xbfb8aa3b, v24
	v_exp_f32_e32 v17, v17
	s_nop 0
	v_add_f32_e32 v17, 1.0, v17
	v_rcp_f32_e32 v25, v17
	s_nop 0
	v_fma_f32 v27, -v17, v25, 1.0
	v_fmac_f32_e32 v25, v27, v25
	v_div_fixup_f32 v17, v25, v17, 1.0
	v_mul_f32_e32 v17, 0xbf1b4598, v17
.LBB0_1235:
	v_add_f32_e32 v24, v18, v66
	s_and_b64 vcc, exec, s[2:3]
	s_mov_b64 s[4:5], -1
	s_cbranch_vccnz .LBB0_1239
	s_and_b64 vcc, exec, s[0:1]
	v_mov_b32_e32 v18, v24
	s_cbranch_vccnz .LBB0_1238
	v_mul_f32_e32 v18, 0xbfb8aa3b, v24
	v_exp_f32_e32 v18, v18
	s_nop 0
	v_add_f32_e32 v18, 1.0, v18
	v_rcp_f32_e32 v26, v18
	s_nop 0
	v_fma_f32 v28, -v18, v26, 1.0
	v_fmac_f32_e32 v26, v28, v26
	v_div_fixup_f32 v18, v26, v18, 1.0

; __device__ __forceinline__ float sigmoidf_(float x) { return 1.f / (1.f + __expf(-x)); }
;     __device__ __forceinline__ void operator()(const f32x4 (&acc)[2][2][4][2], const Unit& u, int wr, int wc, int fr, int fq) const {
;     ...
;                     for (int e = 0; e < 8; ++e) { float x = (e < 4) ? v0[e & 3] : v1[e & 3];
;                         if (kind == 0) x = -0.6065306597126334f * sigmoidf_(x);
;                         else if (kind == 1) x = sigmoidf_(x);
;                         o[e] = x; }
.LBB0_1240:
	v_mul_f32_e32 v18, 0xbfb8aa3b, v24
	v_exp_f32_e32 v18, v18
	s_nop 0
	v_add_f32_e32 v18, 1.0, v18
	v_rcp_f32_e32 v25, v18
	s_nop 0
	v_fma_f32 v27, -v18, v25, 1.0
	v_fmac_f32_e32 v25, v27, v25
	v_div_fixup_f32 v18, v25, v18, 1.0
	v_mul_f32_e32 v18, 0xbf1b4598, v18
.LBB0_1241:
	v_add_f32_e32 v19, v19, v67
	s_and_b64 vcc, exec, s[2:3]
	s_mov_b64 s[4:5], -1
	s_cbranch_vccnz .LBB0_1245
	s_and_b64 vcc, exec, s[0:1]
	v_mov_b32_e32 v24, v19
	s_cbranch_vccnz .LBB0_1244
	v_mul_f32_e32 v24, 0xbfb8aa3b, v19
	v_exp_f32_e32 v24, v24
	s_nop 0
	v_add_f32_e32 v24, 1.0, v24
	v_rcp_f32_e32 v26, v24
	s_nop 0
	v_fma_f32 v28, -v24, v26, 1.0
	v_fmac_f32_e32 v26, v28, v26
	v_div_fixup_f32 v24, v26, v24, 1.0

; __device__ __forceinline__ unsigned cvt_pk_bf16(float lo, float hi) { const f32x2c v = {lo, hi}; const bf16x2c b = __builtin_convertvector(v, bf16x2c); return __builtin_bit_cast(unsigned, b); }
; __device__ __forceinline__ float sigmoidf_(float x) { return 1.f / (1.f + __expf(-x)); }
;     __device__ __forceinline__ void operator()(const f32x4 (&acc)[2][2][4][2], const Unit& u, int wr, int wc, int fr, int fq) const {
;     ...
;                     const f32x4 v0 = acc[ai][bj][m][0] + b0, v1 = acc[ai][bj][m][1] + b1; float o[8];
; #pragma unroll
;                     for (int e = 0; e < 8; ++e) { float x = (e < 4) ? v0[e & 3] : v1[e & 3];
;                         if (kind == 0) x = -0.6065306597126334f * sigmoidf_(x);
;                         else if (kind == 1) x = sigmoidf_(x);
;                         o[e] = x; }
;                     u32x4 w; w.x = cvt_pk_bf16(o[0], o[1]); w.y = cvt_pk_bf16(o[2], o[3]); w.z = cvt_pk_bf16(o[4], o[5]); w.w = cvt_pk_bf16(o[6], o[7]);
;                     *(u32x4*)(O + row * 512 + col) = w; } }
.LBB0_1246:
	v_mul_f32_e32 v19, 0xbfb8aa3b, v19
	v_exp_f32_e32 v19, v19
	s_nop 0
	v_add_f32_e32 v19, 1.0, v19
	v_rcp_f32_e32 v25, v19
	s_nop 0
	v_fma_f32 v27, -v19, v25, 1.0
	v_fmac_f32_e32 v25, v27, v25
	v_div_fixup_f32 v19, v25, v19, 1.0
	v_mul_f32_e32 v24, 0xbf1b4598, v19
.LBB0_1247:
	s_mov_b64 s[4:5], 0x24000
	v_lshl_add_u64 v[26:27], v[84:85], 0, s[4:5]
	v_cvt_pk_bf16_f32 v20, v20, v21
	v_cvt_pk_bf16_f32 v21, v22, v23
	v_cvt_pk_bf16_f32 v22, v16, v17
	v_cvt_pk_bf16_f32 v23, v18, v24
	v_add_f32_e32 v16, v12, v68
	s_and_b64 vcc, exec, s[2:3]
	s_mov_b64 s[4:5], -1
	global_store_dwordx4 v[26:27], v[20:23], off offset:256
	s_cbranch_vccnz .LBB0_1251
	s_and_b64 vcc, exec, s[0:1]
	v_mov_b32_e32 v12, v16
	s_cbranch_vccnz .LBB0_1250
	v_mul_f32_e32 v12, 0xbfb8aa3b, v16
	v_exp_f32_e32 v12, v12
	s_nop 0
	v_add_f32_e32 v12, 1.0, v12
	v_rcp_f32_e32 v18, v12
	s_nop 0
	v_fma_f32 v20, -v12, v18, 1.0
	v_fmac_f32_e32 v18, v20, v18
	v_div_fixup_f32 v12, v18, v12, 1.0

; __device__ __forceinline__ float sigmoidf_(float x) { return 1.f / (1.f + __expf(-x)); }
;     __device__ __forceinline__ void operator()(const f32x4 (&acc)[2][2][4][2], const Unit& u, int wr, int wc, int fr, int fq) const {
;     ...
;                     for (int e = 0; e < 8; ++e) { float x = (e < 4) ? v0[e & 3] : v1[e & 3];
;                         if (kind == 0) x = -0.6065306597126334f * sigmoidf_(x);
;                         else if (kind == 1) x = sigmoidf_(x);
;                         o[e] = x; }
.LBB0_1252:
	v_mul_f32_e32 v12, 0xbfb8aa3b, v16
	v_exp_f32_e32 v12, v12
	s_nop 0
	v_add_f32_e32 v12, 1.0, v12
	v_rcp_f32_e32 v17, v12
	s_nop 0
	v_fma_f32 v19, -v12, v17, 1.0
	v_fmac_f32_e32 v17, v19, v17
	v_div_fixup_f32 v12, v17, v12, 1.0
	v_mul_f32_e32 v12, 0xbf1b4598, v12
.LBB0_1253:
	v_add_f32_e32 v16, v13, v69
	s_and_b64 vcc, exec, s[2:3]
	s_mov_b64 s[4:5], -1
	s_cbranch_vccnz .LBB0_1257
	s_and_b64 vcc, exec, s[0:1]
	v_mov_b32_e32 v13, v16
	s_cbranch_vccnz .LBB0_1256
	v_mul_f32_e32 v13, 0xbfb8aa3b, v16
	v_exp_f32_e32 v13, v13
	s_nop 0
	v_add_f32_e32 v13, 1.0, v13
	v_rcp_f32_e32 v18, v13
	s_nop 0
	v_fma_f32 v20, -v13, v18, 1.0
	v_fmac_f32_e32 v18, v20, v18
	v_div_fixup_f32 v13, v18, v13, 1.0

; __device__ __forceinline__ float sigmoidf_(float x) { return 1.f / (1.f + __expf(-x)); }
;     __device__ __forceinline__ void operator()(const f32x4 (&acc)[2][2][4][2], const Unit& u, int wr, int wc, int fr, int fq) const {
;     ...
;                     for (int e = 0; e < 8; ++e) { float x = (e < 4) ? v0[e & 3] : v1[e & 3];
;                         if (kind == 0) x = -0.6065306597126334f * sigmoidf_(x);
;                         else if (kind == 1) x = sigmoidf_(x);
;                         o[e] = x; }
.LBB0_1258:
	v_mul_f32_e32 v13, 0xbfb8aa3b, v16
	v_exp_f32_e32 v13, v13
	s_nop 0
	v_add_f32_e32 v13, 1.0, v13
	v_rcp_f32_e32 v17, v13
	s_nop 0
	v_fma_f32 v19, -v13, v17, 1.0
	v_fmac_f32_e32 v17, v19, v17
	v_div_fixup_f32 v13, v17, v13, 1.0
	v_mul_f32_e32 v13, 0xbf1b4598, v13
.LBB0_1259:
	v_add_f32_e32 v16, v14, v70
	s_and_b64 vcc, exec, s[2:3]
	s_mov_b64 s[4:5], -1
	s_cbranch_vccnz .LBB0_1263
	s_and_b64 vcc, exec, s[0:1]
	v_mov_b32_e32 v14, v16
	s_cbranch_vccnz .LBB0_1262
	v_mul_f32_e32 v14, 0xbfb8aa3b, v16
	v_exp_f32_e32 v14, v14
	s_nop 0
	v_add_f32_e32 v14, 1.0, v14
	v_rcp_f32_e32 v18, v14
	s_nop 0
	v_fma_f32 v20, -v14, v18, 1.0
	v_fmac_f32_e32 v18, v20, v18
	v_div_fixup_f32 v14, v18, v14, 1.0

; __device__ __forceinline__ float sigmoidf_(float x) { return 1.f / (1.f + __expf(-x)); }
;     __device__ __forceinline__ void operator()(const f32x4 (&acc)[2][2][4][2], const Unit& u, int wr, int wc, int fr, int fq) const {
;     ...
;                     for (int e = 0; e < 8; ++e) { float x = (e < 4) ? v0[e & 3] : v1[e & 3];
;                         if (kind == 0) x = -0.6065306597126334f * sigmoidf_(x);
;                         else if (kind == 1) x = sigmoidf_(x);
;                         o[e] = x; }
.LBB0_1264:
	v_mul_f32_e32 v14, 0xbfb8aa3b, v16
	v_exp_f32_e32 v14, v14
	s_nop 0
	v_add_f32_e32 v14, 1.0, v14
	v_rcp_f32_e32 v17, v14
	s_nop 0
	v_fma_f32 v19, -v14, v17, 1.0
	v_fmac_f32_e32 v17, v19, v17
	v_div_fixup_f32 v14, v17, v14, 1.0
	v_mul_f32_e32 v14, 0xbf1b4598, v14
.LBB0_1265:
	v_add_f32_e32 v16, v15, v71
	s_and_b64 vcc, exec, s[2:3]
	s_mov_b64 s[4:5], -1
	s_cbranch_vccnz .LBB0_1269
	s_and_b64 vcc, exec, s[0:1]
	v_mov_b32_e32 v15, v16
	s_cbranch_vccnz .LBB0_1268
	v_mul_f32_e32 v15, 0xbfb8aa3b, v16
	v_exp_f32_e32 v15, v15
	s_nop 0
	v_add_f32_e32 v15, 1.0, v15
	v_rcp_f32_e32 v18, v15
	s_nop 0
	v_fma_f32 v20, -v15, v18, 1.0
	v_fmac_f32_e32 v18, v20, v18
	v_div_fixup_f32 v15, v18, v15, 1.0

; __device__ __forceinline__ float sigmoidf_(float x) { return 1.f / (1.f + __expf(-x)); }
;     __device__ __forceinline__ void operator()(const f32x4 (&acc)[2][2][4][2], const Unit& u, int wr, int wc, int fr, int fq) const {
;     ...
;                     for (int e = 0; e < 8; ++e) { float x = (e < 4) ? v0[e & 3] : v1[e & 3];
;                         if (kind == 0) x = -0.6065306597126334f * sigmoidf_(x);
;                         else if (kind == 1) x = sigmoidf_(x);
;                         o[e] = x; }
.LBB0_1270:
	v_mul_f32_e32 v15, 0xbfb8aa3b, v16
	v_exp_f32_e32 v15, v15
	s_nop 0
	v_add_f32_e32 v15, 1.0, v15
	v_rcp_f32_e32 v17, v15
	s_nop 0
	v_fma_f32 v19, -v15, v17, 1.0
	v_fmac_f32_e32 v17, v19, v17
	v_div_fixup_f32 v15, v17, v15, 1.0
	v_mul_f32_e32 v15, 0xbf1b4598, v15
.LBB0_1271:
	v_add_f32_e32 v16, v8, v64
	s_and_b64 vcc, exec, s[2:3]
	s_mov_b64 s[4:5], -1
	s_cbranch_vccnz .LBB0_1275
	s_and_b64 vcc, exec, s[0:1]
	v_mov_b32_e32 v8, v16
	s_cbranch_vccnz .LBB0_1274
	v_mul_f32_e32 v8, 0xbfb8aa3b, v16
	v_exp_f32_e32 v8, v8
	s_nop 0
	v_add_f32_e32 v8, 1.0, v8
	v_rcp_f32_e32 v18, v8
	s_nop 0
	v_fma_f32 v20, -v8, v18, 1.0
	v_fmac_f32_e32 v18, v20, v18
	v_div_fixup_f32 v8, v18, v8, 1.0

; __device__ __forceinline__ float sigmoidf_(float x) { return 1.f / (1.f + __expf(-x)); }
;     __device__ __forceinline__ void operator()(const f32x4 (&acc)[2][2][4][2], const Unit& u, int wr, int wc, int fr, int fq) const {
;     ...
;                     for (int e = 0; e < 8; ++e) { float x = (e < 4) ? v0[e & 3] : v1[e & 3];
;                         if (kind == 0) x = -0.6065306597126334f * sigmoidf_(x);
;                         else if (kind == 1) x = sigmoidf_(x);
;                         o[e] = x; }
.LBB0_1276:
	v_mul_f32_e32 v8, 0xbfb8aa3b, v16
	v_exp_f32_e32 v8, v8
	s_nop 0
	v_add_f32_e32 v8, 1.0, v8
	v_rcp_f32_e32 v17, v8
	s_nop 0
	v_fma_f32 v19, -v8, v17, 1.0
	v_fmac_f32_e32 v17, v19, v17
	v_div_fixup_f32 v8, v17, v8, 1.0
	v_mul_f32_e32 v8, 0xbf1b4598, v8
.LBB0_1277:
	v_add_f32_e32 v16, v9, v65
	s_and_b64 vcc, exec, s[2:3]
	s_mov_b64 s[4:5], -1
	s_cbranch_vccnz .LBB0_1281
	s_and_b64 vcc, exec, s[0:1]
	v_mov_b32_e32 v9, v16
	s_cbranch_vccnz .LBB0_1280
	v_mul_f32_e32 v9, 0xbfb8aa3b, v16
	v_exp_f32_e32 v9, v9
	s_nop 0
	v_add_f32_e32 v9, 1.0, v9
	v_rcp_f32_e32 v18, v9
	s_nop 0
	v_fma_f32 v20, -v9, v18, 1.0
	v_fmac_f32_e32 v18, v20, v18
	v_div_fixup_f32 v9, v18, v9, 1.0

; __device__ __forceinline__ float sigmoidf_(float x) { return 1.f / (1.f + __expf(-x)); }
;     __device__ __forceinline__ void operator()(const f32x4 (&acc)[2][2][4][2], const Unit& u, int wr, int wc, int fr, int fq) const {
;     ...
;                     for (int e = 0; e < 8; ++e) { float x = (e < 4) ? v0[e & 3] : v1[e & 3];
;                         if (kind == 0) x = -0.6065306597126334f * sigmoidf_(x);
;                         else if (kind == 1) x = sigmoidf_(x);
;                         o[e] = x; }
.LBB0_1282:
	v_mul_f32_e32 v9, 0xbfb8aa3b, v16
	v_exp_f32_e32 v9, v9
	s_nop 0
	v_add_f32_e32 v9, 1.0, v9
	v_rcp_f32_e32 v17, v9
	s_nop 0
	v_fma_f32 v19, -v9, v17, 1.0
	v_fmac_f32_e32 v17, v19, v17
	v_div_fixup_f32 v9, v17, v9, 1.0
	v_mul_f32_e32 v9, 0xbf1b4598, v9
.LBB0_1283:
	v_add_f32_e32 v16, v10, v66
	s_and_b64 vcc, exec, s[2:3]
	s_mov_b64 s[4:5], -1
	s_cbranch_vccnz .LBB0_1287
	s_and_b64 vcc, exec, s[0:1]
	v_mov_b32_e32 v10, v16
	s_cbranch_vccnz .LBB0_1286
	v_mul_f32_e32 v10, 0xbfb8aa3b, v16
	v_exp_f32_e32 v10, v10
	s_nop 0
	v_add_f32_e32 v10, 1.0, v10
	v_rcp_f32_e32 v18, v10
	s_nop 0
	v_fma_f32 v20, -v10, v18, 1.0
	v_fmac_f32_e32 v18, v20, v18
	v_div_fixup_f32 v10, v18, v10, 1.0

; __device__ __forceinline__ float sigmoidf_(float x) { return 1.f / (1.f + __expf(-x)); }
;     __device__ __forceinline__ void operator()(const f32x4 (&acc)[2][2][4][2], const Unit& u, int wr, int wc, int fr, int fq) const {
;     ...
;                     for (int e = 0; e < 8; ++e) { float x = (e < 4) ? v0[e & 3] : v1[e & 3];
;                         if (kind == 0) x = -0.6065306597126334f * sigmoidf_(x);
;                         else if (kind == 1) x = sigmoidf_(x);
;                         o[e] = x; }
.LBB0_1288:
	v_mul_f32_e32 v10, 0xbfb8aa3b, v16
	v_exp_f32_e32 v10, v10
	s_nop 0
	v_add_f32_e32 v10, 1.0, v10
	v_rcp_f32_e32 v17, v10
	s_nop 0
	v_fma_f32 v19, -v10, v17, 1.0
	v_fmac_f32_e32 v17, v19, v17
	v_div_fixup_f32 v10, v17, v10, 1.0
	v_mul_f32_e32 v10, 0xbf1b4598, v10
.LBB0_1289:
	v_add_f32_e32 v11, v11, v67
	s_and_b64 vcc, exec, s[2:3]
	s_mov_b64 s[4:5], -1
	s_cbranch_vccnz .LBB0_1293
	s_and_b64 vcc, exec, s[0:1]
	v_mov_b32_e32 v16, v11
	s_cbranch_vccnz .LBB0_1292
	v_mul_f32_e32 v16, 0xbfb8aa3b, v11
	v_exp_f32_e32 v16, v16
	s_nop 0
	v_add_f32_e32 v16, 1.0, v16
	v_rcp_f32_e32 v18, v16
	s_nop 0
	v_fma_f32 v20, -v16, v18, 1.0
	v_fmac_f32_e32 v18, v20, v18
	v_div_fixup_f32 v16, v18, v16, 1.0

; __device__ __forceinline__ unsigned cvt_pk_bf16(float lo, float hi) { const f32x2c v = {lo, hi}; const bf16x2c b = __builtin_convertvector(v, bf16x2c); return __builtin_bit_cast(unsigned, b); }
; __device__ __forceinline__ float sigmoidf_(float x) { return 1.f / (1.f + __expf(-x)); }
;     __device__ __forceinline__ void operator()(const f32x4 (&acc)[2][2][4][2], const Unit& u, int wr, int wc, int fr, int fq) const {
;     ...
;                     const f32x4 v0 = acc[ai][bj][m][0] + b0, v1 = acc[ai][bj][m][1] + b1; float o[8];
; #pragma unroll
;                     for (int e = 0; e < 8; ++e) { float x = (e < 4) ? v0[e & 3] : v1[e & 3];
;                         if (kind == 0) x = -0.6065306597126334f * sigmoidf_(x);
;                         else if (kind == 1) x = sigmoidf_(x);
;                         o[e] = x; }
;                     u32x4 w; w.x = cvt_pk_bf16(o[0], o[1]); w.y = cvt_pk_bf16(o[2], o[3]); w.z = cvt_pk_bf16(o[4], o[5]); w.w = cvt_pk_bf16(o[6], o[7]);
;                     *(u32x4*)(O + row * 512 + col) = w; } }
.LBB0_1294:
	v_mul_f32_e32 v11, 0xbfb8aa3b, v11
	v_exp_f32_e32 v11, v11
	s_nop 0
	v_add_f32_e32 v11, 1.0, v11
	v_rcp_f32_e32 v17, v11
	s_nop 0
	v_fma_f32 v19, -v11, v17, 1.0
	v_fmac_f32_e32 v17, v19, v17
	v_div_fixup_f32 v11, v17, v11, 1.0
	v_mul_f32_e32 v16, 0xbf1b4598, v11
.LBB0_1295:
	s_mov_b64 s[4:5], 0x28000
	v_lshl_add_u64 v[18:19], v[72:73], 0, s[4:5]
	v_cvt_pk_bf16_f32 v12, v12, v13
	v_cvt_pk_bf16_f32 v13, v14, v15
	v_cvt_pk_bf16_f32 v14, v8, v9
	v_cvt_pk_bf16_f32 v15, v10, v16
	v_add_f32_e32 v8, v4, v68
	s_and_b64 vcc, exec, s[2:3]
	s_mov_b64 s[4:5], -1
	global_store_dwordx4 v[18:19], v[12:15], off offset:256
	s_cbranch_vccnz .LBB0_1299
	s_and_b64 vcc, exec, s[0:1]
	v_mov_b32_e32 v4, v8
	s_cbranch_vccnz .LBB0_1298
	v_mul_f32_e32 v4, 0xbfb8aa3b, v8
	v_exp_f32_e32 v4, v4
	s_nop 0
	v_add_f32_e32 v4, 1.0, v4
	v_rcp_f32_e32 v10, v4
	s_nop 0
	v_fma_f32 v12, -v4, v10, 1.0
	v_fmac_f32_e32 v10, v12, v10
	v_div_fixup_f32 v4, v10, v4, 1.0

; __device__ __forceinline__ float sigmoidf_(float x) { return 1.f / (1.f + __expf(-x)); }
;     __device__ __forceinline__ void operator()(const f32x4 (&acc)[2][2][4][2], const Unit& u, int wr, int wc, int fr, int fq) const {
;     ...
;                     for (int e = 0; e < 8; ++e) { float x = (e < 4) ? v0[e & 3] : v1[e & 3];
;                         if (kind == 0) x = -0.6065306597126334f * sigmoidf_(x);
;                         else if (kind == 1) x = sigmoidf_(x);
;                         o[e] = x; }
.LBB0_1300:
	v_mul_f32_e32 v4, 0xbfb8aa3b, v8
	v_exp_f32_e32 v4, v4
	s_nop 0
	v_add_f32_e32 v4, 1.0, v4
	v_rcp_f32_e32 v9, v4
	s_nop 0
	v_fma_f32 v11, -v4, v9, 1.0
	v_fmac_f32_e32 v9, v11, v9
	v_div_fixup_f32 v4, v9, v4, 1.0
	v_mul_f32_e32 v4, 0xbf1b4598, v4
.LBB0_1301:
	v_add_f32_e32 v8, v5, v69
	s_and_b64 vcc, exec, s[2:3]
	s_mov_b64 s[4:5], -1
	s_cbranch_vccnz .LBB0_1305
	s_and_b64 vcc, exec, s[0:1]
	v_mov_b32_e32 v5, v8
	s_cbranch_vccnz .LBB0_1304
	v_mul_f32_e32 v5, 0xbfb8aa3b, v8
	v_exp_f32_e32 v5, v5
	s_nop 0
	v_add_f32_e32 v5, 1.0, v5
	v_rcp_f32_e32 v10, v5
	s_nop 0
	v_fma_f32 v12, -v5, v10, 1.0
	v_fmac_f32_e32 v10, v12, v10
	v_div_fixup_f32 v5, v10, v5, 1.0

; __device__ __forceinline__ unsigned cvt_pk_bf16(float lo, float hi) { const f32x2c v = {lo, hi}; const bf16x2c b = __builtin_convertvector(v, bf16x2c); return __builtin_bit_cast(unsigned, b); }
; __device__ __forceinline__ float sigmoidf_(float x) { return 1.f / (1.f + __expf(-x)); }
;     __device__ __forceinline__ void operator()(const f32x4 (&acc)[2][2][4][2], const Unit& u, int wr, int wc, int fr, int fq) const {
;     ...
;                 for (int m = 0; m < 4; ++m) { const size_t row = (size_t)(row0 + ai * HALF + m * 16);
;                     const f32x4 v0 = acc[ai][bj][m][0] + b0, v1 = acc[ai][bj][m][1] + b1; float o[8];
; #pragma unroll
;                     for (int e = 0; e < 8; ++e) { float x = (e < 4) ? v0[e & 3] : v1[e & 3];
;                         if (kind == 0) x = -0.6065306597126334f * sigmoidf_(x);
;                         else if (kind == 1) x = sigmoidf_(x);
;                         o[e] = x; }
;                     u32x4 w; w.x = cvt_pk_bf16(o[0], o[1]); w.y = cvt_pk_bf16(o[2], o[3]); w.z = cvt_pk_bf16(o[4], o[5]); w.w = cvt_pk_bf16(o[6], o[7]);
;                     *(u32x4*)(O + row * 512 + col) = w; } }
.LBB0_1306:
	v_mul_f32_e32 v5, 0xbfb8aa3b, v8
	v_exp_f32_e32 v5, v5
	s_nop 0
	v_add_f32_e32 v5, 1.0, v5
	v_rcp_f32_e32 v9, v5
	s_nop 0
	v_fma_f32 v11, -v5, v9, 1.0
	v_fmac_f32_e32 v9, v11, v9
	v_div_fixup_f32 v5, v9, v5, 1.0
	v_mul_f32_e32 v5, 0xbf1b4598, v5
.LBB0_1307:
	v_add_f32_e32 v8, v6, v70
	s_and_b64 vcc, exec, s[2:3]
	s_mov_b64 s[4:5], -1
	s_cbranch_vccnz .LBB0_1311
	s_and_b64 vcc, exec, s[0:1]
	v_mov_b32_e32 v6, v8
	s_cbranch_vccnz .LBB0_1310
	v_mul_f32_e32 v6, 0xbfb8aa3b, v8
	v_exp_f32_e32 v6, v6
	s_nop 0
	v_add_f32_e32 v6, 1.0, v6
	v_rcp_f32_e32 v10, v6
	s_nop 0
	v_fma_f32 v12, -v6, v10, 1.0
	v_fmac_f32_e32 v10, v12, v10
	v_div_fixup_f32 v6, v10, v6, 1.0

; __device__ __forceinline__ unsigned cvt_pk_bf16(float lo, float hi) { const f32x2c v = {lo, hi}; const bf16x2c b = __builtin_convertvector(v, bf16x2c); return __builtin_bit_cast(unsigned, b); }
; __device__ __forceinline__ float sigmoidf_(float x) { return 1.f / (1.f + __expf(-x)); }
;     __device__ __forceinline__ void operator()(const f32x4 (&acc)[2][2][4][2], const Unit& u, int wr, int wc, int fr, int fq) const {
;     ...
;                 for (int m = 0; m < 4; ++m) { const size_t row = (size_t)(row0 + ai * HALF + m * 16);
;                     const f32x4 v0 = acc[ai][bj][m][0] + b0, v1 = acc[ai][bj][m][1] + b1; float o[8];
; #pragma unroll
;                     for (int e = 0; e < 8; ++e) { float x = (e < 4) ? v0[e & 3] : v1[e & 3];
;                         if (kind == 0) x = -0.6065306597126334f * sigmoidf_(x);
;                         else if (kind == 1) x = sigmoidf_(x);
;                         o[e] = x; }
;                     u32x4 w; w.x = cvt_pk_bf16(o[0], o[1]); w.y = cvt_pk_bf16(o[2], o[3]); w.z = cvt_pk_bf16(o[4], o[5]); w.w = cvt_pk_bf16(o[6], o[7]);
;                     *(u32x4*)(O + row * 512 + col) = w; } }
.LBB0_1312:
	v_mul_f32_e32 v6, 0xbfb8aa3b, v8
	v_exp_f32_e32 v6, v6
	s_nop 0
	v_add_f32_e32 v6, 1.0, v6
	v_rcp_f32_e32 v9, v6
	s_nop 0
	v_fma_f32 v11, -v6, v9, 1.0
	v_fmac_f32_e32 v9, v11, v9
	v_div_fixup_f32 v6, v9, v6, 1.0
	v_mul_f32_e32 v6, 0xbf1b4598, v6
.LBB0_1313:
	v_add_f32_e32 v8, v7, v71
	s_and_b64 vcc, exec, s[2:3]
	s_mov_b64 s[4:5], -1
	s_cbranch_vccnz .LBB0_1317
	s_and_b64 vcc, exec, s[0:1]
	v_mov_b32_e32 v7, v8
	s_cbranch_vccnz .LBB0_1316
	v_mul_f32_e32 v7, 0xbfb8aa3b, v8
	v_exp_f32_e32 v7, v7
	s_nop 0
	v_add_f32_e32 v7, 1.0, v7
	v_rcp_f32_e32 v10, v7
	s_nop 0
	v_fma_f32 v12, -v7, v10, 1.0
	v_fmac_f32_e32 v10, v12, v10
	v_div_fixup_f32 v7, v10, v7, 1.0

; __device__ __forceinline__ unsigned cvt_pk_bf16(float lo, float hi) { const f32x2c v = {lo, hi}; const bf16x2c b = __builtin_convertvector(v, bf16x2c); return __builtin_bit_cast(unsigned, b); }
; __device__ __forceinline__ float sigmoidf_(float x) { return 1.f / (1.f + __expf(-x)); }
;     __device__ __forceinline__ void operator()(const f32x4 (&acc)[2][2][4][2], const Unit& u, int wr, int wc, int fr, int fq) const {
;     ...
;                 for (int m = 0; m < 4; ++m) { const size_t row = (size_t)(row0 + ai * HALF + m * 16);
;                     const f32x4 v0 = acc[ai][bj][m][0] + b0, v1 = acc[ai][bj][m][1] + b1; float o[8];
; #pragma unroll
;                     for (int e = 0; e < 8; ++e) { float x = (e < 4) ? v0[e & 3] : v1[e & 3];
;                         if (kind == 0) x = -0.6065306597126334f * sigmoidf_(x);
;                         else if (kind == 1) x = sigmoidf_(x);
;                         o[e] = x; }
;                     u32x4 w; w.x = cvt_pk_bf16(o[0], o[1]); w.y = cvt_pk_bf16(o[2], o[3]); w.z = cvt_pk_bf16(o[4], o[5]); w.w = cvt_pk_bf16(o[6], o[7]);
;                     *(u32x4*)(O + row * 512 + col) = w; } }
.LBB0_1318:
	v_mul_f32_e32 v7, 0xbfb8aa3b, v8
	v_exp_f32_e32 v7, v7
	s_nop 0
	v_add_f32_e32 v7, 1.0, v7
	v_rcp_f32_e32 v9, v7
	s_nop 0
	v_fma_f32 v11, -v7, v9, 1.0
	v_fmac_f32_e32 v9, v11, v9
	v_div_fixup_f32 v7, v9, v7, 1.0
	v_mul_f32_e32 v7, 0xbf1b4598, v7
.LBB0_1319:
	v_add_f32_e32 v8, v0, v64
	s_and_b64 vcc, exec, s[2:3]
	s_mov_b64 s[4:5], -1
	s_cbranch_vccnz .LBB0_1323
	s_and_b64 vcc, exec, s[0:1]
	v_mov_b32_e32 v0, v8
	s_cbranch_vccnz .LBB0_1322
	v_mul_f32_e32 v0, 0xbfb8aa3b, v8
	v_exp_f32_e32 v0, v0
	s_nop 0
	v_add_f32_e32 v0, 1.0, v0
	v_rcp_f32_e32 v10, v0
	s_nop 0
	v_fma_f32 v12, -v0, v10, 1.0
	v_fmac_f32_e32 v10, v12, v10
	v_div_fixup_f32 v0, v10, v0, 1.0

; __device__ __forceinline__ unsigned cvt_pk_bf16(float lo, float hi) { const f32x2c v = {lo, hi}; const bf16x2c b = __builtin_convertvector(v, bf16x2c); return __builtin_bit_cast(unsigned, b); }
; __device__ __forceinline__ float sigmoidf_(float x) { return 1.f / (1.f + __expf(-x)); }
;     __device__ __forceinline__ void operator()(const f32x4 (&acc)[2][2][4][2], const Unit& u, int wr, int wc, int fr, int fq) const {
;     ...
;                 for (int m = 0; m < 4; ++m) { const size_t row = (size_t)(row0 + ai * HALF + m * 16);
;                     const f32x4 v0 = acc[ai][bj][m][0] + b0, v1 = acc[ai][bj][m][1] + b1; float o[8];
; #pragma unroll
;                     for (int e = 0; e < 8; ++e) { float x = (e < 4) ? v0[e & 3] : v1[e & 3];
;                         if (kind == 0) x = -0.6065306597126334f * sigmoidf_(x);
;                         else if (kind == 1) x = sigmoidf_(x);
;                         o[e] = x; }
;                     u32x4 w; w.x = cvt_pk_bf16(o[0], o[1]); w.y = cvt_pk_bf16(o[2], o[3]); w.z = cvt_pk_bf16(o[4], o[5]); w.w = cvt_pk_bf16(o[6], o[7]);
;                     *(u32x4*)(O + row * 512 + col) = w; } }
.LBB0_1324:
	v_mul_f32_e32 v0, 0xbfb8aa3b, v8
	v_exp_f32_e32 v0, v0
	s_nop 0
	v_add_f32_e32 v0, 1.0, v0
	v_rcp_f32_e32 v9, v0
	s_nop 0
	v_fma_f32 v11, -v0, v9, 1.0
	v_fmac_f32_e32 v9, v11, v9
	v_div_fixup_f32 v0, v9, v0, 1.0
	v_mul_f32_e32 v0, 0xbf1b4598, v0
.LBB0_1325:
	v_add_f32_e32 v8, v1, v65
	s_and_b64 vcc, exec, s[2:3]
	s_mov_b64 s[4:5], -1
	s_cbranch_vccnz .LBB0_1329
	s_and_b64 vcc, exec, s[0:1]
	v_mov_b32_e32 v1, v8
	s_cbranch_vccnz .LBB0_1328
	v_mul_f32_e32 v1, 0xbfb8aa3b, v8
	v_exp_f32_e32 v1, v1
	s_nop 0
	v_add_f32_e32 v1, 1.0, v1
	v_rcp_f32_e32 v10, v1
	s_nop 0
	v_fma_f32 v12, -v1, v10, 1.0
	v_fmac_f32_e32 v10, v12, v10
	v_div_fixup_f32 v1, v10, v1, 1.0

; __device__ __forceinline__ unsigned cvt_pk_bf16(float lo, float hi) { const f32x2c v = {lo, hi}; const bf16x2c b = __builtin_convertvector(v, bf16x2c); return __builtin_bit_cast(unsigned, b); }
; __device__ __forceinline__ float sigmoidf_(float x) { return 1.f / (1.f + __expf(-x)); }
;     __device__ __forceinline__ void operator()(const f32x4 (&acc)[2][2][4][2], const Unit& u, int wr, int wc, int fr, int fq) const {
;     ...
;                 for (int m = 0; m < 4; ++m) { const size_t row = (size_t)(row0 + ai * HALF + m * 16);
;                     const f32x4 v0 = acc[ai][bj][m][0] + b0, v1 = acc[ai][bj][m][1] + b1; float o[8];
; #pragma unroll
;                     for (int e = 0; e < 8; ++e) { float x = (e < 4) ? v0[e & 3] : v1[e & 3];
;                         if (kind == 0) x = -0.6065306597126334f * sigmoidf_(x);
;                         else if (kind == 1) x = sigmoidf_(x);
;                         o[e] = x; }
;                     u32x4 w; w.x = cvt_pk_bf16(o[0], o[1]); w.y = cvt_pk_bf16(o[2], o[3]); w.z = cvt_pk_bf16(o[4], o[5]); w.w = cvt_pk_bf16(o[6], o[7]);
;                     *(u32x4*)(O + row * 512 + col) = w; } }
.LBB0_1330:
	v_mul_f32_e32 v1, 0xbfb8aa3b, v8
	v_exp_f32_e32 v1, v1
	s_nop 0
	v_add_f32_e32 v1, 1.0, v1
	v_rcp_f32_e32 v9, v1
	s_nop 0
	v_fma_f32 v11, -v1, v9, 1.0
	v_fmac_f32_e32 v9, v11, v9
	v_div_fixup_f32 v1, v9, v1, 1.0
	v_mul_f32_e32 v1, 0xbf1b4598, v1
.LBB0_1331:
	v_add_f32_e32 v8, v2, v66
	s_and_b64 vcc, exec, s[2:3]
	s_mov_b64 s[4:5], -1
	s_cbranch_vccnz .LBB0_1335
	s_and_b64 vcc, exec, s[0:1]
	v_mov_b32_e32 v2, v8
	s_cbranch_vccnz .LBB0_1334
	v_mul_f32_e32 v2, 0xbfb8aa3b, v8
	v_exp_f32_e32 v2, v2
	s_nop 0
	v_add_f32_e32 v2, 1.0, v2
	v_rcp_f32_e32 v10, v2
	s_nop 0
	v_fma_f32 v12, -v2, v10, 1.0
	v_fmac_f32_e32 v10, v12, v10
	v_div_fixup_f32 v2, v10, v2, 1.0

; __device__ __forceinline__ unsigned cvt_pk_bf16(float lo, float hi) { const f32x2c v = {lo, hi}; const bf16x2c b = __builtin_convertvector(v, bf16x2c); return __builtin_bit_cast(unsigned, b); }
; __device__ __forceinline__ float sigmoidf_(float x) { return 1.f / (1.f + __expf(-x)); }
;     __device__ __forceinline__ void operator()(const f32x4 (&acc)[2][2][4][2], const Unit& u, int wr, int wc, int fr, int fq) const {
;     ...
;                 for (int m = 0; m < 4; ++m) { const size_t row = (size_t)(row0 + ai * HALF + m * 16);
;                     const f32x4 v0 = acc[ai][bj][m][0] + b0, v1 = acc[ai][bj][m][1] + b1; float o[8];
; #pragma unroll
;                     for (int e = 0; e < 8; ++e) { float x = (e < 4) ? v0[e & 3] : v1[e & 3];
;                         if (kind == 0) x = -0.6065306597126334f * sigmoidf_(x);
;                         else if (kind == 1) x = sigmoidf_(x);
;                         o[e] = x; }
;                     u32x4 w; w.x = cvt_pk_bf16(o[0], o[1]); w.y = cvt_pk_bf16(o[2], o[3]); w.z = cvt_pk_bf16(o[4], o[5]); w.w = cvt_pk_bf16(o[6], o[7]);
;                     *(u32x4*)(O + row * 512 + col) = w; } }
.LBB0_1336:
	v_mul_f32_e32 v2, 0xbfb8aa3b, v8
	v_exp_f32_e32 v2, v2
	s_nop 0
	v_add_f32_e32 v2, 1.0, v2
	v_rcp_f32_e32 v9, v2
	s_nop 0
	v_fma_f32 v11, -v2, v9, 1.0
	v_fmac_f32_e32 v9, v11, v9
	v_div_fixup_f32 v2, v9, v2, 1.0
	v_mul_f32_e32 v2, 0xbf1b4598, v2
.LBB0_1337:
	v_add_f32_e32 v3, v3, v67
	s_and_b64 vcc, exec, s[2:3]
	s_mov_b64 s[2:3], -1
	s_cbranch_vccnz .LBB0_1341
	s_and_b64 vcc, exec, s[0:1]
	v_mov_b32_e32 v8, v3
	s_cbranch_vccnz .LBB0_1340
	v_mul_f32_e32 v8, 0xbfb8aa3b, v3
	v_exp_f32_e32 v8, v8
	s_nop 0
	v_add_f32_e32 v8, 1.0, v8
	v_rcp_f32_e32 v10, v8
	s_nop 0
	v_fma_f32 v12, -v8, v10, 1.0
	v_fmac_f32_e32 v10, v12, v10
	v_div_fixup_f32 v8, v10, v8, 1.0

; __device__ __forceinline__ unsigned cvt_pk_bf16(float lo, float hi) { const f32x2c v = {lo, hi}; const bf16x2c b = __builtin_convertvector(v, bf16x2c); return __builtin_bit_cast(unsigned, b); }
; __device__ __forceinline__ float sigmoidf_(float x) { return 1.f / (1.f + __expf(-x)); }
;     __device__ __forceinline__ void operator()(const f32x4 (&acc)[2][2][4][2], const Unit& u, int wr, int wc, int fr, int fq) const {
;     ...
;                 for (int m = 0; m < 4; ++m) { const size_t row = (size_t)(row0 + ai * HALF + m * 16);
;                     const f32x4 v0 = acc[ai][bj][m][0] + b0, v1 = acc[ai][bj][m][1] + b1; float o[8];
; #pragma unroll
;                     for (int e = 0; e < 8; ++e) { float x = (e < 4) ? v0[e & 3] : v1[e & 3];
;                         if (kind == 0) x = -0.6065306597126334f * sigmoidf_(x);
;                         else if (kind == 1) x = sigmoidf_(x);
;                         o[e] = x; }
;                     u32x4 w; w.x = cvt_pk_bf16(o[0], o[1]); w.y = cvt_pk_bf16(o[2], o[3]); w.z = cvt_pk_bf16(o[4], o[5]); w.w = cvt_pk_bf16(o[6], o[7]);
;                     *(u32x4*)(O + row * 512 + col) = w; } }
.LBB0_1342:
	v_mul_f32_e32 v3, 0xbfb8aa3b, v3
	v_exp_f32_e32 v3, v3
	s_nop 0
	v_add_f32_e32 v3, 1.0, v3
	v_rcp_f32_e32 v9, v3
	s_nop 0
	v_fma_f32 v11, -v3, v9, 1.0
	v_fmac_f32_e32 v9, v11, v9
	v_div_fixup_f32 v3, v9, v3, 1.0
	v_mul_f32_e32 v8, 0xbf1b4598, v3

; __device__ __forceinline__ unsigned cvt_pk_bf16(float lo, float hi) { const f32x2c v = {lo, hi}; const bf16x2c b = __builtin_convertvector(v, bf16x2c); return __builtin_bit_cast(unsigned, b); }
; __device__ __forceinline__ float sigmoidf_(float x) { return 1.f / (1.f + __expf(-x)); }
; __device__ __forceinline__ float gelu_tanh(float x) { return x * sigmoidf_(1.5957691216057308f * (x + 0.044715f * x * x * x)); }
;     __device__ __forceinline__ void operator()(const f32x4 (&acc)[2][2][4][2], const Unit& u, int wr, int wc, int fr, int fq) const {
;     ...
;         for (int ai = 0; ai < 2; ++ai)
; #pragma unroll
;             for (int m = 0; m < 4; ++m) { const int row = row0 + ai * HALF + m * 16; const int g = row / S5R, rl = row % S5R;
; #pragma unroll
;                 for (int bj = 0; bj < 2; ++bj) { const int col = col0 + bj * HALF;
;                     const u32x4 yi = *(const u32x4*)(YI + (size_t)row * 512 + col);
;                     const unsigned yw[4] = {yi.x, yi.y, yi.z, yi.w};
;                     const f32x4 v0 = acc[ai][bj][m][0], v1 = acc[ai][bj][m][1];
;                     float o[8];
; #pragma unroll
;                     for (int q = 0; q < 4; ++q) { const float al = (q < 2) ? v0[2 * q] : v1[2 * q - 4], ah = (q < 2) ? v0[2 * q + 1] : v1[2 * q - 3];
;                         o[2 * q] = gelu_tanh(al + __builtin_bit_cast(float, yw[q] << 16)); o[2 * q + 1] = gelu_tanh(ah + __builtin_bit_cast(float, yw[q] & 0xffff0000u)); }
;                     u32x4 w; w.x = cvt_pk_bf16(o[0], o[1]); w.y = cvt_pk_bf16(o[2], o[3]); w.z = cvt_pk_bf16(o[4], o[5]); w.w = cvt_pk_bf16(o[6], o[7]);
;                     const size_t tok = (size_t)rl * S5L + (col >> 4);
;                     *(u32x4*)(Z + tok * 512 + g * 16 + (col & 15)) = w; } }
.LBB0_1895:
	v_lshl_add_u32 v142, s33, 8, v154
	v_ashrrev_i32_e32 v143, 31, v142
	v_lshrrev_b32_e32 v160, 21, v143
	v_add_u32_e32 v128, v142, v160
	v_ashrrev_i32_e32 v144, 11, v128
	v_mul_i32_i24_e32 v128, 0x800, v144
	v_lshl_or_b32 v146, s46, 8, v156
	v_sub_u32_e32 v128, v142, v128
	v_lshlrev_b64 v[130:131], 10, v[142:143]
	v_ashrrev_i32_e32 v129, 31, v128
	v_ashrrev_i32_e32 v147, 31, v146
	v_lshlrev_b64 v[150:151], 15, v[128:129]
	v_lshlrev_b32_e32 v148, 4, v144
	v_lshl_add_u64 v[128:129], s[30:31], 0, v[130:131]
	v_lshlrev_b64 v[144:145], 1, v[146:147]
	v_lshl_add_u64 v[152:153], v[128:129], 0, v[144:145]
	global_load_dwordx4 v[128:131], v[152:153], off
	v_ashrrev_i32_e32 v149, 31, v148
	v_readlane_b32 s86, v243, 25
	s_waitcnt vmcnt(0)
	v_lshlrev_b32_e32 v162, 16, v128
	v_and_b32_e32 v163, 0xffff0000, v128
	v_pk_add_f32 v[124:125], v[124:125], v[162:163]
	s_nop 0
	v_mul_f32_e32 v128, 0x3d372713, v124
	v_mul_f32_e32 v128, v124, v128
	v_fma_f32 v128, v124, v128, v124
	v_mul_f32_e32 v128, 0x3fcc422a, v128
	v_mul_f32_e32 v128, 0xbfb8aa3b, v128
	v_exp_f32_e32 v162, v128
	v_mul_f32_e32 v128, 0x3d372713, v125
	v_mul_f32_e32 v128, v125, v128
	v_fma_f32 v128, v125, v128, v125
	v_mul_f32_e32 v128, 0x3fcc422a, v128
	v_mul_f32_e32 v128, 0xbfb8aa3b, v128
	v_exp_f32_e32 v163, v128
	s_nop 0
	v_pk_add_f32 v[162:163], v[162:163], 1.0 op_sel_hi:[1,0]
	s_nop 0
	v_rcp_f32_e32 v143, v163
	s_nop 0
	v_fma_f32 v147, -v163, v143, 1.0
	v_fmac_f32_e32 v143, v147, v143
	v_div_fixup_f32 v163, v143, v163, 1.0
	v_rcp_f32_e32 v143, v162
	s_nop 0
	v_fma_f32 v147, -v162, v143, 1.0
	v_fmac_f32_e32 v143, v147, v143
	v_div_fixup_f32 v162, v143, v162, 1.0
	v_lshlrev_b32_e32 v128, 16, v129
	v_and_b32_e32 v129, 0xffff0000, v129
	v_pk_add_f32 v[126:127], v[126:127], v[128:129]
	v_pk_mul_f32 v[124:125], v[124:125], v[162:163]
	v_mul_f32_e32 v128, 0x3d372713, v126
	v_mul_f32_e32 v129, 0x3d372713, v127
	v_mul_f32_e32 v128, v126, v128
	v_mul_f32_e32 v129, v127, v129
	v_fma_f32 v128, v126, v128, v126
	v_fma_f32 v129, v127, v129, v127
	v_mul_f32_e32 v128, 0x3fcc422a, v128
	v_mul_f32_e32 v129, 0x3fcc422a, v129
	v_mul_f32_e32 v128, 0xbfb8aa3b, v128
	v_mul_f32_e32 v129, 0xbfb8aa3b, v129
	v_exp_f32_e32 v128, v128
	v_exp_f32_e32 v129, v129
	s_nop 0
	v_pk_add_f32 v[128:129], v[128:129], 1.0 op_sel_hi:[1,0]
	s_nop 0
	v_rcp_f32_e32 v147, v129
	s_nop 0
	v_fma_f32 v161, -v129, v147, 1.0
	v_fmac_f32_e32 v147, v161, v147
	v_div_fixup_f32 v129, v147, v129, 1.0
	v_rcp_f32_e32 v147, v128
	s_nop 0
	v_fma_f32 v161, -v128, v147, 1.0
	v_fmac_f32_e32 v147, v161, v147
	v_div_fixup_f32 v128, v147, v128, 1.0
	v_pk_mul_f32 v[126:127], v[126:127], v[128:129]
	v_lshlrev_b32_e32 v128, 16, v130
	v_and_b32_e32 v129, 0xffff0000, v130
	v_pk_add_f32 v[120:121], v[120:121], v[128:129]
	s_nop 0
	v_mul_f32_e32 v128, 0x3d372713, v120
	v_mul_f32_e32 v129, 0x3d372713, v121
	v_mul_f32_e32 v128, v120, v128
	v_mul_f32_e32 v129, v121, v129
	v_fma_f32 v128, v120, v128, v120
	v_fma_f32 v129, v121, v129, v121
	v_mul_f32_e32 v128, 0x3fcc422a, v128
	v_mul_f32_e32 v129, 0x3fcc422a, v129
	v_mul_f32_e32 v128, 0xbfb8aa3b, v128
	v_mul_f32_e32 v129, 0xbfb8aa3b, v129
	v_exp_f32_e32 v128, v128
	v_exp_f32_e32 v129, v129
	s_nop 0
	v_pk_add_f32 v[128:129], v[128:129], 1.0 op_sel_hi:[1,0]
	s_nop 0
	v_rcp_f32_e32 v143, v129
	s_nop 0
	v_fma_f32 v147, -v129, v143, 1.0
	v_fmac_f32_e32 v143, v147, v143
	v_div_fixup_f32 v129, v143, v129, 1.0
	v_rcp_f32_e32 v143, v128
	s_nop 0
	v_fma_f32 v147, -v128, v143, 1.0
	v_fmac_f32_e32 v143, v147, v143
	v_div_fixup_f32 v128, v143, v128, 1.0
	v_pk_mul_f32 v[128:129], v[120:121], v[128:129]
	v_lshlrev_b32_e32 v120, 16, v131
	v_and_b32_e32 v121, 0xffff0000, v131
	v_pk_add_f32 v[120:121], v[122:123], v[120:121]
	s_nop 0
	v_mul_f32_e32 v122, 0x3d372713, v120
	v_mul_f32_e32 v123, 0x3d372713, v121
	v_mul_f32_e32 v122, v120, v122
	v_mul_f32_e32 v123, v121, v123
	v_fma_f32 v122, v120, v122, v120
	v_fma_f32 v123, v121, v123, v121
	v_mul_f32_e32 v122, 0x3fcc422a, v122
	v_mul_f32_e32 v123, 0x3fcc422a, v123
	v_mul_f32_e32 v122, 0xbfb8aa3b, v122
	v_mul_f32_e32 v123, 0xbfb8aa3b, v123
	v_exp_f32_e32 v122, v122
	v_exp_f32_e32 v123, v123
	s_nop 0
	v_pk_add_f32 v[122:123], v[122:123], 1.0 op_sel_hi:[1,0]
	s_nop 0
	v_rcp_f32_e32 v131, v123
	s_nop 0
	v_fma_f32 v143, -v123, v131, 1.0
	v_fmac_f32_e32 v131, v143, v131
	v_div_fixup_f32 v123, v131, v123, 1.0
	v_rcp_f32_e32 v131, v122
	s_nop 0
	v_fma_f32 v143, -v122, v131, 1.0
	v_fmac_f32_e32 v131, v143, v131
	v_div_fixup_f32 v122, v131, v122, 1.0
	v_pk_mul_f32 v[130:131], v[120:121], v[122:123]
	v_cvt_pk_bf16_f32 v120, v124, v125
	v_ashrrev_i32_e32 v124, 4, v146
	v_ashrrev_i32_e32 v125, 31, v124
	v_cvt_pk_bf16_f32 v121, v126, v127
	v_lshl_add_u64 v[126:127], s[36:37], 0, v[150:151]
	v_lshlrev_b64 v[124:125], 10, v[124:125]
	v_cvt_pk_bf16_f32 v122, v128, v129
	v_cvt_pk_bf16_f32 v123, v130, v131
	v_lshl_add_u64 v[130:131], v[126:127], 0, v[124:125]
	v_lshlrev_b64 v[128:129], 1, v[148:149]
	v_lshl_add_u64 v[130:131], v[130:131], 0, v[128:129]
	v_lshl_add_u64 v[130:131], v[130:131], 0, v[140:141]
	global_store_dwordx4 v[130:131], v[120:123], off
	global_load_dwordx4 v[120:123], v[152:153], off offset:256
	v_or_b32_e32 v143, 0x80, v146
	s_waitcnt vmcnt(0)
; __device__ __forceinline__ unsigned cvt_pk_bf16(float lo, float hi) { const f32x2c v = {lo, hi}; const bf16x2c b = __builtin_convertvector(v, bf16x2c); return __builtin_bit_cast(unsigned, b); }
; __device__ __forceinline__ float sigmoidf_(float x) { return 1.f / (1.f + __expf(-x)); }
; __device__ __forceinline__ float gelu_tanh(float x) { return x * sigmoidf_(1.5957691216057308f * (x + 0.044715f * x * x * x)); }
;     __device__ __forceinline__ void operator()(const f32x4 (&acc)[2][2][4][2], const Unit& u, int wr, int wc, int fr, int fq) const {
;     ...
;         for (int ai = 0; ai < 2; ++ai)
; #pragma unroll
;             for (int m = 0; m < 4; ++m) { const int row = row0 + ai * HALF + m * 16; const int g = row / S5R, rl = row % S5R;
; #pragma unroll
;                 for (int bj = 0; bj < 2; ++bj) { const int col = col0 + bj * HALF;
;                     const u32x4 yi = *(const u32x4*)(YI + (size_t)row * 512 + col);
;                     const unsigned yw[4] = {yi.x, yi.y, yi.z, yi.w};
;                     const f32x4 v0 = acc[ai][bj][m][0], v1 = acc[ai][bj][m][1];
;                     float o[8];
; #pragma unroll
;                     for (int q = 0; q < 4; ++q) { const float al = (q < 2) ? v0[2 * q] : v1[2 * q - 4], ah = (q < 2) ? v0[2 * q + 1] : v1[2 * q - 3];
;                         o[2 * q] = gelu_tanh(al + __builtin_bit_cast(float, yw[q] << 16)); o[2 * q + 1] = gelu_tanh(ah + __builtin_bit_cast(float, yw[q] & 0xffff0000u)); }
;                     u32x4 w; w.x = cvt_pk_bf16(o[0], o[1]); w.y = cvt_pk_bf16(o[2], o[3]); w.z = cvt_pk_bf16(o[4], o[5]); w.w = cvt_pk_bf16(o[6], o[7]);
;                     const size_t tok = (size_t)rl * S5L + (col >> 4);
;                     *(u32x4*)(Z + tok * 512 + g * 16 + (col & 15)) = w; } }
	v_lshlrev_b32_e32 v130, 16, v120
	v_and_b32_e32 v131, 0xffff0000, v120
	v_pk_add_f32 v[116:117], v[116:117], v[130:131]
	s_nop 0
	v_mul_f32_e32 v120, 0x3d372713, v116
	v_mul_f32_e32 v120, v116, v120
	v_fma_f32 v120, v116, v120, v116
	v_mul_f32_e32 v120, 0x3fcc422a, v120
	v_mul_f32_e32 v120, 0xbfb8aa3b, v120
	v_exp_f32_e32 v130, v120
	v_mul_f32_e32 v120, 0x3d372713, v117
	v_mul_f32_e32 v120, v117, v120
	v_fma_f32 v120, v117, v120, v117
	v_mul_f32_e32 v120, 0x3fcc422a, v120
	v_mul_f32_e32 v120, 0xbfb8aa3b, v120
	v_exp_f32_e32 v131, v120
	s_nop 0
	v_pk_add_f32 v[130:131], v[130:131], 1.0 op_sel_hi:[1,0]
	s_nop 0
	v_rcp_f32_e32 v146, v131
	s_nop 0
	v_fma_f32 v147, -v131, v146, 1.0
	v_fmac_f32_e32 v146, v147, v146
	v_div_fixup_f32 v131, v146, v131, 1.0
	v_rcp_f32_e32 v146, v130
	s_nop 0
	v_fma_f32 v147, -v130, v146, 1.0
	v_fmac_f32_e32 v146, v147, v146
	v_div_fixup_f32 v130, v146, v130, 1.0
	v_lshlrev_b32_e32 v120, 16, v121
	v_and_b32_e32 v121, 0xffff0000, v121
	v_pk_add_f32 v[118:119], v[118:119], v[120:121]
	v_pk_mul_f32 v[116:117], v[116:117], v[130:131]
	v_mul_f32_e32 v120, 0x3d372713, v118
	v_mul_f32_e32 v121, 0x3d372713, v119
	v_mul_f32_e32 v120, v118, v120
	v_mul_f32_e32 v121, v119, v121
	v_fma_f32 v120, v118, v120, v118
	v_fma_f32 v121, v119, v121, v119
	v_mul_f32_e32 v120, 0x3fcc422a, v120
	v_mul_f32_e32 v121, 0x3fcc422a, v121
	v_mul_f32_e32 v120, 0xbfb8aa3b, v120
	v_mul_f32_e32 v121, 0xbfb8aa3b, v121
	v_exp_f32_e32 v120, v120
	v_exp_f32_e32 v121, v121
	s_nop 0
	v_pk_add_f32 v[120:121], v[120:121], 1.0 op_sel_hi:[1,0]
	s_nop 0
	v_rcp_f32_e32 v131, v121
	s_nop 0
	v_fma_f32 v146, -v121, v131, 1.0
	v_fmac_f32_e32 v131, v146, v131
	v_div_fixup_f32 v121, v131, v121, 1.0
	v_rcp_f32_e32 v131, v120
	s_nop 0
	v_fma_f32 v146, -v120, v131, 1.0
	v_fmac_f32_e32 v131, v146, v131
	v_div_fixup_f32 v120, v131, v120, 1.0
	v_pk_mul_f32 v[118:119], v[118:119], v[120:121]
	v_lshlrev_b32_e32 v120, 16, v122
	v_and_b32_e32 v121, 0xffff0000, v122
	v_pk_add_f32 v[112:113], v[112:113], v[120:121]
	s_nop 0
	v_mul_f32_e32 v120, 0x3d372713, v112
	v_mul_f32_e32 v121, 0x3d372713, v113
	v_mul_f32_e32 v120, v112, v120
	v_mul_f32_e32 v121, v113, v121
	v_fma_f32 v120, v112, v120, v112
	v_fma_f32 v121, v113, v121, v113
	v_mul_f32_e32 v120, 0x3fcc422a, v120
	v_mul_f32_e32 v121, 0x3fcc422a, v121
	v_mul_f32_e32 v120, 0xbfb8aa3b, v120
	v_mul_f32_e32 v121, 0xbfb8aa3b, v121
	v_exp_f32_e32 v120, v120
	v_exp_f32_e32 v121, v121
	s_nop 0
	v_pk_add_f32 v[120:121], v[120:121], 1.0 op_sel_hi:[1,0]
	s_nop 0
	v_rcp_f32_e32 v130, v121
	s_nop 0
	v_fma_f32 v131, -v121, v130, 1.0
	v_fmac_f32_e32 v130, v131, v130
	v_div_fixup_f32 v121, v130, v121, 1.0
	v_rcp_f32_e32 v130, v120
	s_nop 0
	v_fma_f32 v131, -v120, v130, 1.0
	v_fmac_f32_e32 v130, v131, v130
	v_div_fixup_f32 v120, v130, v120, 1.0
	v_pk_mul_f32 v[120:121], v[112:113], v[120:121]
	v_lshlrev_b32_e32 v112, 16, v123
	v_and_b32_e32 v113, 0xffff0000, v123
	v_pk_add_f32 v[112:113], v[114:115], v[112:113]
	s_nop 0
	v_mul_f32_e32 v114, 0x3d372713, v112
	v_mul_f32_e32 v115, 0x3d372713, v113
	v_mul_f32_e32 v114, v112, v114
	v_mul_f32_e32 v115, v113, v115
	v_fma_f32 v114, v112, v114, v112
	v_fma_f32 v115, v113, v115, v113
	v_mul_f32_e32 v114, 0x3fcc422a, v114
	v_mul_f32_e32 v115, 0x3fcc422a, v115
	v_mul_f32_e32 v114, 0xbfb8aa3b, v114
	v_mul_f32_e32 v115, 0xbfb8aa3b, v115
	v_exp_f32_e32 v114, v114
	v_exp_f32_e32 v115, v115
	s_nop 0
	v_pk_add_f32 v[114:115], v[114:115], 1.0 op_sel_hi:[1,0]
	s_nop 0
	v_rcp_f32_e32 v123, v115
	s_nop 0
	v_fma_f32 v130, -v115, v123, 1.0
	v_fmac_f32_e32 v123, v130, v123
	v_div_fixup_f32 v115, v123, v115, 1.0
	v_rcp_f32_e32 v123, v114
	s_nop 0
	v_fma_f32 v130, -v114, v123, 1.0
	v_fmac_f32_e32 v123, v130, v123
	v_div_fixup_f32 v114, v123, v114, 1.0
	v_pk_mul_f32 v[122:123], v[112:113], v[114:115]
	v_cvt_pk_bf16_f32 v112, v116, v117
	v_ashrrev_i32_e32 v116, 4, v143
	v_ashrrev_i32_e32 v117, 31, v116
	v_lshlrev_b64 v[116:117], 10, v[116:117]
	v_cvt_pk_bf16_f32 v113, v118, v119
	v_lshl_add_u64 v[118:119], v[126:127], 0, v[116:117]
	v_lshl_add_u64 v[118:119], v[118:119], 0, v[128:129]
	v_cvt_pk_bf16_f32 v114, v120, v121
	v_cvt_pk_bf16_f32 v115, v122, v123
	v_lshl_add_u64 v[118:119], v[118:119], 0, v[140:141]
	global_store_dwordx4 v[118:119], v[112:115], off
	s_nop 1
	v_or_b32_e32 v112, 16, v142
	v_add_u32_e32 v113, v112, v160
	v_ashrrev_i32_e32 v118, 11, v113
	v_mul_i32_i24_e32 v113, 0x800, v118
	v_sub_u32_e32 v114, v112, v113
	v_ashrrev_i32_e32 v113, 31, v112
	v_lshlrev_b64 v[112:113], 10, v[112:113]
	v_lshl_add_u64 v[112:113], s[30:31], 0, v[112:113]
	v_ashrrev_i32_e32 v115, 31, v114
	v_lshl_add_u64 v[122:123], v[112:113], 0, v[144:145]
	v_lshlrev_b64 v[120:121], 15, v[114:115]
	global_load_dwordx4 v[112:115], v[122:123], off
	v_lshlrev_b32_e32 v118, 4, v118
	v_ashrrev_i32_e32 v119, 31, v118
	s_waitcnt vmcnt(0)
; __device__ __forceinline__ unsigned cvt_pk_bf16(float lo, float hi) { const f32x2c v = {lo, hi}; const bf16x2c b = __builtin_convertvector(v, bf16x2c); return __builtin_bit_cast(unsigned, b); }
; __device__ __forceinline__ float sigmoidf_(float x) { return 1.f / (1.f + __expf(-x)); }
; __device__ __forceinline__ float gelu_tanh(float x) { return x * sigmoidf_(1.5957691216057308f * (x + 0.044715f * x * x * x)); }
;     __device__ __forceinline__ void operator()(const f32x4 (&acc)[2][2][4][2], const Unit& u, int wr, int wc, int fr, int fq) const {
;     ...
;         for (int ai = 0; ai < 2; ++ai)
; #pragma unroll
;             for (int m = 0; m < 4; ++m) { const int row = row0 + ai * HALF + m * 16; const int g = row / S5R, rl = row % S5R;
; #pragma unroll
;                 for (int bj = 0; bj < 2; ++bj) { const int col = col0 + bj * HALF;
;                     const u32x4 yi = *(const u32x4*)(YI + (size_t)row * 512 + col);
;                     const unsigned yw[4] = {yi.x, yi.y, yi.z, yi.w};
;                     const f32x4 v0 = acc[ai][bj][m][0], v1 = acc[ai][bj][m][1];
;                     float o[8];
; #pragma unroll
;                     for (int q = 0; q < 4; ++q) { const float al = (q < 2) ? v0[2 * q] : v1[2 * q - 4], ah = (q < 2) ? v0[2 * q + 1] : v1[2 * q - 3];
;                         o[2 * q] = gelu_tanh(al + __builtin_bit_cast(float, yw[q] << 16)); o[2 * q + 1] = gelu_tanh(ah + __builtin_bit_cast(float, yw[q] & 0xffff0000u)); }
;                     u32x4 w; w.x = cvt_pk_bf16(o[0], o[1]); w.y = cvt_pk_bf16(o[2], o[3]); w.z = cvt_pk_bf16(o[4], o[5]); w.w = cvt_pk_bf16(o[6], o[7]);
;                     const size_t tok = (size_t)rl * S5L + (col >> 4);
;                     *(u32x4*)(Z + tok * 512 + g * 16 + (col & 15)) = w; } }
	v_lshlrev_b32_e32 v126, 16, v112
	v_and_b32_e32 v127, 0xffff0000, v112
	v_pk_add_f32 v[108:109], v[108:109], v[126:127]
	s_nop 0
	v_mul_f32_e32 v112, 0x3d372713, v108
	v_mul_f32_e32 v112, v108, v112
	v_fma_f32 v112, v108, v112, v108
	v_mul_f32_e32 v112, 0x3fcc422a, v112
	v_mul_f32_e32 v112, 0xbfb8aa3b, v112
	v_exp_f32_e32 v126, v112
	v_mul_f32_e32 v112, 0x3d372713, v109
	v_mul_f32_e32 v112, v109, v112
	v_fma_f32 v112, v109, v112, v109
	v_mul_f32_e32 v112, 0x3fcc422a, v112
	v_mul_f32_e32 v112, 0xbfb8aa3b, v112
	v_exp_f32_e32 v127, v112
	s_nop 0
	v_pk_add_f32 v[126:127], v[126:127], 1.0 op_sel_hi:[1,0]
	s_nop 0
	v_rcp_f32_e32 v128, v127
	s_nop 0
	v_fma_f32 v129, -v127, v128, 1.0
	v_fmac_f32_e32 v128, v129, v128
	v_div_fixup_f32 v127, v128, v127, 1.0
	v_rcp_f32_e32 v128, v126
	s_nop 0
	v_fma_f32 v129, -v126, v128, 1.0
	v_fmac_f32_e32 v128, v129, v128
	v_div_fixup_f32 v126, v128, v126, 1.0
	v_lshlrev_b32_e32 v112, 16, v113
	v_and_b32_e32 v113, 0xffff0000, v113
	v_pk_add_f32 v[110:111], v[110:111], v[112:113]
	v_pk_mul_f32 v[108:109], v[108:109], v[126:127]
	v_mul_f32_e32 v112, 0x3d372713, v110
	v_mul_f32_e32 v113, 0x3d372713, v111
	v_mul_f32_e32 v112, v110, v112
	v_mul_f32_e32 v113, v111, v113
	v_fma_f32 v112, v110, v112, v110
	v_fma_f32 v113, v111, v113, v111
	v_mul_f32_e32 v112, 0x3fcc422a, v112
	v_mul_f32_e32 v113, 0x3fcc422a, v113
	v_mul_f32_e32 v112, 0xbfb8aa3b, v112
	v_mul_f32_e32 v113, 0xbfb8aa3b, v113
	v_exp_f32_e32 v112, v112
	v_exp_f32_e32 v113, v113
	s_nop 0
	v_pk_add_f32 v[112:113], v[112:113], 1.0 op_sel_hi:[1,0]
	s_nop 0
	v_rcp_f32_e32 v127, v113
	s_nop 0
	v_fma_f32 v128, -v113, v127, 1.0
	v_fmac_f32_e32 v127, v128, v127
	v_div_fixup_f32 v113, v127, v113, 1.0
	v_rcp_f32_e32 v127, v112
	s_nop 0
	v_fma_f32 v128, -v112, v127, 1.0
	v_fmac_f32_e32 v127, v128, v127
	v_div_fixup_f32 v112, v127, v112, 1.0
	v_pk_mul_f32 v[110:111], v[110:111], v[112:113]
	v_lshlrev_b32_e32 v112, 16, v114
	v_and_b32_e32 v113, 0xffff0000, v114
	v_pk_add_f32 v[104:105], v[104:105], v[112:113]
	s_nop 0
	v_mul_f32_e32 v112, 0x3d372713, v104
	v_mul_f32_e32 v113, 0x3d372713, v105
	v_mul_f32_e32 v112, v104, v112
	v_mul_f32_e32 v113, v105, v113
	v_fma_f32 v112, v104, v112, v104
	v_fma_f32 v113, v105, v113, v105
	v_mul_f32_e32 v112, 0x3fcc422a, v112
	v_mul_f32_e32 v113, 0x3fcc422a, v113
	v_mul_f32_e32 v112, 0xbfb8aa3b, v112
	v_mul_f32_e32 v113, 0xbfb8aa3b, v113
	v_exp_f32_e32 v112, v112
	v_exp_f32_e32 v113, v113
	s_nop 0
	v_pk_add_f32 v[112:113], v[112:113], 1.0 op_sel_hi:[1,0]
	s_nop 0
	v_rcp_f32_e32 v126, v113
	s_nop 0
	v_fma_f32 v127, -v113, v126, 1.0
	v_fmac_f32_e32 v126, v127, v126
	v_div_fixup_f32 v113, v126, v113, 1.0
	v_rcp_f32_e32 v126, v112
	s_nop 0
	v_fma_f32 v127, -v112, v126, 1.0
	v_fmac_f32_e32 v126, v127, v126
	v_div_fixup_f32 v112, v126, v112, 1.0
	v_pk_mul_f32 v[112:113], v[104:105], v[112:113]
	v_lshlrev_b32_e32 v104, 16, v115
	v_and_b32_e32 v105, 0xffff0000, v115
	v_pk_add_f32 v[104:105], v[106:107], v[104:105]
	s_nop 0
	v_mul_f32_e32 v106, 0x3d372713, v104
	v_mul_f32_e32 v107, 0x3d372713, v105
	v_mul_f32_e32 v106, v104, v106
	v_mul_f32_e32 v107, v105, v107
	v_fma_f32 v106, v104, v106, v104
	v_fma_f32 v107, v105, v107, v105
	v_mul_f32_e32 v106, 0x3fcc422a, v106
	v_mul_f32_e32 v107, 0x3fcc422a, v107
	v_mul_f32_e32 v106, 0xbfb8aa3b, v106
	v_mul_f32_e32 v107, 0xbfb8aa3b, v107
	v_exp_f32_e32 v106, v106
	v_exp_f32_e32 v107, v107
	s_nop 0
	v_pk_add_f32 v[106:107], v[106:107], 1.0 op_sel_hi:[1,0]
	s_nop 0
	v_rcp_f32_e32 v115, v107
	s_nop 0
	v_fma_f32 v126, -v107, v115, 1.0
	v_fmac_f32_e32 v115, v126, v115
	v_div_fixup_f32 v107, v115, v107, 1.0
	v_rcp_f32_e32 v115, v106
	s_nop 0
	v_fma_f32 v126, -v106, v115, 1.0
	v_fmac_f32_e32 v115, v126, v115
	v_div_fixup_f32 v106, v115, v106, 1.0
	v_pk_mul_f32 v[114:115], v[104:105], v[106:107]
	v_cvt_pk_bf16_f32 v104, v108, v109
	v_lshl_add_u64 v[108:109], s[36:37], 0, v[120:121]
	v_cvt_pk_bf16_f32 v105, v110, v111
	v_cvt_pk_bf16_f32 v106, v112, v113
	v_lshl_add_u64 v[112:113], v[108:109], 0, v[124:125]
	v_lshlrev_b64 v[110:111], 1, v[118:119]
	v_lshl_add_u64 v[112:113], v[112:113], 0, v[110:111]
	v_cvt_pk_bf16_f32 v107, v114, v115
	v_lshl_add_u64 v[112:113], v[112:113], 0, v[140:141]
	global_store_dwordx4 v[112:113], v[104:107], off
	global_load_dwordx4 v[104:107], v[122:123], off offset:256
	s_waitcnt vmcnt(0)
; __device__ __forceinline__ unsigned cvt_pk_bf16(float lo, float hi) { const f32x2c v = {lo, hi}; const bf16x2c b = __builtin_convertvector(v, bf16x2c); return __builtin_bit_cast(unsigned, b); }
; __device__ __forceinline__ float sigmoidf_(float x) { return 1.f / (1.f + __expf(-x)); }
; __device__ __forceinline__ float gelu_tanh(float x) { return x * sigmoidf_(1.5957691216057308f * (x + 0.044715f * x * x * x)); }
;     __device__ __forceinline__ void operator()(const f32x4 (&acc)[2][2][4][2], const Unit& u, int wr, int wc, int fr, int fq) const {
;     ...
;         for (int ai = 0; ai < 2; ++ai)
; #pragma unroll
;             for (int m = 0; m < 4; ++m) { const int row = row0 + ai * HALF + m * 16; const int g = row / S5R, rl = row % S5R;
; #pragma unroll
;                 for (int bj = 0; bj < 2; ++bj) { const int col = col0 + bj * HALF;
;                     const u32x4 yi = *(const u32x4*)(YI + (size_t)row * 512 + col);
;                     const unsigned yw[4] = {yi.x, yi.y, yi.z, yi.w};
;                     const f32x4 v0 = acc[ai][bj][m][0], v1 = acc[ai][bj][m][1];
;                     float o[8];
; #pragma unroll
;                     for (int q = 0; q < 4; ++q) { const float al = (q < 2) ? v0[2 * q] : v1[2 * q - 4], ah = (q < 2) ? v0[2 * q + 1] : v1[2 * q - 3];
;                         o[2 * q] = gelu_tanh(al + __builtin_bit_cast(float, yw[q] << 16)); o[2 * q + 1] = gelu_tanh(ah + __builtin_bit_cast(float, yw[q] & 0xffff0000u)); }
;                     u32x4 w; w.x = cvt_pk_bf16(o[0], o[1]); w.y = cvt_pk_bf16(o[2], o[3]); w.z = cvt_pk_bf16(o[4], o[5]); w.w = cvt_pk_bf16(o[6], o[7]);
;                     const size_t tok = (size_t)rl * S5L + (col >> 4);
;                     *(u32x4*)(Z + tok * 512 + g * 16 + (col & 15)) = w; } }
	v_lshlrev_b32_e32 v112, 16, v104
	v_and_b32_e32 v113, 0xffff0000, v104
	v_pk_add_f32 v[100:101], v[100:101], v[112:113]
	s_nop 0
	v_mul_f32_e32 v104, 0x3d372713, v100
	v_mul_f32_e32 v104, v100, v104
	v_fma_f32 v104, v100, v104, v100
	v_mul_f32_e32 v104, 0x3fcc422a, v104
	v_mul_f32_e32 v104, 0xbfb8aa3b, v104
	v_exp_f32_e32 v112, v104
	v_mul_f32_e32 v104, 0x3d372713, v101
	v_mul_f32_e32 v104, v101, v104
	v_fma_f32 v104, v101, v104, v101
	v_mul_f32_e32 v104, 0x3fcc422a, v104
	v_mul_f32_e32 v104, 0xbfb8aa3b, v104
	v_exp_f32_e32 v113, v104
	s_nop 0
	v_pk_add_f32 v[112:113], v[112:113], 1.0 op_sel_hi:[1,0]
	s_nop 0
	v_rcp_f32_e32 v114, v113
	s_nop 0
	v_fma_f32 v115, -v113, v114, 1.0
	v_fmac_f32_e32 v114, v115, v114
	v_div_fixup_f32 v113, v114, v113, 1.0
	v_rcp_f32_e32 v114, v112
	s_nop 0
	v_fma_f32 v115, -v112, v114, 1.0
	v_fmac_f32_e32 v114, v115, v114
	v_div_fixup_f32 v112, v114, v112, 1.0
	v_lshlrev_b32_e32 v104, 16, v105
	v_and_b32_e32 v105, 0xffff0000, v105
	v_pk_add_f32 v[102:103], v[102:103], v[104:105]
	v_pk_mul_f32 v[100:101], v[100:101], v[112:113]
	v_mul_f32_e32 v104, 0x3d372713, v102
	v_mul_f32_e32 v105, 0x3d372713, v103
	v_mul_f32_e32 v104, v102, v104
	v_mul_f32_e32 v105, v103, v105
	v_fma_f32 v104, v102, v104, v102
	v_fma_f32 v105, v103, v105, v103
	v_mul_f32_e32 v104, 0x3fcc422a, v104
	v_mul_f32_e32 v105, 0x3fcc422a, v105
	v_mul_f32_e32 v104, 0xbfb8aa3b, v104
	v_mul_f32_e32 v105, 0xbfb8aa3b, v105
	v_exp_f32_e32 v104, v104
	v_exp_f32_e32 v105, v105
	s_nop 0
	v_pk_add_f32 v[104:105], v[104:105], 1.0 op_sel_hi:[1,0]
	s_nop 0
	v_rcp_f32_e32 v113, v105
	s_nop 0
	v_fma_f32 v114, -v105, v113, 1.0
	v_fmac_f32_e32 v113, v114, v113
	v_div_fixup_f32 v105, v113, v105, 1.0
	v_rcp_f32_e32 v113, v104
	s_nop 0
	v_fma_f32 v114, -v104, v113, 1.0
	v_fmac_f32_e32 v113, v114, v113
	v_div_fixup_f32 v104, v113, v104, 1.0
	v_pk_mul_f32 v[102:103], v[102:103], v[104:105]
	v_lshlrev_b32_e32 v104, 16, v106
	v_and_b32_e32 v105, 0xffff0000, v106
	v_pk_add_f32 v[96:97], v[96:97], v[104:105]
	s_nop 0
	v_mul_f32_e32 v104, 0x3d372713, v96
	v_mul_f32_e32 v105, 0x3d372713, v97
	v_mul_f32_e32 v104, v96, v104
	v_mul_f32_e32 v105, v97, v105
	v_fma_f32 v104, v96, v104, v96
	v_fma_f32 v105, v97, v105, v97
	v_mul_f32_e32 v104, 0x3fcc422a, v104
	v_mul_f32_e32 v105, 0x3fcc422a, v105
	v_mul_f32_e32 v104, 0xbfb8aa3b, v104
	v_mul_f32_e32 v105, 0xbfb8aa3b, v105
	v_exp_f32_e32 v104, v104
	v_exp_f32_e32 v105, v105
	s_nop 0
	v_pk_add_f32 v[104:105], v[104:105], 1.0 op_sel_hi:[1,0]
	s_nop 0
	v_rcp_f32_e32 v112, v105
	s_nop 0
	v_fma_f32 v113, -v105, v112, 1.0
	v_fmac_f32_e32 v112, v113, v112
	v_div_fixup_f32 v105, v112, v105, 1.0
	v_rcp_f32_e32 v112, v104
	s_nop 0
	v_fma_f32 v113, -v104, v112, 1.0
	v_fmac_f32_e32 v112, v113, v112
	v_div_fixup_f32 v104, v112, v104, 1.0
	v_pk_mul_f32 v[104:105], v[96:97], v[104:105]
	v_lshlrev_b32_e32 v96, 16, v107
	v_and_b32_e32 v97, 0xffff0000, v107
	v_pk_add_f32 v[96:97], v[98:99], v[96:97]
	s_nop 0
	v_mul_f32_e32 v98, 0x3d372713, v96
	v_mul_f32_e32 v99, 0x3d372713, v97
	v_mul_f32_e32 v98, v96, v98
	v_mul_f32_e32 v99, v97, v99
	v_fma_f32 v98, v96, v98, v96
	v_fma_f32 v99, v97, v99, v97
	v_mul_f32_e32 v98, 0x3fcc422a, v98
	v_mul_f32_e32 v99, 0x3fcc422a, v99
	v_mul_f32_e32 v98, 0xbfb8aa3b, v98
	v_mul_f32_e32 v99, 0xbfb8aa3b, v99
	v_exp_f32_e32 v98, v98
	v_exp_f32_e32 v99, v99
	s_nop 0
	v_pk_add_f32 v[98:99], v[98:99], 1.0 op_sel_hi:[1,0]
	s_nop 0
	v_rcp_f32_e32 v107, v99
	s_nop 0
	v_fma_f32 v112, -v99, v107, 1.0
	v_fmac_f32_e32 v107, v112, v107
	v_div_fixup_f32 v99, v107, v99, 1.0
	v_rcp_f32_e32 v107, v98
	s_nop 0
	v_fma_f32 v112, -v98, v107, 1.0
	v_fmac_f32_e32 v107, v112, v107
	v_div_fixup_f32 v98, v107, v98, 1.0
	v_pk_mul_f32 v[106:107], v[96:97], v[98:99]
	v_cvt_pk_bf16_f32 v96, v100, v101
	v_lshl_add_u64 v[100:101], v[108:109], 0, v[116:117]
	v_lshl_add_u64 v[100:101], v[100:101], 0, v[110:111]
	v_cvt_pk_bf16_f32 v97, v102, v103
	v_cvt_pk_bf16_f32 v98, v104, v105
	v_cvt_pk_bf16_f32 v99, v106, v107
	v_lshl_add_u64 v[100:101], v[100:101], 0, v[140:141]
	global_store_dwordx4 v[100:101], v[96:99], off
	s_nop 1
	v_or_b32_e32 v96, 32, v142
	v_add_u32_e32 v97, v96, v160
	v_ashrrev_i32_e32 v100, 11, v97
	v_mul_i32_i24_e32 v97, 0x800, v100
	v_sub_u32_e32 v98, v96, v97
	v_ashrrev_i32_e32 v97, 31, v96
	v_lshlrev_b64 v[96:97], 10, v[96:97]
	v_lshl_add_u64 v[96:97], s[30:31], 0, v[96:97]
	v_ashrrev_i32_e32 v99, 31, v98
	v_lshl_add_u64 v[104:105], v[96:97], 0, v[144:145]
	v_lshlrev_b64 v[102:103], 15, v[98:99]
	global_load_dwordx4 v[96:99], v[104:105], off
	v_lshlrev_b32_e32 v100, 4, v100
	v_ashrrev_i32_e32 v101, 31, v100
	s_waitcnt vmcnt(0)
; __device__ __forceinline__ unsigned cvt_pk_bf16(float lo, float hi) { const f32x2c v = {lo, hi}; const bf16x2c b = __builtin_convertvector(v, bf16x2c); return __builtin_bit_cast(unsigned, b); }
; __device__ __forceinline__ float sigmoidf_(float x) { return 1.f / (1.f + __expf(-x)); }
; __device__ __forceinline__ float gelu_tanh(float x) { return x * sigmoidf_(1.5957691216057308f * (x + 0.044715f * x * x * x)); }
;     __device__ __forceinline__ void operator()(const f32x4 (&acc)[2][2][4][2], const Unit& u, int wr, int wc, int fr, int fq) const {
;     ...
;         for (int ai = 0; ai < 2; ++ai)
; #pragma unroll
;             for (int m = 0; m < 4; ++m) { const int row = row0 + ai * HALF + m * 16; const int g = row / S5R, rl = row % S5R;
; #pragma unroll
;                 for (int bj = 0; bj < 2; ++bj) { const int col = col0 + bj * HALF;
;                     const u32x4 yi = *(const u32x4*)(YI + (size_t)row * 512 + col);
;                     const unsigned yw[4] = {yi.x, yi.y, yi.z, yi.w};
;                     const f32x4 v0 = acc[ai][bj][m][0], v1 = acc[ai][bj][m][1];
;                     float o[8];
; #pragma unroll
;                     for (int q = 0; q < 4; ++q) { const float al = (q < 2) ? v0[2 * q] : v1[2 * q - 4], ah = (q < 2) ? v0[2 * q + 1] : v1[2 * q - 3];
;                         o[2 * q] = gelu_tanh(al + __builtin_bit_cast(float, yw[q] << 16)); o[2 * q + 1] = gelu_tanh(ah + __builtin_bit_cast(float, yw[q] & 0xffff0000u)); }
;                     u32x4 w; w.x = cvt_pk_bf16(o[0], o[1]); w.y = cvt_pk_bf16(o[2], o[3]); w.z = cvt_pk_bf16(o[4], o[5]); w.w = cvt_pk_bf16(o[6], o[7]);
;                     const size_t tok = (size_t)rl * S5L + (col >> 4);
;                     *(u32x4*)(Z + tok * 512 + g * 16 + (col & 15)) = w; } }
	v_lshlrev_b32_e32 v106, 16, v96
	v_and_b32_e32 v107, 0xffff0000, v96
	v_pk_add_f32 v[92:93], v[92:93], v[106:107]
	s_nop 0
	v_mul_f32_e32 v96, 0x3d372713, v92
	v_mul_f32_e32 v96, v92, v96
	v_fma_f32 v96, v92, v96, v92
	v_mul_f32_e32 v96, 0x3fcc422a, v96
	v_mul_f32_e32 v96, 0xbfb8aa3b, v96
	v_exp_f32_e32 v106, v96
	v_mul_f32_e32 v96, 0x3d372713, v93
	v_mul_f32_e32 v96, v93, v96
	v_fma_f32 v96, v93, v96, v93
	v_mul_f32_e32 v96, 0x3fcc422a, v96
	v_mul_f32_e32 v96, 0xbfb8aa3b, v96
	v_exp_f32_e32 v107, v96
	s_nop 0
	v_pk_add_f32 v[106:107], v[106:107], 1.0 op_sel_hi:[1,0]
	s_nop 0
	v_rcp_f32_e32 v108, v107
	s_nop 0
	v_fma_f32 v109, -v107, v108, 1.0
	v_fmac_f32_e32 v108, v109, v108
	v_div_fixup_f32 v107, v108, v107, 1.0
	v_rcp_f32_e32 v108, v106
	s_nop 0
	v_fma_f32 v109, -v106, v108, 1.0
	v_fmac_f32_e32 v108, v109, v108
	v_div_fixup_f32 v106, v108, v106, 1.0
	v_lshlrev_b32_e32 v96, 16, v97
	v_and_b32_e32 v97, 0xffff0000, v97
	v_pk_add_f32 v[94:95], v[94:95], v[96:97]
	v_pk_mul_f32 v[92:93], v[92:93], v[106:107]
	v_mul_f32_e32 v96, 0x3d372713, v94
	v_mul_f32_e32 v97, 0x3d372713, v95
	v_mul_f32_e32 v96, v94, v96
	v_mul_f32_e32 v97, v95, v97
	v_fma_f32 v96, v94, v96, v94
	v_fma_f32 v97, v95, v97, v95
	v_mul_f32_e32 v96, 0x3fcc422a, v96
	v_mul_f32_e32 v97, 0x3fcc422a, v97
	v_mul_f32_e32 v96, 0xbfb8aa3b, v96
	v_mul_f32_e32 v97, 0xbfb8aa3b, v97
	v_exp_f32_e32 v96, v96
	v_exp_f32_e32 v97, v97
	s_nop 0
	v_pk_add_f32 v[96:97], v[96:97], 1.0 op_sel_hi:[1,0]
	s_nop 0
	v_rcp_f32_e32 v107, v97
	s_nop 0
	v_fma_f32 v108, -v97, v107, 1.0
	v_fmac_f32_e32 v107, v108, v107
	v_div_fixup_f32 v97, v107, v97, 1.0
	v_rcp_f32_e32 v107, v96
	s_nop 0
	v_fma_f32 v108, -v96, v107, 1.0
	v_fmac_f32_e32 v107, v108, v107
	v_div_fixup_f32 v96, v107, v96, 1.0
	v_pk_mul_f32 v[94:95], v[94:95], v[96:97]
	v_lshlrev_b32_e32 v96, 16, v98
	v_and_b32_e32 v97, 0xffff0000, v98
	v_pk_add_f32 v[88:89], v[88:89], v[96:97]
	s_nop 0
	v_mul_f32_e32 v96, 0x3d372713, v88
	v_mul_f32_e32 v97, 0x3d372713, v89
	v_mul_f32_e32 v96, v88, v96
	v_mul_f32_e32 v97, v89, v97
	v_fma_f32 v96, v88, v96, v88
	v_fma_f32 v97, v89, v97, v89
	v_mul_f32_e32 v96, 0x3fcc422a, v96
	v_mul_f32_e32 v97, 0x3fcc422a, v97
	v_mul_f32_e32 v96, 0xbfb8aa3b, v96
	v_mul_f32_e32 v97, 0xbfb8aa3b, v97
	v_exp_f32_e32 v96, v96
	v_exp_f32_e32 v97, v97
	s_nop 0
	v_pk_add_f32 v[96:97], v[96:97], 1.0 op_sel_hi:[1,0]
	s_nop 0
	v_rcp_f32_e32 v106, v97
	s_nop 0
	v_fma_f32 v107, -v97, v106, 1.0
	v_fmac_f32_e32 v106, v107, v106
	v_div_fixup_f32 v97, v106, v97, 1.0
	v_rcp_f32_e32 v106, v96
	s_nop 0
	v_fma_f32 v107, -v96, v106, 1.0
	v_fmac_f32_e32 v106, v107, v106
	v_div_fixup_f32 v96, v106, v96, 1.0
	v_pk_mul_f32 v[96:97], v[88:89], v[96:97]
	v_lshlrev_b32_e32 v88, 16, v99
	v_and_b32_e32 v89, 0xffff0000, v99
	v_pk_add_f32 v[88:89], v[90:91], v[88:89]
	s_nop 0
	v_mul_f32_e32 v90, 0x3d372713, v88
	v_mul_f32_e32 v91, 0x3d372713, v89
	v_mul_f32_e32 v90, v88, v90
	v_mul_f32_e32 v91, v89, v91
	v_fma_f32 v90, v88, v90, v88
	v_fma_f32 v91, v89, v91, v89
	v_mul_f32_e32 v90, 0x3fcc422a, v90
	v_mul_f32_e32 v91, 0x3fcc422a, v91
	v_mul_f32_e32 v90, 0xbfb8aa3b, v90
	v_mul_f32_e32 v91, 0xbfb8aa3b, v91
	v_exp_f32_e32 v90, v90
	v_exp_f32_e32 v91, v91
	s_nop 0
	v_pk_add_f32 v[90:91], v[90:91], 1.0 op_sel_hi:[1,0]
	s_nop 0
	v_rcp_f32_e32 v99, v91
	s_nop 0
	v_fma_f32 v106, -v91, v99, 1.0
	v_fmac_f32_e32 v99, v106, v99
	v_div_fixup_f32 v91, v99, v91, 1.0
	v_rcp_f32_e32 v99, v90
	s_nop 0
	v_fma_f32 v106, -v90, v99, 1.0
	v_fmac_f32_e32 v99, v106, v99
	v_div_fixup_f32 v90, v99, v90, 1.0
	v_pk_mul_f32 v[98:99], v[88:89], v[90:91]
	v_cvt_pk_bf16_f32 v88, v92, v93
	v_lshl_add_u64 v[92:93], s[36:37], 0, v[102:103]
	v_cvt_pk_bf16_f32 v89, v94, v95
	v_cvt_pk_bf16_f32 v90, v96, v97
	v_lshl_add_u64 v[96:97], v[92:93], 0, v[124:125]
	v_lshlrev_b64 v[94:95], 1, v[100:101]
	v_lshl_add_u64 v[96:97], v[96:97], 0, v[94:95]
	v_cvt_pk_bf16_f32 v91, v98, v99
	v_lshl_add_u64 v[96:97], v[96:97], 0, v[140:141]
	global_store_dwordx4 v[96:97], v[88:91], off
	global_load_dwordx4 v[88:91], v[104:105], off offset:256
	s_waitcnt vmcnt(0)
	v_lshlrev_b32_e32 v96, 16, v88
	v_and_b32_e32 v97, 0xffff0000, v88
	v_pk_add_f32 v[84:85], v[84:85], v[96:97]
	s_nop 0
	v_mul_f32_e32 v88, 0x3d372713, v84
	v_mul_f32_e32 v88, v84, v88
	v_fma_f32 v88, v84, v88, v84
	v_mul_f32_e32 v88, 0x3fcc422a, v88
	v_mul_f32_e32 v88, 0xbfb8aa3b, v88
	v_exp_f32_e32 v96, v88
	v_mul_f32_e32 v88, 0x3d372713, v85
	v_mul_f32_e32 v88, v85, v88
	v_fma_f32 v88, v85, v88, v85
	v_mul_f32_e32 v88, 0x3fcc422a, v88
	v_mul_f32_e32 v88, 0xbfb8aa3b, v88
	v_exp_f32_e32 v97, v88
	s_nop 0
	v_pk_add_f32 v[96:97], v[96:97], 1.0 op_sel_hi:[1,0]
	s_nop 0
	v_rcp_f32_e32 v98, v97
	s_nop 0
	v_fma_f32 v99, -v97, v98, 1.0
	v_fmac_f32_e32 v98, v99, v98
	v_div_fixup_f32 v97, v98, v97, 1.0
	v_rcp_f32_e32 v98, v96
	s_nop 0
	v_fma_f32 v99, -v96, v98, 1.0
	v_fmac_f32_e32 v98, v99, v98
	v_div_fixup_f32 v96, v98, v96, 1.0
	v_lshlrev_b32_e32 v88, 16, v89
	v_and_b32_e32 v89, 0xffff0000, v89
	v_pk_add_f32 v[86:87], v[86:87], v[88:89]
	v_pk_mul_f32 v[84:85], v[84:85], v[96:97]
	v_mul_f32_e32 v88, 0x3d372713, v86
	v_mul_f32_e32 v89, 0x3d372713, v87
	v_mul_f32_e32 v88, v86, v88
	v_mul_f32_e32 v89, v87, v89
	v_fma_f32 v88, v86, v88, v86
	v_fma_f32 v89, v87, v89, v87
	v_mul_f32_e32 v88, 0x3fcc422a, v88
	v_mul_f32_e32 v89, 0x3fcc422a, v89
	v_mul_f32_e32 v88, 0xbfb8aa3b, v88
	v_mul_f32_e32 v89, 0xbfb8aa3b, v89
	v_exp_f32_e32 v88, v88
	v_exp_f32_e32 v89, v89
	s_nop 0
	v_pk_add_f32 v[88:89], v[88:89], 1.0 op_sel_hi:[1,0]
	s_nop 0
	v_rcp_f32_e32 v97, v89
	s_nop 0
	v_fma_f32 v98, -v89, v97, 1.0
	v_fmac_f32_e32 v97, v98, v97
	v_div_fixup_f32 v89, v97, v89, 1.0
; __device__ __forceinline__ unsigned cvt_pk_bf16(float lo, float hi) { const f32x2c v = {lo, hi}; const bf16x2c b = __builtin_convertvector(v, bf16x2c); return __builtin_bit_cast(unsigned, b); }
; __device__ __forceinline__ float sigmoidf_(float x) { return 1.f / (1.f + __expf(-x)); }
; __device__ __forceinline__ float gelu_tanh(float x) { return x * sigmoidf_(1.5957691216057308f * (x + 0.044715f * x * x * x)); }
;     __device__ __forceinline__ void operator()(const f32x4 (&acc)[2][2][4][2], const Unit& u, int wr, int wc, int fr, int fq) const {
;     ...
;         for (int ai = 0; ai < 2; ++ai)
; #pragma unroll
;             for (int m = 0; m < 4; ++m) { const int row = row0 + ai * HALF + m * 16; const int g = row / S5R, rl = row % S5R;
; #pragma unroll
;                 for (int bj = 0; bj < 2; ++bj) { const int col = col0 + bj * HALF;
;                     const u32x4 yi = *(const u32x4*)(YI + (size_t)row * 512 + col);
;                     const unsigned yw[4] = {yi.x, yi.y, yi.z, yi.w};
;                     const f32x4 v0 = acc[ai][bj][m][0], v1 = acc[ai][bj][m][1];
;                     float o[8];
; #pragma unroll
;                     for (int q = 0; q < 4; ++q) { const float al = (q < 2) ? v0[2 * q] : v1[2 * q - 4], ah = (q < 2) ? v0[2 * q + 1] : v1[2 * q - 3];
;                         o[2 * q] = gelu_tanh(al + __builtin_bit_cast(float, yw[q] << 16)); o[2 * q + 1] = gelu_tanh(ah + __builtin_bit_cast(float, yw[q] & 0xffff0000u)); }
;                     u32x4 w; w.x = cvt_pk_bf16(o[0], o[1]); w.y = cvt_pk_bf16(o[2], o[3]); w.z = cvt_pk_bf16(o[4], o[5]); w.w = cvt_pk_bf16(o[6], o[7]);
;                     const size_t tok = (size_t)rl * S5L + (col >> 4);
;                     *(u32x4*)(Z + tok * 512 + g * 16 + (col & 15)) = w; } }
	v_rcp_f32_e32 v97, v88
	s_nop 0
	v_fma_f32 v98, -v88, v97, 1.0
	v_fmac_f32_e32 v97, v98, v97
	v_div_fixup_f32 v88, v97, v88, 1.0
	v_pk_mul_f32 v[86:87], v[86:87], v[88:89]
	v_lshlrev_b32_e32 v88, 16, v90
	v_and_b32_e32 v89, 0xffff0000, v90
	v_pk_add_f32 v[80:81], v[80:81], v[88:89]
	s_nop 0
	v_mul_f32_e32 v88, 0x3d372713, v80
	v_mul_f32_e32 v89, 0x3d372713, v81
	v_mul_f32_e32 v88, v80, v88
	v_mul_f32_e32 v89, v81, v89
	v_fma_f32 v88, v80, v88, v80
	v_fma_f32 v89, v81, v89, v81
	v_mul_f32_e32 v88, 0x3fcc422a, v88
	v_mul_f32_e32 v89, 0x3fcc422a, v89
	v_mul_f32_e32 v88, 0xbfb8aa3b, v88
	v_mul_f32_e32 v89, 0xbfb8aa3b, v89
	v_exp_f32_e32 v88, v88
	v_exp_f32_e32 v89, v89
	s_nop 0
	v_pk_add_f32 v[88:89], v[88:89], 1.0 op_sel_hi:[1,0]
	s_nop 0
	v_rcp_f32_e32 v96, v89
	s_nop 0
	v_fma_f32 v97, -v89, v96, 1.0
	v_fmac_f32_e32 v96, v97, v96
	v_div_fixup_f32 v89, v96, v89, 1.0
	v_rcp_f32_e32 v96, v88
	s_nop 0
	v_fma_f32 v97, -v88, v96, 1.0
	v_fmac_f32_e32 v96, v97, v96
	v_div_fixup_f32 v88, v96, v88, 1.0
	v_pk_mul_f32 v[88:89], v[80:81], v[88:89]
	v_lshlrev_b32_e32 v80, 16, v91
	v_and_b32_e32 v81, 0xffff0000, v91
	v_pk_add_f32 v[80:81], v[82:83], v[80:81]
	s_nop 0
	v_mul_f32_e32 v82, 0x3d372713, v80
	v_mul_f32_e32 v83, 0x3d372713, v81
	v_mul_f32_e32 v82, v80, v82
	v_mul_f32_e32 v83, v81, v83
	v_fma_f32 v82, v80, v82, v80
	v_fma_f32 v83, v81, v83, v81
	v_mul_f32_e32 v82, 0x3fcc422a, v82
	v_mul_f32_e32 v83, 0x3fcc422a, v83
	v_mul_f32_e32 v82, 0xbfb8aa3b, v82
	v_mul_f32_e32 v83, 0xbfb8aa3b, v83
	v_exp_f32_e32 v82, v82
	v_exp_f32_e32 v83, v83
	s_nop 0
	v_pk_add_f32 v[82:83], v[82:83], 1.0 op_sel_hi:[1,0]
	s_nop 0
	v_rcp_f32_e32 v91, v83
	s_nop 0
	v_fma_f32 v96, -v83, v91, 1.0
	v_fmac_f32_e32 v91, v96, v91
	v_div_fixup_f32 v83, v91, v83, 1.0
	v_rcp_f32_e32 v91, v82
	s_nop 0
	v_fma_f32 v96, -v82, v91, 1.0
	v_fmac_f32_e32 v91, v96, v91
	v_div_fixup_f32 v82, v91, v82, 1.0
	v_pk_mul_f32 v[90:91], v[80:81], v[82:83]
	v_cvt_pk_bf16_f32 v80, v84, v85
	v_lshl_add_u64 v[84:85], v[92:93], 0, v[116:117]
	v_lshl_add_u64 v[84:85], v[84:85], 0, v[94:95]
	v_cvt_pk_bf16_f32 v81, v86, v87
	v_cvt_pk_bf16_f32 v82, v88, v89
	v_cvt_pk_bf16_f32 v83, v90, v91
	v_lshl_add_u64 v[84:85], v[84:85], 0, v[140:141]
	global_store_dwordx4 v[84:85], v[80:83], off
	s_nop 1
	v_or_b32_e32 v80, 48, v142
	v_add_u32_e32 v81, v80, v160
	v_ashrrev_i32_e32 v84, 11, v81
	v_mul_i32_i24_e32 v81, 0x800, v84
	v_sub_u32_e32 v82, v80, v81
	v_ashrrev_i32_e32 v81, 31, v80
	v_lshlrev_b64 v[80:81], 10, v[80:81]
	v_lshl_add_u64 v[80:81], s[30:31], 0, v[80:81]
	v_ashrrev_i32_e32 v83, 31, v82
	v_lshl_add_u64 v[88:89], v[80:81], 0, v[144:145]
	v_lshlrev_b64 v[86:87], 15, v[82:83]
	global_load_dwordx4 v[80:83], v[88:89], off
	v_lshlrev_b32_e32 v84, 4, v84
	v_ashrrev_i32_e32 v85, 31, v84
	s_waitcnt vmcnt(0)
	v_lshlrev_b32_e32 v90, 16, v80
	v_and_b32_e32 v91, 0xffff0000, v80
	v_pk_add_f32 v[76:77], v[76:77], v[90:91]
	s_nop 0
	v_mul_f32_e32 v80, 0x3d372713, v76
	v_mul_f32_e32 v80, v76, v80
	v_fma_f32 v80, v76, v80, v76
	v_mul_f32_e32 v80, 0x3fcc422a, v80
	v_mul_f32_e32 v80, 0xbfb8aa3b, v80
	v_exp_f32_e32 v90, v80
	v_mul_f32_e32 v80, 0x3d372713, v77
	v_mul_f32_e32 v80, v77, v80
	v_fma_f32 v80, v77, v80, v77
	v_mul_f32_e32 v80, 0x3fcc422a, v80
	v_mul_f32_e32 v80, 0xbfb8aa3b, v80
	v_exp_f32_e32 v91, v80
	s_nop 0
	v_pk_add_f32 v[90:91], v[90:91], 1.0 op_sel_hi:[1,0]
	s_nop 0
	v_rcp_f32_e32 v92, v91
	s_nop 0
	v_fma_f32 v93, -v91, v92, 1.0
	v_fmac_f32_e32 v92, v93, v92
	v_div_fixup_f32 v91, v92, v91, 1.0
	v_rcp_f32_e32 v92, v90
	s_nop 0
	v_fma_f32 v93, -v90, v92, 1.0
	v_fmac_f32_e32 v92, v93, v92
	v_div_fixup_f32 v90, v92, v90, 1.0
	v_lshlrev_b32_e32 v80, 16, v81
	v_and_b32_e32 v81, 0xffff0000, v81
	v_pk_add_f32 v[78:79], v[78:79], v[80:81]
	v_pk_mul_f32 v[76:77], v[76:77], v[90:91]
	v_mul_f32_e32 v80, 0x3d372713, v78
	v_mul_f32_e32 v81, 0x3d372713, v79
	v_mul_f32_e32 v80, v78, v80
	v_mul_f32_e32 v81, v79, v81
	v_fma_f32 v80, v78, v80, v78
	v_fma_f32 v81, v79, v81, v79
	v_mul_f32_e32 v80, 0x3fcc422a, v80
	v_mul_f32_e32 v81, 0x3fcc422a, v81
	v_mul_f32_e32 v80, 0xbfb8aa3b, v80
	v_mul_f32_e32 v81, 0xbfb8aa3b, v81
	v_exp_f32_e32 v80, v80
	v_exp_f32_e32 v81, v81
	s_nop 0
	v_pk_add_f32 v[80:81], v[80:81], 1.0 op_sel_hi:[1,0]
	s_nop 0
	v_rcp_f32_e32 v91, v81
	s_nop 0
	v_fma_f32 v92, -v81, v91, 1.0
	v_fmac_f32_e32 v91, v92, v91
	v_div_fixup_f32 v81, v91, v81, 1.0
	v_rcp_f32_e32 v91, v80
	s_nop 0
	v_fma_f32 v92, -v80, v91, 1.0
	v_fmac_f32_e32 v91, v92, v91
	v_div_fixup_f32 v80, v91, v80, 1.0
	v_pk_mul_f32 v[78:79], v[78:79], v[80:81]
	v_lshlrev_b32_e32 v80, 16, v82
	v_and_b32_e32 v81, 0xffff0000, v82
	v_pk_add_f32 v[72:73], v[72:73], v[80:81]
	s_nop 0
	v_mul_f32_e32 v80, 0x3d372713, v72
	v_mul_f32_e32 v81, 0x3d372713, v73
	v_mul_f32_e32 v80, v72, v80
	v_mul_f32_e32 v81, v73, v81
	v_fma_f32 v80, v72, v80, v72
	v_fma_f32 v81, v73, v81, v73
	v_mul_f32_e32 v80, 0x3fcc422a, v80
	v_mul_f32_e32 v81, 0x3fcc422a, v81
	v_mul_f32_e32 v80, 0xbfb8aa3b, v80
	v_mul_f32_e32 v81, 0xbfb8aa3b, v81
	v_exp_f32_e32 v80, v80
	v_exp_f32_e32 v81, v81
	s_nop 0
	v_pk_add_f32 v[80:81], v[80:81], 1.0 op_sel_hi:[1,0]
	s_nop 0
	v_rcp_f32_e32 v90, v81
	s_nop 0
	v_fma_f32 v91, -v81, v90, 1.0
	v_fmac_f32_e32 v90, v91, v90
	v_div_fixup_f32 v81, v90, v81, 1.0
	v_rcp_f32_e32 v90, v80
	s_nop 0
	v_fma_f32 v91, -v80, v90, 1.0
	v_fmac_f32_e32 v90, v91, v90
	v_div_fixup_f32 v80, v90, v80, 1.0
	v_pk_mul_f32 v[80:81], v[72:73], v[80:81]
	v_lshlrev_b32_e32 v72, 16, v83
	v_and_b32_e32 v73, 0xffff0000, v83
	v_pk_add_f32 v[72:73], v[74:75], v[72:73]
	s_nop 0
	v_mul_f32_e32 v74, 0x3d372713, v72
	v_mul_f32_e32 v75, 0x3d372713, v73
	v_mul_f32_e32 v74, v72, v74
	v_mul_f32_e32 v75, v73, v75
	v_fma_f32 v74, v72, v74, v72
	v_fma_f32 v75, v73, v75, v73
	v_mul_f32_e32 v74, 0x3fcc422a, v74
	v_mul_f32_e32 v75, 0x3fcc422a, v75
	v_mul_f32_e32 v74, 0xbfb8aa3b, v74
	v_mul_f32_e32 v75, 0xbfb8aa3b, v75
	v_exp_f32_e32 v74, v74
	v_exp_f32_e32 v75, v75
	s_nop 0
	v_pk_add_f32 v[74:75], v[74:75], 1.0 op_sel_hi:[1,0]
	s_nop 0
	v_rcp_f32_e32 v83, v75
	s_nop 0
	v_fma_f32 v90, -v75, v83, 1.0
	v_fmac_f32_e32 v83, v90, v83
	v_div_fixup_f32 v75, v83, v75, 1.0
	v_rcp_f32_e32 v83, v74
	s_nop 0
	v_fma_f32 v90, -v74, v83, 1.0
	v_fmac_f32_e32 v83, v90, v83
	v_div_fixup_f32 v74, v83, v74, 1.0
	v_pk_mul_f32 v[82:83], v[72:73], v[74:75]
	v_cvt_pk_bf16_f32 v72, v76, v77
	v_lshl_add_u64 v[76:77], s[36:37], 0, v[86:87]
	v_cvt_pk_bf16_f32 v73, v78, v79
	v_cvt_pk_bf16_f32 v74, v80, v81
	v_lshl_add_u64 v[80:81], v[76:77], 0, v[124:125]
	v_lshlrev_b64 v[78:79], 1, v[84:85]
	v_lshl_add_u64 v[80:81], v[80:81], 0, v[78:79]
	v_cvt_pk_bf16_f32 v75, v82, v83
	v_lshl_add_u64 v[80:81], v[80:81], 0, v[140:141]
	global_store_dwordx4 v[80:81], v[72:75], off
	global_load_dwordx4 v[72:75], v[88:89], off offset:256
	s_waitcnt vmcnt(0)
; __device__ __forceinline__ unsigned cvt_pk_bf16(float lo, float hi) { const f32x2c v = {lo, hi}; const bf16x2c b = __builtin_convertvector(v, bf16x2c); return __builtin_bit_cast(unsigned, b); }
; __device__ __forceinline__ float sigmoidf_(float x) { return 1.f / (1.f + __expf(-x)); }
; __device__ __forceinline__ float gelu_tanh(float x) { return x * sigmoidf_(1.5957691216057308f * (x + 0.044715f * x * x * x)); }
;     __device__ __forceinline__ void operator()(const f32x4 (&acc)[2][2][4][2], const Unit& u, int wr, int wc, int fr, int fq) const {
;     ...
;         for (int ai = 0; ai < 2; ++ai)
; #pragma unroll
;             for (int m = 0; m < 4; ++m) { const int row = row0 + ai * HALF + m * 16; const int g = row / S5R, rl = row % S5R;
; #pragma unroll
;                 for (int bj = 0; bj < 2; ++bj) { const int col = col0 + bj * HALF;
;                     const u32x4 yi = *(const u32x4*)(YI + (size_t)row * 512 + col);
;                     const unsigned yw[4] = {yi.x, yi.y, yi.z, yi.w};
;                     const f32x4 v0 = acc[ai][bj][m][0], v1 = acc[ai][bj][m][1];
;                     float o[8];
; #pragma unroll
;                     for (int q = 0; q < 4; ++q) { const float al = (q < 2) ? v0[2 * q] : v1[2 * q - 4], ah = (q < 2) ? v0[2 * q + 1] : v1[2 * q - 3];
;                         o[2 * q] = gelu_tanh(al + __builtin_bit_cast(float, yw[q] << 16)); o[2 * q + 1] = gelu_tanh(ah + __builtin_bit_cast(float, yw[q] & 0xffff0000u)); }
;                     u32x4 w; w.x = cvt_pk_bf16(o[0], o[1]); w.y = cvt_pk_bf16(o[2], o[3]); w.z = cvt_pk_bf16(o[4], o[5]); w.w = cvt_pk_bf16(o[6], o[7]);
;                     const size_t tok = (size_t)rl * S5L + (col >> 4);
;                     *(u32x4*)(Z + tok * 512 + g * 16 + (col & 15)) = w; } }
	v_lshlrev_b32_e32 v80, 16, v72
	v_and_b32_e32 v81, 0xffff0000, v72
	v_pk_add_f32 v[68:69], v[68:69], v[80:81]
	s_nop 0
	v_mul_f32_e32 v72, 0x3d372713, v68
	v_mul_f32_e32 v72, v68, v72
	v_fma_f32 v72, v68, v72, v68
	v_mul_f32_e32 v72, 0x3fcc422a, v72
	v_mul_f32_e32 v72, 0xbfb8aa3b, v72
	v_exp_f32_e32 v80, v72
	v_mul_f32_e32 v72, 0x3d372713, v69
	v_mul_f32_e32 v72, v69, v72
	v_fma_f32 v72, v69, v72, v69
	v_mul_f32_e32 v72, 0x3fcc422a, v72
	v_mul_f32_e32 v72, 0xbfb8aa3b, v72
	v_exp_f32_e32 v81, v72
	s_nop 0
	v_pk_add_f32 v[80:81], v[80:81], 1.0 op_sel_hi:[1,0]
	s_nop 0
	v_rcp_f32_e32 v82, v81
	s_nop 0
	v_fma_f32 v83, -v81, v82, 1.0
	v_fmac_f32_e32 v82, v83, v82
	v_div_fixup_f32 v81, v82, v81, 1.0
	v_rcp_f32_e32 v82, v80
	s_nop 0
	v_fma_f32 v83, -v80, v82, 1.0
	v_fmac_f32_e32 v82, v83, v82
	v_div_fixup_f32 v80, v82, v80, 1.0
	v_lshlrev_b32_e32 v72, 16, v73
	v_and_b32_e32 v73, 0xffff0000, v73
	v_pk_add_f32 v[70:71], v[70:71], v[72:73]
	v_pk_mul_f32 v[68:69], v[68:69], v[80:81]
	v_mul_f32_e32 v72, 0x3d372713, v70
	v_mul_f32_e32 v73, 0x3d372713, v71
	v_mul_f32_e32 v72, v70, v72
	v_mul_f32_e32 v73, v71, v73
	v_fma_f32 v72, v70, v72, v70
	v_fma_f32 v73, v71, v73, v71
	v_mul_f32_e32 v72, 0x3fcc422a, v72
	v_mul_f32_e32 v73, 0x3fcc422a, v73
	v_mul_f32_e32 v72, 0xbfb8aa3b, v72
	v_mul_f32_e32 v73, 0xbfb8aa3b, v73
	v_exp_f32_e32 v72, v72
	v_exp_f32_e32 v73, v73
	s_nop 0
	v_pk_add_f32 v[72:73], v[72:73], 1.0 op_sel_hi:[1,0]
	s_nop 0
	v_rcp_f32_e32 v81, v73
	s_nop 0
	v_fma_f32 v82, -v73, v81, 1.0
	v_fmac_f32_e32 v81, v82, v81
	v_div_fixup_f32 v73, v81, v73, 1.0
	v_rcp_f32_e32 v81, v72
	s_nop 0
	v_fma_f32 v82, -v72, v81, 1.0
	v_fmac_f32_e32 v81, v82, v81
	v_div_fixup_f32 v72, v81, v72, 1.0
	v_pk_mul_f32 v[70:71], v[70:71], v[72:73]
	v_lshlrev_b32_e32 v72, 16, v74
	v_and_b32_e32 v73, 0xffff0000, v74
	v_pk_add_f32 v[64:65], v[64:65], v[72:73]
	s_nop 0
	v_mul_f32_e32 v72, 0x3d372713, v64
	v_mul_f32_e32 v73, 0x3d372713, v65
	v_mul_f32_e32 v72, v64, v72
	v_mul_f32_e32 v73, v65, v73
	v_fma_f32 v72, v64, v72, v64
	v_fma_f32 v73, v65, v73, v65
	v_mul_f32_e32 v72, 0x3fcc422a, v72
	v_mul_f32_e32 v73, 0x3fcc422a, v73
	v_mul_f32_e32 v72, 0xbfb8aa3b, v72
	v_mul_f32_e32 v73, 0xbfb8aa3b, v73
	v_exp_f32_e32 v72, v72
	v_exp_f32_e32 v73, v73
	s_nop 0
	v_pk_add_f32 v[72:73], v[72:73], 1.0 op_sel_hi:[1,0]
	s_nop 0
	v_rcp_f32_e32 v80, v73
	s_nop 0
	v_fma_f32 v81, -v73, v80, 1.0
	v_fmac_f32_e32 v80, v81, v80
	v_div_fixup_f32 v73, v80, v73, 1.0
	v_rcp_f32_e32 v80, v72
	s_nop 0
	v_fma_f32 v81, -v72, v80, 1.0
	v_fmac_f32_e32 v80, v81, v80
	v_div_fixup_f32 v72, v80, v72, 1.0
	v_pk_mul_f32 v[72:73], v[64:65], v[72:73]
	v_lshlrev_b32_e32 v64, 16, v75
	v_and_b32_e32 v65, 0xffff0000, v75
	v_pk_add_f32 v[64:65], v[66:67], v[64:65]
	s_nop 0
	v_mul_f32_e32 v66, 0x3d372713, v64
	v_mul_f32_e32 v67, 0x3d372713, v65
	v_mul_f32_e32 v66, v64, v66
	v_mul_f32_e32 v67, v65, v67
	v_fma_f32 v66, v64, v66, v64
	v_fma_f32 v67, v65, v67, v65
	v_mul_f32_e32 v66, 0x3fcc422a, v66
	v_mul_f32_e32 v67, 0x3fcc422a, v67
	v_mul_f32_e32 v66, 0xbfb8aa3b, v66
	v_mul_f32_e32 v67, 0xbfb8aa3b, v67
	v_exp_f32_e32 v66, v66
	v_exp_f32_e32 v67, v67
	s_nop 0
	v_pk_add_f32 v[66:67], v[66:67], 1.0 op_sel_hi:[1,0]
	s_nop 0
	v_rcp_f32_e32 v75, v67
	s_nop 0
	v_fma_f32 v80, -v67, v75, 1.0
	v_fmac_f32_e32 v75, v80, v75
	v_div_fixup_f32 v67, v75, v67, 1.0
	v_rcp_f32_e32 v75, v66
	s_nop 0
	v_fma_f32 v80, -v66, v75, 1.0
	v_fmac_f32_e32 v75, v80, v75
	v_div_fixup_f32 v66, v75, v66, 1.0
	v_pk_mul_f32 v[74:75], v[64:65], v[66:67]
	v_cvt_pk_bf16_f32 v64, v68, v69
	v_lshl_add_u64 v[68:69], v[76:77], 0, v[116:117]
	v_lshl_add_u64 v[68:69], v[68:69], 0, v[78:79]
	v_cvt_pk_bf16_f32 v65, v70, v71
	v_cvt_pk_bf16_f32 v66, v72, v73
	v_cvt_pk_bf16_f32 v67, v74, v75
	v_lshl_add_u64 v[68:69], v[68:69], 0, v[140:141]
	global_store_dwordx4 v[68:69], v[64:67], off
	s_nop 1
	v_add_u32_e32 v64, 0x80, v142
	v_ashrrev_i32_e32 v65, 31, v64
	v_lshrrev_b32_e32 v66, 21, v65
	v_add_u32_e32 v66, v64, v66
	v_ashrrev_i32_e32 v68, 11, v66
	v_mul_i32_i24_e32 v66, 0x800, v68
	v_sub_u32_e32 v66, v64, v66
	v_lshlrev_b64 v[64:65], 10, v[64:65]
	v_lshl_add_u64 v[64:65], s[30:31], 0, v[64:65]
	v_ashrrev_i32_e32 v67, 31, v66
	v_lshl_add_u64 v[72:73], v[64:65], 0, v[144:145]
	v_lshlrev_b64 v[70:71], 15, v[66:67]
	global_load_dwordx4 v[64:67], v[72:73], off
	v_lshlrev_b32_e32 v68, 4, v68
	v_ashrrev_i32_e32 v69, 31, v68
	s_waitcnt vmcnt(0)
; __device__ __forceinline__ unsigned cvt_pk_bf16(float lo, float hi) { const f32x2c v = {lo, hi}; const bf16x2c b = __builtin_convertvector(v, bf16x2c); return __builtin_bit_cast(unsigned, b); }
; __device__ __forceinline__ float sigmoidf_(float x) { return 1.f / (1.f + __expf(-x)); }
; __device__ __forceinline__ float gelu_tanh(float x) { return x * sigmoidf_(1.5957691216057308f * (x + 0.044715f * x * x * x)); }
;     __device__ __forceinline__ void operator()(const f32x4 (&acc)[2][2][4][2], const Unit& u, int wr, int wc, int fr, int fq) const {
;     ...
;         for (int ai = 0; ai < 2; ++ai)
; #pragma unroll
;             for (int m = 0; m < 4; ++m) { const int row = row0 + ai * HALF + m * 16; const int g = row / S5R, rl = row % S5R;
; #pragma unroll
;                 for (int bj = 0; bj < 2; ++bj) { const int col = col0 + bj * HALF;
;                     const u32x4 yi = *(const u32x4*)(YI + (size_t)row * 512 + col);
;                     const unsigned yw[4] = {yi.x, yi.y, yi.z, yi.w};
;                     const f32x4 v0 = acc[ai][bj][m][0], v1 = acc[ai][bj][m][1];
;                     float o[8];
; #pragma unroll
;                     for (int q = 0; q < 4; ++q) { const float al = (q < 2) ? v0[2 * q] : v1[2 * q - 4], ah = (q < 2) ? v0[2 * q + 1] : v1[2 * q - 3];
;                         o[2 * q] = gelu_tanh(al + __builtin_bit_cast(float, yw[q] << 16)); o[2 * q + 1] = gelu_tanh(ah + __builtin_bit_cast(float, yw[q] & 0xffff0000u)); }
;                     u32x4 w; w.x = cvt_pk_bf16(o[0], o[1]); w.y = cvt_pk_bf16(o[2], o[3]); w.z = cvt_pk_bf16(o[4], o[5]); w.w = cvt_pk_bf16(o[6], o[7]);
;                     const size_t tok = (size_t)rl * S5L + (col >> 4);
;                     *(u32x4*)(Z + tok * 512 + g * 16 + (col & 15)) = w; } }
	v_lshlrev_b32_e32 v74, 16, v64
	v_and_b32_e32 v75, 0xffff0000, v64
	v_pk_add_f32 v[60:61], v[60:61], v[74:75]
	s_nop 0
	v_mul_f32_e32 v64, 0x3d372713, v60
	v_mul_f32_e32 v64, v60, v64
	v_fma_f32 v64, v60, v64, v60
	v_mul_f32_e32 v64, 0x3fcc422a, v64
	v_mul_f32_e32 v64, 0xbfb8aa3b, v64
	v_exp_f32_e32 v74, v64
	v_mul_f32_e32 v64, 0x3d372713, v61
	v_mul_f32_e32 v64, v61, v64
	v_fma_f32 v64, v61, v64, v61
	v_mul_f32_e32 v64, 0x3fcc422a, v64
	v_mul_f32_e32 v64, 0xbfb8aa3b, v64
	v_exp_f32_e32 v75, v64
	s_nop 0
	v_pk_add_f32 v[74:75], v[74:75], 1.0 op_sel_hi:[1,0]
	s_nop 0
	v_rcp_f32_e32 v76, v75
	s_nop 0
	v_fma_f32 v77, -v75, v76, 1.0
	v_fmac_f32_e32 v76, v77, v76
	v_div_fixup_f32 v75, v76, v75, 1.0
	v_rcp_f32_e32 v76, v74
	s_nop 0
	v_fma_f32 v77, -v74, v76, 1.0
	v_fmac_f32_e32 v76, v77, v76
	v_div_fixup_f32 v74, v76, v74, 1.0
	v_lshlrev_b32_e32 v64, 16, v65
	v_and_b32_e32 v65, 0xffff0000, v65
	v_pk_add_f32 v[62:63], v[62:63], v[64:65]
	v_pk_mul_f32 v[60:61], v[60:61], v[74:75]
	v_mul_f32_e32 v64, 0x3d372713, v62
	v_mul_f32_e32 v65, 0x3d372713, v63
	v_mul_f32_e32 v64, v62, v64
	v_mul_f32_e32 v65, v63, v65
	v_fma_f32 v64, v62, v64, v62
	v_fma_f32 v65, v63, v65, v63
	v_mul_f32_e32 v64, 0x3fcc422a, v64
	v_mul_f32_e32 v65, 0x3fcc422a, v65
	v_mul_f32_e32 v64, 0xbfb8aa3b, v64
	v_mul_f32_e32 v65, 0xbfb8aa3b, v65
	v_exp_f32_e32 v64, v64
	v_exp_f32_e32 v65, v65
	s_nop 0
	v_pk_add_f32 v[64:65], v[64:65], 1.0 op_sel_hi:[1,0]
	s_nop 0
	v_rcp_f32_e32 v75, v65
	s_nop 0
	v_fma_f32 v76, -v65, v75, 1.0
	v_fmac_f32_e32 v75, v76, v75
	v_div_fixup_f32 v65, v75, v65, 1.0
	v_rcp_f32_e32 v75, v64
	s_nop 0
	v_fma_f32 v76, -v64, v75, 1.0
	v_fmac_f32_e32 v75, v76, v75
	v_div_fixup_f32 v64, v75, v64, 1.0
	v_pk_mul_f32 v[62:63], v[62:63], v[64:65]
	v_lshlrev_b32_e32 v64, 16, v66
	v_and_b32_e32 v65, 0xffff0000, v66
	v_pk_add_f32 v[56:57], v[56:57], v[64:65]
	s_nop 0
	v_mul_f32_e32 v64, 0x3d372713, v56
	v_mul_f32_e32 v65, 0x3d372713, v57
	v_mul_f32_e32 v64, v56, v64
	v_mul_f32_e32 v65, v57, v65
	v_fma_f32 v64, v56, v64, v56
	v_fma_f32 v65, v57, v65, v57
	v_mul_f32_e32 v64, 0x3fcc422a, v64
	v_mul_f32_e32 v65, 0x3fcc422a, v65
	v_mul_f32_e32 v64, 0xbfb8aa3b, v64
	v_mul_f32_e32 v65, 0xbfb8aa3b, v65
	v_exp_f32_e32 v64, v64
	v_exp_f32_e32 v65, v65
	s_nop 0
	v_pk_add_f32 v[64:65], v[64:65], 1.0 op_sel_hi:[1,0]
	s_nop 0
	v_rcp_f32_e32 v74, v65
	s_nop 0
	v_fma_f32 v75, -v65, v74, 1.0
	v_fmac_f32_e32 v74, v75, v74
	v_div_fixup_f32 v65, v74, v65, 1.0
	v_rcp_f32_e32 v74, v64
	s_nop 0
	v_fma_f32 v75, -v64, v74, 1.0
	v_fmac_f32_e32 v74, v75, v74
	v_div_fixup_f32 v64, v74, v64, 1.0
	v_pk_mul_f32 v[64:65], v[56:57], v[64:65]
	v_lshlrev_b32_e32 v56, 16, v67
	v_and_b32_e32 v57, 0xffff0000, v67
	v_pk_add_f32 v[56:57], v[58:59], v[56:57]
	s_nop 0
	v_mul_f32_e32 v58, 0x3d372713, v56
	v_mul_f32_e32 v59, 0x3d372713, v57
	v_mul_f32_e32 v58, v56, v58
	v_mul_f32_e32 v59, v57, v59
	v_fma_f32 v58, v56, v58, v56
	v_fma_f32 v59, v57, v59, v57
	v_mul_f32_e32 v58, 0x3fcc422a, v58
	v_mul_f32_e32 v59, 0x3fcc422a, v59
	v_mul_f32_e32 v58, 0xbfb8aa3b, v58
	v_mul_f32_e32 v59, 0xbfb8aa3b, v59
	v_exp_f32_e32 v58, v58
	v_exp_f32_e32 v59, v59
	s_nop 0
	v_pk_add_f32 v[58:59], v[58:59], 1.0 op_sel_hi:[1,0]
	s_nop 0
	v_rcp_f32_e32 v67, v59
	s_nop 0
	v_fma_f32 v74, -v59, v67, 1.0
	v_fmac_f32_e32 v67, v74, v67
	v_div_fixup_f32 v59, v67, v59, 1.0
	v_rcp_f32_e32 v67, v58
	s_nop 0
	v_fma_f32 v74, -v58, v67, 1.0
	v_fmac_f32_e32 v67, v74, v67
	v_div_fixup_f32 v58, v67, v58, 1.0
	v_pk_mul_f32 v[66:67], v[56:57], v[58:59]
	v_cvt_pk_bf16_f32 v56, v60, v61
	v_lshl_add_u64 v[60:61], s[36:37], 0, v[70:71]
	v_cvt_pk_bf16_f32 v57, v62, v63
	v_cvt_pk_bf16_f32 v58, v64, v65
	v_lshl_add_u64 v[64:65], v[60:61], 0, v[124:125]
	v_lshlrev_b64 v[62:63], 1, v[68:69]
	v_lshl_add_u64 v[64:65], v[64:65], 0, v[62:63]
	v_cvt_pk_bf16_f32 v59, v66, v67
	v_lshl_add_u64 v[64:65], v[64:65], 0, v[140:141]
	global_store_dwordx4 v[64:65], v[56:59], off
	global_load_dwordx4 v[56:59], v[72:73], off offset:256
	s_waitcnt vmcnt(0)
	v_lshlrev_b32_e32 v64, 16, v56
	v_and_b32_e32 v65, 0xffff0000, v56
	v_pk_add_f32 v[52:53], v[52:53], v[64:65]
	s_nop 0
	v_mul_f32_e32 v56, 0x3d372713, v52
	v_mul_f32_e32 v56, v52, v56
	v_fma_f32 v56, v52, v56, v52
	v_mul_f32_e32 v56, 0x3fcc422a, v56
	v_mul_f32_e32 v56, 0xbfb8aa3b, v56
	v_exp_f32_e32 v64, v56
	v_mul_f32_e32 v56, 0x3d372713, v53
	v_mul_f32_e32 v56, v53, v56
	v_fma_f32 v56, v53, v56, v53
	v_mul_f32_e32 v56, 0x3fcc422a, v56
	v_mul_f32_e32 v56, 0xbfb8aa3b, v56
	v_exp_f32_e32 v65, v56
	s_nop 0
	v_pk_add_f32 v[64:65], v[64:65], 1.0 op_sel_hi:[1,0]
	s_nop 0
	v_rcp_f32_e32 v66, v65
	s_nop 0
	v_fma_f32 v67, -v65, v66, 1.0
	v_fmac_f32_e32 v66, v67, v66
	v_div_fixup_f32 v65, v66, v65, 1.0
	v_rcp_f32_e32 v66, v64
	s_nop 0
	v_fma_f32 v67, -v64, v66, 1.0
	v_fmac_f32_e32 v66, v67, v66
	v_div_fixup_f32 v64, v66, v64, 1.0
	v_lshlrev_b32_e32 v56, 16, v57
	v_and_b32_e32 v57, 0xffff0000, v57
	v_pk_add_f32 v[54:55], v[54:55], v[56:57]
	v_pk_mul_f32 v[52:53], v[52:53], v[64:65]
	v_mul_f32_e32 v56, 0x3d372713, v54
	v_mul_f32_e32 v57, 0x3d372713, v55
	v_mul_f32_e32 v56, v54, v56
	v_mul_f32_e32 v57, v55, v57
	v_fma_f32 v56, v54, v56, v54
	v_fma_f32 v57, v55, v57, v55
	v_mul_f32_e32 v56, 0x3fcc422a, v56
	v_mul_f32_e32 v57, 0x3fcc422a, v57
	v_mul_f32_e32 v56, 0xbfb8aa3b, v56
	v_mul_f32_e32 v57, 0xbfb8aa3b, v57
	v_exp_f32_e32 v56, v56
	v_exp_f32_e32 v57, v57
	s_nop 0
	v_pk_add_f32 v[56:57], v[56:57], 1.0 op_sel_hi:[1,0]
	s_nop 0
	v_rcp_f32_e32 v65, v57
	s_nop 0
	v_fma_f32 v66, -v57, v65, 1.0
	v_fmac_f32_e32 v65, v66, v65
	v_div_fixup_f32 v57, v65, v57, 1.0
	v_rcp_f32_e32 v65, v56
	s_nop 0
	v_fma_f32 v66, -v56, v65, 1.0
	v_fmac_f32_e32 v65, v66, v65
; __device__ __forceinline__ unsigned cvt_pk_bf16(float lo, float hi) { const f32x2c v = {lo, hi}; const bf16x2c b = __builtin_convertvector(v, bf16x2c); return __builtin_bit_cast(unsigned, b); }
; __device__ __forceinline__ float sigmoidf_(float x) { return 1.f / (1.f + __expf(-x)); }
; __device__ __forceinline__ float gelu_tanh(float x) { return x * sigmoidf_(1.5957691216057308f * (x + 0.044715f * x * x * x)); }
;     __device__ __forceinline__ void operator()(const f32x4 (&acc)[2][2][4][2], const Unit& u, int wr, int wc, int fr, int fq) const {
;     ...
;         for (int ai = 0; ai < 2; ++ai)
; #pragma unroll
;             for (int m = 0; m < 4; ++m) { const int row = row0 + ai * HALF + m * 16; const int g = row / S5R, rl = row % S5R;
; #pragma unroll
;                 for (int bj = 0; bj < 2; ++bj) { const int col = col0 + bj * HALF;
;                     const u32x4 yi = *(const u32x4*)(YI + (size_t)row * 512 + col);
;                     const unsigned yw[4] = {yi.x, yi.y, yi.z, yi.w};
;                     const f32x4 v0 = acc[ai][bj][m][0], v1 = acc[ai][bj][m][1];
;                     float o[8];
; #pragma unroll
;                     for (int q = 0; q < 4; ++q) { const float al = (q < 2) ? v0[2 * q] : v1[2 * q - 4], ah = (q < 2) ? v0[2 * q + 1] : v1[2 * q - 3];
;                         o[2 * q] = gelu_tanh(al + __builtin_bit_cast(float, yw[q] << 16)); o[2 * q + 1] = gelu_tanh(ah + __builtin_bit_cast(float, yw[q] & 0xffff0000u)); }
;                     u32x4 w; w.x = cvt_pk_bf16(o[0], o[1]); w.y = cvt_pk_bf16(o[2], o[3]); w.z = cvt_pk_bf16(o[4], o[5]); w.w = cvt_pk_bf16(o[6], o[7]);
;                     const size_t tok = (size_t)rl * S5L + (col >> 4);
;                     *(u32x4*)(Z + tok * 512 + g * 16 + (col & 15)) = w; } }
	v_div_fixup_f32 v56, v65, v56, 1.0
	v_pk_mul_f32 v[54:55], v[54:55], v[56:57]
	v_lshlrev_b32_e32 v56, 16, v58
	v_and_b32_e32 v57, 0xffff0000, v58
	v_pk_add_f32 v[48:49], v[48:49], v[56:57]
	s_nop 0
	v_mul_f32_e32 v56, 0x3d372713, v48
	v_mul_f32_e32 v57, 0x3d372713, v49
	v_mul_f32_e32 v56, v48, v56
	v_mul_f32_e32 v57, v49, v57
	v_fma_f32 v56, v48, v56, v48
	v_fma_f32 v57, v49, v57, v49
	v_mul_f32_e32 v56, 0x3fcc422a, v56
	v_mul_f32_e32 v57, 0x3fcc422a, v57
	v_mul_f32_e32 v56, 0xbfb8aa3b, v56
	v_mul_f32_e32 v57, 0xbfb8aa3b, v57
	v_exp_f32_e32 v56, v56
	v_exp_f32_e32 v57, v57
	s_nop 0
	v_pk_add_f32 v[56:57], v[56:57], 1.0 op_sel_hi:[1,0]
	s_nop 0
	v_rcp_f32_e32 v64, v57
	s_nop 0
	v_fma_f32 v65, -v57, v64, 1.0
	v_fmac_f32_e32 v64, v65, v64
	v_div_fixup_f32 v57, v64, v57, 1.0
	v_rcp_f32_e32 v64, v56
	s_nop 0
	v_fma_f32 v65, -v56, v64, 1.0
	v_fmac_f32_e32 v64, v65, v64
	v_div_fixup_f32 v56, v64, v56, 1.0
	v_pk_mul_f32 v[56:57], v[48:49], v[56:57]
	v_lshlrev_b32_e32 v48, 16, v59
	v_and_b32_e32 v49, 0xffff0000, v59
	v_pk_add_f32 v[48:49], v[50:51], v[48:49]
	s_nop 0
	v_mul_f32_e32 v50, 0x3d372713, v48
	v_mul_f32_e32 v51, 0x3d372713, v49
	v_mul_f32_e32 v50, v48, v50
	v_mul_f32_e32 v51, v49, v51
	v_fma_f32 v50, v48, v50, v48
	v_fma_f32 v51, v49, v51, v49
	v_mul_f32_e32 v50, 0x3fcc422a, v50
	v_mul_f32_e32 v51, 0x3fcc422a, v51
	v_mul_f32_e32 v50, 0xbfb8aa3b, v50
	v_mul_f32_e32 v51, 0xbfb8aa3b, v51
	v_exp_f32_e32 v50, v50
	v_exp_f32_e32 v51, v51
	s_nop 0
	v_pk_add_f32 v[50:51], v[50:51], 1.0 op_sel_hi:[1,0]
	s_nop 0
	v_rcp_f32_e32 v59, v51
	s_nop 0
	v_fma_f32 v64, -v51, v59, 1.0
	v_fmac_f32_e32 v59, v64, v59
	v_div_fixup_f32 v51, v59, v51, 1.0
	v_rcp_f32_e32 v59, v50
	s_nop 0
	v_fma_f32 v64, -v50, v59, 1.0
	v_fmac_f32_e32 v59, v64, v59
	v_div_fixup_f32 v50, v59, v50, 1.0
	v_pk_mul_f32 v[58:59], v[48:49], v[50:51]
	v_cvt_pk_bf16_f32 v48, v52, v53
	v_lshl_add_u64 v[52:53], v[60:61], 0, v[116:117]
	v_lshl_add_u64 v[52:53], v[52:53], 0, v[62:63]
	v_cvt_pk_bf16_f32 v49, v54, v55
	v_cvt_pk_bf16_f32 v50, v56, v57
	v_cvt_pk_bf16_f32 v51, v58, v59
	v_lshl_add_u64 v[52:53], v[52:53], 0, v[140:141]
	global_store_dwordx4 v[52:53], v[48:51], off
	s_nop 1
	v_add_u32_e32 v48, 0x90, v142
	v_ashrrev_i32_e32 v49, 31, v48
	v_lshrrev_b32_e32 v50, 21, v49
	v_add_u32_e32 v50, v48, v50
	v_ashrrev_i32_e32 v52, 11, v50
	v_mul_i32_i24_e32 v50, 0x800, v52
	v_sub_u32_e32 v50, v48, v50
	v_lshlrev_b64 v[48:49], 10, v[48:49]
	v_lshl_add_u64 v[48:49], s[30:31], 0, v[48:49]
	v_ashrrev_i32_e32 v51, 31, v50
	v_lshl_add_u64 v[56:57], v[48:49], 0, v[144:145]
	v_lshlrev_b64 v[54:55], 15, v[50:51]
	global_load_dwordx4 v[48:51], v[56:57], off
	v_lshlrev_b32_e32 v52, 4, v52
	v_ashrrev_i32_e32 v53, 31, v52
	s_waitcnt vmcnt(0)
	v_lshlrev_b32_e32 v58, 16, v48
	v_and_b32_e32 v59, 0xffff0000, v48
	v_pk_add_f32 v[44:45], v[44:45], v[58:59]
	s_nop 0
	v_mul_f32_e32 v48, 0x3d372713, v44
	v_mul_f32_e32 v48, v44, v48
	v_fma_f32 v48, v44, v48, v44
	v_mul_f32_e32 v48, 0x3fcc422a, v48
	v_mul_f32_e32 v48, 0xbfb8aa3b, v48
	v_exp_f32_e32 v58, v48
	v_mul_f32_e32 v48, 0x3d372713, v45
	v_mul_f32_e32 v48, v45, v48
	v_fma_f32 v48, v45, v48, v45
	v_mul_f32_e32 v48, 0x3fcc422a, v48
	v_mul_f32_e32 v48, 0xbfb8aa3b, v48
	v_exp_f32_e32 v59, v48
	s_nop 0
	v_pk_add_f32 v[58:59], v[58:59], 1.0 op_sel_hi:[1,0]
	s_nop 0
	v_rcp_f32_e32 v60, v59
	s_nop 0
	v_fma_f32 v61, -v59, v60, 1.0
	v_fmac_f32_e32 v60, v61, v60
	v_div_fixup_f32 v59, v60, v59, 1.0
	v_rcp_f32_e32 v60, v58
	s_nop 0
	v_fma_f32 v61, -v58, v60, 1.0
	v_fmac_f32_e32 v60, v61, v60
	v_div_fixup_f32 v58, v60, v58, 1.0
	v_lshlrev_b32_e32 v48, 16, v49
	v_and_b32_e32 v49, 0xffff0000, v49
	v_pk_add_f32 v[46:47], v[46:47], v[48:49]
	v_pk_mul_f32 v[44:45], v[44:45], v[58:59]
	v_mul_f32_e32 v48, 0x3d372713, v46
	v_mul_f32_e32 v49, 0x3d372713, v47
	v_mul_f32_e32 v48, v46, v48
	v_mul_f32_e32 v49, v47, v49
	v_fma_f32 v48, v46, v48, v46
	v_fma_f32 v49, v47, v49, v47
	v_mul_f32_e32 v48, 0x3fcc422a, v48
	v_mul_f32_e32 v49, 0x3fcc422a, v49
	v_mul_f32_e32 v48, 0xbfb8aa3b, v48
	v_mul_f32_e32 v49, 0xbfb8aa3b, v49
	v_exp_f32_e32 v48, v48
	v_exp_f32_e32 v49, v49
	s_nop 0
	v_pk_add_f32 v[48:49], v[48:49], 1.0 op_sel_hi:[1,0]
	s_nop 0
	v_rcp_f32_e32 v59, v49
	s_nop 0
	v_fma_f32 v60, -v49, v59, 1.0
	v_fmac_f32_e32 v59, v60, v59
	v_div_fixup_f32 v49, v59, v49, 1.0
	v_rcp_f32_e32 v59, v48
	s_nop 0
	v_fma_f32 v60, -v48, v59, 1.0
	v_fmac_f32_e32 v59, v60, v59
	v_div_fixup_f32 v48, v59, v48, 1.0
	v_pk_mul_f32 v[46:47], v[46:47], v[48:49]
	v_lshlrev_b32_e32 v48, 16, v50
	v_and_b32_e32 v49, 0xffff0000, v50
	v_pk_add_f32 v[40:41], v[40:41], v[48:49]
	s_nop 0
	v_mul_f32_e32 v48, 0x3d372713, v40
	v_mul_f32_e32 v49, 0x3d372713, v41
	v_mul_f32_e32 v48, v40, v48
	v_mul_f32_e32 v49, v41, v49
	v_fma_f32 v48, v40, v48, v40
	v_fma_f32 v49, v41, v49, v41
	v_mul_f32_e32 v48, 0x3fcc422a, v48
	v_mul_f32_e32 v49, 0x3fcc422a, v49
	v_mul_f32_e32 v48, 0xbfb8aa3b, v48
	v_mul_f32_e32 v49, 0xbfb8aa3b, v49
	v_exp_f32_e32 v48, v48
	v_exp_f32_e32 v49, v49
	s_nop 0
	v_pk_add_f32 v[48:49], v[48:49], 1.0 op_sel_hi:[1,0]
	s_nop 0
	v_rcp_f32_e32 v58, v49
	s_nop 0
	v_fma_f32 v59, -v49, v58, 1.0
	v_fmac_f32_e32 v58, v59, v58
	v_div_fixup_f32 v49, v58, v49, 1.0
	v_rcp_f32_e32 v58, v48
	s_nop 0
	v_fma_f32 v59, -v48, v58, 1.0
	v_fmac_f32_e32 v58, v59, v58
	v_div_fixup_f32 v48, v58, v48, 1.0
	v_pk_mul_f32 v[48:49], v[40:41], v[48:49]
	v_lshlrev_b32_e32 v40, 16, v51
	v_and_b32_e32 v41, 0xffff0000, v51
	v_pk_add_f32 v[40:41], v[42:43], v[40:41]
	s_nop 0
	v_mul_f32_e32 v42, 0x3d372713, v40
	v_mul_f32_e32 v43, 0x3d372713, v41
	v_mul_f32_e32 v42, v40, v42
	v_mul_f32_e32 v43, v41, v43
	v_fma_f32 v42, v40, v42, v40
	v_fma_f32 v43, v41, v43, v41
	v_mul_f32_e32 v42, 0x3fcc422a, v42
	v_mul_f32_e32 v43, 0x3fcc422a, v43
	v_mul_f32_e32 v42, 0xbfb8aa3b, v42
	v_mul_f32_e32 v43, 0xbfb8aa3b, v43
	v_exp_f32_e32 v42, v42
	v_exp_f32_e32 v43, v43
	s_nop 0
	v_pk_add_f32 v[42:43], v[42:43], 1.0 op_sel_hi:[1,0]
	s_nop 0
	v_rcp_f32_e32 v51, v43
	s_nop 0
	v_fma_f32 v58, -v43, v51, 1.0
	v_fmac_f32_e32 v51, v58, v51
	v_div_fixup_f32 v43, v51, v43, 1.0
	v_rcp_f32_e32 v51, v42
	s_nop 0
	v_fma_f32 v58, -v42, v51, 1.0
	v_fmac_f32_e32 v51, v58, v51
	v_div_fixup_f32 v42, v51, v42, 1.0
	v_pk_mul_f32 v[50:51], v[40:41], v[42:43]
	v_cvt_pk_bf16_f32 v40, v44, v45
	v_lshl_add_u64 v[44:45], s[36:37], 0, v[54:55]
	v_cvt_pk_bf16_f32 v41, v46, v47
	v_cvt_pk_bf16_f32 v42, v48, v49
	v_lshl_add_u64 v[48:49], v[44:45], 0, v[124:125]
	v_lshlrev_b64 v[46:47], 1, v[52:53]
	v_lshl_add_u64 v[48:49], v[48:49], 0, v[46:47]
	v_cvt_pk_bf16_f32 v43, v50, v51
	v_lshl_add_u64 v[48:49], v[48:49], 0, v[140:141]
	global_store_dwordx4 v[48:49], v[40:43], off
	global_load_dwordx4 v[40:43], v[56:57], off offset:256
	s_waitcnt vmcnt(0)
; __device__ __forceinline__ unsigned cvt_pk_bf16(float lo, float hi) { const f32x2c v = {lo, hi}; const bf16x2c b = __builtin_convertvector(v, bf16x2c); return __builtin_bit_cast(unsigned, b); }
; __device__ __forceinline__ float sigmoidf_(float x) { return 1.f / (1.f + __expf(-x)); }
; __device__ __forceinline__ float gelu_tanh(float x) { return x * sigmoidf_(1.5957691216057308f * (x + 0.044715f * x * x * x)); }
;     __device__ __forceinline__ void operator()(const f32x4 (&acc)[2][2][4][2], const Unit& u, int wr, int wc, int fr, int fq) const {
;     ...
;         for (int ai = 0; ai < 2; ++ai)
; #pragma unroll
;             for (int m = 0; m < 4; ++m) { const int row = row0 + ai * HALF + m * 16; const int g = row / S5R, rl = row % S5R;
; #pragma unroll
;                 for (int bj = 0; bj < 2; ++bj) { const int col = col0 + bj * HALF;
;                     const u32x4 yi = *(const u32x4*)(YI + (size_t)row * 512 + col);
;                     const unsigned yw[4] = {yi.x, yi.y, yi.z, yi.w};
;                     const f32x4 v0 = acc[ai][bj][m][0], v1 = acc[ai][bj][m][1];
;                     float o[8];
; #pragma unroll
;                     for (int q = 0; q < 4; ++q) { const float al = (q < 2) ? v0[2 * q] : v1[2 * q - 4], ah = (q < 2) ? v0[2 * q + 1] : v1[2 * q - 3];
;                         o[2 * q] = gelu_tanh(al + __builtin_bit_cast(float, yw[q] << 16)); o[2 * q + 1] = gelu_tanh(ah + __builtin_bit_cast(float, yw[q] & 0xffff0000u)); }
;                     u32x4 w; w.x = cvt_pk_bf16(o[0], o[1]); w.y = cvt_pk_bf16(o[2], o[3]); w.z = cvt_pk_bf16(o[4], o[5]); w.w = cvt_pk_bf16(o[6], o[7]);
;                     const size_t tok = (size_t)rl * S5L + (col >> 4);
;                     *(u32x4*)(Z + tok * 512 + g * 16 + (col & 15)) = w; } }
	v_lshlrev_b32_e32 v48, 16, v40
	v_and_b32_e32 v49, 0xffff0000, v40
	v_pk_add_f32 v[36:37], v[36:37], v[48:49]
	s_nop 0
	v_mul_f32_e32 v40, 0x3d372713, v36
	v_mul_f32_e32 v40, v36, v40
	v_fma_f32 v40, v36, v40, v36
	v_mul_f32_e32 v40, 0x3fcc422a, v40
	v_mul_f32_e32 v40, 0xbfb8aa3b, v40
	v_exp_f32_e32 v48, v40
	v_mul_f32_e32 v40, 0x3d372713, v37
	v_mul_f32_e32 v40, v37, v40
	v_fma_f32 v40, v37, v40, v37
	v_mul_f32_e32 v40, 0x3fcc422a, v40
	v_mul_f32_e32 v40, 0xbfb8aa3b, v40
	v_exp_f32_e32 v49, v40
	s_nop 0
	v_pk_add_f32 v[48:49], v[48:49], 1.0 op_sel_hi:[1,0]
	s_nop 0
	v_rcp_f32_e32 v50, v49
	s_nop 0
	v_fma_f32 v51, -v49, v50, 1.0
	v_fmac_f32_e32 v50, v51, v50
	v_div_fixup_f32 v49, v50, v49, 1.0
	v_rcp_f32_e32 v50, v48
	s_nop 0
	v_fma_f32 v51, -v48, v50, 1.0
	v_fmac_f32_e32 v50, v51, v50
	v_div_fixup_f32 v48, v50, v48, 1.0
	v_lshlrev_b32_e32 v40, 16, v41
	v_and_b32_e32 v41, 0xffff0000, v41
	v_pk_add_f32 v[38:39], v[38:39], v[40:41]
	v_pk_mul_f32 v[36:37], v[36:37], v[48:49]
	v_mul_f32_e32 v40, 0x3d372713, v38
	v_mul_f32_e32 v41, 0x3d372713, v39
	v_mul_f32_e32 v40, v38, v40
	v_mul_f32_e32 v41, v39, v41
	v_fma_f32 v40, v38, v40, v38
	v_fma_f32 v41, v39, v41, v39
	v_mul_f32_e32 v40, 0x3fcc422a, v40
	v_mul_f32_e32 v41, 0x3fcc422a, v41
	v_mul_f32_e32 v40, 0xbfb8aa3b, v40
	v_mul_f32_e32 v41, 0xbfb8aa3b, v41
	v_exp_f32_e32 v40, v40
	v_exp_f32_e32 v41, v41
	s_nop 0
	v_pk_add_f32 v[40:41], v[40:41], 1.0 op_sel_hi:[1,0]
	s_nop 0
	v_rcp_f32_e32 v49, v41
	s_nop 0
	v_fma_f32 v50, -v41, v49, 1.0
	v_fmac_f32_e32 v49, v50, v49
	v_div_fixup_f32 v41, v49, v41, 1.0
	v_rcp_f32_e32 v49, v40
	s_nop 0
	v_fma_f32 v50, -v40, v49, 1.0
	v_fmac_f32_e32 v49, v50, v49
	v_div_fixup_f32 v40, v49, v40, 1.0
	v_pk_mul_f32 v[38:39], v[38:39], v[40:41]
	v_lshlrev_b32_e32 v40, 16, v42
	v_and_b32_e32 v41, 0xffff0000, v42
	v_pk_add_f32 v[32:33], v[32:33], v[40:41]
	s_nop 0
	v_mul_f32_e32 v40, 0x3d372713, v32
	v_mul_f32_e32 v41, 0x3d372713, v33
	v_mul_f32_e32 v40, v32, v40
	v_mul_f32_e32 v41, v33, v41
	v_fma_f32 v40, v32, v40, v32
	v_fma_f32 v41, v33, v41, v33
	v_mul_f32_e32 v40, 0x3fcc422a, v40
	v_mul_f32_e32 v41, 0x3fcc422a, v41
	v_mul_f32_e32 v40, 0xbfb8aa3b, v40
	v_mul_f32_e32 v41, 0xbfb8aa3b, v41
	v_exp_f32_e32 v40, v40
	v_exp_f32_e32 v41, v41
	s_nop 0
	v_pk_add_f32 v[40:41], v[40:41], 1.0 op_sel_hi:[1,0]
	s_nop 0
	v_rcp_f32_e32 v48, v41
	s_nop 0
	v_fma_f32 v49, -v41, v48, 1.0
	v_fmac_f32_e32 v48, v49, v48
	v_div_fixup_f32 v41, v48, v41, 1.0
	v_rcp_f32_e32 v48, v40
	s_nop 0
	v_fma_f32 v49, -v40, v48, 1.0
	v_fmac_f32_e32 v48, v49, v48
	v_div_fixup_f32 v40, v48, v40, 1.0
	v_pk_mul_f32 v[40:41], v[32:33], v[40:41]
	v_lshlrev_b32_e32 v32, 16, v43
	v_and_b32_e32 v33, 0xffff0000, v43
	v_pk_add_f32 v[32:33], v[34:35], v[32:33]
	s_nop 0
	v_mul_f32_e32 v34, 0x3d372713, v32
	v_mul_f32_e32 v35, 0x3d372713, v33
	v_mul_f32_e32 v34, v32, v34
	v_mul_f32_e32 v35, v33, v35
	v_fma_f32 v34, v32, v34, v32
	v_fma_f32 v35, v33, v35, v33
	v_mul_f32_e32 v34, 0x3fcc422a, v34
	v_mul_f32_e32 v35, 0x3fcc422a, v35
	v_mul_f32_e32 v34, 0xbfb8aa3b, v34
	v_mul_f32_e32 v35, 0xbfb8aa3b, v35
	v_exp_f32_e32 v34, v34
	v_exp_f32_e32 v35, v35
	s_nop 0
	v_pk_add_f32 v[34:35], v[34:35], 1.0 op_sel_hi:[1,0]
	s_nop 0
	v_rcp_f32_e32 v43, v35
	s_nop 0
	v_fma_f32 v48, -v35, v43, 1.0
	v_fmac_f32_e32 v43, v48, v43
	v_div_fixup_f32 v35, v43, v35, 1.0
	v_rcp_f32_e32 v43, v34
	s_nop 0
	v_fma_f32 v48, -v34, v43, 1.0
	v_fmac_f32_e32 v43, v48, v43
	v_div_fixup_f32 v34, v43, v34, 1.0
	v_pk_mul_f32 v[42:43], v[32:33], v[34:35]
	v_cvt_pk_bf16_f32 v32, v36, v37
	v_lshl_add_u64 v[36:37], v[44:45], 0, v[116:117]
	v_lshl_add_u64 v[36:37], v[36:37], 0, v[46:47]
	v_cvt_pk_bf16_f32 v33, v38, v39
	v_cvt_pk_bf16_f32 v34, v40, v41
	v_cvt_pk_bf16_f32 v35, v42, v43
	v_lshl_add_u64 v[36:37], v[36:37], 0, v[140:141]
	global_store_dwordx4 v[36:37], v[32:35], off
	s_nop 1
	v_add_u32_e32 v32, 0xa0, v142
	v_ashrrev_i32_e32 v33, 31, v32
	v_lshrrev_b32_e32 v34, 21, v33
	v_add_u32_e32 v34, v32, v34
	v_ashrrev_i32_e32 v36, 11, v34
	v_mul_i32_i24_e32 v34, 0x800, v36
	v_sub_u32_e32 v34, v32, v34
	v_lshlrev_b64 v[32:33], 10, v[32:33]
	v_lshl_add_u64 v[32:33], s[30:31], 0, v[32:33]
	v_ashrrev_i32_e32 v35, 31, v34
	v_lshl_add_u64 v[40:41], v[32:33], 0, v[144:145]
	v_lshlrev_b64 v[38:39], 15, v[34:35]
	global_load_dwordx4 v[32:35], v[40:41], off
	v_lshlrev_b32_e32 v36, 4, v36
	v_ashrrev_i32_e32 v37, 31, v36
	s_waitcnt vmcnt(0)
; __device__ __forceinline__ unsigned cvt_pk_bf16(float lo, float hi) { const f32x2c v = {lo, hi}; const bf16x2c b = __builtin_convertvector(v, bf16x2c); return __builtin_bit_cast(unsigned, b); }
; __device__ __forceinline__ float sigmoidf_(float x) { return 1.f / (1.f + __expf(-x)); }
; __device__ __forceinline__ float gelu_tanh(float x) { return x * sigmoidf_(1.5957691216057308f * (x + 0.044715f * x * x * x)); }
;     __device__ __forceinline__ void operator()(const f32x4 (&acc)[2][2][4][2], const Unit& u, int wr, int wc, int fr, int fq) const {
;     ...
;         for (int ai = 0; ai < 2; ++ai)
; #pragma unroll
;             for (int m = 0; m < 4; ++m) { const int row = row0 + ai * HALF + m * 16; const int g = row / S5R, rl = row % S5R;
; #pragma unroll
;                 for (int bj = 0; bj < 2; ++bj) { const int col = col0 + bj * HALF;
;                     const u32x4 yi = *(const u32x4*)(YI + (size_t)row * 512 + col);
;                     const unsigned yw[4] = {yi.x, yi.y, yi.z, yi.w};
;                     const f32x4 v0 = acc[ai][bj][m][0], v1 = acc[ai][bj][m][1];
;                     float o[8];
; #pragma unroll
;                     for (int q = 0; q < 4; ++q) { const float al = (q < 2) ? v0[2 * q] : v1[2 * q - 4], ah = (q < 2) ? v0[2 * q + 1] : v1[2 * q - 3];
;                         o[2 * q] = gelu_tanh(al + __builtin_bit_cast(float, yw[q] << 16)); o[2 * q + 1] = gelu_tanh(ah + __builtin_bit_cast(float, yw[q] & 0xffff0000u)); }
;                     u32x4 w; w.x = cvt_pk_bf16(o[0], o[1]); w.y = cvt_pk_bf16(o[2], o[3]); w.z = cvt_pk_bf16(o[4], o[5]); w.w = cvt_pk_bf16(o[6], o[7]);
;                     const size_t tok = (size_t)rl * S5L + (col >> 4);
;                     *(u32x4*)(Z + tok * 512 + g * 16 + (col & 15)) = w; } }
	v_lshlrev_b32_e32 v42, 16, v32
	v_and_b32_e32 v43, 0xffff0000, v32
	v_pk_add_f32 v[28:29], v[28:29], v[42:43]
	s_nop 0
	v_mul_f32_e32 v32, 0x3d372713, v28
	v_mul_f32_e32 v32, v28, v32
	v_fma_f32 v32, v28, v32, v28
	v_mul_f32_e32 v32, 0x3fcc422a, v32
	v_mul_f32_e32 v32, 0xbfb8aa3b, v32
	v_exp_f32_e32 v42, v32
	v_mul_f32_e32 v32, 0x3d372713, v29
	v_mul_f32_e32 v32, v29, v32
	v_fma_f32 v32, v29, v32, v29
	v_mul_f32_e32 v32, 0x3fcc422a, v32
	v_mul_f32_e32 v32, 0xbfb8aa3b, v32
	v_exp_f32_e32 v43, v32
	s_nop 0
	v_pk_add_f32 v[42:43], v[42:43], 1.0 op_sel_hi:[1,0]
	s_nop 0
	v_rcp_f32_e32 v44, v43
	s_nop 0
	v_fma_f32 v45, -v43, v44, 1.0
	v_fmac_f32_e32 v44, v45, v44
	v_div_fixup_f32 v43, v44, v43, 1.0
	v_rcp_f32_e32 v44, v42
	s_nop 0
	v_fma_f32 v45, -v42, v44, 1.0
	v_fmac_f32_e32 v44, v45, v44
	v_div_fixup_f32 v42, v44, v42, 1.0
	v_lshlrev_b32_e32 v32, 16, v33
	v_and_b32_e32 v33, 0xffff0000, v33
	v_pk_add_f32 v[30:31], v[30:31], v[32:33]
	v_pk_mul_f32 v[28:29], v[28:29], v[42:43]
	v_mul_f32_e32 v32, 0x3d372713, v30
	v_mul_f32_e32 v33, 0x3d372713, v31
	v_mul_f32_e32 v32, v30, v32
	v_mul_f32_e32 v33, v31, v33
	v_fma_f32 v32, v30, v32, v30
	v_fma_f32 v33, v31, v33, v31
	v_mul_f32_e32 v32, 0x3fcc422a, v32
	v_mul_f32_e32 v33, 0x3fcc422a, v33
	v_mul_f32_e32 v32, 0xbfb8aa3b, v32
	v_mul_f32_e32 v33, 0xbfb8aa3b, v33
	v_exp_f32_e32 v32, v32
	v_exp_f32_e32 v33, v33
	s_nop 0
	v_pk_add_f32 v[32:33], v[32:33], 1.0 op_sel_hi:[1,0]
	s_nop 0
	v_rcp_f32_e32 v43, v33
	s_nop 0
	v_fma_f32 v44, -v33, v43, 1.0
	v_fmac_f32_e32 v43, v44, v43
	v_div_fixup_f32 v33, v43, v33, 1.0
	v_rcp_f32_e32 v43, v32
	s_nop 0
	v_fma_f32 v44, -v32, v43, 1.0
	v_fmac_f32_e32 v43, v44, v43
	v_div_fixup_f32 v32, v43, v32, 1.0
	v_pk_mul_f32 v[30:31], v[30:31], v[32:33]
	v_lshlrev_b32_e32 v32, 16, v34
	v_and_b32_e32 v33, 0xffff0000, v34
	v_pk_add_f32 v[24:25], v[24:25], v[32:33]
	s_nop 0
	v_mul_f32_e32 v32, 0x3d372713, v24
	v_mul_f32_e32 v33, 0x3d372713, v25
	v_mul_f32_e32 v32, v24, v32
	v_mul_f32_e32 v33, v25, v33
	v_fma_f32 v32, v24, v32, v24
	v_fma_f32 v33, v25, v33, v25
	v_mul_f32_e32 v32, 0x3fcc422a, v32
	v_mul_f32_e32 v33, 0x3fcc422a, v33
	v_mul_f32_e32 v32, 0xbfb8aa3b, v32
	v_mul_f32_e32 v33, 0xbfb8aa3b, v33
	v_exp_f32_e32 v32, v32
	v_exp_f32_e32 v33, v33
	s_nop 0
	v_pk_add_f32 v[32:33], v[32:33], 1.0 op_sel_hi:[1,0]
	s_nop 0
	v_rcp_f32_e32 v42, v33
	s_nop 0
	v_fma_f32 v43, -v33, v42, 1.0
	v_fmac_f32_e32 v42, v43, v42
	v_div_fixup_f32 v33, v42, v33, 1.0
	v_rcp_f32_e32 v42, v32
	s_nop 0
	v_fma_f32 v43, -v32, v42, 1.0
	v_fmac_f32_e32 v42, v43, v42
	v_div_fixup_f32 v32, v42, v32, 1.0
	v_pk_mul_f32 v[32:33], v[24:25], v[32:33]
	v_lshlrev_b32_e32 v24, 16, v35
	v_and_b32_e32 v25, 0xffff0000, v35
	v_pk_add_f32 v[24:25], v[26:27], v[24:25]
	s_nop 0
	v_mul_f32_e32 v26, 0x3d372713, v24
	v_mul_f32_e32 v27, 0x3d372713, v25
	v_mul_f32_e32 v26, v24, v26
	v_mul_f32_e32 v27, v25, v27
	v_fma_f32 v26, v24, v26, v24
	v_fma_f32 v27, v25, v27, v25
	v_mul_f32_e32 v26, 0x3fcc422a, v26
	v_mul_f32_e32 v27, 0x3fcc422a, v27
	v_mul_f32_e32 v26, 0xbfb8aa3b, v26
	v_mul_f32_e32 v27, 0xbfb8aa3b, v27
	v_exp_f32_e32 v26, v26
	v_exp_f32_e32 v27, v27
	s_nop 0
	v_pk_add_f32 v[26:27], v[26:27], 1.0 op_sel_hi:[1,0]
	s_nop 0
	v_rcp_f32_e32 v35, v27
	s_nop 0
	v_fma_f32 v42, -v27, v35, 1.0
	v_fmac_f32_e32 v35, v42, v35
	v_div_fixup_f32 v27, v35, v27, 1.0
	v_rcp_f32_e32 v35, v26
	s_nop 0
	v_fma_f32 v42, -v26, v35, 1.0
	v_fmac_f32_e32 v35, v42, v35
	v_div_fixup_f32 v26, v35, v26, 1.0
	v_pk_mul_f32 v[34:35], v[24:25], v[26:27]
	v_cvt_pk_bf16_f32 v24, v28, v29
	v_lshl_add_u64 v[28:29], s[36:37], 0, v[38:39]
	v_cvt_pk_bf16_f32 v25, v30, v31
	v_cvt_pk_bf16_f32 v26, v32, v33
	v_lshl_add_u64 v[32:33], v[28:29], 0, v[124:125]
	v_lshlrev_b64 v[30:31], 1, v[36:37]
	v_lshl_add_u64 v[32:33], v[32:33], 0, v[30:31]
	v_cvt_pk_bf16_f32 v27, v34, v35
	v_lshl_add_u64 v[32:33], v[32:33], 0, v[140:141]
	global_store_dwordx4 v[32:33], v[24:27], off
	global_load_dwordx4 v[24:27], v[40:41], off offset:256
	s_waitcnt vmcnt(0)
	v_lshlrev_b32_e32 v32, 16, v24
	v_and_b32_e32 v33, 0xffff0000, v24
	v_pk_add_f32 v[20:21], v[20:21], v[32:33]
	s_nop 0
	v_mul_f32_e32 v24, 0x3d372713, v20
	v_mul_f32_e32 v24, v20, v24
	v_fma_f32 v24, v20, v24, v20
	v_mul_f32_e32 v24, 0x3fcc422a, v24
	v_mul_f32_e32 v24, 0xbfb8aa3b, v24
	v_exp_f32_e32 v32, v24
	v_mul_f32_e32 v24, 0x3d372713, v21
	v_mul_f32_e32 v24, v21, v24
	v_fma_f32 v24, v21, v24, v21
	v_mul_f32_e32 v24, 0x3fcc422a, v24
	v_mul_f32_e32 v24, 0xbfb8aa3b, v24
	v_exp_f32_e32 v33, v24
	s_nop 0
	v_pk_add_f32 v[32:33], v[32:33], 1.0 op_sel_hi:[1,0]
	s_nop 0
	v_rcp_f32_e32 v34, v33
	s_nop 0
	v_fma_f32 v35, -v33, v34, 1.0
	v_fmac_f32_e32 v34, v35, v34
	v_div_fixup_f32 v33, v34, v33, 1.0
	v_rcp_f32_e32 v34, v32
	s_nop 0
	v_fma_f32 v35, -v32, v34, 1.0
	v_fmac_f32_e32 v34, v35, v34
	v_div_fixup_f32 v32, v34, v32, 1.0
	v_lshlrev_b32_e32 v24, 16, v25
	v_and_b32_e32 v25, 0xffff0000, v25
	v_pk_add_f32 v[22:23], v[22:23], v[24:25]
	v_pk_mul_f32 v[20:21], v[20:21], v[32:33]
	v_mul_f32_e32 v24, 0x3d372713, v22
	v_mul_f32_e32 v25, 0x3d372713, v23
	v_mul_f32_e32 v24, v22, v24
	v_mul_f32_e32 v25, v23, v25
	v_fma_f32 v24, v22, v24, v22
	v_fma_f32 v25, v23, v25, v23
	v_mul_f32_e32 v24, 0x3fcc422a, v24
	v_mul_f32_e32 v25, 0x3fcc422a, v25
	v_mul_f32_e32 v24, 0xbfb8aa3b, v24
	v_mul_f32_e32 v25, 0xbfb8aa3b, v25
	v_exp_f32_e32 v24, v24
	v_exp_f32_e32 v25, v25
	s_nop 0
	v_pk_add_f32 v[24:25], v[24:25], 1.0 op_sel_hi:[1,0]
	s_nop 0
	v_rcp_f32_e32 v33, v25
	s_nop 0
	v_fma_f32 v34, -v25, v33, 1.0
	v_fmac_f32_e32 v33, v34, v33
	v_div_fixup_f32 v25, v33, v25, 1.0
	v_rcp_f32_e32 v33, v24
	s_nop 0
	v_fma_f32 v34, -v24, v33, 1.0
	v_fmac_f32_e32 v33, v34, v33
; __device__ __forceinline__ unsigned cvt_pk_bf16(float lo, float hi) { const f32x2c v = {lo, hi}; const bf16x2c b = __builtin_convertvector(v, bf16x2c); return __builtin_bit_cast(unsigned, b); }
; __device__ __forceinline__ float sigmoidf_(float x) { return 1.f / (1.f + __expf(-x)); }
; __device__ __forceinline__ float gelu_tanh(float x) { return x * sigmoidf_(1.5957691216057308f * (x + 0.044715f * x * x * x)); }
;     __device__ __forceinline__ void operator()(const f32x4 (&acc)[2][2][4][2], const Unit& u, int wr, int wc, int fr, int fq) const {
;     ...
;         for (int ai = 0; ai < 2; ++ai)
; #pragma unroll
;             for (int m = 0; m < 4; ++m) { const int row = row0 + ai * HALF + m * 16; const int g = row / S5R, rl = row % S5R;
; #pragma unroll
;                 for (int bj = 0; bj < 2; ++bj) { const int col = col0 + bj * HALF;
;                     const u32x4 yi = *(const u32x4*)(YI + (size_t)row * 512 + col);
;                     const unsigned yw[4] = {yi.x, yi.y, yi.z, yi.w};
;                     const f32x4 v0 = acc[ai][bj][m][0], v1 = acc[ai][bj][m][1];
;                     float o[8];
; #pragma unroll
;                     for (int q = 0; q < 4; ++q) { const float al = (q < 2) ? v0[2 * q] : v1[2 * q - 4], ah = (q < 2) ? v0[2 * q + 1] : v1[2 * q - 3];
;                         o[2 * q] = gelu_tanh(al + __builtin_bit_cast(float, yw[q] << 16)); o[2 * q + 1] = gelu_tanh(ah + __builtin_bit_cast(float, yw[q] & 0xffff0000u)); }
;                     u32x4 w; w.x = cvt_pk_bf16(o[0], o[1]); w.y = cvt_pk_bf16(o[2], o[3]); w.z = cvt_pk_bf16(o[4], o[5]); w.w = cvt_pk_bf16(o[6], o[7]);
;                     const size_t tok = (size_t)rl * S5L + (col >> 4);
;                     *(u32x4*)(Z + tok * 512 + g * 16 + (col & 15)) = w; } }
	v_div_fixup_f32 v24, v33, v24, 1.0
	v_pk_mul_f32 v[22:23], v[22:23], v[24:25]
	v_lshlrev_b32_e32 v24, 16, v26
	v_and_b32_e32 v25, 0xffff0000, v26
	v_pk_add_f32 v[16:17], v[16:17], v[24:25]
	s_nop 0
	v_mul_f32_e32 v24, 0x3d372713, v16
	v_mul_f32_e32 v25, 0x3d372713, v17
	v_mul_f32_e32 v24, v16, v24
	v_mul_f32_e32 v25, v17, v25
	v_fma_f32 v24, v16, v24, v16
	v_fma_f32 v25, v17, v25, v17
	v_mul_f32_e32 v24, 0x3fcc422a, v24
	v_mul_f32_e32 v25, 0x3fcc422a, v25
	v_mul_f32_e32 v24, 0xbfb8aa3b, v24
	v_mul_f32_e32 v25, 0xbfb8aa3b, v25
	v_exp_f32_e32 v24, v24
	v_exp_f32_e32 v25, v25
	s_nop 0
	v_pk_add_f32 v[24:25], v[24:25], 1.0 op_sel_hi:[1,0]
	s_nop 0
	v_rcp_f32_e32 v32, v25
	s_nop 0
	v_fma_f32 v33, -v25, v32, 1.0
	v_fmac_f32_e32 v32, v33, v32
	v_div_fixup_f32 v25, v32, v25, 1.0
	v_rcp_f32_e32 v32, v24
	s_nop 0
	v_fma_f32 v33, -v24, v32, 1.0
	v_fmac_f32_e32 v32, v33, v32
	v_div_fixup_f32 v24, v32, v24, 1.0
	v_pk_mul_f32 v[24:25], v[16:17], v[24:25]
	v_lshlrev_b32_e32 v16, 16, v27
	v_and_b32_e32 v17, 0xffff0000, v27
	v_pk_add_f32 v[16:17], v[18:19], v[16:17]
	s_nop 0
	v_mul_f32_e32 v18, 0x3d372713, v16
	v_mul_f32_e32 v19, 0x3d372713, v17
	v_mul_f32_e32 v18, v16, v18
	v_mul_f32_e32 v19, v17, v19
	v_fma_f32 v18, v16, v18, v16
	v_fma_f32 v19, v17, v19, v17
	v_mul_f32_e32 v18, 0x3fcc422a, v18
	v_mul_f32_e32 v19, 0x3fcc422a, v19
	v_mul_f32_e32 v18, 0xbfb8aa3b, v18
	v_mul_f32_e32 v19, 0xbfb8aa3b, v19
	v_exp_f32_e32 v18, v18
	v_exp_f32_e32 v19, v19
	s_nop 0
	v_pk_add_f32 v[18:19], v[18:19], 1.0 op_sel_hi:[1,0]
	s_nop 0
	v_rcp_f32_e32 v27, v19
	s_nop 0
	v_fma_f32 v32, -v19, v27, 1.0
	v_fmac_f32_e32 v27, v32, v27
	v_div_fixup_f32 v19, v27, v19, 1.0
	v_rcp_f32_e32 v27, v18
	s_nop 0
	v_fma_f32 v32, -v18, v27, 1.0
	v_fmac_f32_e32 v27, v32, v27
	v_div_fixup_f32 v18, v27, v18, 1.0
	v_pk_mul_f32 v[26:27], v[16:17], v[18:19]
	v_cvt_pk_bf16_f32 v16, v20, v21
	v_lshl_add_u64 v[20:21], v[28:29], 0, v[116:117]
	v_lshl_add_u64 v[20:21], v[20:21], 0, v[30:31]
	v_cvt_pk_bf16_f32 v17, v22, v23
	v_cvt_pk_bf16_f32 v18, v24, v25
	v_cvt_pk_bf16_f32 v19, v26, v27
	v_lshl_add_u64 v[20:21], v[20:21], 0, v[140:141]
	global_store_dwordx4 v[20:21], v[16:19], off
	s_nop 1
	v_add_u32_e32 v16, 0xb0, v142
	v_ashrrev_i32_e32 v17, 31, v16
	v_lshrrev_b32_e32 v18, 21, v17
	v_add_u32_e32 v18, v16, v18
	v_ashrrev_i32_e32 v20, 11, v18
	v_mul_i32_i24_e32 v18, 0x800, v20
	v_sub_u32_e32 v18, v16, v18
	v_lshlrev_b64 v[16:17], 10, v[16:17]
	v_lshl_add_u64 v[16:17], s[30:31], 0, v[16:17]
	v_ashrrev_i32_e32 v19, 31, v18
	v_lshl_add_u64 v[24:25], v[16:17], 0, v[144:145]
	v_lshlrev_b64 v[22:23], 15, v[18:19]
	global_load_dwordx4 v[16:19], v[24:25], off
	v_lshlrev_b32_e32 v20, 4, v20
	v_ashrrev_i32_e32 v21, 31, v20
	s_waitcnt vmcnt(0)
	v_lshlrev_b32_e32 v26, 16, v16
	v_and_b32_e32 v27, 0xffff0000, v16
	v_pk_add_f32 v[12:13], v[12:13], v[26:27]
	s_nop 0
	v_mul_f32_e32 v16, 0x3d372713, v12
	v_mul_f32_e32 v16, v12, v16
	v_fma_f32 v16, v12, v16, v12
	v_mul_f32_e32 v16, 0x3fcc422a, v16
	v_mul_f32_e32 v16, 0xbfb8aa3b, v16
	v_exp_f32_e32 v26, v16
	v_mul_f32_e32 v16, 0x3d372713, v13
	v_mul_f32_e32 v16, v13, v16
	v_fma_f32 v16, v13, v16, v13
	v_mul_f32_e32 v16, 0x3fcc422a, v16
	v_mul_f32_e32 v16, 0xbfb8aa3b, v16
	v_exp_f32_e32 v27, v16
	s_nop 0
	v_pk_add_f32 v[26:27], v[26:27], 1.0 op_sel_hi:[1,0]
	s_nop 0
	v_rcp_f32_e32 v28, v27
	s_nop 0
	v_fma_f32 v29, -v27, v28, 1.0
	v_fmac_f32_e32 v28, v29, v28
	v_div_fixup_f32 v27, v28, v27, 1.0
	v_rcp_f32_e32 v28, v26
	s_nop 0
	v_fma_f32 v29, -v26, v28, 1.0
	v_fmac_f32_e32 v28, v29, v28
	v_div_fixup_f32 v26, v28, v26, 1.0
	v_lshlrev_b32_e32 v16, 16, v17
	v_and_b32_e32 v17, 0xffff0000, v17
	v_pk_add_f32 v[14:15], v[14:15], v[16:17]
	v_pk_mul_f32 v[12:13], v[12:13], v[26:27]
	v_mul_f32_e32 v16, 0x3d372713, v14
	v_mul_f32_e32 v17, 0x3d372713, v15
	v_mul_f32_e32 v16, v14, v16
	v_mul_f32_e32 v17, v15, v17
	v_fma_f32 v16, v14, v16, v14
	v_fma_f32 v17, v15, v17, v15
	v_mul_f32_e32 v16, 0x3fcc422a, v16
	v_mul_f32_e32 v17, 0x3fcc422a, v17
	v_mul_f32_e32 v16, 0xbfb8aa3b, v16
	v_mul_f32_e32 v17, 0xbfb8aa3b, v17
	v_exp_f32_e32 v16, v16
	v_exp_f32_e32 v17, v17
	s_nop 0
	v_pk_add_f32 v[16:17], v[16:17], 1.0 op_sel_hi:[1,0]
	s_nop 0
	v_rcp_f32_e32 v27, v17
	s_nop 0
	v_fma_f32 v28, -v17, v27, 1.0
	v_fmac_f32_e32 v27, v28, v27
	v_div_fixup_f32 v17, v27, v17, 1.0
	v_rcp_f32_e32 v27, v16
	s_nop 0
	v_fma_f32 v28, -v16, v27, 1.0
	v_fmac_f32_e32 v27, v28, v27
	v_div_fixup_f32 v16, v27, v16, 1.0
	v_pk_mul_f32 v[14:15], v[14:15], v[16:17]
	v_lshlrev_b32_e32 v16, 16, v18
	v_and_b32_e32 v17, 0xffff0000, v18
	v_pk_add_f32 v[8:9], v[8:9], v[16:17]
	s_nop 0
	v_mul_f32_e32 v16, 0x3d372713, v8
	v_mul_f32_e32 v17, 0x3d372713, v9
	v_mul_f32_e32 v16, v8, v16
	v_mul_f32_e32 v17, v9, v17
	v_fma_f32 v16, v8, v16, v8
	v_fma_f32 v17, v9, v17, v9
	v_mul_f32_e32 v16, 0x3fcc422a, v16
	v_mul_f32_e32 v17, 0x3fcc422a, v17
	v_mul_f32_e32 v16, 0xbfb8aa3b, v16
	v_mul_f32_e32 v17, 0xbfb8aa3b, v17
	v_exp_f32_e32 v16, v16
	v_exp_f32_e32 v17, v17
	s_nop 0
	v_pk_add_f32 v[16:17], v[16:17], 1.0 op_sel_hi:[1,0]
	s_nop 0
	v_rcp_f32_e32 v26, v17
	s_nop 0
	v_fma_f32 v27, -v17, v26, 1.0
	v_fmac_f32_e32 v26, v27, v26
	v_div_fixup_f32 v17, v26, v17, 1.0
	v_rcp_f32_e32 v26, v16
	s_nop 0
	v_fma_f32 v27, -v16, v26, 1.0
	v_fmac_f32_e32 v26, v27, v26
	v_div_fixup_f32 v16, v26, v16, 1.0
	v_pk_mul_f32 v[16:17], v[8:9], v[16:17]
	v_lshlrev_b32_e32 v8, 16, v19
	v_and_b32_e32 v9, 0xffff0000, v19
	v_pk_add_f32 v[8:9], v[10:11], v[8:9]
	s_nop 0
	v_mul_f32_e32 v10, 0x3d372713, v8
	v_mul_f32_e32 v11, 0x3d372713, v9
	v_mul_f32_e32 v10, v8, v10
	v_mul_f32_e32 v11, v9, v11
	v_fma_f32 v10, v8, v10, v8
	v_fma_f32 v11, v9, v11, v9
	v_mul_f32_e32 v10, 0x3fcc422a, v10
	v_mul_f32_e32 v11, 0x3fcc422a, v11
	v_mul_f32_e32 v10, 0xbfb8aa3b, v10
	v_mul_f32_e32 v11, 0xbfb8aa3b, v11
	v_exp_f32_e32 v10, v10
	v_exp_f32_e32 v11, v11
	s_nop 0
	v_pk_add_f32 v[10:11], v[10:11], 1.0 op_sel_hi:[1,0]
	s_nop 0
	v_rcp_f32_e32 v19, v11
	s_nop 0
	v_fma_f32 v26, -v11, v19, 1.0
	v_fmac_f32_e32 v19, v26, v19
	v_div_fixup_f32 v11, v19, v11, 1.0
	v_rcp_f32_e32 v19, v10
	s_nop 0
	v_fma_f32 v26, -v10, v19, 1.0
	v_fmac_f32_e32 v19, v26, v19
	v_div_fixup_f32 v10, v19, v10, 1.0
	v_pk_mul_f32 v[18:19], v[8:9], v[10:11]
	v_cvt_pk_bf16_f32 v8, v12, v13
	v_lshl_add_u64 v[12:13], s[36:37], 0, v[22:23]
	v_cvt_pk_bf16_f32 v9, v14, v15
	v_cvt_pk_bf16_f32 v10, v16, v17
	v_lshl_add_u64 v[16:17], v[12:13], 0, v[124:125]
	v_lshlrev_b64 v[14:15], 1, v[20:21]
	v_lshl_add_u64 v[16:17], v[16:17], 0, v[14:15]
	v_cvt_pk_bf16_f32 v11, v18, v19
	v_lshl_add_u64 v[16:17], v[16:17], 0, v[140:141]
	global_store_dwordx4 v[16:17], v[8:11], off
	global_load_dwordx4 v[8:11], v[24:25], off offset:256
	s_waitcnt vmcnt(0)
; __device__ __forceinline__ unsigned cvt_pk_bf16(float lo, float hi) { const f32x2c v = {lo, hi}; const bf16x2c b = __builtin_convertvector(v, bf16x2c); return __builtin_bit_cast(unsigned, b); }
; __device__ __forceinline__ float sigmoidf_(float x) { return 1.f / (1.f + __expf(-x)); }
; __device__ __forceinline__ float gelu_tanh(float x) { return x * sigmoidf_(1.5957691216057308f * (x + 0.044715f * x * x * x)); }
;     __device__ __forceinline__ void operator()(const f32x4 (&acc)[2][2][4][2], const Unit& u, int wr, int wc, int fr, int fq) const {
;     ...
;         for (int ai = 0; ai < 2; ++ai)
; #pragma unroll
;             for (int m = 0; m < 4; ++m) { const int row = row0 + ai * HALF + m * 16; const int g = row / S5R, rl = row % S5R;
; #pragma unroll
;                 for (int bj = 0; bj < 2; ++bj) { const int col = col0 + bj * HALF;
;                     const u32x4 yi = *(const u32x4*)(YI + (size_t)row * 512 + col);
;                     const unsigned yw[4] = {yi.x, yi.y, yi.z, yi.w};
;                     const f32x4 v0 = acc[ai][bj][m][0], v1 = acc[ai][bj][m][1];
;                     float o[8];
; #pragma unroll
;                     for (int q = 0; q < 4; ++q) { const float al = (q < 2) ? v0[2 * q] : v1[2 * q - 4], ah = (q < 2) ? v0[2 * q + 1] : v1[2 * q - 3];
;                         o[2 * q] = gelu_tanh(al + __builtin_bit_cast(float, yw[q] << 16)); o[2 * q + 1] = gelu_tanh(ah + __builtin_bit_cast(float, yw[q] & 0xffff0000u)); }
;                     u32x4 w; w.x = cvt_pk_bf16(o[0], o[1]); w.y = cvt_pk_bf16(o[2], o[3]); w.z = cvt_pk_bf16(o[4], o[5]); w.w = cvt_pk_bf16(o[6], o[7]);
;                     const size_t tok = (size_t)rl * S5L + (col >> 4);
;                     *(u32x4*)(Z + tok * 512 + g * 16 + (col & 15)) = w; } }
	v_lshlrev_b32_e32 v16, 16, v8
	v_and_b32_e32 v17, 0xffff0000, v8
	v_pk_add_f32 v[4:5], v[4:5], v[16:17]
	s_nop 0
	v_mul_f32_e32 v8, 0x3d372713, v4
	v_mul_f32_e32 v8, v4, v8
	v_fma_f32 v8, v4, v8, v4
	v_mul_f32_e32 v8, 0x3fcc422a, v8
	v_mul_f32_e32 v8, 0xbfb8aa3b, v8
	v_exp_f32_e32 v16, v8
	v_mul_f32_e32 v8, 0x3d372713, v5
	v_mul_f32_e32 v8, v5, v8
	v_fma_f32 v8, v5, v8, v5
	v_mul_f32_e32 v8, 0x3fcc422a, v8
	v_mul_f32_e32 v8, 0xbfb8aa3b, v8
	v_exp_f32_e32 v17, v8
	s_nop 0
	v_pk_add_f32 v[16:17], v[16:17], 1.0 op_sel_hi:[1,0]
	s_nop 0
	v_rcp_f32_e32 v18, v17
	s_nop 0
	v_fma_f32 v19, -v17, v18, 1.0
	v_fmac_f32_e32 v18, v19, v18
	v_div_fixup_f32 v17, v18, v17, 1.0
	v_rcp_f32_e32 v18, v16
	s_nop 0
	v_fma_f32 v19, -v16, v18, 1.0
	v_fmac_f32_e32 v18, v19, v18
	v_div_fixup_f32 v16, v18, v16, 1.0
	v_lshlrev_b32_e32 v8, 16, v9
	v_and_b32_e32 v9, 0xffff0000, v9
	v_pk_add_f32 v[6:7], v[6:7], v[8:9]
	v_pk_mul_f32 v[4:5], v[4:5], v[16:17]
	v_mul_f32_e32 v8, 0x3d372713, v6
	v_mul_f32_e32 v9, 0x3d372713, v7
	v_mul_f32_e32 v8, v6, v8
	v_mul_f32_e32 v9, v7, v9
	v_fma_f32 v8, v6, v8, v6
	v_fma_f32 v9, v7, v9, v7
	v_mul_f32_e32 v8, 0x3fcc422a, v8
	v_mul_f32_e32 v9, 0x3fcc422a, v9
	v_mul_f32_e32 v8, 0xbfb8aa3b, v8
	v_mul_f32_e32 v9, 0xbfb8aa3b, v9
	v_exp_f32_e32 v8, v8
	v_exp_f32_e32 v9, v9
	s_nop 0
	v_pk_add_f32 v[8:9], v[8:9], 1.0 op_sel_hi:[1,0]
	s_nop 0
	v_rcp_f32_e32 v17, v9
	s_nop 0
	v_fma_f32 v18, -v9, v17, 1.0
	v_fmac_f32_e32 v17, v18, v17
	v_div_fixup_f32 v9, v17, v9, 1.0
	v_rcp_f32_e32 v17, v8
	s_nop 0
	v_fma_f32 v18, -v8, v17, 1.0
	v_fmac_f32_e32 v17, v18, v17
	v_div_fixup_f32 v8, v17, v8, 1.0
	v_pk_mul_f32 v[6:7], v[6:7], v[8:9]
	v_lshlrev_b32_e32 v8, 16, v10
	v_and_b32_e32 v9, 0xffff0000, v10
	v_pk_add_f32 v[0:1], v[0:1], v[8:9]
	s_nop 0
	v_mul_f32_e32 v8, 0x3d372713, v0
	v_mul_f32_e32 v9, 0x3d372713, v1
	v_mul_f32_e32 v8, v0, v8
	v_mul_f32_e32 v9, v1, v9
	v_fma_f32 v8, v0, v8, v0
	v_fma_f32 v9, v1, v9, v1
	v_mul_f32_e32 v8, 0x3fcc422a, v8
	v_mul_f32_e32 v9, 0x3fcc422a, v9
	v_mul_f32_e32 v8, 0xbfb8aa3b, v8
	v_mul_f32_e32 v9, 0xbfb8aa3b, v9
	v_exp_f32_e32 v8, v8
	v_exp_f32_e32 v9, v9
	s_nop 0
	v_pk_add_f32 v[8:9], v[8:9], 1.0 op_sel_hi:[1,0]
	s_nop 0
	v_rcp_f32_e32 v16, v9
	s_nop 0
	v_fma_f32 v17, -v9, v16, 1.0
	v_fmac_f32_e32 v16, v17, v16
	v_div_fixup_f32 v9, v16, v9, 1.0
	v_rcp_f32_e32 v16, v8
	s_nop 0
	v_fma_f32 v17, -v8, v16, 1.0
	v_fmac_f32_e32 v16, v17, v16
	v_div_fixup_f32 v8, v16, v8, 1.0
	v_pk_mul_f32 v[8:9], v[0:1], v[8:9]
	v_lshlrev_b32_e32 v0, 16, v11
	v_and_b32_e32 v1, 0xffff0000, v11
	v_pk_add_f32 v[0:1], v[2:3], v[0:1]
	s_nop 0
	v_mul_f32_e32 v2, 0x3d372713, v0
	v_mul_f32_e32 v3, 0x3d372713, v1
	v_mul_f32_e32 v2, v0, v2
	v_mul_f32_e32 v3, v1, v3
	v_fma_f32 v2, v0, v2, v0
	v_fma_f32 v3, v1, v3, v1
	v_mul_f32_e32 v2, 0x3fcc422a, v2
	v_mul_f32_e32 v3, 0x3fcc422a, v3
	v_mul_f32_e32 v2, 0xbfb8aa3b, v2
	v_mul_f32_e32 v3, 0xbfb8aa3b, v3
	v_exp_f32_e32 v2, v2
	v_exp_f32_e32 v3, v3
	s_nop 0
	v_pk_add_f32 v[2:3], v[2:3], 1.0 op_sel_hi:[1,0]
	s_nop 0
	v_rcp_f32_e32 v11, v3
	s_nop 0
	v_fma_f32 v16, -v3, v11, 1.0
	v_fmac_f32_e32 v11, v16, v11
	v_div_fixup_f32 v3, v11, v3, 1.0
	v_rcp_f32_e32 v11, v2
	s_mov_b64 s[46:47], -1
	v_fma_f32 v16, -v2, v11, 1.0
	v_fmac_f32_e32 v11, v16, v11
	v_div_fixup_f32 v2, v11, v2, 1.0
	v_pk_mul_f32 v[10:11], v[0:1], v[2:3]
	v_cvt_pk_bf16_f32 v0, v4, v5
	v_lshl_add_u64 v[4:5], v[12:13], 0, v[116:117]
	v_lshl_add_u64 v[4:5], v[4:5], 0, v[14:15]
	v_cvt_pk_bf16_f32 v1, v6, v7
	v_cvt_pk_bf16_f32 v2, v8, v9
	v_cvt_pk_bf16_f32 v3, v10, v11
	v_lshl_add_u64 v[4:5], v[4:5], 0, v[140:141]
	s_and_b64 vcc, exec, s[0:1]
	global_store_dwordx4 v[4:5], v[0:3], off
	s_cbranch_vccnz .LBB0_1884
	s_andn2_b64 vcc, exec, s[2:3]
	s_cbranch_vccnz .LBB0_1883
	s_barrier
	s_branch .LBB0_1883

; __device__ __forceinline__ float sigmoidf_(float x) { return 1.f / (1.f + __expf(-x)); }
; __device__ __forceinline__ unsigned cvt_pk_bf16(float lo, float hi) { const f32x2c v = {lo, hi}; const bf16x2c b = __builtin_convertvector(v, bf16x2c); return __builtin_bit_cast(unsigned, b); }
;     __device__ __forceinline__ void operator()(const f32x4 (&acc)[2][2][4][2], const Unit& u, int wr, int wc, int fr, int fq) const {
;         const int row0 = u.pm * BM + wr * 64 + fr, col0 = u.pn * BM + wc * 32 + 8 * fq;
; #pragma unroll
;         for (int ai = 0; ai < 2; ++ai)
; #pragma unroll
;             for (int m = 0; m < 4; ++m) { const size_t row = (size_t)(row0 + ai * HALF + m * 16);
; #pragma unroll
;                 for (int bj = 0; bj < 2; ++bj) { const int col = col0 + bj * HALF;
;                     const u32x4 zz = *(const u32x4*)(Z + row * 512 + col);
;                     const f32x4 b0 = *(const f32x4*)(bias + col), b1 = *(const f32x4*)(bias + col + 4);
;                     const f32x4 v0 = acc[ai][bj][m][0] + b0, v1 = acc[ai][bj][m][1] + b1;
;                     float o[8]; const unsigned zw[4] = {zz.x, zz.y, zz.z, zz.w};
; #pragma unroll
;                     for (int q = 0; q < 4; ++q) { const float zl = __builtin_bit_cast(float, zw[q] << 16), zh = __builtin_bit_cast(float, zw[q] & 0xffff0000u);
;                         const float al = (q < 2) ? v0[2 * q] : v1[2 * q - 4], ah = (q < 2) ? v0[2 * q + 1] : v1[2 * q - 3];
;                         o[2 * q] = zl * sigmoidf_(al); o[2 * q + 1] = zh * sigmoidf_(ah); }
;                     u32x4 w; w.x = cvt_pk_bf16(o[0], o[1]); w.y = cvt_pk_bf16(o[2], o[3]); w.z = cvt_pk_bf16(o[4], o[5]); w.w = cvt_pk_bf16(o[6], o[7]);
;                     *(u32x4*)(YM + row * D + 512 + col) = w; } }
.LBB0_2021:
	v_lshl_add_u32 v144, s14, 8, v150
	v_lshl_or_b32 v140, s15, 8, v152
	v_ashrrev_i32_e32 v145, 31, v144
	v_lshlrev_b64 v[142:143], 10, v[144:145]
	v_ashrrev_i32_e32 v141, 31, v140
	v_readlane_b32 s0, v243, 26
	v_lshl_add_u64 v[148:149], s[36:37], 0, v[142:143]
	v_lshlrev_b64 v[142:143], 1, v[140:141]
	v_readlane_b32 s1, v243, 27
	v_lshl_add_u64 v[148:149], v[148:149], 0, v[142:143]
	v_lshl_add_u64 v[140:141], v[140:141], 2, s[0:1]
	v_mov_b32_e32 v166, v148
	v_mov_b32_e32 v167, v149
	global_load_dwordx4 v[170:173], v[140:141], off
	global_load_dwordx4 v[174:177], v[140:141], off offset:16
	global_load_dwordx4 v[178:181], v[140:141], off offset:512
	global_load_dwordx4 v[182:185], v[140:141], off offset:528
	global_load_dwordx4 v[186:189], v[166:167], off
	global_load_dwordx4 v[190:193], v[166:167], off offset:256
	s_mov_b64 s[98:99], 0x4000
	v_lshl_add_u64 v[168:169], v[166:167], 0, s[98:99]
	global_load_dwordx4 v[198:201], v[168:169], off
	global_load_dwordx4 v[202:205], v[168:169], off offset:256
	s_mov_b64 s[98:99], 0x8000
	v_lshl_add_u64 v[168:169], v[166:167], 0, s[98:99]
	global_load_dwordx4 v[206:209], v[168:169], off
	global_load_dwordx4 v[210:213], v[168:169], off offset:256
	v_readlane_b32 s14, v243, 40
	v_readlane_b32 s15, v243, 41
	v_lshlrev_b64 v[146:147], 11, v[144:145]
	v_readlane_b32 s2, v243, 28
	v_readlane_b32 s3, v243, 29
	v_readlane_b32 s4, v243, 30
	v_readlane_b32 s5, v243, 31
	v_readlane_b32 s6, v243, 32
	v_readlane_b32 s7, v243, 33
	v_readlane_b32 s8, v243, 34
	v_readlane_b32 s9, v243, 35
	v_readlane_b32 s10, v243, 36
	v_readlane_b32 s11, v243, 37
	v_readlane_b32 s12, v243, 38
	v_readlane_b32 s13, v243, 39
	s_waitcnt vmcnt(5)
	v_mov_b32_e32 v154, v186
	v_mov_b32_e32 v155, v187
	v_mov_b32_e32 v156, v188
	v_mov_b32_e32 v157, v189
	v_mov_b32_e32 v158, v174
	v_mov_b32_e32 v159, v175
	v_mov_b32_e32 v160, v176
	v_mov_b32_e32 v161, v177
	v_mov_b32_e32 v162, v170
	v_mov_b32_e32 v163, v171
	v_mov_b32_e32 v164, v172
	v_mov_b32_e32 v165, v173
	s_mov_b64 s[98:99], 0xc000
	v_lshl_add_u64 v[168:169], v[166:167], 0, s[98:99]
	global_load_dwordx4 v[186:189], v[168:169], off
	v_pk_add_f32 v[120:121], v[120:121], v[158:159]
	v_pk_add_f32 v[124:125], v[124:125], v[162:163]
	v_lshlrev_b32_e32 v158, 16, v154
	v_mul_f32_e32 v124, 0xbfb8aa3b, v124
	v_mul_f32_e32 v125, 0xbfb8aa3b, v125
	v_exp_f32_e32 v124, v124
	v_exp_f32_e32 v125, v125
	v_and_b32_e32 v159, 0xffff0000, v154
	v_pk_add_f32 v[122:123], v[122:123], v[160:161]
	v_pk_add_f32 v[126:127], v[126:127], v[164:165]
	v_pk_add_f32 v[124:125], v[124:125], 1.0 op_sel_hi:[1,0]
	v_mul_f32_e32 v126, 0xbfb8aa3b, v126
	v_rcp_f32_e32 v154, v125
	v_mul_f32_e32 v127, 0xbfb8aa3b, v127
	v_exp_f32_e32 v126, v126
	v_exp_f32_e32 v127, v127
	v_fma_f32 v160, -v125, v154, 1.0
	v_fmac_f32_e32 v154, v160, v154
	v_div_fixup_f32 v125, v154, v125, 1.0
	v_rcp_f32_e32 v154, v124
	v_pk_add_f32 v[126:127], v[126:127], 1.0 op_sel_hi:[1,0]
	v_mul_f32_e32 v120, 0xbfb8aa3b, v120
	v_mul_f32_e32 v121, 0xbfb8aa3b, v121
	v_fma_f32 v160, -v124, v154, 1.0
	v_fmac_f32_e32 v154, v160, v154
	v_div_fixup_f32 v124, v154, v124, 1.0
	v_div_scale_f32 v145, s[14:15], v127, v127, 1.0
	v_pk_mul_f32 v[124:125], v[124:125], v[158:159]
	v_rcp_f32_e32 v158, v145
	v_exp_f32_e32 v120, v120
	v_exp_f32_e32 v121, v121
	v_lshlrev_b32_e32 v154, 16, v155
	v_fma_f32 v159, -v145, v158, 1.0
	v_fmac_f32_e32 v158, v159, v158
	v_div_scale_f32 v159, vcc, 1.0, v127, 1.0
	v_mul_f32_e32 v160, v159, v158
	v_fma_f32 v161, -v145, v160, v159
	v_fmac_f32_e32 v160, v161, v158
	v_fma_f32 v145, -v145, v160, v159
	v_div_fmas_f32 v145, v145, v158, v160
	v_div_fixup_f32 v127, v145, v127, 1.0
	v_rcp_f32_e32 v158, v126
	v_pk_add_f32 v[120:121], v[120:121], 1.0 op_sel_hi:[1,0]
	v_and_b32_e32 v155, 0xffff0000, v155
	v_fma_f32 v159, -v126, v158, 1.0
	v_fmac_f32_e32 v158, v159, v158
	v_div_fixup_f32 v126, v158, v126, 1.0
	v_div_scale_f32 v145, s[14:15], v121, v121, 1.0
	v_pk_mul_f32 v[126:127], v[126:127], v[154:155]
	v_lshlrev_b32_e32 v154, 16, v156
	v_and_b32_e32 v155, 0xffff0000, v156
	v_rcp_f32_e32 v156, v145
	s_nop 0
	v_fma_f32 v158, -v145, v156, 1.0
	v_fmac_f32_e32 v156, v158, v156
	v_div_scale_f32 v158, vcc, 1.0, v121, 1.0
	v_mul_f32_e32 v159, v158, v156
	v_fma_f32 v160, -v145, v159, v158
	v_fmac_f32_e32 v159, v160, v156
	v_fma_f32 v145, -v145, v159, v158
	v_div_fmas_f32 v145, v145, v156, v159
	v_div_fixup_f32 v121, v145, v121, 1.0
	v_rcp_f32_e32 v156, v120
	s_nop 0
	v_fma_f32 v158, -v120, v156, 1.0
	v_fmac_f32_e32 v156, v158, v156
	v_div_fixup_f32 v120, v156, v120, 1.0
	v_pk_mul_f32 v[154:155], v[120:121], v[154:155]
	v_mul_f32_e32 v120, 0xbfb8aa3b, v122
	v_mul_f32_e32 v121, 0xbfb8aa3b, v123
	v_exp_f32_e32 v120, v120
	v_exp_f32_e32 v121, v121
	v_lshlrev_b32_e32 v122, 16, v157
	v_and_b32_e32 v123, 0xffff0000, v157
	v_pk_add_f32 v[120:121], v[120:121], 1.0 op_sel_hi:[1,0]
	s_nop 0
	v_rcp_f32_e32 v156, v121
	s_nop 0
	v_fma_f32 v157, -v121, v156, 1.0
	v_fmac_f32_e32 v156, v157, v156
	v_div_fixup_f32 v121, v156, v121, 1.0
	v_rcp_f32_e32 v156, v120
	s_nop 0
	v_fma_f32 v157, -v120, v156, 1.0
	v_fmac_f32_e32 v156, v157, v156
	v_div_fixup_f32 v120, v156, v120, 1.0
	v_pk_mul_f32 v[156:157], v[120:121], v[122:123]
	v_cvt_pk_bf16_f32 v120, v124, v125
	v_lshl_add_u64 v[124:125], s[26:27], 0, v[146:147]
	v_cvt_pk_bf16_f32 v121, v126, v127
	v_cvt_pk_bf16_f32 v122, v154, v155
	v_cvt_pk_bf16_f32 v123, v156, v157
	v_lshl_add_u64 v[146:147], v[124:125], 0, v[142:143]
	global_store_dwordx4 v[146:147], v[120:123], off offset:1024
	s_nop 1
	s_nop 0
	s_waitcnt vmcnt(6)
; __device__ __forceinline__ float sigmoidf_(float x) { return 1.f / (1.f + __expf(-x)); }
; __device__ __forceinline__ unsigned cvt_pk_bf16(float lo, float hi) { const f32x2c v = {lo, hi}; const bf16x2c b = __builtin_convertvector(v, bf16x2c); return __builtin_bit_cast(unsigned, b); }
;     __device__ __forceinline__ void operator()(const f32x4 (&acc)[2][2][4][2], const Unit& u, int wr, int wc, int fr, int fq) const {
;     ...
;             for (int m = 0; m < 4; ++m) { const size_t row = (size_t)(row0 + ai * HALF + m * 16);
; #pragma unroll
;                 for (int bj = 0; bj < 2; ++bj) { const int col = col0 + bj * HALF;
;                     const u32x4 zz = *(const u32x4*)(Z + row * 512 + col);
;                     const f32x4 b0 = *(const f32x4*)(bias + col), b1 = *(const f32x4*)(bias + col + 4);
;                     const f32x4 v0 = acc[ai][bj][m][0] + b0, v1 = acc[ai][bj][m][1] + b1;
;                     float o[8]; const unsigned zw[4] = {zz.x, zz.y, zz.z, zz.w};
; #pragma unroll
;                     for (int q = 0; q < 4; ++q) { const float zl = __builtin_bit_cast(float, zw[q] << 16), zh = __builtin_bit_cast(float, zw[q] & 0xffff0000u);
;                         const float al = (q < 2) ? v0[2 * q] : v1[2 * q - 4], ah = (q < 2) ? v0[2 * q + 1] : v1[2 * q - 3];
;                         o[2 * q] = zl * sigmoidf_(al); o[2 * q + 1] = zh * sigmoidf_(ah); }
;                     u32x4 w; w.x = cvt_pk_bf16(o[0], o[1]); w.y = cvt_pk_bf16(o[2], o[3]); w.z = cvt_pk_bf16(o[4], o[5]); w.w = cvt_pk_bf16(o[6], o[7]);
;                     *(u32x4*)(YM + row * D + 512 + col) = w; } }
	v_mov_b32_e32 v120, v190
	v_mov_b32_e32 v121, v191
	v_mov_b32_e32 v122, v192
	v_mov_b32_e32 v123, v193
	v_mov_b32_e32 v124, v182
	v_mov_b32_e32 v125, v183
	v_mov_b32_e32 v126, v184
	v_mov_b32_e32 v127, v185
	v_mov_b32_e32 v154, v178
	v_mov_b32_e32 v155, v179
	v_mov_b32_e32 v156, v180
	v_mov_b32_e32 v157, v181
	global_load_dwordx4 v[190:193], v[168:169], off offset:256
	v_pk_add_f32 v[114:115], v[114:115], v[126:127]
	v_pk_add_f32 v[148:149], v[116:117], v[154:155]
	v_pk_add_f32 v[116:117], v[112:113], v[124:125]
	v_mul_f32_e32 v112, 0xbfb8aa3b, v148
	v_mul_f32_e32 v113, 0xbfb8aa3b, v149
	v_exp_f32_e32 v112, v112
	v_exp_f32_e32 v113, v113
	v_lshlrev_b32_e32 v124, 16, v120
	v_and_b32_e32 v125, 0xffff0000, v120
	v_pk_add_f32 v[118:119], v[118:119], v[156:157]
	v_pk_add_f32 v[112:113], v[112:113], 1.0 op_sel_hi:[1,0]
	v_mul_f32_e32 v118, 0xbfb8aa3b, v118
	v_rcp_f32_e32 v126, v113
	v_mul_f32_e32 v119, 0xbfb8aa3b, v119
	v_exp_f32_e32 v118, v118
	v_exp_f32_e32 v119, v119
	v_fma_f32 v127, -v113, v126, 1.0
	v_fmac_f32_e32 v126, v127, v126
	v_div_fixup_f32 v113, v126, v113, 1.0
	v_rcp_f32_e32 v126, v112
	v_pk_add_f32 v[118:119], v[118:119], 1.0 op_sel_hi:[1,0]
	v_mul_f32_e32 v116, 0xbfb8aa3b, v116
	v_mul_f32_e32 v117, 0xbfb8aa3b, v117
	v_fma_f32 v127, -v112, v126, 1.0
	v_fmac_f32_e32 v126, v127, v126
	v_div_fixup_f32 v112, v126, v112, 1.0
	v_pk_mul_f32 v[112:113], v[112:113], v[124:125]
	v_rcp_f32_e32 v125, v119
	v_exp_f32_e32 v116, v116
	v_exp_f32_e32 v117, v117
	v_lshlrev_b32_e32 v120, 16, v121
	v_fma_f32 v126, -v119, v125, 1.0
	v_fmac_f32_e32 v125, v126, v125
	v_div_fixup_f32 v119, v125, v119, 1.0
	v_rcp_f32_e32 v125, v118
	v_and_b32_e32 v121, 0xffff0000, v121
	v_pk_add_f32 v[116:117], v[116:117], 1.0 op_sel_hi:[1,0]
	v_mul_f32_e32 v114, 0xbfb8aa3b, v114
	v_fma_f32 v126, -v118, v125, 1.0
	v_fmac_f32_e32 v125, v126, v125
	v_div_fixup_f32 v118, v125, v118, 1.0
	v_pk_mul_f32 v[118:119], v[118:119], v[120:121]
	v_lshlrev_b32_e32 v120, 16, v122
	v_and_b32_e32 v121, 0xffff0000, v122
	v_rcp_f32_e32 v124, v117
	v_mul_f32_e32 v115, 0xbfb8aa3b, v115
	v_exp_f32_e32 v114, v114
	v_exp_f32_e32 v115, v115
	v_fma_f32 v125, -v117, v124, 1.0
	v_fmac_f32_e32 v124, v125, v124
	v_div_fixup_f32 v117, v124, v117, 1.0
	v_rcp_f32_e32 v124, v116
	v_pk_add_f32 v[114:115], v[114:115], 1.0 op_sel_hi:[1,0]
	v_cvt_pk_bf16_f32 v112, v112, v113
	v_cvt_pk_bf16_f32 v113, v118, v119
	v_fma_f32 v125, -v116, v124, 1.0
	v_fmac_f32_e32 v124, v125, v124
	v_div_fixup_f32 v116, v124, v116, 1.0
	v_div_scale_f32 v122, s[14:15], v115, v115, 1.0
	v_pk_mul_f32 v[116:117], v[116:117], v[120:121]
	v_lshlrev_b32_e32 v120, 16, v123
	v_and_b32_e32 v121, 0xffff0000, v123
	v_rcp_f32_e32 v123, v122
	s_nop 0
	v_fma_f32 v124, -v122, v123, 1.0
	v_fmac_f32_e32 v123, v124, v123
	v_div_scale_f32 v124, vcc, 1.0, v115, 1.0
	v_mul_f32_e32 v125, v124, v123
	v_fma_f32 v126, -v122, v125, v124
	v_fmac_f32_e32 v125, v126, v123
	v_fma_f32 v122, -v122, v125, v124
	v_div_fmas_f32 v122, v122, v123, v125
	v_div_fixup_f32 v115, v122, v115, 1.0
	v_rcp_f32_e32 v123, v114
	s_nop 0
	v_fma_f32 v124, -v114, v123, 1.0
	v_fmac_f32_e32 v123, v124, v123
	v_div_fixup_f32 v114, v123, v114, 1.0
	v_pk_mul_f32 v[120:121], v[114:115], v[120:121]
	v_cvt_pk_bf16_f32 v114, v116, v117
	v_cvt_pk_bf16_f32 v115, v120, v121
	global_store_dwordx4 v[146:147], v[112:115], off offset:1280
	s_nop 1
	v_or_b32_e32 v112, 16, v144
	v_ashrrev_i32_e32 v113, 31, v112
	v_lshlrev_b64 v[114:115], 10, v[112:113]
	v_lshl_add_u64 v[114:115], s[36:37], 0, v[114:115]
	v_lshl_add_u64 v[114:115], v[114:115], 0, v[142:143]
	s_nop 1
	v_lshlrev_b64 v[112:113], 11, v[112:113]
	s_waitcnt vmcnt(7)
	v_mov_b32_e32 v116, v198
	v_mov_b32_e32 v117, v199
	v_mov_b32_e32 v118, v200
	v_mov_b32_e32 v119, v201
	v_mov_b32_e32 v120, v174
	v_mov_b32_e32 v121, v175
	v_mov_b32_e32 v122, v176
	v_mov_b32_e32 v123, v177
	v_mov_b32_e32 v124, v170
	v_mov_b32_e32 v125, v171
	v_mov_b32_e32 v126, v172
	v_mov_b32_e32 v127, v173
	s_mov_b64 s[98:99], 0x20000
	v_lshl_add_u64 v[168:169], v[166:167], 0, s[98:99]
	global_load_dwordx4 v[198:201], v[168:169], off
	v_pk_add_f32 v[104:105], v[104:105], v[120:121]
	v_pk_add_f32 v[108:109], v[108:109], v[124:125]
	v_lshlrev_b32_e32 v120, 16, v116
	v_mul_f32_e32 v108, 0xbfb8aa3b, v108
	v_mul_f32_e32 v109, 0xbfb8aa3b, v109
	v_exp_f32_e32 v108, v108
	v_exp_f32_e32 v109, v109
	v_and_b32_e32 v121, 0xffff0000, v116
	v_pk_add_f32 v[106:107], v[106:107], v[122:123]
	v_pk_add_f32 v[110:111], v[110:111], v[126:127]
	v_pk_add_f32 v[108:109], v[108:109], 1.0 op_sel_hi:[1,0]
	v_mul_f32_e32 v110, 0xbfb8aa3b, v110
	v_rcp_f32_e32 v122, v109
	v_mul_f32_e32 v111, 0xbfb8aa3b, v111
	v_exp_f32_e32 v110, v110
	v_exp_f32_e32 v111, v111
	v_fma_f32 v123, -v109, v122, 1.0
	v_fmac_f32_e32 v122, v123, v122
	v_div_fixup_f32 v109, v122, v109, 1.0
	v_rcp_f32_e32 v122, v108
	v_pk_add_f32 v[110:111], v[110:111], 1.0 op_sel_hi:[1,0]
	v_mul_f32_e32 v104, 0xbfb8aa3b, v104
	v_mul_f32_e32 v105, 0xbfb8aa3b, v105
	v_fma_f32 v123, -v108, v122, 1.0
	v_fmac_f32_e32 v122, v123, v122
	v_div_fixup_f32 v108, v122, v108, 1.0
	v_pk_mul_f32 v[108:109], v[108:109], v[120:121]
	v_rcp_f32_e32 v121, v111
	v_exp_f32_e32 v104, v104
	v_exp_f32_e32 v105, v105
	v_lshlrev_b32_e32 v116, 16, v117
	v_fma_f32 v122, -v111, v121, 1.0
	v_fmac_f32_e32 v121, v122, v121
	v_div_fixup_f32 v111, v121, v111, 1.0
	v_rcp_f32_e32 v121, v110
	v_and_b32_e32 v117, 0xffff0000, v117
	v_pk_add_f32 v[104:105], v[104:105], 1.0 op_sel_hi:[1,0]
	v_fma_f32 v122, -v110, v121, 1.0
	v_fmac_f32_e32 v121, v122, v121
	v_div_fixup_f32 v110, v121, v110, 1.0
	v_pk_mul_f32 v[110:111], v[110:111], v[116:117]
	v_lshlrev_b32_e32 v116, 16, v118
	v_and_b32_e32 v117, 0xffff0000, v118
	v_rcp_f32_e32 v120, v105
	s_nop 0
	v_fma_f32 v121, -v105, v120, 1.0
	v_fmac_f32_e32 v120, v121, v120
	v_div_fixup_f32 v105, v120, v105, 1.0
	v_rcp_f32_e32 v120, v104
	s_nop 0
	v_fma_f32 v121, -v104, v120, 1.0
	v_fmac_f32_e32 v120, v121, v120
	v_div_fixup_f32 v104, v120, v104, 1.0
	v_pk_mul_f32 v[116:117], v[104:105], v[116:117]
	v_mul_f32_e32 v104, 0xbfb8aa3b, v106
	v_mul_f32_e32 v105, 0xbfb8aa3b, v107
	v_exp_f32_e32 v104, v104
	v_exp_f32_e32 v105, v105
	v_lshlrev_b32_e32 v106, 16, v119
	v_and_b32_e32 v107, 0xffff0000, v119
	v_pk_add_f32 v[104:105], v[104:105], 1.0 op_sel_hi:[1,0]
	s_nop 0
	v_rcp_f32_e32 v119, v105
	s_nop 0
	v_fma_f32 v120, -v105, v119, 1.0
	v_fmac_f32_e32 v119, v120, v119
	v_div_fixup_f32 v105, v119, v105, 1.0
	v_rcp_f32_e32 v119, v104
	s_nop 0
	v_fma_f32 v120, -v104, v119, 1.0
	v_fmac_f32_e32 v119, v120, v119
	v_div_fixup_f32 v104, v119, v104, 1.0
	v_pk_mul_f32 v[118:119], v[104:105], v[106:107]
	v_cvt_pk_bf16_f32 v104, v108, v109
	v_lshl_add_u64 v[108:109], s[26:27], 0, v[112:113]
	v_cvt_pk_bf16_f32 v105, v110, v111
	v_cvt_pk_bf16_f32 v106, v116, v117
	v_cvt_pk_bf16_f32 v107, v118, v119
	v_lshl_add_u64 v[112:113], v[108:109], 0, v[142:143]
	global_store_dwordx4 v[112:113], v[104:107], off offset:1024
	s_nop 1
	s_nop 0
	s_waitcnt vmcnt(8)
; __device__ __forceinline__ float sigmoidf_(float x) { return 1.f / (1.f + __expf(-x)); }
; __device__ __forceinline__ unsigned cvt_pk_bf16(float lo, float hi) { const f32x2c v = {lo, hi}; const bf16x2c b = __builtin_convertvector(v, bf16x2c); return __builtin_bit_cast(unsigned, b); }
;     __device__ __forceinline__ void operator()(const f32x4 (&acc)[2][2][4][2], const Unit& u, int wr, int wc, int fr, int fq) const {
;     ...
;             for (int m = 0; m < 4; ++m) { const size_t row = (size_t)(row0 + ai * HALF + m * 16);
; #pragma unroll
;                 for (int bj = 0; bj < 2; ++bj) { const int col = col0 + bj * HALF;
;                     const u32x4 zz = *(const u32x4*)(Z + row * 512 + col);
;                     const f32x4 b0 = *(const f32x4*)(bias + col), b1 = *(const f32x4*)(bias + col + 4);
;                     const f32x4 v0 = acc[ai][bj][m][0] + b0, v1 = acc[ai][bj][m][1] + b1;
;                     float o[8]; const unsigned zw[4] = {zz.x, zz.y, zz.z, zz.w};
; #pragma unroll
;                     for (int q = 0; q < 4; ++q) { const float zl = __builtin_bit_cast(float, zw[q] << 16), zh = __builtin_bit_cast(float, zw[q] & 0xffff0000u);
;                         const float al = (q < 2) ? v0[2 * q] : v1[2 * q - 4], ah = (q < 2) ? v0[2 * q + 1] : v1[2 * q - 3];
;                         o[2 * q] = zl * sigmoidf_(al); o[2 * q + 1] = zh * sigmoidf_(ah); }
;                     u32x4 w; w.x = cvt_pk_bf16(o[0], o[1]); w.y = cvt_pk_bf16(o[2], o[3]); w.z = cvt_pk_bf16(o[4], o[5]); w.w = cvt_pk_bf16(o[6], o[7]);
;                     *(u32x4*)(YM + row * D + 512 + col) = w; } }
	v_mov_b32_e32 v104, v202
	v_mov_b32_e32 v105, v203
	v_mov_b32_e32 v106, v204
	v_mov_b32_e32 v107, v205
	v_mov_b32_e32 v108, v182
	v_mov_b32_e32 v109, v183
	v_mov_b32_e32 v110, v184
	v_mov_b32_e32 v111, v185
	v_mov_b32_e32 v114, v178
	v_mov_b32_e32 v115, v179
	v_mov_b32_e32 v116, v180
	v_mov_b32_e32 v117, v181
	global_load_dwordx4 v[202:205], v[168:169], off offset:256
	v_pk_add_f32 v[108:109], v[96:97], v[108:109]
	v_pk_add_f32 v[100:101], v[100:101], v[114:115]
	v_pk_add_f32 v[98:99], v[98:99], v[110:111]
	v_mul_f32_e32 v96, 0xbfb8aa3b, v100
	v_mul_f32_e32 v97, 0xbfb8aa3b, v101
	v_exp_f32_e32 v96, v96
	v_exp_f32_e32 v97, v97
	v_lshlrev_b32_e32 v100, 16, v104
	v_and_b32_e32 v101, 0xffff0000, v104
	v_pk_add_f32 v[102:103], v[102:103], v[116:117]
	v_pk_add_f32 v[96:97], v[96:97], 1.0 op_sel_hi:[1,0]
	v_mul_f32_e32 v98, 0xbfb8aa3b, v98
	v_rcp_f32_e32 v110, v97
	v_mul_f32_e32 v99, 0xbfb8aa3b, v99
	v_exp_f32_e32 v98, v98
	v_exp_f32_e32 v99, v99
	v_fma_f32 v111, -v97, v110, 1.0
	v_fmac_f32_e32 v110, v111, v110
	v_div_fixup_f32 v97, v110, v97, 1.0
	v_rcp_f32_e32 v110, v96
	v_pk_add_f32 v[98:99], v[98:99], 1.0 op_sel_hi:[1,0]
	v_fma_f32 v111, -v96, v110, 1.0
	v_fmac_f32_e32 v110, v111, v110
	v_div_fixup_f32 v96, v110, v96, 1.0
	v_pk_mul_f32 v[96:97], v[96:97], v[100:101]
	v_mul_f32_e32 v100, 0xbfb8aa3b, v102
	v_mul_f32_e32 v101, 0xbfb8aa3b, v103
	v_exp_f32_e32 v100, v100
	v_exp_f32_e32 v101, v101
	v_lshlrev_b32_e32 v102, 16, v105
	v_and_b32_e32 v103, 0xffff0000, v105
	v_cvt_pk_bf16_f32 v96, v96, v97
	v_pk_add_f32 v[100:101], v[100:101], 1.0 op_sel_hi:[1,0]
	s_nop 0
	v_rcp_f32_e32 v105, v101
	s_nop 0
	v_fma_f32 v110, -v101, v105, 1.0
	v_fmac_f32_e32 v105, v110, v105
	v_div_fixup_f32 v101, v105, v101, 1.0
	v_rcp_f32_e32 v105, v100
	s_nop 0
	v_fma_f32 v110, -v100, v105, 1.0
	v_fmac_f32_e32 v105, v110, v105
	v_div_fixup_f32 v100, v105, v100, 1.0
	v_pk_mul_f32 v[100:101], v[100:101], v[102:103]
	v_mul_f32_e32 v102, 0xbfb8aa3b, v108
	v_mul_f32_e32 v103, 0xbfb8aa3b, v109
	v_exp_f32_e32 v102, v102
	v_exp_f32_e32 v103, v103
	v_lshlrev_b32_e32 v104, 16, v106
	v_and_b32_e32 v105, 0xffff0000, v106
	v_cvt_pk_bf16_f32 v97, v100, v101
	v_pk_add_f32 v[102:103], v[102:103], 1.0 op_sel_hi:[1,0]
	s_nop 0
	v_rcp_f32_e32 v108, v103
	s_nop 0
	v_fma_f32 v109, -v103, v108, 1.0
	v_fmac_f32_e32 v108, v109, v108
	v_div_fixup_f32 v103, v108, v103, 1.0
	v_rcp_f32_e32 v108, v102
	s_nop 0
	v_fma_f32 v109, -v102, v108, 1.0
	v_fmac_f32_e32 v108, v109, v108
	v_div_fixup_f32 v102, v108, v102, 1.0
	v_div_scale_f32 v106, s[14:15], v99, v99, 1.0
	v_pk_mul_f32 v[102:103], v[102:103], v[104:105]
	v_lshlrev_b32_e32 v104, 16, v107
	v_and_b32_e32 v105, 0xffff0000, v107
	v_rcp_f32_e32 v107, v106
	s_nop 0
	v_fma_f32 v108, -v106, v107, 1.0
	v_fmac_f32_e32 v107, v108, v107
	v_div_scale_f32 v108, vcc, 1.0, v99, 1.0
	v_mul_f32_e32 v109, v108, v107
	v_fma_f32 v110, -v106, v109, v108
	v_fmac_f32_e32 v109, v110, v107
	v_fma_f32 v106, -v106, v109, v108
	v_div_fmas_f32 v106, v106, v107, v109
	v_div_fixup_f32 v99, v106, v99, 1.0
	v_rcp_f32_e32 v107, v98
	s_nop 0
	v_fma_f32 v108, -v98, v107, 1.0
	v_fmac_f32_e32 v107, v108, v107
	v_div_fixup_f32 v98, v107, v98, 1.0
	v_pk_mul_f32 v[104:105], v[98:99], v[104:105]
	v_cvt_pk_bf16_f32 v98, v102, v103
	v_cvt_pk_bf16_f32 v99, v104, v105
	global_store_dwordx4 v[112:113], v[96:99], off offset:1280
	s_nop 1
	v_or_b32_e32 v96, 32, v144
	v_ashrrev_i32_e32 v97, 31, v96
	v_lshlrev_b64 v[98:99], 10, v[96:97]
	v_lshl_add_u64 v[98:99], s[36:37], 0, v[98:99]
	v_lshl_add_u64 v[98:99], v[98:99], 0, v[142:143]
	s_nop 1
	v_lshlrev_b64 v[96:97], 11, v[96:97]
	s_waitcnt vmcnt(9)
	v_mov_b32_e32 v100, v206
	v_mov_b32_e32 v101, v207
	v_mov_b32_e32 v102, v208
	v_mov_b32_e32 v103, v209
	v_mov_b32_e32 v104, v174
	v_mov_b32_e32 v105, v175
	v_mov_b32_e32 v106, v176
	v_mov_b32_e32 v107, v177
	v_mov_b32_e32 v108, v170
	v_mov_b32_e32 v109, v171
	v_mov_b32_e32 v110, v172
	v_mov_b32_e32 v111, v173
	s_mov_b64 s[98:99], 0x24000
	v_lshl_add_u64 v[168:169], v[166:167], 0, s[98:99]
	global_load_dwordx4 v[206:209], v[168:169], off
	v_pk_add_f32 v[88:89], v[88:89], v[104:105]
	v_pk_add_f32 v[92:93], v[92:93], v[108:109]
	v_lshlrev_b32_e32 v104, 16, v100
	v_mul_f32_e32 v92, 0xbfb8aa3b, v92
	v_mul_f32_e32 v93, 0xbfb8aa3b, v93
	v_exp_f32_e32 v92, v92
	v_exp_f32_e32 v93, v93
	v_and_b32_e32 v105, 0xffff0000, v100
	v_pk_add_f32 v[90:91], v[90:91], v[106:107]
	v_pk_add_f32 v[94:95], v[94:95], v[110:111]
	v_pk_add_f32 v[92:93], v[92:93], 1.0 op_sel_hi:[1,0]
	v_mul_f32_e32 v94, 0xbfb8aa3b, v94
	v_rcp_f32_e32 v106, v93
	v_mul_f32_e32 v95, 0xbfb8aa3b, v95
	v_exp_f32_e32 v94, v94
	v_exp_f32_e32 v95, v95
	v_fma_f32 v107, -v93, v106, 1.0
	v_fmac_f32_e32 v106, v107, v106
	v_div_fixup_f32 v93, v106, v93, 1.0
	v_rcp_f32_e32 v106, v92
	v_pk_add_f32 v[94:95], v[94:95], 1.0 op_sel_hi:[1,0]
	v_mul_f32_e32 v88, 0xbfb8aa3b, v88
	v_mul_f32_e32 v89, 0xbfb8aa3b, v89
	v_fma_f32 v107, -v92, v106, 1.0
	v_fmac_f32_e32 v106, v107, v106
	v_div_fixup_f32 v92, v106, v92, 1.0
	v_pk_mul_f32 v[92:93], v[92:93], v[104:105]
	v_rcp_f32_e32 v105, v95
	v_exp_f32_e32 v88, v88
	v_exp_f32_e32 v89, v89
	v_lshlrev_b32_e32 v100, 16, v101
	v_fma_f32 v106, -v95, v105, 1.0
	v_fmac_f32_e32 v105, v106, v105
	v_div_fixup_f32 v95, v105, v95, 1.0
	v_rcp_f32_e32 v105, v94
	v_and_b32_e32 v101, 0xffff0000, v101
	v_pk_add_f32 v[88:89], v[88:89], 1.0 op_sel_hi:[1,0]
	v_fma_f32 v106, -v94, v105, 1.0
	v_fmac_f32_e32 v105, v106, v105
	v_div_fixup_f32 v94, v105, v94, 1.0
	v_pk_mul_f32 v[94:95], v[94:95], v[100:101]
	v_lshlrev_b32_e32 v100, 16, v102
	v_and_b32_e32 v101, 0xffff0000, v102
	v_rcp_f32_e32 v104, v89
	s_nop 0
	v_fma_f32 v105, -v89, v104, 1.0
	v_fmac_f32_e32 v104, v105, v104
	v_div_fixup_f32 v89, v104, v89, 1.0
	v_rcp_f32_e32 v104, v88
	s_nop 0
	v_fma_f32 v105, -v88, v104, 1.0
	v_fmac_f32_e32 v104, v105, v104
	v_div_fixup_f32 v88, v104, v88, 1.0
	v_pk_mul_f32 v[100:101], v[88:89], v[100:101]
	v_mul_f32_e32 v88, 0xbfb8aa3b, v90
	v_mul_f32_e32 v89, 0xbfb8aa3b, v91
	v_exp_f32_e32 v88, v88
	v_exp_f32_e32 v89, v89
	v_lshlrev_b32_e32 v90, 16, v103
	v_and_b32_e32 v91, 0xffff0000, v103
	v_pk_add_f32 v[88:89], v[88:89], 1.0 op_sel_hi:[1,0]
	s_nop 0
	v_rcp_f32_e32 v103, v89
	s_nop 0
	v_fma_f32 v104, -v89, v103, 1.0
	v_fmac_f32_e32 v103, v104, v103
	v_div_fixup_f32 v89, v103, v89, 1.0
	v_rcp_f32_e32 v103, v88
	s_nop 0
	v_fma_f32 v104, -v88, v103, 1.0
	v_fmac_f32_e32 v103, v104, v103
	v_div_fixup_f32 v88, v103, v88, 1.0
	v_pk_mul_f32 v[102:103], v[88:89], v[90:91]
	v_cvt_pk_bf16_f32 v88, v92, v93
	v_lshl_add_u64 v[92:93], s[26:27], 0, v[96:97]
	v_cvt_pk_bf16_f32 v89, v94, v95
	v_cvt_pk_bf16_f32 v90, v100, v101
	v_cvt_pk_bf16_f32 v91, v102, v103
	v_lshl_add_u64 v[96:97], v[92:93], 0, v[142:143]
	global_store_dwordx4 v[96:97], v[88:91], off offset:1024
	s_nop 1
	s_nop 0
	s_waitcnt vmcnt(10)
; __device__ __forceinline__ float sigmoidf_(float x) { return 1.f / (1.f + __expf(-x)); }
; __device__ __forceinline__ unsigned cvt_pk_bf16(float lo, float hi) { const f32x2c v = {lo, hi}; const bf16x2c b = __builtin_convertvector(v, bf16x2c); return __builtin_bit_cast(unsigned, b); }
;     __device__ __forceinline__ void operator()(const f32x4 (&acc)[2][2][4][2], const Unit& u, int wr, int wc, int fr, int fq) const {
;     ...
;             for (int m = 0; m < 4; ++m) { const size_t row = (size_t)(row0 + ai * HALF + m * 16);
; #pragma unroll
;                 for (int bj = 0; bj < 2; ++bj) { const int col = col0 + bj * HALF;
;                     const u32x4 zz = *(const u32x4*)(Z + row * 512 + col);
;                     const f32x4 b0 = *(const f32x4*)(bias + col), b1 = *(const f32x4*)(bias + col + 4);
;                     const f32x4 v0 = acc[ai][bj][m][0] + b0, v1 = acc[ai][bj][m][1] + b1;
;                     float o[8]; const unsigned zw[4] = {zz.x, zz.y, zz.z, zz.w};
; #pragma unroll
;                     for (int q = 0; q < 4; ++q) { const float zl = __builtin_bit_cast(float, zw[q] << 16), zh = __builtin_bit_cast(float, zw[q] & 0xffff0000u);
;                         const float al = (q < 2) ? v0[2 * q] : v1[2 * q - 4], ah = (q < 2) ? v0[2 * q + 1] : v1[2 * q - 3];
;                         o[2 * q] = zl * sigmoidf_(al); o[2 * q + 1] = zh * sigmoidf_(ah); }
;                     u32x4 w; w.x = cvt_pk_bf16(o[0], o[1]); w.y = cvt_pk_bf16(o[2], o[3]); w.z = cvt_pk_bf16(o[4], o[5]); w.w = cvt_pk_bf16(o[6], o[7]);
;                     *(u32x4*)(YM + row * D + 512 + col) = w; } }
	v_mov_b32_e32 v88, v210
	v_mov_b32_e32 v89, v211
	v_mov_b32_e32 v90, v212
	v_mov_b32_e32 v91, v213
	v_mov_b32_e32 v92, v182
	v_mov_b32_e32 v93, v183
	v_mov_b32_e32 v94, v184
	v_mov_b32_e32 v95, v185
	v_mov_b32_e32 v98, v178
	v_mov_b32_e32 v99, v179
	v_mov_b32_e32 v100, v180
	v_mov_b32_e32 v101, v181
	global_load_dwordx4 v[210:213], v[168:169], off offset:256
	v_pk_add_f32 v[92:93], v[80:81], v[92:93]
	v_pk_add_f32 v[84:85], v[84:85], v[98:99]
	v_pk_add_f32 v[82:83], v[82:83], v[94:95]
	v_mul_f32_e32 v80, 0xbfb8aa3b, v84
	v_mul_f32_e32 v81, 0xbfb8aa3b, v85
	v_exp_f32_e32 v80, v80
	v_exp_f32_e32 v81, v81
	v_lshlrev_b32_e32 v84, 16, v88
	v_and_b32_e32 v85, 0xffff0000, v88
	v_pk_add_f32 v[86:87], v[86:87], v[100:101]
	v_pk_add_f32 v[80:81], v[80:81], 1.0 op_sel_hi:[1,0]
	v_mul_f32_e32 v82, 0xbfb8aa3b, v82
	v_rcp_f32_e32 v94, v81
	v_mul_f32_e32 v83, 0xbfb8aa3b, v83
	v_exp_f32_e32 v82, v82
	v_exp_f32_e32 v83, v83
	v_fma_f32 v95, -v81, v94, 1.0
	v_fmac_f32_e32 v94, v95, v94
	v_div_fixup_f32 v81, v94, v81, 1.0
	v_rcp_f32_e32 v94, v80
	v_pk_add_f32 v[82:83], v[82:83], 1.0 op_sel_hi:[1,0]
	v_fma_f32 v95, -v80, v94, 1.0
	v_fmac_f32_e32 v94, v95, v94
	v_div_fixup_f32 v80, v94, v80, 1.0
	v_pk_mul_f32 v[80:81], v[80:81], v[84:85]
	v_mul_f32_e32 v84, 0xbfb8aa3b, v86
	v_mul_f32_e32 v85, 0xbfb8aa3b, v87
	v_exp_f32_e32 v84, v84
	v_exp_f32_e32 v85, v85
	v_lshlrev_b32_e32 v86, 16, v89
	v_and_b32_e32 v87, 0xffff0000, v89
	v_cvt_pk_bf16_f32 v80, v80, v81
	v_pk_add_f32 v[84:85], v[84:85], 1.0 op_sel_hi:[1,0]
	s_nop 0
	v_rcp_f32_e32 v89, v85
	s_nop 0
	v_fma_f32 v94, -v85, v89, 1.0
	v_fmac_f32_e32 v89, v94, v89
	v_div_fixup_f32 v85, v89, v85, 1.0
	v_rcp_f32_e32 v89, v84
	s_nop 0
	v_fma_f32 v94, -v84, v89, 1.0
	v_fmac_f32_e32 v89, v94, v89
	v_div_fixup_f32 v84, v89, v84, 1.0
	v_pk_mul_f32 v[84:85], v[84:85], v[86:87]
	v_mul_f32_e32 v86, 0xbfb8aa3b, v92
	v_mul_f32_e32 v87, 0xbfb8aa3b, v93
	v_exp_f32_e32 v86, v86
	v_exp_f32_e32 v87, v87
	v_lshlrev_b32_e32 v88, 16, v90
	v_and_b32_e32 v89, 0xffff0000, v90
	v_cvt_pk_bf16_f32 v81, v84, v85
	v_pk_add_f32 v[86:87], v[86:87], 1.0 op_sel_hi:[1,0]
	s_nop 0
	v_rcp_f32_e32 v92, v87
	s_nop 0
	v_fma_f32 v93, -v87, v92, 1.0
	v_fmac_f32_e32 v92, v93, v92
	v_div_fixup_f32 v87, v92, v87, 1.0
	v_rcp_f32_e32 v92, v86
	s_nop 0
	v_fma_f32 v93, -v86, v92, 1.0
	v_fmac_f32_e32 v92, v93, v92
	v_div_fixup_f32 v86, v92, v86, 1.0
	v_div_scale_f32 v90, s[14:15], v83, v83, 1.0
	v_pk_mul_f32 v[86:87], v[86:87], v[88:89]
	v_lshlrev_b32_e32 v88, 16, v91
	v_and_b32_e32 v89, 0xffff0000, v91
	v_rcp_f32_e32 v91, v90
	s_nop 0
	v_fma_f32 v92, -v90, v91, 1.0
	v_fmac_f32_e32 v91, v92, v91
	v_div_scale_f32 v92, vcc, 1.0, v83, 1.0
	v_mul_f32_e32 v93, v92, v91
	v_fma_f32 v94, -v90, v93, v92
	v_fmac_f32_e32 v93, v94, v91
	v_fma_f32 v90, -v90, v93, v92
	v_div_fmas_f32 v90, v90, v91, v93
	v_div_fixup_f32 v83, v90, v83, 1.0
	v_rcp_f32_e32 v91, v82
	s_nop 0
	v_fma_f32 v92, -v82, v91, 1.0
	v_fmac_f32_e32 v91, v92, v91
	v_div_fixup_f32 v82, v91, v82, 1.0
	v_pk_mul_f32 v[88:89], v[82:83], v[88:89]
	v_cvt_pk_bf16_f32 v82, v86, v87
	v_cvt_pk_bf16_f32 v83, v88, v89
	global_store_dwordx4 v[96:97], v[80:83], off offset:1280
	s_nop 1
	v_or_b32_e32 v80, 48, v144
	v_ashrrev_i32_e32 v81, 31, v80
	v_lshlrev_b64 v[82:83], 10, v[80:81]
	v_lshl_add_u64 v[82:83], s[36:37], 0, v[82:83]
	v_lshl_add_u64 v[82:83], v[82:83], 0, v[142:143]
	s_nop 1
	v_lshlrev_b64 v[80:81], 11, v[80:81]
	s_waitcnt vmcnt(11)
	v_mov_b32_e32 v84, v186
	v_mov_b32_e32 v85, v187
	v_mov_b32_e32 v86, v188
	v_mov_b32_e32 v87, v189
	v_mov_b32_e32 v88, v174
	v_mov_b32_e32 v89, v175
	v_mov_b32_e32 v90, v176
	v_mov_b32_e32 v91, v177
	v_mov_b32_e32 v92, v170
	v_mov_b32_e32 v93, v171
	v_mov_b32_e32 v94, v172
	v_mov_b32_e32 v95, v173
	s_mov_b64 s[98:99], 0x28000
	v_lshl_add_u64 v[168:169], v[166:167], 0, s[98:99]
	global_load_dwordx4 v[186:189], v[168:169], off
	v_pk_add_f32 v[72:73], v[72:73], v[88:89]
	v_pk_add_f32 v[76:77], v[76:77], v[92:93]
	v_lshlrev_b32_e32 v88, 16, v84
	v_mul_f32_e32 v76, 0xbfb8aa3b, v76
	v_mul_f32_e32 v77, 0xbfb8aa3b, v77
	v_exp_f32_e32 v76, v76
	v_exp_f32_e32 v77, v77
	v_and_b32_e32 v89, 0xffff0000, v84
	v_pk_add_f32 v[74:75], v[74:75], v[90:91]
	v_pk_add_f32 v[78:79], v[78:79], v[94:95]
	v_pk_add_f32 v[76:77], v[76:77], 1.0 op_sel_hi:[1,0]
	v_mul_f32_e32 v78, 0xbfb8aa3b, v78
	v_rcp_f32_e32 v90, v77
	v_mul_f32_e32 v79, 0xbfb8aa3b, v79
	v_exp_f32_e32 v78, v78
	v_exp_f32_e32 v79, v79
	v_fma_f32 v91, -v77, v90, 1.0
	v_fmac_f32_e32 v90, v91, v90
	v_div_fixup_f32 v77, v90, v77, 1.0
	v_rcp_f32_e32 v90, v76
	v_pk_add_f32 v[78:79], v[78:79], 1.0 op_sel_hi:[1,0]
	v_mul_f32_e32 v72, 0xbfb8aa3b, v72
	v_mul_f32_e32 v73, 0xbfb8aa3b, v73
	v_fma_f32 v91, -v76, v90, 1.0
	v_fmac_f32_e32 v90, v91, v90
	v_div_fixup_f32 v76, v90, v76, 1.0
	v_pk_mul_f32 v[76:77], v[76:77], v[88:89]
	v_rcp_f32_e32 v89, v79
	v_exp_f32_e32 v72, v72
	v_exp_f32_e32 v73, v73
	v_lshlrev_b32_e32 v84, 16, v85
	v_fma_f32 v90, -v79, v89, 1.0
	v_fmac_f32_e32 v89, v90, v89
	v_div_fixup_f32 v79, v89, v79, 1.0
	v_rcp_f32_e32 v89, v78
	v_and_b32_e32 v85, 0xffff0000, v85
	v_pk_add_f32 v[72:73], v[72:73], 1.0 op_sel_hi:[1,0]
	v_fma_f32 v90, -v78, v89, 1.0
	v_fmac_f32_e32 v89, v90, v89
	v_div_fixup_f32 v78, v89, v78, 1.0
	v_pk_mul_f32 v[78:79], v[78:79], v[84:85]
	v_lshlrev_b32_e32 v84, 16, v86
	v_and_b32_e32 v85, 0xffff0000, v86
	v_rcp_f32_e32 v88, v73
	s_nop 0
	v_fma_f32 v89, -v73, v88, 1.0
	v_fmac_f32_e32 v88, v89, v88
	v_div_fixup_f32 v73, v88, v73, 1.0
	v_rcp_f32_e32 v88, v72
	s_nop 0
	v_fma_f32 v89, -v72, v88, 1.0
	v_fmac_f32_e32 v88, v89, v88
	v_div_fixup_f32 v72, v88, v72, 1.0
	v_pk_mul_f32 v[84:85], v[72:73], v[84:85]
	v_mul_f32_e32 v72, 0xbfb8aa3b, v74
	v_mul_f32_e32 v73, 0xbfb8aa3b, v75
	v_exp_f32_e32 v72, v72
	v_exp_f32_e32 v73, v73
	v_lshlrev_b32_e32 v74, 16, v87
	v_and_b32_e32 v75, 0xffff0000, v87
	v_pk_add_f32 v[72:73], v[72:73], 1.0 op_sel_hi:[1,0]
	s_nop 0
	v_rcp_f32_e32 v87, v73
	s_nop 0
	v_fma_f32 v88, -v73, v87, 1.0
	v_fmac_f32_e32 v87, v88, v87
	v_div_fixup_f32 v73, v87, v73, 1.0
	v_rcp_f32_e32 v87, v72
	s_nop 0
	v_fma_f32 v88, -v72, v87, 1.0
	v_fmac_f32_e32 v87, v88, v87
	v_div_fixup_f32 v72, v87, v72, 1.0
	v_pk_mul_f32 v[86:87], v[72:73], v[74:75]
	v_cvt_pk_bf16_f32 v72, v76, v77
	v_lshl_add_u64 v[76:77], s[26:27], 0, v[80:81]
	v_cvt_pk_bf16_f32 v73, v78, v79
	v_cvt_pk_bf16_f32 v74, v84, v85
	v_cvt_pk_bf16_f32 v75, v86, v87
	v_lshl_add_u64 v[80:81], v[76:77], 0, v[142:143]
	global_store_dwordx4 v[80:81], v[72:75], off offset:1024
	s_nop 1
	s_nop 0
	s_waitcnt vmcnt(11)
; __device__ __forceinline__ float sigmoidf_(float x) { return 1.f / (1.f + __expf(-x)); }
; __device__ __forceinline__ unsigned cvt_pk_bf16(float lo, float hi) { const f32x2c v = {lo, hi}; const bf16x2c b = __builtin_convertvector(v, bf16x2c); return __builtin_bit_cast(unsigned, b); }
;     __device__ __forceinline__ void operator()(const f32x4 (&acc)[2][2][4][2], const Unit& u, int wr, int wc, int fr, int fq) const {
;     ...
;             for (int m = 0; m < 4; ++m) { const size_t row = (size_t)(row0 + ai * HALF + m * 16);
; #pragma unroll
;                 for (int bj = 0; bj < 2; ++bj) { const int col = col0 + bj * HALF;
;                     const u32x4 zz = *(const u32x4*)(Z + row * 512 + col);
;                     const f32x4 b0 = *(const f32x4*)(bias + col), b1 = *(const f32x4*)(bias + col + 4);
;                     const f32x4 v0 = acc[ai][bj][m][0] + b0, v1 = acc[ai][bj][m][1] + b1;
;                     float o[8]; const unsigned zw[4] = {zz.x, zz.y, zz.z, zz.w};
; #pragma unroll
;                     for (int q = 0; q < 4; ++q) { const float zl = __builtin_bit_cast(float, zw[q] << 16), zh = __builtin_bit_cast(float, zw[q] & 0xffff0000u);
;                         const float al = (q < 2) ? v0[2 * q] : v1[2 * q - 4], ah = (q < 2) ? v0[2 * q + 1] : v1[2 * q - 3];
;                         o[2 * q] = zl * sigmoidf_(al); o[2 * q + 1] = zh * sigmoidf_(ah); }
;                     u32x4 w; w.x = cvt_pk_bf16(o[0], o[1]); w.y = cvt_pk_bf16(o[2], o[3]); w.z = cvt_pk_bf16(o[4], o[5]); w.w = cvt_pk_bf16(o[6], o[7]);
;                     *(u32x4*)(YM + row * D + 512 + col) = w; } }
	v_mov_b32_e32 v72, v190
	v_mov_b32_e32 v73, v191
	v_mov_b32_e32 v74, v192
	v_mov_b32_e32 v75, v193
	v_mov_b32_e32 v76, v182
	v_mov_b32_e32 v77, v183
	v_mov_b32_e32 v78, v184
	v_mov_b32_e32 v79, v185
	v_mov_b32_e32 v82, v178
	v_mov_b32_e32 v83, v179
	v_mov_b32_e32 v84, v180
	v_mov_b32_e32 v85, v181
	global_load_dwordx4 v[190:193], v[168:169], off offset:256
	v_pk_add_f32 v[76:77], v[64:65], v[76:77]
	v_pk_add_f32 v[68:69], v[68:69], v[82:83]
	v_pk_add_f32 v[66:67], v[66:67], v[78:79]
	v_mul_f32_e32 v64, 0xbfb8aa3b, v68
	v_mul_f32_e32 v65, 0xbfb8aa3b, v69
	v_exp_f32_e32 v64, v64
	v_exp_f32_e32 v65, v65
	v_lshlrev_b32_e32 v68, 16, v72
	v_and_b32_e32 v69, 0xffff0000, v72
	v_pk_add_f32 v[70:71], v[70:71], v[84:85]
	v_pk_add_f32 v[64:65], v[64:65], 1.0 op_sel_hi:[1,0]
	v_mul_f32_e32 v66, 0xbfb8aa3b, v66
	v_rcp_f32_e32 v78, v65
	v_mul_f32_e32 v67, 0xbfb8aa3b, v67
	v_exp_f32_e32 v66, v66
	v_exp_f32_e32 v67, v67
	v_fma_f32 v79, -v65, v78, 1.0
	v_fmac_f32_e32 v78, v79, v78
	v_div_fixup_f32 v65, v78, v65, 1.0
	v_rcp_f32_e32 v78, v64
	v_pk_add_f32 v[66:67], v[66:67], 1.0 op_sel_hi:[1,0]
	v_fma_f32 v79, -v64, v78, 1.0
	v_fmac_f32_e32 v78, v79, v78
	v_div_fixup_f32 v64, v78, v64, 1.0
	v_pk_mul_f32 v[64:65], v[64:65], v[68:69]
	v_mul_f32_e32 v68, 0xbfb8aa3b, v70
	v_mul_f32_e32 v69, 0xbfb8aa3b, v71
	v_exp_f32_e32 v68, v68
	v_exp_f32_e32 v69, v69
	v_lshlrev_b32_e32 v70, 16, v73
	v_and_b32_e32 v71, 0xffff0000, v73
	v_cvt_pk_bf16_f32 v64, v64, v65
	v_pk_add_f32 v[68:69], v[68:69], 1.0 op_sel_hi:[1,0]
	s_nop 0
	v_rcp_f32_e32 v73, v69
	s_nop 0
	v_fma_f32 v78, -v69, v73, 1.0
	v_fmac_f32_e32 v73, v78, v73
	v_div_fixup_f32 v69, v73, v69, 1.0
	v_rcp_f32_e32 v73, v68
	s_nop 0
	v_fma_f32 v78, -v68, v73, 1.0
	v_fmac_f32_e32 v73, v78, v73
	v_div_fixup_f32 v68, v73, v68, 1.0
	v_pk_mul_f32 v[68:69], v[68:69], v[70:71]
	v_mul_f32_e32 v70, 0xbfb8aa3b, v76
	v_mul_f32_e32 v71, 0xbfb8aa3b, v77
	v_exp_f32_e32 v70, v70
	v_exp_f32_e32 v71, v71
	v_lshlrev_b32_e32 v72, 16, v74
	v_and_b32_e32 v73, 0xffff0000, v74
	v_cvt_pk_bf16_f32 v65, v68, v69
	v_pk_add_f32 v[70:71], v[70:71], 1.0 op_sel_hi:[1,0]
	s_nop 0
	v_rcp_f32_e32 v76, v71
	s_nop 0
	v_fma_f32 v77, -v71, v76, 1.0
	v_fmac_f32_e32 v76, v77, v76
	v_div_fixup_f32 v71, v76, v71, 1.0
	v_rcp_f32_e32 v76, v70
	s_nop 0
	v_fma_f32 v77, -v70, v76, 1.0
	v_fmac_f32_e32 v76, v77, v76
	v_div_fixup_f32 v70, v76, v70, 1.0
	v_div_scale_f32 v74, s[14:15], v67, v67, 1.0
	v_pk_mul_f32 v[70:71], v[70:71], v[72:73]
	v_lshlrev_b32_e32 v72, 16, v75
	v_and_b32_e32 v73, 0xffff0000, v75
	v_rcp_f32_e32 v75, v74
	s_nop 0
	v_fma_f32 v76, -v74, v75, 1.0
	v_fmac_f32_e32 v75, v76, v75
	v_div_scale_f32 v76, vcc, 1.0, v67, 1.0
	v_mul_f32_e32 v77, v76, v75
	v_fma_f32 v78, -v74, v77, v76
	v_fmac_f32_e32 v77, v78, v75
	v_fma_f32 v74, -v74, v77, v76
	v_div_fmas_f32 v74, v74, v75, v77
	v_div_fixup_f32 v67, v74, v67, 1.0
	v_rcp_f32_e32 v75, v66
	s_nop 0
	v_fma_f32 v76, -v66, v75, 1.0
	v_fmac_f32_e32 v75, v76, v75
	v_div_fixup_f32 v66, v75, v66, 1.0
	v_pk_mul_f32 v[72:73], v[66:67], v[72:73]
	v_cvt_pk_bf16_f32 v66, v70, v71
	v_cvt_pk_bf16_f32 v67, v72, v73
	global_store_dwordx4 v[80:81], v[64:67], off offset:1280
	s_nop 1
	v_add_u32_e32 v64, 0x80, v144
	v_ashrrev_i32_e32 v65, 31, v64
	v_lshlrev_b64 v[66:67], 10, v[64:65]
	v_lshl_add_u64 v[66:67], s[36:37], 0, v[66:67]
	v_lshl_add_u64 v[66:67], v[66:67], 0, v[142:143]
	s_nop 1
	v_lshlrev_b64 v[64:65], 11, v[64:65]
	s_waitcnt vmcnt(11)
	v_mov_b32_e32 v68, v198
	v_mov_b32_e32 v69, v199
	v_mov_b32_e32 v70, v200
	v_mov_b32_e32 v71, v201
	v_mov_b32_e32 v72, v174
	v_mov_b32_e32 v73, v175
	v_mov_b32_e32 v74, v176
	v_mov_b32_e32 v75, v177
	v_mov_b32_e32 v76, v170
	v_mov_b32_e32 v77, v171
	v_mov_b32_e32 v78, v172
	v_mov_b32_e32 v79, v173
	s_mov_b64 s[98:99], 0x2c000
	v_lshl_add_u64 v[168:169], v[166:167], 0, s[98:99]
	global_load_dwordx4 v[198:201], v[168:169], off
	v_pk_add_f32 v[56:57], v[56:57], v[72:73]
	v_pk_add_f32 v[60:61], v[60:61], v[76:77]
	v_lshlrev_b32_e32 v72, 16, v68
	v_mul_f32_e32 v60, 0xbfb8aa3b, v60
	v_mul_f32_e32 v61, 0xbfb8aa3b, v61
	v_exp_f32_e32 v60, v60
	v_exp_f32_e32 v61, v61
	v_and_b32_e32 v73, 0xffff0000, v68
	v_pk_add_f32 v[58:59], v[58:59], v[74:75]
	v_pk_add_f32 v[62:63], v[62:63], v[78:79]
	v_pk_add_f32 v[60:61], v[60:61], 1.0 op_sel_hi:[1,0]
	v_mul_f32_e32 v62, 0xbfb8aa3b, v62
	v_rcp_f32_e32 v74, v61
	v_mul_f32_e32 v63, 0xbfb8aa3b, v63
	v_exp_f32_e32 v62, v62
	v_exp_f32_e32 v63, v63
	v_fma_f32 v75, -v61, v74, 1.0
	v_fmac_f32_e32 v74, v75, v74
	v_div_fixup_f32 v61, v74, v61, 1.0
	v_rcp_f32_e32 v74, v60
	v_pk_add_f32 v[62:63], v[62:63], 1.0 op_sel_hi:[1,0]
	v_mul_f32_e32 v56, 0xbfb8aa3b, v56
	v_mul_f32_e32 v57, 0xbfb8aa3b, v57
	v_fma_f32 v75, -v60, v74, 1.0
	v_fmac_f32_e32 v74, v75, v74
	v_div_fixup_f32 v60, v74, v60, 1.0
	v_pk_mul_f32 v[60:61], v[60:61], v[72:73]
	v_rcp_f32_e32 v73, v63
	v_exp_f32_e32 v56, v56
	v_exp_f32_e32 v57, v57
	v_lshlrev_b32_e32 v68, 16, v69
	v_fma_f32 v74, -v63, v73, 1.0
	v_fmac_f32_e32 v73, v74, v73
	v_div_fixup_f32 v63, v73, v63, 1.0
	v_rcp_f32_e32 v73, v62
	v_and_b32_e32 v69, 0xffff0000, v69
	v_pk_add_f32 v[56:57], v[56:57], 1.0 op_sel_hi:[1,0]
	v_fma_f32 v74, -v62, v73, 1.0
	v_fmac_f32_e32 v73, v74, v73
	v_div_fixup_f32 v62, v73, v62, 1.0
	v_pk_mul_f32 v[62:63], v[62:63], v[68:69]
	v_lshlrev_b32_e32 v68, 16, v70
	v_and_b32_e32 v69, 0xffff0000, v70
	v_rcp_f32_e32 v72, v57
	s_nop 0
	v_fma_f32 v73, -v57, v72, 1.0
	v_fmac_f32_e32 v72, v73, v72
	v_div_fixup_f32 v57, v72, v57, 1.0
	v_rcp_f32_e32 v72, v56
	s_nop 0
	v_fma_f32 v73, -v56, v72, 1.0
	v_fmac_f32_e32 v72, v73, v72
	v_div_fixup_f32 v56, v72, v56, 1.0
	v_pk_mul_f32 v[68:69], v[56:57], v[68:69]
	v_mul_f32_e32 v56, 0xbfb8aa3b, v58
	v_mul_f32_e32 v57, 0xbfb8aa3b, v59
	v_exp_f32_e32 v56, v56
	v_exp_f32_e32 v57, v57
	v_lshlrev_b32_e32 v58, 16, v71
	v_and_b32_e32 v59, 0xffff0000, v71
	v_pk_add_f32 v[56:57], v[56:57], 1.0 op_sel_hi:[1,0]
	s_nop 0
	v_rcp_f32_e32 v71, v57
	s_nop 0
	v_fma_f32 v72, -v57, v71, 1.0
	v_fmac_f32_e32 v71, v72, v71
	v_div_fixup_f32 v57, v71, v57, 1.0
	v_rcp_f32_e32 v71, v56
	s_nop 0
	v_fma_f32 v72, -v56, v71, 1.0
	v_fmac_f32_e32 v71, v72, v71
	v_div_fixup_f32 v56, v71, v56, 1.0
	v_pk_mul_f32 v[70:71], v[56:57], v[58:59]
	v_cvt_pk_bf16_f32 v56, v60, v61
	v_lshl_add_u64 v[60:61], s[26:27], 0, v[64:65]
	v_cvt_pk_bf16_f32 v57, v62, v63
	v_cvt_pk_bf16_f32 v58, v68, v69
	v_cvt_pk_bf16_f32 v59, v70, v71
	v_lshl_add_u64 v[64:65], v[60:61], 0, v[142:143]
	global_store_dwordx4 v[64:65], v[56:59], off offset:1024
	s_nop 1
	s_nop 0
	s_waitcnt vmcnt(11)
; __device__ __forceinline__ float sigmoidf_(float x) { return 1.f / (1.f + __expf(-x)); }
; __device__ __forceinline__ unsigned cvt_pk_bf16(float lo, float hi) { const f32x2c v = {lo, hi}; const bf16x2c b = __builtin_convertvector(v, bf16x2c); return __builtin_bit_cast(unsigned, b); }
;     __device__ __forceinline__ void operator()(const f32x4 (&acc)[2][2][4][2], const Unit& u, int wr, int wc, int fr, int fq) const {
;     ...
;             for (int m = 0; m < 4; ++m) { const size_t row = (size_t)(row0 + ai * HALF + m * 16);
; #pragma unroll
;                 for (int bj = 0; bj < 2; ++bj) { const int col = col0 + bj * HALF;
;                     const u32x4 zz = *(const u32x4*)(Z + row * 512 + col);
;                     const f32x4 b0 = *(const f32x4*)(bias + col), b1 = *(const f32x4*)(bias + col + 4);
;                     const f32x4 v0 = acc[ai][bj][m][0] + b0, v1 = acc[ai][bj][m][1] + b1;
;                     float o[8]; const unsigned zw[4] = {zz.x, zz.y, zz.z, zz.w};
; #pragma unroll
;                     for (int q = 0; q < 4; ++q) { const float zl = __builtin_bit_cast(float, zw[q] << 16), zh = __builtin_bit_cast(float, zw[q] & 0xffff0000u);
;                         const float al = (q < 2) ? v0[2 * q] : v1[2 * q - 4], ah = (q < 2) ? v0[2 * q + 1] : v1[2 * q - 3];
;                         o[2 * q] = zl * sigmoidf_(al); o[2 * q + 1] = zh * sigmoidf_(ah); }
;                     u32x4 w; w.x = cvt_pk_bf16(o[0], o[1]); w.y = cvt_pk_bf16(o[2], o[3]); w.z = cvt_pk_bf16(o[4], o[5]); w.w = cvt_pk_bf16(o[6], o[7]);
;                     *(u32x4*)(YM + row * D + 512 + col) = w; } }
	v_mov_b32_e32 v56, v202
	v_mov_b32_e32 v57, v203
	v_mov_b32_e32 v58, v204
	v_mov_b32_e32 v59, v205
	v_mov_b32_e32 v60, v182
	v_mov_b32_e32 v61, v183
	v_mov_b32_e32 v62, v184
	v_mov_b32_e32 v63, v185
	v_mov_b32_e32 v66, v178
	v_mov_b32_e32 v67, v179
	v_mov_b32_e32 v68, v180
	v_mov_b32_e32 v69, v181
	global_load_dwordx4 v[202:205], v[168:169], off offset:256
	v_pk_add_f32 v[60:61], v[48:49], v[60:61]
	v_pk_add_f32 v[52:53], v[52:53], v[66:67]
	v_pk_add_f32 v[50:51], v[50:51], v[62:63]
	v_mul_f32_e32 v48, 0xbfb8aa3b, v52
	v_mul_f32_e32 v49, 0xbfb8aa3b, v53
	v_exp_f32_e32 v48, v48
	v_exp_f32_e32 v49, v49
	v_lshlrev_b32_e32 v52, 16, v56
	v_and_b32_e32 v53, 0xffff0000, v56
	v_pk_add_f32 v[54:55], v[54:55], v[68:69]
	v_pk_add_f32 v[48:49], v[48:49], 1.0 op_sel_hi:[1,0]
	v_mul_f32_e32 v50, 0xbfb8aa3b, v50
	v_rcp_f32_e32 v62, v49
	v_mul_f32_e32 v51, 0xbfb8aa3b, v51
	v_exp_f32_e32 v50, v50
	v_exp_f32_e32 v51, v51
	v_fma_f32 v63, -v49, v62, 1.0
	v_fmac_f32_e32 v62, v63, v62
	v_div_fixup_f32 v49, v62, v49, 1.0
	v_rcp_f32_e32 v62, v48
	v_pk_add_f32 v[50:51], v[50:51], 1.0 op_sel_hi:[1,0]
	v_fma_f32 v63, -v48, v62, 1.0
	v_fmac_f32_e32 v62, v63, v62
	v_div_fixup_f32 v48, v62, v48, 1.0
	v_pk_mul_f32 v[48:49], v[48:49], v[52:53]
	v_mul_f32_e32 v52, 0xbfb8aa3b, v54
	v_mul_f32_e32 v53, 0xbfb8aa3b, v55
	v_exp_f32_e32 v52, v52
	v_exp_f32_e32 v53, v53
	v_lshlrev_b32_e32 v54, 16, v57
	v_and_b32_e32 v55, 0xffff0000, v57
	v_cvt_pk_bf16_f32 v48, v48, v49
	v_pk_add_f32 v[52:53], v[52:53], 1.0 op_sel_hi:[1,0]
	s_nop 0
	v_rcp_f32_e32 v57, v53
	s_nop 0
	v_fma_f32 v62, -v53, v57, 1.0
	v_fmac_f32_e32 v57, v62, v57
	v_div_fixup_f32 v53, v57, v53, 1.0
	v_rcp_f32_e32 v57, v52
	s_nop 0
	v_fma_f32 v62, -v52, v57, 1.0
	v_fmac_f32_e32 v57, v62, v57
	v_div_fixup_f32 v52, v57, v52, 1.0
	v_pk_mul_f32 v[52:53], v[52:53], v[54:55]
	v_mul_f32_e32 v54, 0xbfb8aa3b, v60
	v_mul_f32_e32 v55, 0xbfb8aa3b, v61
	v_exp_f32_e32 v54, v54
	v_exp_f32_e32 v55, v55
	v_lshlrev_b32_e32 v56, 16, v58
	v_and_b32_e32 v57, 0xffff0000, v58
	v_cvt_pk_bf16_f32 v49, v52, v53
	v_pk_add_f32 v[54:55], v[54:55], 1.0 op_sel_hi:[1,0]
	s_nop 0
	v_rcp_f32_e32 v60, v55
	s_nop 0
	v_fma_f32 v61, -v55, v60, 1.0
	v_fmac_f32_e32 v60, v61, v60
	v_div_fixup_f32 v55, v60, v55, 1.0
	v_rcp_f32_e32 v60, v54
	s_nop 0
	v_fma_f32 v61, -v54, v60, 1.0
	v_fmac_f32_e32 v60, v61, v60
	v_div_fixup_f32 v54, v60, v54, 1.0
	v_div_scale_f32 v58, s[14:15], v51, v51, 1.0
	v_pk_mul_f32 v[54:55], v[54:55], v[56:57]
	v_lshlrev_b32_e32 v56, 16, v59
	v_and_b32_e32 v57, 0xffff0000, v59
	v_rcp_f32_e32 v59, v58
	s_nop 0
	v_fma_f32 v60, -v58, v59, 1.0
	v_fmac_f32_e32 v59, v60, v59
	v_div_scale_f32 v60, vcc, 1.0, v51, 1.0
	v_mul_f32_e32 v61, v60, v59
	v_fma_f32 v62, -v58, v61, v60
	v_fmac_f32_e32 v61, v62, v59
	v_fma_f32 v58, -v58, v61, v60
	v_div_fmas_f32 v58, v58, v59, v61
	v_div_fixup_f32 v51, v58, v51, 1.0
	v_rcp_f32_e32 v59, v50
	s_nop 0
	v_fma_f32 v60, -v50, v59, 1.0
	v_fmac_f32_e32 v59, v60, v59
	v_div_fixup_f32 v50, v59, v50, 1.0
	v_pk_mul_f32 v[56:57], v[50:51], v[56:57]
	v_cvt_pk_bf16_f32 v50, v54, v55
	v_cvt_pk_bf16_f32 v51, v56, v57
	global_store_dwordx4 v[64:65], v[48:51], off offset:1280
	s_nop 1
	v_add_u32_e32 v48, 0x90, v144
	v_ashrrev_i32_e32 v49, 31, v48
	v_lshlrev_b64 v[50:51], 10, v[48:49]
	v_lshl_add_u64 v[50:51], s[36:37], 0, v[50:51]
	v_lshl_add_u64 v[50:51], v[50:51], 0, v[142:143]
	s_nop 1
	v_lshlrev_b64 v[48:49], 11, v[48:49]
	s_waitcnt vmcnt(11)
	v_mov_b32_e32 v52, v206
	v_mov_b32_e32 v53, v207
	v_mov_b32_e32 v54, v208
	v_mov_b32_e32 v55, v209
	v_mov_b32_e32 v56, v174
	v_mov_b32_e32 v57, v175
	v_mov_b32_e32 v58, v176
	v_mov_b32_e32 v59, v177
	v_mov_b32_e32 v60, v170
	v_mov_b32_e32 v61, v171
	v_mov_b32_e32 v62, v172
	v_mov_b32_e32 v63, v173
	v_pk_add_f32 v[40:41], v[40:41], v[56:57]
	v_pk_add_f32 v[44:45], v[44:45], v[60:61]
	v_lshlrev_b32_e32 v56, 16, v52
	v_mul_f32_e32 v44, 0xbfb8aa3b, v44
	v_mul_f32_e32 v45, 0xbfb8aa3b, v45
	v_exp_f32_e32 v44, v44
	v_exp_f32_e32 v45, v45
	v_and_b32_e32 v57, 0xffff0000, v52
	v_pk_add_f32 v[42:43], v[42:43], v[58:59]
	v_pk_add_f32 v[46:47], v[46:47], v[62:63]
	v_pk_add_f32 v[44:45], v[44:45], 1.0 op_sel_hi:[1,0]
	v_mul_f32_e32 v46, 0xbfb8aa3b, v46
	v_rcp_f32_e32 v58, v45
	v_mul_f32_e32 v47, 0xbfb8aa3b, v47
	v_exp_f32_e32 v46, v46
	v_exp_f32_e32 v47, v47
	v_fma_f32 v59, -v45, v58, 1.0
	v_fmac_f32_e32 v58, v59, v58
	v_div_fixup_f32 v45, v58, v45, 1.0
	v_rcp_f32_e32 v58, v44
	v_pk_add_f32 v[46:47], v[46:47], 1.0 op_sel_hi:[1,0]
	v_mul_f32_e32 v40, 0xbfb8aa3b, v40
	v_mul_f32_e32 v41, 0xbfb8aa3b, v41
	v_fma_f32 v59, -v44, v58, 1.0
	v_fmac_f32_e32 v58, v59, v58
	v_div_fixup_f32 v44, v58, v44, 1.0
	v_pk_mul_f32 v[44:45], v[44:45], v[56:57]
	v_rcp_f32_e32 v57, v47
	v_exp_f32_e32 v40, v40
	v_exp_f32_e32 v41, v41
	v_lshlrev_b32_e32 v52, 16, v53
	v_fma_f32 v58, -v47, v57, 1.0
	v_fmac_f32_e32 v57, v58, v57
	v_div_fixup_f32 v47, v57, v47, 1.0
	v_rcp_f32_e32 v57, v46
	v_and_b32_e32 v53, 0xffff0000, v53
	v_pk_add_f32 v[40:41], v[40:41], 1.0 op_sel_hi:[1,0]
	v_fma_f32 v58, -v46, v57, 1.0
	v_fmac_f32_e32 v57, v58, v57
	v_div_fixup_f32 v46, v57, v46, 1.0
	v_pk_mul_f32 v[46:47], v[46:47], v[52:53]
	v_lshlrev_b32_e32 v52, 16, v54
	v_and_b32_e32 v53, 0xffff0000, v54
	v_rcp_f32_e32 v56, v41
	s_nop 0
	v_fma_f32 v57, -v41, v56, 1.0
	v_fmac_f32_e32 v56, v57, v56
	v_div_fixup_f32 v41, v56, v41, 1.0
	v_rcp_f32_e32 v56, v40
	s_nop 0
	v_fma_f32 v57, -v40, v56, 1.0
	v_fmac_f32_e32 v56, v57, v56
	v_div_fixup_f32 v40, v56, v40, 1.0
	v_pk_mul_f32 v[52:53], v[40:41], v[52:53]
	v_mul_f32_e32 v40, 0xbfb8aa3b, v42
	v_mul_f32_e32 v41, 0xbfb8aa3b, v43
	v_exp_f32_e32 v40, v40
	v_exp_f32_e32 v41, v41
	v_lshlrev_b32_e32 v42, 16, v55
	v_and_b32_e32 v43, 0xffff0000, v55
	v_pk_add_f32 v[40:41], v[40:41], 1.0 op_sel_hi:[1,0]
	s_nop 0
	v_rcp_f32_e32 v55, v41
	s_nop 0
	v_fma_f32 v56, -v41, v55, 1.0
	v_fmac_f32_e32 v55, v56, v55
	v_div_fixup_f32 v41, v55, v41, 1.0
	v_rcp_f32_e32 v55, v40
	s_nop 0
	v_fma_f32 v56, -v40, v55, 1.0
	v_fmac_f32_e32 v55, v56, v55
	v_div_fixup_f32 v40, v55, v40, 1.0
	v_pk_mul_f32 v[54:55], v[40:41], v[42:43]
	v_cvt_pk_bf16_f32 v40, v44, v45
	v_lshl_add_u64 v[44:45], s[26:27], 0, v[48:49]
	v_cvt_pk_bf16_f32 v41, v46, v47
	v_cvt_pk_bf16_f32 v42, v52, v53
	v_cvt_pk_bf16_f32 v43, v54, v55
	v_lshl_add_u64 v[48:49], v[44:45], 0, v[142:143]
	global_store_dwordx4 v[48:49], v[40:43], off offset:1024
	s_nop 1
	s_nop 0
	s_waitcnt vmcnt(10)
; __device__ __forceinline__ float sigmoidf_(float x) { return 1.f / (1.f + __expf(-x)); }
; __device__ __forceinline__ unsigned cvt_pk_bf16(float lo, float hi) { const f32x2c v = {lo, hi}; const bf16x2c b = __builtin_convertvector(v, bf16x2c); return __builtin_bit_cast(unsigned, b); }
;     __device__ __forceinline__ void operator()(const f32x4 (&acc)[2][2][4][2], const Unit& u, int wr, int wc, int fr, int fq) const {
;     ...
;             for (int m = 0; m < 4; ++m) { const size_t row = (size_t)(row0 + ai * HALF + m * 16);
; #pragma unroll
;                 for (int bj = 0; bj < 2; ++bj) { const int col = col0 + bj * HALF;
;                     const u32x4 zz = *(const u32x4*)(Z + row * 512 + col);
;                     const f32x4 b0 = *(const f32x4*)(bias + col), b1 = *(const f32x4*)(bias + col + 4);
;                     const f32x4 v0 = acc[ai][bj][m][0] + b0, v1 = acc[ai][bj][m][1] + b1;
;                     float o[8]; const unsigned zw[4] = {zz.x, zz.y, zz.z, zz.w};
; #pragma unroll
;                     for (int q = 0; q < 4; ++q) { const float zl = __builtin_bit_cast(float, zw[q] << 16), zh = __builtin_bit_cast(float, zw[q] & 0xffff0000u);
;                         const float al = (q < 2) ? v0[2 * q] : v1[2 * q - 4], ah = (q < 2) ? v0[2 * q + 1] : v1[2 * q - 3];
;                         o[2 * q] = zl * sigmoidf_(al); o[2 * q + 1] = zh * sigmoidf_(ah); }
;                     u32x4 w; w.x = cvt_pk_bf16(o[0], o[1]); w.y = cvt_pk_bf16(o[2], o[3]); w.z = cvt_pk_bf16(o[4], o[5]); w.w = cvt_pk_bf16(o[6], o[7]);
;                     *(u32x4*)(YM + row * D + 512 + col) = w; } }
	v_mov_b32_e32 v40, v210
	v_mov_b32_e32 v41, v211
	v_mov_b32_e32 v42, v212
	v_mov_b32_e32 v43, v213
	v_mov_b32_e32 v44, v182
	v_mov_b32_e32 v45, v183
	v_mov_b32_e32 v46, v184
	v_mov_b32_e32 v47, v185
	v_mov_b32_e32 v50, v178
	v_mov_b32_e32 v51, v179
	v_mov_b32_e32 v52, v180
	v_mov_b32_e32 v53, v181
	v_pk_add_f32 v[44:45], v[32:33], v[44:45]
	v_pk_add_f32 v[36:37], v[36:37], v[50:51]
	v_pk_add_f32 v[34:35], v[34:35], v[46:47]
	v_mul_f32_e32 v32, 0xbfb8aa3b, v36
	v_mul_f32_e32 v33, 0xbfb8aa3b, v37
	v_exp_f32_e32 v32, v32
	v_exp_f32_e32 v33, v33
	v_lshlrev_b32_e32 v36, 16, v40
	v_and_b32_e32 v37, 0xffff0000, v40
	v_pk_add_f32 v[38:39], v[38:39], v[52:53]
	v_pk_add_f32 v[32:33], v[32:33], 1.0 op_sel_hi:[1,0]
	v_mul_f32_e32 v34, 0xbfb8aa3b, v34
	v_rcp_f32_e32 v46, v33
	v_mul_f32_e32 v35, 0xbfb8aa3b, v35
	v_exp_f32_e32 v34, v34
	v_exp_f32_e32 v35, v35
	v_fma_f32 v47, -v33, v46, 1.0
	v_fmac_f32_e32 v46, v47, v46
	v_div_fixup_f32 v33, v46, v33, 1.0
	v_rcp_f32_e32 v46, v32
	v_pk_add_f32 v[34:35], v[34:35], 1.0 op_sel_hi:[1,0]
	v_fma_f32 v47, -v32, v46, 1.0
	v_fmac_f32_e32 v46, v47, v46
	v_div_fixup_f32 v32, v46, v32, 1.0
	v_pk_mul_f32 v[32:33], v[32:33], v[36:37]
	v_mul_f32_e32 v36, 0xbfb8aa3b, v38
	v_mul_f32_e32 v37, 0xbfb8aa3b, v39
	v_exp_f32_e32 v36, v36
	v_exp_f32_e32 v37, v37
	v_lshlrev_b32_e32 v38, 16, v41
	v_and_b32_e32 v39, 0xffff0000, v41
	v_cvt_pk_bf16_f32 v32, v32, v33
	v_pk_add_f32 v[36:37], v[36:37], 1.0 op_sel_hi:[1,0]
	s_nop 0
	v_rcp_f32_e32 v41, v37
	s_nop 0
	v_fma_f32 v46, -v37, v41, 1.0
	v_fmac_f32_e32 v41, v46, v41
	v_div_fixup_f32 v37, v41, v37, 1.0
	v_rcp_f32_e32 v41, v36
	s_nop 0
	v_fma_f32 v46, -v36, v41, 1.0
	v_fmac_f32_e32 v41, v46, v41
	v_div_fixup_f32 v36, v41, v36, 1.0
	v_pk_mul_f32 v[36:37], v[36:37], v[38:39]
	v_mul_f32_e32 v38, 0xbfb8aa3b, v44
	v_mul_f32_e32 v39, 0xbfb8aa3b, v45
	v_exp_f32_e32 v38, v38
	v_exp_f32_e32 v39, v39
	v_lshlrev_b32_e32 v40, 16, v42
	v_and_b32_e32 v41, 0xffff0000, v42
	v_cvt_pk_bf16_f32 v33, v36, v37
	v_pk_add_f32 v[38:39], v[38:39], 1.0 op_sel_hi:[1,0]
	s_nop 0
	v_rcp_f32_e32 v44, v39
	s_nop 0
	v_fma_f32 v45, -v39, v44, 1.0
	v_fmac_f32_e32 v44, v45, v44
	v_div_fixup_f32 v39, v44, v39, 1.0
	v_rcp_f32_e32 v44, v38
	s_nop 0
	v_fma_f32 v45, -v38, v44, 1.0
	v_fmac_f32_e32 v44, v45, v44
	v_div_fixup_f32 v38, v44, v38, 1.0
	v_div_scale_f32 v42, s[14:15], v35, v35, 1.0
	v_pk_mul_f32 v[38:39], v[38:39], v[40:41]
	v_lshlrev_b32_e32 v40, 16, v43
	v_and_b32_e32 v41, 0xffff0000, v43
	v_rcp_f32_e32 v43, v42
	s_nop 0
	v_fma_f32 v44, -v42, v43, 1.0
	v_fmac_f32_e32 v43, v44, v43
	v_div_scale_f32 v44, vcc, 1.0, v35, 1.0
	v_mul_f32_e32 v45, v44, v43
	v_fma_f32 v46, -v42, v45, v44
	v_fmac_f32_e32 v45, v46, v43
	v_fma_f32 v42, -v42, v45, v44
	v_div_fmas_f32 v42, v42, v43, v45
	v_div_fixup_f32 v35, v42, v35, 1.0
	v_rcp_f32_e32 v43, v34
	s_nop 0
	v_fma_f32 v44, -v34, v43, 1.0
	v_fmac_f32_e32 v43, v44, v43
	v_div_fixup_f32 v34, v43, v34, 1.0
	v_pk_mul_f32 v[40:41], v[34:35], v[40:41]
	v_cvt_pk_bf16_f32 v34, v38, v39
	v_cvt_pk_bf16_f32 v35, v40, v41
	global_store_dwordx4 v[48:49], v[32:35], off offset:1280
	s_nop 1
	v_add_u32_e32 v32, 0xa0, v144
	v_ashrrev_i32_e32 v33, 31, v32
	v_lshlrev_b64 v[34:35], 10, v[32:33]
	v_lshl_add_u64 v[34:35], s[36:37], 0, v[34:35]
	v_lshl_add_u64 v[34:35], v[34:35], 0, v[142:143]
	s_nop 1
	v_lshlrev_b64 v[32:33], 11, v[32:33]
	s_waitcnt vmcnt(9)
	v_mov_b32_e32 v36, v186
	v_mov_b32_e32 v37, v187
	v_mov_b32_e32 v38, v188
	v_mov_b32_e32 v39, v189
	v_mov_b32_e32 v40, v174
	v_mov_b32_e32 v41, v175
	v_mov_b32_e32 v42, v176
	v_mov_b32_e32 v43, v177
	v_mov_b32_e32 v44, v170
	v_mov_b32_e32 v45, v171
	v_mov_b32_e32 v46, v172
	v_mov_b32_e32 v47, v173
	v_pk_add_f32 v[24:25], v[24:25], v[40:41]
	v_pk_add_f32 v[28:29], v[28:29], v[44:45]
	v_lshlrev_b32_e32 v40, 16, v36
	v_mul_f32_e32 v28, 0xbfb8aa3b, v28
	v_mul_f32_e32 v29, 0xbfb8aa3b, v29
	v_exp_f32_e32 v28, v28
	v_exp_f32_e32 v29, v29
	v_and_b32_e32 v41, 0xffff0000, v36
	v_pk_add_f32 v[26:27], v[26:27], v[42:43]
	v_pk_add_f32 v[30:31], v[30:31], v[46:47]
	v_pk_add_f32 v[28:29], v[28:29], 1.0 op_sel_hi:[1,0]
	v_mul_f32_e32 v30, 0xbfb8aa3b, v30
	v_rcp_f32_e32 v42, v29
	v_mul_f32_e32 v31, 0xbfb8aa3b, v31
	v_exp_f32_e32 v30, v30
	v_exp_f32_e32 v31, v31
	v_fma_f32 v43, -v29, v42, 1.0
	v_fmac_f32_e32 v42, v43, v42
	v_div_fixup_f32 v29, v42, v29, 1.0
	v_rcp_f32_e32 v42, v28
	v_pk_add_f32 v[30:31], v[30:31], 1.0 op_sel_hi:[1,0]
	v_mul_f32_e32 v24, 0xbfb8aa3b, v24
	v_mul_f32_e32 v25, 0xbfb8aa3b, v25
	v_fma_f32 v43, -v28, v42, 1.0
	v_fmac_f32_e32 v42, v43, v42
	v_div_fixup_f32 v28, v42, v28, 1.0
	v_pk_mul_f32 v[28:29], v[28:29], v[40:41]
	v_rcp_f32_e32 v41, v31
	v_exp_f32_e32 v24, v24
	v_exp_f32_e32 v25, v25
	v_lshlrev_b32_e32 v36, 16, v37
	v_fma_f32 v42, -v31, v41, 1.0
	v_fmac_f32_e32 v41, v42, v41
	v_div_fixup_f32 v31, v41, v31, 1.0
	v_rcp_f32_e32 v41, v30
	v_and_b32_e32 v37, 0xffff0000, v37
	v_pk_add_f32 v[24:25], v[24:25], 1.0 op_sel_hi:[1,0]
	v_fma_f32 v42, -v30, v41, 1.0
	v_fmac_f32_e32 v41, v42, v41
	v_div_fixup_f32 v30, v41, v30, 1.0
	v_pk_mul_f32 v[30:31], v[30:31], v[36:37]
	v_lshlrev_b32_e32 v36, 16, v38
	v_and_b32_e32 v37, 0xffff0000, v38
	v_rcp_f32_e32 v40, v25
	s_nop 0
	v_fma_f32 v41, -v25, v40, 1.0
	v_fmac_f32_e32 v40, v41, v40
	v_div_fixup_f32 v25, v40, v25, 1.0
	v_rcp_f32_e32 v40, v24
	s_nop 0
	v_fma_f32 v41, -v24, v40, 1.0
	v_fmac_f32_e32 v40, v41, v40
	v_div_fixup_f32 v24, v40, v24, 1.0
	v_pk_mul_f32 v[36:37], v[24:25], v[36:37]
	v_mul_f32_e32 v24, 0xbfb8aa3b, v26
	v_mul_f32_e32 v25, 0xbfb8aa3b, v27
	v_exp_f32_e32 v24, v24
	v_exp_f32_e32 v25, v25
	v_lshlrev_b32_e32 v26, 16, v39
	v_and_b32_e32 v27, 0xffff0000, v39
	v_pk_add_f32 v[24:25], v[24:25], 1.0 op_sel_hi:[1,0]
	s_nop 0
	v_rcp_f32_e32 v39, v25
	s_nop 0
	v_fma_f32 v40, -v25, v39, 1.0
	v_fmac_f32_e32 v39, v40, v39
	v_div_fixup_f32 v25, v39, v25, 1.0
	v_rcp_f32_e32 v39, v24
	s_nop 0
	v_fma_f32 v40, -v24, v39, 1.0
	v_fmac_f32_e32 v39, v40, v39
	v_div_fixup_f32 v24, v39, v24, 1.0
	v_pk_mul_f32 v[38:39], v[24:25], v[26:27]
	v_cvt_pk_bf16_f32 v24, v28, v29
	v_lshl_add_u64 v[28:29], s[26:27], 0, v[32:33]
	v_cvt_pk_bf16_f32 v25, v30, v31
	v_cvt_pk_bf16_f32 v26, v36, v37
	v_cvt_pk_bf16_f32 v27, v38, v39
	v_lshl_add_u64 v[32:33], v[28:29], 0, v[142:143]
	global_store_dwordx4 v[32:33], v[24:27], off offset:1024
	s_nop 1
	s_nop 0
	s_waitcnt vmcnt(8)
; __device__ __forceinline__ float sigmoidf_(float x) { return 1.f / (1.f + __expf(-x)); }
; __device__ __forceinline__ unsigned cvt_pk_bf16(float lo, float hi) { const f32x2c v = {lo, hi}; const bf16x2c b = __builtin_convertvector(v, bf16x2c); return __builtin_bit_cast(unsigned, b); }
;     __device__ __forceinline__ void operator()(const f32x4 (&acc)[2][2][4][2], const Unit& u, int wr, int wc, int fr, int fq) const {
;     ...
;             for (int m = 0; m < 4; ++m) { const size_t row = (size_t)(row0 + ai * HALF + m * 16);
; #pragma unroll
;                 for (int bj = 0; bj < 2; ++bj) { const int col = col0 + bj * HALF;
;                     const u32x4 zz = *(const u32x4*)(Z + row * 512 + col);
;                     const f32x4 b0 = *(const f32x4*)(bias + col), b1 = *(const f32x4*)(bias + col + 4);
;                     const f32x4 v0 = acc[ai][bj][m][0] + b0, v1 = acc[ai][bj][m][1] + b1;
;                     float o[8]; const unsigned zw[4] = {zz.x, zz.y, zz.z, zz.w};
; #pragma unroll
;                     for (int q = 0; q < 4; ++q) { const float zl = __builtin_bit_cast(float, zw[q] << 16), zh = __builtin_bit_cast(float, zw[q] & 0xffff0000u);
;                         const float al = (q < 2) ? v0[2 * q] : v1[2 * q - 4], ah = (q < 2) ? v0[2 * q + 1] : v1[2 * q - 3];
;                         o[2 * q] = zl * sigmoidf_(al); o[2 * q + 1] = zh * sigmoidf_(ah); }
;                     u32x4 w; w.x = cvt_pk_bf16(o[0], o[1]); w.y = cvt_pk_bf16(o[2], o[3]); w.z = cvt_pk_bf16(o[4], o[5]); w.w = cvt_pk_bf16(o[6], o[7]);
;                     *(u32x4*)(YM + row * D + 512 + col) = w; } }
	v_mov_b32_e32 v24, v190
	v_mov_b32_e32 v25, v191
	v_mov_b32_e32 v26, v192
	v_mov_b32_e32 v27, v193
	v_mov_b32_e32 v28, v182
	v_mov_b32_e32 v29, v183
	v_mov_b32_e32 v30, v184
	v_mov_b32_e32 v31, v185
	v_mov_b32_e32 v34, v178
	v_mov_b32_e32 v35, v179
	v_mov_b32_e32 v36, v180
	v_mov_b32_e32 v37, v181
	v_pk_add_f32 v[28:29], v[16:17], v[28:29]
	v_pk_add_f32 v[20:21], v[20:21], v[34:35]
	v_pk_add_f32 v[18:19], v[18:19], v[30:31]
	v_mul_f32_e32 v16, 0xbfb8aa3b, v20
	v_mul_f32_e32 v17, 0xbfb8aa3b, v21
	v_exp_f32_e32 v16, v16
	v_exp_f32_e32 v17, v17
	v_lshlrev_b32_e32 v20, 16, v24
	v_and_b32_e32 v21, 0xffff0000, v24
	v_pk_add_f32 v[22:23], v[22:23], v[36:37]
	v_pk_add_f32 v[16:17], v[16:17], 1.0 op_sel_hi:[1,0]
	v_mul_f32_e32 v18, 0xbfb8aa3b, v18
	v_rcp_f32_e32 v30, v17
	v_mul_f32_e32 v19, 0xbfb8aa3b, v19
	v_exp_f32_e32 v18, v18
	v_exp_f32_e32 v19, v19
	v_fma_f32 v31, -v17, v30, 1.0
	v_fmac_f32_e32 v30, v31, v30
	v_div_fixup_f32 v17, v30, v17, 1.0
	v_rcp_f32_e32 v30, v16
	v_pk_add_f32 v[18:19], v[18:19], 1.0 op_sel_hi:[1,0]
	v_fma_f32 v31, -v16, v30, 1.0
	v_fmac_f32_e32 v30, v31, v30
	v_div_fixup_f32 v16, v30, v16, 1.0
	v_pk_mul_f32 v[16:17], v[16:17], v[20:21]
	v_mul_f32_e32 v20, 0xbfb8aa3b, v22
	v_mul_f32_e32 v21, 0xbfb8aa3b, v23
	v_exp_f32_e32 v20, v20
	v_exp_f32_e32 v21, v21
	v_lshlrev_b32_e32 v22, 16, v25
	v_and_b32_e32 v23, 0xffff0000, v25
	v_cvt_pk_bf16_f32 v16, v16, v17
	v_pk_add_f32 v[20:21], v[20:21], 1.0 op_sel_hi:[1,0]
	s_nop 0
	v_rcp_f32_e32 v25, v21
	s_nop 0
	v_fma_f32 v30, -v21, v25, 1.0
	v_fmac_f32_e32 v25, v30, v25
	v_div_fixup_f32 v21, v25, v21, 1.0
	v_rcp_f32_e32 v25, v20
	s_nop 0
	v_fma_f32 v30, -v20, v25, 1.0
	v_fmac_f32_e32 v25, v30, v25
	v_div_fixup_f32 v20, v25, v20, 1.0
	v_pk_mul_f32 v[20:21], v[20:21], v[22:23]
	v_mul_f32_e32 v22, 0xbfb8aa3b, v28
	v_mul_f32_e32 v23, 0xbfb8aa3b, v29
	v_exp_f32_e32 v22, v22
	v_exp_f32_e32 v23, v23
	v_lshlrev_b32_e32 v24, 16, v26
	v_and_b32_e32 v25, 0xffff0000, v26
	v_cvt_pk_bf16_f32 v17, v20, v21
	v_pk_add_f32 v[22:23], v[22:23], 1.0 op_sel_hi:[1,0]
	s_nop 0
	v_rcp_f32_e32 v28, v23
	s_nop 0
	v_fma_f32 v29, -v23, v28, 1.0
	v_fmac_f32_e32 v28, v29, v28
	v_div_fixup_f32 v23, v28, v23, 1.0
	v_rcp_f32_e32 v28, v22
	s_nop 0
	v_fma_f32 v29, -v22, v28, 1.0
	v_fmac_f32_e32 v28, v29, v28
	v_div_fixup_f32 v22, v28, v22, 1.0
	v_div_scale_f32 v26, s[14:15], v19, v19, 1.0
	v_pk_mul_f32 v[22:23], v[22:23], v[24:25]
	v_lshlrev_b32_e32 v24, 16, v27
	v_and_b32_e32 v25, 0xffff0000, v27
	v_rcp_f32_e32 v27, v26
	s_nop 0
	v_fma_f32 v28, -v26, v27, 1.0
	v_fmac_f32_e32 v27, v28, v27
	v_div_scale_f32 v28, vcc, 1.0, v19, 1.0
	v_mul_f32_e32 v29, v28, v27
	v_fma_f32 v30, -v26, v29, v28
	v_fmac_f32_e32 v29, v30, v27
	v_fma_f32 v26, -v26, v29, v28
	v_div_fmas_f32 v26, v26, v27, v29
	v_div_fixup_f32 v19, v26, v19, 1.0
	v_rcp_f32_e32 v27, v18
	s_nop 0
	v_fma_f32 v28, -v18, v27, 1.0
	v_fmac_f32_e32 v27, v28, v27
	v_div_fixup_f32 v18, v27, v18, 1.0
	v_pk_mul_f32 v[24:25], v[18:19], v[24:25]
	v_cvt_pk_bf16_f32 v18, v22, v23
	v_cvt_pk_bf16_f32 v19, v24, v25
	global_store_dwordx4 v[32:33], v[16:19], off offset:1280
	s_nop 1
	v_add_u32_e32 v16, 0xb0, v144
	v_ashrrev_i32_e32 v17, 31, v16
	v_lshlrev_b64 v[18:19], 10, v[16:17]
	v_lshlrev_b64 v[30:31], 11, v[16:17]
	v_lshl_add_u64 v[16:17], s[36:37], 0, v[18:19]
	v_lshl_add_u64 v[16:17], v[16:17], 0, v[142:143]
	s_nop 1
	s_waitcnt vmcnt(7)
; __device__ __forceinline__ float sigmoidf_(float x) { return 1.f / (1.f + __expf(-x)); }
; __device__ __forceinline__ unsigned cvt_pk_bf16(float lo, float hi) { const f32x2c v = {lo, hi}; const bf16x2c b = __builtin_convertvector(v, bf16x2c); return __builtin_bit_cast(unsigned, b); }
; #define PG8_BAR __builtin_amdgcn_s_barrier()
; template <class Epi, class Sched>
; __device__ __forceinline__ void gemm_phase(const int WID_, PG8_LAS unsigned char* lds, const Sched& S, const Epi& E) {
;     ...
;         if (wr == 0) PG8_BAR;
;     __device__ __forceinline__ void operator()(const f32x4 (&acc)[2][2][4][2], const Unit& u, int wr, int wc, int fr, int fq) const {
;     ...
;             for (int m = 0; m < 4; ++m) { const size_t row = (size_t)(row0 + ai * HALF + m * 16);
; #pragma unroll
;                 for (int bj = 0; bj < 2; ++bj) { const int col = col0 + bj * HALF;
;                     const u32x4 zz = *(const u32x4*)(Z + row * 512 + col);
;                     const f32x4 b0 = *(const f32x4*)(bias + col), b1 = *(const f32x4*)(bias + col + 4);
;                     const f32x4 v0 = acc[ai][bj][m][0] + b0, v1 = acc[ai][bj][m][1] + b1;
;                     float o[8]; const unsigned zw[4] = {zz.x, zz.y, zz.z, zz.w};
; #pragma unroll
;                     for (int q = 0; q < 4; ++q) { const float zl = __builtin_bit_cast(float, zw[q] << 16), zh = __builtin_bit_cast(float, zw[q] & 0xffff0000u);
;                         const float al = (q < 2) ? v0[2 * q] : v1[2 * q - 4], ah = (q < 2) ? v0[2 * q + 1] : v1[2 * q - 3];
;                         o[2 * q] = zl * sigmoidf_(al); o[2 * q + 1] = zh * sigmoidf_(ah); }
;                     u32x4 w; w.x = cvt_pk_bf16(o[0], o[1]); w.y = cvt_pk_bf16(o[2], o[3]); w.z = cvt_pk_bf16(o[4], o[5]); w.w = cvt_pk_bf16(o[6], o[7]);
;                     *(u32x4*)(YM + row * D + 512 + col) = w; } }
	v_mov_b32_e32 v18, v198
	v_mov_b32_e32 v19, v199
	v_mov_b32_e32 v20, v200
	v_mov_b32_e32 v21, v201
	v_mov_b32_e32 v22, v174
	v_mov_b32_e32 v23, v175
	v_mov_b32_e32 v24, v176
	v_mov_b32_e32 v25, v177
	v_mov_b32_e32 v26, v170
	v_mov_b32_e32 v27, v171
	v_mov_b32_e32 v28, v172
	v_mov_b32_e32 v29, v173
	v_pk_add_f32 v[8:9], v[8:9], v[22:23]
	v_pk_add_f32 v[12:13], v[12:13], v[26:27]
	v_lshlrev_b32_e32 v22, 16, v18
	v_mul_f32_e32 v12, 0xbfb8aa3b, v12
	v_mul_f32_e32 v13, 0xbfb8aa3b, v13
	v_exp_f32_e32 v12, v12
	v_exp_f32_e32 v13, v13
	v_and_b32_e32 v23, 0xffff0000, v18
	v_pk_add_f32 v[10:11], v[10:11], v[24:25]
	v_pk_add_f32 v[14:15], v[14:15], v[28:29]
	v_pk_add_f32 v[12:13], v[12:13], 1.0 op_sel_hi:[1,0]
	v_mul_f32_e32 v14, 0xbfb8aa3b, v14
	v_rcp_f32_e32 v24, v13
	v_mul_f32_e32 v15, 0xbfb8aa3b, v15
	v_exp_f32_e32 v14, v14
	v_exp_f32_e32 v15, v15
	v_fma_f32 v25, -v13, v24, 1.0
	v_fmac_f32_e32 v24, v25, v24
	v_div_fixup_f32 v13, v24, v13, 1.0
	v_rcp_f32_e32 v24, v12
	v_pk_add_f32 v[14:15], v[14:15], 1.0 op_sel_hi:[1,0]
	v_mul_f32_e32 v8, 0xbfb8aa3b, v8
	v_mul_f32_e32 v9, 0xbfb8aa3b, v9
	v_fma_f32 v25, -v12, v24, 1.0
	v_fmac_f32_e32 v24, v25, v24
	v_div_fixup_f32 v12, v24, v12, 1.0
	v_pk_mul_f32 v[12:13], v[12:13], v[22:23]
	v_rcp_f32_e32 v23, v15
	v_exp_f32_e32 v8, v8
	v_exp_f32_e32 v9, v9
	v_lshlrev_b32_e32 v18, 16, v19
	v_fma_f32 v24, -v15, v23, 1.0
	v_fmac_f32_e32 v23, v24, v23
	v_div_fixup_f32 v15, v23, v15, 1.0
	v_rcp_f32_e32 v23, v14
	v_and_b32_e32 v19, 0xffff0000, v19
	v_pk_add_f32 v[8:9], v[8:9], 1.0 op_sel_hi:[1,0]
	v_fma_f32 v24, -v14, v23, 1.0
	v_fmac_f32_e32 v23, v24, v23
	v_div_fixup_f32 v14, v23, v14, 1.0
	v_pk_mul_f32 v[14:15], v[14:15], v[18:19]
	v_lshlrev_b32_e32 v18, 16, v20
	v_and_b32_e32 v19, 0xffff0000, v20
	v_rcp_f32_e32 v22, v9
	s_nop 0
	v_fma_f32 v23, -v9, v22, 1.0
	v_fmac_f32_e32 v22, v23, v22
	v_div_fixup_f32 v9, v22, v9, 1.0
	v_rcp_f32_e32 v22, v8
	s_nop 0
	v_fma_f32 v23, -v8, v22, 1.0
	v_fmac_f32_e32 v22, v23, v22
	v_div_fixup_f32 v8, v22, v8, 1.0
	v_pk_mul_f32 v[18:19], v[8:9], v[18:19]
	v_mul_f32_e32 v8, 0xbfb8aa3b, v10
	v_mul_f32_e32 v9, 0xbfb8aa3b, v11
	v_exp_f32_e32 v8, v8
	v_exp_f32_e32 v9, v9
	v_lshlrev_b32_e32 v10, 16, v21
	v_and_b32_e32 v11, 0xffff0000, v21
	v_pk_add_f32 v[8:9], v[8:9], 1.0 op_sel_hi:[1,0]
	s_nop 0
	v_rcp_f32_e32 v21, v9
	s_nop 0
	v_fma_f32 v22, -v9, v21, 1.0
	v_fmac_f32_e32 v21, v22, v21
	v_div_fixup_f32 v9, v21, v9, 1.0
	v_rcp_f32_e32 v21, v8
	s_nop 0
	v_fma_f32 v22, -v8, v21, 1.0
	v_fmac_f32_e32 v21, v22, v21
	v_div_fixup_f32 v8, v21, v8, 1.0
	v_pk_mul_f32 v[20:21], v[8:9], v[10:11]
	v_cvt_pk_bf16_f32 v8, v12, v13
	v_lshl_add_u64 v[12:13], s[26:27], 0, v[30:31]
	v_cvt_pk_bf16_f32 v9, v14, v15
	v_cvt_pk_bf16_f32 v10, v18, v19
	v_cvt_pk_bf16_f32 v11, v20, v21
	v_lshl_add_u64 v[12:13], v[12:13], 0, v[142:143]
	global_store_dwordx4 v[12:13], v[8:11], off offset:1024
	s_nop 1
	s_nop 0
	s_waitcnt vmcnt(6)
	v_mov_b32_e32 v8, v202
	v_mov_b32_e32 v9, v203
	v_mov_b32_e32 v10, v204
	v_mov_b32_e32 v11, v205
	v_mov_b32_e32 v18, v182
	v_mov_b32_e32 v19, v183
	v_mov_b32_e32 v20, v184
	v_mov_b32_e32 v21, v185
	v_mov_b32_e32 v14, v178
	v_mov_b32_e32 v15, v179
	v_mov_b32_e32 v16, v180
	v_mov_b32_e32 v17, v181
	v_pk_add_f32 v[0:1], v[0:1], v[14:15]
	s_nop 0
	v_mul_f32_e32 v0, 0xbfb8aa3b, v0
	v_mul_f32_e32 v1, 0xbfb8aa3b, v1
	v_exp_f32_e32 v0, v0
	v_exp_f32_e32 v1, v1
	v_pk_add_f32 v[2:3], v[2:3], v[16:17]
	v_pk_add_f32 v[4:5], v[4:5], v[18:19]
	v_mul_f32_e32 v2, 0xbfb8aa3b, v2
	v_pk_add_f32 v[0:1], v[0:1], 1.0 op_sel_hi:[1,0]
	v_mul_f32_e32 v3, 0xbfb8aa3b, v3
	v_rcp_f32_e32 v15, v1
	v_exp_f32_e32 v2, v2
	v_exp_f32_e32 v3, v3
	v_mul_f32_e32 v4, 0xbfb8aa3b, v4
	v_fma_f32 v16, -v1, v15, 1.0
	v_fmac_f32_e32 v15, v16, v15
	v_div_fixup_f32 v1, v15, v1, 1.0
	v_rcp_f32_e32 v15, v0
	v_pk_add_f32 v[2:3], v[2:3], 1.0 op_sel_hi:[1,0]
	v_mul_f32_e32 v5, 0xbfb8aa3b, v5
	v_exp_f32_e32 v4, v4
	v_fma_f32 v16, -v0, v15, 1.0
	v_fmac_f32_e32 v15, v16, v15
	v_div_fixup_f32 v0, v15, v0, 1.0
	v_lshlrev_b32_e32 v14, 16, v8
	v_and_b32_e32 v15, 0xffff0000, v8
	v_div_scale_f32 v8, s[14:15], v3, v3, 1.0
	v_pk_mul_f32 v[0:1], v[0:1], v[14:15]
	v_rcp_f32_e32 v14, v8
	v_exp_f32_e32 v5, v5
	v_pk_add_f32 v[6:7], v[6:7], v[20:21]
	v_cvt_pk_bf16_f32 v0, v0, v1
	v_fma_f32 v15, -v8, v14, 1.0
	v_fmac_f32_e32 v14, v15, v14
	v_div_scale_f32 v15, vcc, 1.0, v3, 1.0
	v_mul_f32_e32 v16, v15, v14
	v_fma_f32 v17, -v8, v16, v15
	v_fmac_f32_e32 v16, v17, v14
	v_fma_f32 v8, -v8, v16, v15
	v_div_fmas_f32 v8, v8, v14, v16
	v_div_fixup_f32 v3, v8, v3, 1.0
	v_rcp_f32_e32 v14, v2
	v_pk_add_f32 v[4:5], v[4:5], 1.0 op_sel_hi:[1,0]
	v_mul_f32_e32 v6, 0xbfb8aa3b, v6
	v_mul_f32_e32 v7, 0xbfb8aa3b, v7
	v_fma_f32 v15, -v2, v14, 1.0
	v_fmac_f32_e32 v14, v15, v14
	v_div_fixup_f32 v2, v14, v2, 1.0
	v_lshlrev_b32_e32 v8, 16, v9
	v_and_b32_e32 v9, 0xffff0000, v9
	v_pk_mul_f32 v[2:3], v[2:3], v[8:9]
	v_rcp_f32_e32 v9, v5
	v_exp_f32_e32 v6, v6
	v_exp_f32_e32 v7, v7
	v_cvt_pk_bf16_f32 v1, v2, v3
	v_fma_f32 v14, -v5, v9, 1.0
	v_fmac_f32_e32 v9, v14, v9
	v_div_fixup_f32 v5, v9, v5, 1.0
	v_rcp_f32_e32 v9, v4
	v_pk_add_f32 v[6:7], v[6:7], 1.0 op_sel_hi:[1,0]
	v_fma_f32 v14, -v4, v9, 1.0
	v_fmac_f32_e32 v9, v14, v9
	v_div_fixup_f32 v4, v9, v4, 1.0
	v_lshlrev_b32_e32 v8, 16, v10
	v_and_b32_e32 v9, 0xffff0000, v10
	v_div_scale_f32 v10, s[14:15], v7, v7, 1.0
	v_pk_mul_f32 v[4:5], v[4:5], v[8:9]
	v_lshlrev_b32_e32 v8, 16, v11
	v_and_b32_e32 v9, 0xffff0000, v11
	v_rcp_f32_e32 v11, v10
	v_cvt_pk_bf16_f32 v2, v4, v5
	v_fma_f32 v14, -v10, v11, 1.0
	v_fmac_f32_e32 v11, v14, v11
	v_div_scale_f32 v14, vcc, 1.0, v7, 1.0
	v_mul_f32_e32 v15, v14, v11
	v_fma_f32 v16, -v10, v15, v14
	v_fmac_f32_e32 v15, v16, v11
	v_fma_f32 v10, -v10, v15, v14
	v_div_fmas_f32 v10, v10, v11, v15
	v_div_fixup_f32 v7, v10, v7, 1.0
	v_rcp_f32_e32 v11, v6
	s_mov_b64 s[14:15], -1
	v_fma_f32 v14, -v6, v11, 1.0
	v_fmac_f32_e32 v11, v14, v11
	v_div_fixup_f32 v6, v11, v6, 1.0
	v_pk_mul_f32 v[6:7], v[6:7], v[8:9]
	s_and_b64 vcc, exec, s[38:39]
	v_cvt_pk_bf16_f32 v3, v6, v7
	global_store_dwordx4 v[12:13], v[0:3], off offset:1280
	s_cbranch_vccnz .LBB0_2014
	s_andn2_b64 vcc, exec, s[96:97]
	s_cbranch_vccnz .LBB0_2013
	s_barrier
	s_branch .LBB0_2013

; #define PG8_LAS __attribute__((address_space(3)))
;     __device__ __forceinline__ void operator()(f32x4 (&acc)[2][2][4][2], const Unit& u, int wr, int wc, int fr, int fq) const {
;     ...
;             for (int m = 0; m < 4; ++m) { float t = -3.0e38f;
;                 const f32x4 s4 = *(PG8_LAS const f32x4*)(ss + (ai * HALF + wr * 64 + m * 16 + fr) * 4);
;                 const float rs = rsqrtf(((s4[0] + s4[1]) + (s4[2] + s4[3])) * (1.f / D) + 1e-6f);
; #pragma unroll
;                 for (int bj = 0; bj < 2; ++bj)
; #pragma unroll
;                     for (int n = 0; n < 2; ++n) { acc[ai][bj][m][n] = acc[ai][bj][m][n] * rs; const f32x4 v = acc[ai][bj][m][n]; t = fmaxf(t, fmaxf(fmaxf(v[0], v[1]), fmaxf(v[2], v[3]))); }
;                 t = rows_max4(t);
;                 if (fq == 0) smax[(ai * HALF + wr * 64 + m * 16 + fr) * 4 + wc] = t; }
.LBB0_2073:
	ds_read_b128 v[140:143], v201
	s_waitcnt lgkmcnt(0)
	v_mov_b32_e32 v144, v141
	v_mov_b32_e32 v145, v142
	v_mov_b32_e32 v141, v143
	v_pk_add_f32 v[140:141], v[144:145], v[140:141]
	s_nop 0
	v_add_f32_e32 v140, v140, v141
	v_fmamk_f32 v140, v140, 0x3a800000, v194
	v_mul_f32_e32 v141, 0x4b800000, v140
	v_cmp_gt_f32_e32 vcc, s64, v140
	s_nop 1
	v_cndmask_b32_e32 v140, v140, v141, vcc
	v_rsq_f32_e32 v140, v140
	s_nop 0
	v_mul_f32_e32 v141, 0x45800000, v140
	v_cndmask_b32_e32 v142, v140, v141, vcc
	v_pk_mul_f32 v[190:191], v[126:127], v[142:143] op_sel_hi:[1,0]
	v_pk_mul_f32 v[192:193], v[124:125], v[142:143] op_sel_hi:[1,0]
	v_pk_mul_f32 v[124:125], v[122:123], v[142:143] op_sel_hi:[1,0]
	v_pk_mul_f32 v[122:123], v[120:121], v[142:143] op_sel_hi:[1,0]
	v_max_f32_e32 v120, v190, v191
	v_max_f32_e32 v121, v124, v125
	v_pk_mul_f32 v[140:141], v[118:119], v[142:143] op_sel_hi:[1,0]
	v_pk_mul_f32 v[144:145], v[114:115], v[142:143] op_sel_hi:[1,0]
	v_max3_f32 v120, v192, v193, v120
	v_max3_f32 v121, v122, v123, v121
	v_pk_mul_f32 v[126:127], v[116:117], v[142:143] op_sel_hi:[1,0]
	v_max_f32_e32 v116, v140, v141
	v_pk_mul_f32 v[142:143], v[112:113], v[142:143] op_sel_hi:[1,0]
	v_max_f32_e32 v112, v144, v145
	v_max3_f32 v120, v120, s34, v121
	v_max3_f32 v116, v126, v127, v116
	v_max3_f32 v112, v142, v143, v112
	v_max3_f32 v112, v120, v116, v112
	v_mov_b32_e32 v113, v112
	s_nop 1
	v_permlane16_swap_b32_e32 v112, v113
	v_max_f32_e32 v113, v113, v113
	v_max_f32_e32 v112, v112, v112
	v_max_f32_e32 v112, v112, v113
	v_mov_b32_e32 v113, v112
	s_nop 1
	v_permlane32_swap_b32_e32 v112, v113
	s_and_saveexec_b64 s[22:23], s[4:5]
	v_max_f32_e32 v112, v112, v112
	v_max_f32_e32 v113, v113, v113
	v_max_f32_e32 v112, v112, v113
	ds_write_b32 v202, v112
	s_or_b64 exec, exec, s[22:23]
	ds_read_b128 v[112:115], v203
	s_waitcnt lgkmcnt(0)
	v_mov_b32_e32 v116, v113
	v_mov_b32_e32 v117, v114
	v_mov_b32_e32 v113, v115
	v_pk_add_f32 v[112:113], v[116:117], v[112:113]
	s_nop 0
	v_add_f32_e32 v112, v112, v113
	v_fmamk_f32 v112, v112, 0x3a800000, v194
	v_mul_f32_e32 v113, 0x4b800000, v112
	v_cmp_gt_f32_e32 vcc, s64, v112
	s_nop 1
	v_cndmask_b32_e32 v112, v112, v113, vcc
	v_rsq_f32_e32 v112, v112
	s_nop 0
	v_mul_f32_e32 v113, 0x45800000, v112
	v_cndmask_b32_e32 v112, v112, v113, vcc
	v_pk_mul_f32 v[186:187], v[110:111], v[112:113] op_sel_hi:[1,0]
	v_pk_mul_f32 v[180:181], v[106:107], v[112:113] op_sel_hi:[1,0]
	v_pk_mul_f32 v[178:179], v[102:103], v[112:113] op_sel_hi:[1,0]
	v_pk_mul_f32 v[188:189], v[108:109], v[112:113] op_sel_hi:[1,0]
	v_pk_mul_f32 v[184:185], v[104:105], v[112:113] op_sel_hi:[1,0]
	v_max_f32_e32 v104, v186, v187
	v_max_f32_e32 v105, v180, v181
	v_pk_mul_f32 v[182:183], v[100:101], v[112:113] op_sel_hi:[1,0]
	v_max_f32_e32 v100, v178, v179
	v_pk_mul_f32 v[106:107], v[98:99], v[112:113] op_sel_hi:[1,0]
	v_max3_f32 v104, v188, v189, v104
	v_max3_f32 v105, v184, v185, v105
	v_max3_f32 v102, v182, v183, v100
	v_pk_mul_f32 v[100:101], v[96:97], v[112:113] op_sel_hi:[1,0]
	v_max_f32_e32 v96, v106, v107
	v_max3_f32 v104, v104, s34, v105
	v_max3_f32 v96, v100, v101, v96
	v_max3_f32 v96, v104, v102, v96
	v_mov_b32_e32 v97, v96
	s_nop 1
	v_permlane16_swap_b32_e32 v96, v97
	v_max_f32_e32 v97, v97, v97
	v_max_f32_e32 v96, v96, v96
	v_max_f32_e32 v96, v96, v97
	v_mov_b32_e32 v97, v96
	s_nop 1
	v_permlane32_swap_b32_e32 v96, v97
	s_and_saveexec_b64 s[22:23], s[4:5]
	v_max_f32_e32 v96, v96, v96
	v_max_f32_e32 v97, v97, v97
	v_max_f32_e32 v96, v96, v97
	ds_write_b32 v202, v96 offset:256
	s_or_b64 exec, exec, s[22:23]
	ds_read_b128 v[96:99], v204
	s_waitcnt lgkmcnt(0)
	v_mov_b32_e32 v102, v97
	v_mov_b32_e32 v103, v98
	v_mov_b32_e32 v97, v99
	v_pk_add_f32 v[96:97], v[102:103], v[96:97]
	s_nop 0
	v_add_f32_e32 v96, v96, v97
	v_fmamk_f32 v96, v96, 0x3a800000, v194
	v_mul_f32_e32 v97, 0x4b800000, v96
	v_cmp_gt_f32_e32 vcc, s64, v96
	s_nop 1
	v_cndmask_b32_e32 v96, v96, v97, vcc
	v_rsq_f32_e32 v96, v96
	s_nop 0
	v_mul_f32_e32 v97, 0x45800000, v96
	v_cndmask_b32_e32 v96, v96, v97, vcc
	v_pk_mul_f32 v[176:177], v[94:95], v[96:97] op_sel_hi:[1,0]
	v_pk_mul_f32 v[102:103], v[90:91], v[96:97] op_sel_hi:[1,0]
	v_pk_mul_f32 v[92:93], v[92:93], v[96:97] op_sel_hi:[1,0]
	v_pk_mul_f32 v[94:95], v[88:89], v[96:97] op_sel_hi:[1,0]
	v_max_f32_e32 v88, v176, v177
	v_max_f32_e32 v89, v102, v103
	v_pk_mul_f32 v[108:109], v[86:87], v[96:97] op_sel_hi:[1,0]
	v_pk_mul_f32 v[112:113], v[82:83], v[96:97] op_sel_hi:[1,0]
	v_max3_f32 v88, v92, v93, v88
	v_max3_f32 v89, v94, v95, v89
	v_pk_mul_f32 v[104:105], v[84:85], v[96:97] op_sel_hi:[1,0]
	v_max_f32_e32 v84, v108, v109
	v_pk_mul_f32 v[110:111], v[80:81], v[96:97] op_sel_hi:[1,0]
	v_max_f32_e32 v80, v112, v113
	v_max3_f32 v88, v88, s34, v89
	v_max3_f32 v84, v104, v105, v84
	v_max3_f32 v80, v110, v111, v80
	v_max3_f32 v80, v88, v84, v80
	v_mov_b32_e32 v81, v80
	s_nop 1
	v_permlane16_swap_b32_e32 v80, v81
	v_max_f32_e32 v81, v81, v81
	v_max_f32_e32 v80, v80, v80
	v_max_f32_e32 v80, v80, v81
	v_mov_b32_e32 v81, v80
	s_nop 1
	v_permlane32_swap_b32_e32 v80, v81
	s_and_saveexec_b64 s[22:23], s[4:5]
	v_max_f32_e32 v80, v80, v80
	v_max_f32_e32 v81, v81, v81
	v_max_f32_e32 v80, v80, v81
	ds_write_b32 v202, v80 offset:512
	s_or_b64 exec, exec, s[22:23]
	ds_read_b128 v[80:83], v205
	s_waitcnt lgkmcnt(0)
; #define PG8_LAS __attribute__((address_space(3)))
;     __device__ __forceinline__ void operator()(f32x4 (&acc)[2][2][4][2], const Unit& u, int wr, int wc, int fr, int fq) const {
;     ...
;             for (int m = 0; m < 4; ++m) { float t = -3.0e38f;
;                 const f32x4 s4 = *(PG8_LAS const f32x4*)(ss + (ai * HALF + wr * 64 + m * 16 + fr) * 4);
;                 const float rs = rsqrtf(((s4[0] + s4[1]) + (s4[2] + s4[3])) * (1.f / D) + 1e-6f);
; #pragma unroll
;                 for (int bj = 0; bj < 2; ++bj)
; #pragma unroll
;                     for (int n = 0; n < 2; ++n) { acc[ai][bj][m][n] = acc[ai][bj][m][n] * rs; const f32x4 v = acc[ai][bj][m][n]; t = fmaxf(t, fmaxf(fmaxf(v[0], v[1]), fmaxf(v[2], v[3]))); }
;                 t = rows_max4(t);
;                 if (fq == 0) smax[(ai * HALF + wr * 64 + m * 16 + fr) * 4 + wc] = t; }
	v_mov_b32_e32 v84, v81
	v_mov_b32_e32 v85, v82
	v_mov_b32_e32 v81, v83
	v_pk_add_f32 v[80:81], v[84:85], v[80:81]
	s_nop 0
	v_add_f32_e32 v80, v80, v81
	v_fmamk_f32 v80, v80, 0x3a800000, v194
	v_mul_f32_e32 v81, 0x4b800000, v80
	v_cmp_gt_f32_e32 vcc, s64, v80
	s_nop 1
	v_cndmask_b32_e32 v80, v80, v81, vcc
	v_rsq_f32_e32 v80, v80
	s_nop 0
	v_mul_f32_e32 v81, 0x45800000, v80
	v_cndmask_b32_e32 v80, v80, v81, vcc
	v_pk_mul_f32 v[172:173], v[78:79], v[80:81] op_sel_hi:[1,0]
	v_pk_mul_f32 v[166:167], v[74:75], v[80:81] op_sel_hi:[1,0]
	v_pk_mul_f32 v[164:165], v[70:71], v[80:81] op_sel_hi:[1,0]
	v_pk_mul_f32 v[174:175], v[76:77], v[80:81] op_sel_hi:[1,0]
	v_pk_mul_f32 v[170:171], v[72:73], v[80:81] op_sel_hi:[1,0]
	v_max_f32_e32 v72, v172, v173
	v_max_f32_e32 v73, v166, v167
	v_pk_mul_f32 v[168:169], v[68:69], v[80:81] op_sel_hi:[1,0]
	v_max_f32_e32 v68, v164, v165
	v_pk_mul_f32 v[74:75], v[66:67], v[80:81] op_sel_hi:[1,0]
	v_max3_f32 v72, v174, v175, v72
	v_max3_f32 v73, v170, v171, v73
	v_max3_f32 v70, v168, v169, v68
	v_pk_mul_f32 v[68:69], v[64:65], v[80:81] op_sel_hi:[1,0]
	v_max_f32_e32 v64, v74, v75
	v_max3_f32 v72, v72, s34, v73
	v_max3_f32 v64, v68, v69, v64
	v_max3_f32 v64, v72, v70, v64
	v_mov_b32_e32 v65, v64
	s_nop 1
	v_permlane16_swap_b32_e32 v64, v65
	v_max_f32_e32 v65, v65, v65
	v_max_f32_e32 v64, v64, v64
	v_max_f32_e32 v64, v64, v65
	v_mov_b32_e32 v65, v64
	s_nop 1
	v_permlane32_swap_b32_e32 v64, v65
	s_and_saveexec_b64 s[22:23], s[4:5]
	v_max_f32_e32 v64, v64, v64
	v_max_f32_e32 v65, v65, v65
	v_max_f32_e32 v64, v64, v65
	ds_write_b32 v202, v64 offset:768
	s_or_b64 exec, exec, s[22:23]
	ds_read_b128 v[64:67], v206
	s_waitcnt lgkmcnt(0)
	v_mov_b32_e32 v70, v65
	v_mov_b32_e32 v71, v66
	v_mov_b32_e32 v65, v67
	v_pk_add_f32 v[64:65], v[70:71], v[64:65]
	s_nop 0
	v_add_f32_e32 v64, v64, v65
	v_fmamk_f32 v64, v64, 0x3a800000, v194
	v_mul_f32_e32 v65, 0x4b800000, v64
	v_cmp_gt_f32_e32 vcc, s64, v64
	s_nop 1
	v_cndmask_b32_e32 v64, v64, v65, vcc
	v_rsq_f32_e32 v64, v64
	s_nop 0
	v_mul_f32_e32 v65, 0x45800000, v64
	v_cndmask_b32_e32 v64, v64, v65, vcc
	v_pk_mul_f32 v[72:73], v[62:63], v[64:65] op_sel_hi:[1,0]
	v_pk_mul_f32 v[70:71], v[58:59], v[64:65] op_sel_hi:[1,0]
	v_pk_mul_f32 v[60:61], v[60:61], v[64:65] op_sel_hi:[1,0]
	v_pk_mul_f32 v[66:67], v[56:57], v[64:65] op_sel_hi:[1,0]
	v_max_f32_e32 v56, v72, v73
	v_max_f32_e32 v57, v70, v71
	v_pk_mul_f32 v[76:77], v[54:55], v[64:65] op_sel_hi:[1,0]
	v_pk_mul_f32 v[80:81], v[50:51], v[64:65] op_sel_hi:[1,0]
	v_max3_f32 v56, v60, v61, v56
	v_max3_f32 v57, v66, v67, v57
	v_pk_mul_f32 v[162:163], v[52:53], v[64:65] op_sel_hi:[1,0]
	v_max_f32_e32 v52, v76, v77
	v_pk_mul_f32 v[78:79], v[48:49], v[64:65] op_sel_hi:[1,0]
	v_max_f32_e32 v48, v80, v81
	v_max3_f32 v56, v56, s34, v57
	v_max3_f32 v52, v162, v163, v52
	v_max3_f32 v48, v78, v79, v48
	v_max3_f32 v48, v56, v52, v48
	v_mov_b32_e32 v49, v48
	s_nop 1
	v_permlane16_swap_b32_e32 v48, v49
	v_max_f32_e32 v49, v49, v49
	v_max_f32_e32 v48, v48, v48
	v_max_f32_e32 v48, v48, v49
	v_mov_b32_e32 v49, v48
	s_nop 1
	v_permlane32_swap_b32_e32 v48, v49
	s_and_saveexec_b64 s[22:23], s[4:5]
	v_max_f32_e32 v48, v48, v48
	v_max_f32_e32 v49, v49, v49
	v_max_f32_e32 v48, v48, v49
	ds_write_b32 v202, v48 offset:2048
	s_or_b64 exec, exec, s[22:23]
	ds_read_b128 v[48:51], v207
	s_waitcnt lgkmcnt(0)
	v_mov_b32_e32 v52, v49
	v_mov_b32_e32 v53, v50
	v_mov_b32_e32 v49, v51
	v_pk_add_f32 v[48:49], v[52:53], v[48:49]
	s_nop 0
	v_add_f32_e32 v48, v48, v49
	v_fmamk_f32 v48, v48, 0x3a800000, v194
	v_mul_f32_e32 v49, 0x4b800000, v48
	v_cmp_gt_f32_e32 vcc, s64, v48
	s_nop 1
	v_cndmask_b32_e32 v48, v48, v49, vcc
	v_rsq_f32_e32 v48, v48
	s_nop 0
	v_mul_f32_e32 v49, 0x45800000, v48
	v_cndmask_b32_e32 v48, v48, v49, vcc
	v_pk_mul_f32 v[158:159], v[46:47], v[48:49] op_sel_hi:[1,0]
	v_pk_mul_f32 v[152:153], v[42:43], v[48:49] op_sel_hi:[1,0]
	v_pk_mul_f32 v[160:161], v[44:45], v[48:49] op_sel_hi:[1,0]
	v_pk_mul_f32 v[156:157], v[40:41], v[48:49] op_sel_hi:[1,0]
	v_max_f32_e32 v40, v158, v159
	v_max_f32_e32 v41, v152, v153
	v_pk_mul_f32 v[150:151], v[38:39], v[48:49] op_sel_hi:[1,0]
	v_pk_mul_f32 v[42:43], v[34:35], v[48:49] op_sel_hi:[1,0]
	v_max3_f32 v40, v160, v161, v40
	v_max3_f32 v41, v156, v157, v41
	v_pk_mul_f32 v[154:155], v[36:37], v[48:49] op_sel_hi:[1,0]
	v_max_f32_e32 v36, v150, v151
	v_pk_mul_f32 v[34:35], v[32:33], v[48:49] op_sel_hi:[1,0]
	v_max_f32_e32 v32, v42, v43
	v_max3_f32 v40, v40, s34, v41
	v_max3_f32 v36, v154, v155, v36
	v_max3_f32 v32, v34, v35, v32
	v_max3_f32 v32, v40, v36, v32
	v_mov_b32_e32 v33, v32
	s_nop 1
	v_permlane16_swap_b32_e32 v32, v33
	v_max_f32_e32 v33, v33, v33
	v_max_f32_e32 v32, v32, v32
	v_max_f32_e32 v32, v32, v33
	v_mov_b32_e32 v33, v32
	s_nop 1
	v_permlane32_swap_b32_e32 v32, v33
	s_and_saveexec_b64 s[22:23], s[4:5]
	v_max_f32_e32 v32, v32, v32
	v_max_f32_e32 v33, v33, v33
	v_max_f32_e32 v32, v32, v33
	ds_write_b32 v202, v32 offset:2304
	s_or_b64 exec, exec, s[22:23]
	ds_read_b128 v[36:39], v208
	s_waitcnt lgkmcnt(0)
; #define PG8_LAS __attribute__((address_space(3)))
;     __device__ __forceinline__ void operator()(f32x4 (&acc)[2][2][4][2], const Unit& u, int wr, int wc, int fr, int fq) const {
;     ...
;                     for (int n = 0; n < 2; ++n) { acc[ai][bj][m][n] = acc[ai][bj][m][n] * rs; const f32x4 v = acc[ai][bj][m][n]; t = fmaxf(t, fmaxf(fmaxf(v[0], v[1]), fmaxf(v[2], v[3]))); }
;                 t = rows_max4(t);
;                 if (fq == 0) smax[(ai * HALF + wr * 64 + m * 16 + fr) * 4 + wc] = t; }
;         asm volatile("s_waitcnt lgkmcnt(0)" ::: "memory"); __builtin_amdgcn_s_barrier(); asm volatile("" ::: "memory");
; #pragma unroll
;         for (int ai = 0; ai < 2; ++ai)
; #pragma unroll
;             for (int m = 0; m < 4; ++m) { const f32x4 q = *(const PG8_LAS f32x4*)(smax + (ai * HALF + wr * 64 + m * 16 + fr) * 4);
;                 const float mm = fmaxf(fmaxf(q[0], q[1]), fmaxf(q[2], q[3])) * SC; float s = 0.f;
; #pragma unroll
;                 for (int bj = 0; bj < 2; ++bj)
; #pragma unroll
;                     for (int n = 0; n < 2; ++n)
; #pragma unroll
;                         for (int e = 0; e < 4; ++e) { const float p = __builtin_amdgcn_exp2f(acc[ai][bj][m][n][e] * SC - mm); acc[ai][bj][m][n][e] = p; s += p; }
	v_mov_b32_e32 v32, v37
	v_mov_b32_e32 v33, v38
	v_mov_b32_e32 v37, v39
	v_pk_add_f32 v[32:33], v[32:33], v[36:37]
	s_nop 0
	v_add_f32_e32 v32, v32, v33
	v_fmamk_f32 v32, v32, 0x3a800000, v194
	v_mul_f32_e32 v33, 0x4b800000, v32
	v_cmp_gt_f32_e32 vcc, s64, v32
	s_nop 1
	v_cndmask_b32_e32 v32, v32, v33, vcc
	v_rsq_f32_e32 v32, v32
	s_nop 0
	v_mul_f32_e32 v33, 0x45800000, v32
	v_cndmask_b32_e32 v36, v32, v33, vcc
	v_pk_mul_f32 v[40:41], v[30:31], v[36:37] op_sel_hi:[1,0]
	v_pk_mul_f32 v[38:39], v[26:27], v[36:37] op_sel_hi:[1,0]
	v_pk_mul_f32 v[28:29], v[28:29], v[36:37] op_sel_hi:[1,0]
	v_pk_mul_f32 v[32:33], v[24:25], v[36:37] op_sel_hi:[1,0]
	v_max_f32_e32 v24, v40, v41
	v_max_f32_e32 v25, v38, v39
	v_pk_mul_f32 v[44:45], v[22:23], v[36:37] op_sel_hi:[1,0]
	v_pk_mul_f32 v[48:49], v[18:19], v[36:37] op_sel_hi:[1,0]
	v_max3_f32 v24, v28, v29, v24
	v_max3_f32 v25, v32, v33, v25
	v_pk_mul_f32 v[148:149], v[20:21], v[36:37] op_sel_hi:[1,0]
	v_max_f32_e32 v20, v44, v45
	v_pk_mul_f32 v[46:47], v[16:17], v[36:37] op_sel_hi:[1,0]
	v_max_f32_e32 v16, v48, v49
	v_max3_f32 v24, v24, s34, v25
	v_max3_f32 v20, v148, v149, v20
	v_max3_f32 v16, v46, v47, v16
	v_max3_f32 v16, v24, v20, v16
	v_mov_b32_e32 v17, v16
	s_nop 1
	v_permlane16_swap_b32_e32 v16, v17
	v_max_f32_e32 v17, v17, v17
	v_max_f32_e32 v16, v16, v16
	v_max_f32_e32 v16, v16, v17
	v_mov_b32_e32 v17, v16
	s_nop 1
	v_permlane32_swap_b32_e32 v16, v17
	s_and_saveexec_b64 s[22:23], s[4:5]
	v_max_f32_e32 v16, v16, v16
	v_max_f32_e32 v17, v17, v17
	v_max_f32_e32 v16, v16, v17
	ds_write_b32 v202, v16 offset:2560
	s_or_b64 exec, exec, s[22:23]
	ds_read_b128 v[16:19], v209
	s_waitcnt lgkmcnt(0)
	v_mov_b32_e32 v20, v17
	v_mov_b32_e32 v21, v18
	v_mov_b32_e32 v17, v19
	v_pk_add_f32 v[16:17], v[20:21], v[16:17]
	s_nop 0
	v_add_f32_e32 v16, v16, v17
	v_fmamk_f32 v16, v16, 0x3a800000, v194
	v_mul_f32_e32 v17, 0x4b800000, v16
	v_cmp_gt_f32_e32 vcc, s64, v16
	s_nop 1
	v_cndmask_b32_e32 v16, v16, v17, vcc
	v_rsq_f32_e32 v16, v16
	s_nop 0
	v_mul_f32_e32 v17, 0x45800000, v16
	v_cndmask_b32_e32 v18, v16, v17, vcc
	v_pk_mul_f32 v[116:117], v[14:15], v[18:19] op_sel_hi:[1,0]
	v_pk_mul_f32 v[146:147], v[12:13], v[18:19] op_sel_hi:[1,0]
	v_pk_mul_f32 v[12:13], v[10:11], v[18:19] op_sel_hi:[1,0]
	v_pk_mul_f32 v[114:115], v[8:9], v[18:19] op_sel_hi:[1,0]
	v_max_f32_e32 v8, v116, v117
	v_max_f32_e32 v9, v12, v13
	v_max3_f32 v8, v146, v147, v8
	v_max3_f32 v9, v114, v115, v9
	v_max3_f32 v19, v8, s34, v9
	v_pk_mul_f32 v[10:11], v[6:7], v[18:19] op_sel_hi:[1,0]
	v_pk_mul_f32 v[14:15], v[2:3], v[18:19] op_sel_hi:[1,0]
	v_pk_mul_f32 v[16:17], v[4:5], v[18:19] op_sel_hi:[1,0]
	v_max_f32_e32 v4, v10, v11
	v_pk_mul_f32 v[8:9], v[0:1], v[18:19] op_sel_hi:[1,0]
	v_max_f32_e32 v0, v14, v15
	v_max3_f32 v4, v16, v17, v4
	v_max3_f32 v0, v8, v9, v0
	v_max3_f32 v0, v19, v4, v0
	v_mov_b32_e32 v1, v0
	s_nop 1
	v_permlane16_swap_b32_e32 v0, v1
	v_max_f32_e32 v1, v1, v1
	v_max_f32_e32 v0, v0, v0
	v_max_f32_e32 v0, v0, v1
	v_mov_b32_e32 v1, v0
	s_nop 1
	v_permlane32_swap_b32_e32 v0, v1
	s_and_saveexec_b64 s[22:23], s[4:5]
	v_max_f32_e32 v0, v0, v0
	v_max_f32_e32 v1, v1, v1
	v_max_f32_e32 v0, v0, v1
	ds_write_b32 v202, v0 offset:2816
	s_or_b64 exec, exec, s[22:23]
	s_waitcnt lgkmcnt(0)
	s_barrier
	ds_read_b128 v[0:3], v210
	v_mov_b32_e32 v4, v145
	s_waitcnt lgkmcnt(0)
	v_max_f32_e32 v3, v3, v3
	v_max_f32_e32 v2, v2, v2
	v_max_f32_e32 v2, v2, v3
	v_max3_f32 v5, v0, v1, v2
	v_pk_mul_f32 v[0:1], v[4:5], s[70:71] op_sel_hi:[1,0]
	s_nop 0
	v_fma_f32 v2, v192, s70, -v1
	v_exp_f32_e32 v118, v2
	v_fma_f32 v2, v193, s70, -v1
	v_exp_f32_e32 v119, v2
	v_fma_f32 v2, v190, s70, -v1
	v_exp_f32_e32 v120, v2
	v_fma_f32 v2, v191, s70, -v1
	v_exp_f32_e32 v121, v2
	v_fma_f32 v3, v122, s70, -v1
	v_add_f32_e32 v2, 0, v118
	v_exp_f32_e32 v122, v3
	v_fma_f32 v3, v123, s70, -v1
	v_add_f32_e32 v2, v119, v2
	v_exp_f32_e32 v123, v3
	v_fma_f32 v3, v124, s70, -v1
	v_add_f32_e32 v2, v120, v2
	v_exp_f32_e32 v124, v3
	v_fma_f32 v3, v125, s70, -v1
	v_add_f32_e32 v2, v121, v2
	v_exp_f32_e32 v125, v3
	v_fma_f32 v3, v126, s70, -v1
	v_add_f32_e32 v2, v122, v2
	v_exp_f32_e32 v126, v3
	v_fma_f32 v3, v127, s70, -v1
	v_add_f32_e32 v2, v123, v2
	v_exp_f32_e32 v127, v3
	v_fma_f32 v3, v140, s70, -v1
	v_add_f32_e32 v2, v124, v2
	v_exp_f32_e32 v140, v3
	v_fma_f32 v3, v141, s70, -v1
	v_add_f32_e32 v2, v125, v2
	v_exp_f32_e32 v141, v3
	v_fma_f32 v3, v142, s70, -v1
	v_add_f32_e32 v2, v126, v2
	v_exp_f32_e32 v142, v3
	v_fma_f32 v3, v143, s70, -v1
	v_add_f32_e32 v2, v127, v2
	v_exp_f32_e32 v143, v3
	v_fma_f32 v3, v144, s70, -v1
	v_add_f32_e32 v2, v140, v2
	v_exp_f32_e32 v144, v3
	v_sub_f32_e32 v0, v0, v1
	v_add_f32_e32 v2, v141, v2
	v_exp_f32_e32 v145, v0
	v_add_f32_e32 v0, v142, v2
	v_add_f32_e32 v0, v143, v0
	v_add_f32_e32 v0, v144, v0
	v_add_f32_e32 v0, v145, v0
	v_mov_b32_e32 v1, v0
	s_nop 1
	v_permlane16_swap_b32_e32 v0, v1
	v_add_f32_e32 v0, v0, v1
	v_mov_b32_e32 v1, v0
	s_nop 1
	v_permlane32_swap_b32_e32 v0, v1
	s_and_saveexec_b64 s[22:23], s[4:5]
	v_add_f32_e32 v0, v0, v1
	ds_write_b32 v211, v0
	s_or_b64 exec, exec, s[22:23]
	ds_read_b128 v[0:3], v212
	v_mov_b32_e32 v4, v107
	s_waitcnt lgkmcnt(0)
; #define PG8_LAS __attribute__((address_space(3)))
;     __device__ __forceinline__ void operator()(f32x4 (&acc)[2][2][4][2], const Unit& u, int wr, int wc, int fr, int fq) const {
;     ...
;             for (int m = 0; m < 4; ++m) { const f32x4 q = *(const PG8_LAS f32x4*)(smax + (ai * HALF + wr * 64 + m * 16 + fr) * 4);
;                 const float mm = fmaxf(fmaxf(q[0], q[1]), fmaxf(q[2], q[3])) * SC; float s = 0.f;
; #pragma unroll
;                 for (int bj = 0; bj < 2; ++bj)
; #pragma unroll
;                     for (int n = 0; n < 2; ++n)
; #pragma unroll
;                         for (int e = 0; e < 4; ++e) { const float p = __builtin_amdgcn_exp2f(acc[ai][bj][m][n][e] * SC - mm); acc[ai][bj][m][n][e] = p; s += p; }
;                 s = rows_sum4(s);
;                 if (fq == 0) ssum[(ai * HALF + wr * 64 + m * 16 + fr) * 4 + wc] = s; }
	v_max_f32_e32 v3, v3, v3
	v_max_f32_e32 v2, v2, v2
	v_max_f32_e32 v2, v2, v3
	v_max3_f32 v5, v0, v1, v2
	v_pk_mul_f32 v[0:1], v[4:5], s[70:71] op_sel_hi:[1,0]
	s_nop 0
	v_fma_f32 v2, v188, s70, -v1
	v_fma_f32 v3, v189, s70, -v1
	v_exp_f32_e32 v82, v2
	v_exp_f32_e32 v83, v3
	v_fma_f32 v2, v186, s70, -v1
	v_exp_f32_e32 v90, v2
	v_fma_f32 v2, v187, s70, -v1
	v_exp_f32_e32 v91, v2
	v_fma_f32 v3, v184, s70, -v1
	v_add_f32_e32 v2, 0, v82
	v_exp_f32_e32 v88, v3
	v_fma_f32 v3, v185, s70, -v1
	v_add_f32_e32 v2, v83, v2
	v_exp_f32_e32 v89, v3
	v_fma_f32 v3, v180, s70, -v1
	v_add_f32_e32 v2, v90, v2
	v_exp_f32_e32 v98, v3
	v_fma_f32 v3, v181, s70, -v1
	v_add_f32_e32 v2, v91, v2
	v_exp_f32_e32 v99, v3
	v_fma_f32 v3, v182, s70, -v1
	v_add_f32_e32 v2, v88, v2
	v_exp_f32_e32 v86, v3
	v_fma_f32 v3, v183, s70, -v1
	v_add_f32_e32 v2, v89, v2
	v_exp_f32_e32 v87, v3
	v_fma_f32 v3, v178, s70, -v1
	v_add_f32_e32 v2, v98, v2
	v_exp_f32_e32 v96, v3
	v_fma_f32 v3, v179, s70, -v1
	v_add_f32_e32 v2, v99, v2
	v_exp_f32_e32 v97, v3
	v_fma_f32 v3, v100, s70, -v1
	v_add_f32_e32 v2, v86, v2
	v_exp_f32_e32 v100, v3
	v_fma_f32 v3, v101, s70, -v1
	v_add_f32_e32 v2, v87, v2
	v_exp_f32_e32 v101, v3
	v_fma_f32 v3, v106, s70, -v1
	v_add_f32_e32 v2, v96, v2
	v_exp_f32_e32 v106, v3
	v_sub_f32_e32 v0, v0, v1
	v_add_f32_e32 v2, v97, v2
	v_exp_f32_e32 v107, v0
	v_add_f32_e32 v0, v100, v2
	v_add_f32_e32 v0, v101, v0
	v_add_f32_e32 v0, v106, v0
	v_add_f32_e32 v0, v107, v0
	v_mov_b32_e32 v1, v0
	s_nop 1
	v_permlane16_swap_b32_e32 v0, v1
	v_add_f32_e32 v0, v0, v1
	v_mov_b32_e32 v1, v0
	s_nop 1
	v_permlane32_swap_b32_e32 v0, v1
	s_and_saveexec_b64 s[22:23], s[4:5]
	v_add_f32_e32 v0, v0, v1
	ds_write_b32 v211, v0 offset:256
	s_or_b64 exec, exec, s[22:23]
	ds_read_b128 v[0:3], v213
	v_mov_b32_e32 v4, v113
	s_waitcnt lgkmcnt(0)
	v_max_f32_e32 v3, v3, v3
	v_max_f32_e32 v2, v2, v2
	v_max_f32_e32 v2, v2, v3
	v_max3_f32 v5, v0, v1, v2
	v_pk_mul_f32 v[0:1], v[4:5], s[70:71] op_sel_hi:[1,0]
	s_nop 0
	v_fma_f32 v2, v92, s70, -v1
	v_fma_f32 v3, v93, s70, -v1
	v_exp_f32_e32 v84, v2
	v_exp_f32_e32 v85, v3
	v_fma_f32 v2, v176, s70, -v1
	v_exp_f32_e32 v92, v2
	v_fma_f32 v2, v177, s70, -v1
	v_exp_f32_e32 v93, v2
	v_fma_f32 v3, v94, s70, -v1
	v_add_f32_e32 v2, 0, v84
	v_exp_f32_e32 v94, v3
	v_fma_f32 v3, v95, s70, -v1
	v_add_f32_e32 v2, v85, v2
	v_exp_f32_e32 v95, v3
	v_fma_f32 v3, v102, s70, -v1
	v_add_f32_e32 v2, v92, v2
	v_exp_f32_e32 v102, v3
	v_fma_f32 v3, v103, s70, -v1
	v_add_f32_e32 v2, v93, v2
	v_exp_f32_e32 v103, v3
	v_fma_f32 v3, v104, s70, -v1
	v_add_f32_e32 v2, v94, v2
	v_exp_f32_e32 v104, v3
	v_fma_f32 v3, v105, s70, -v1
	v_add_f32_e32 v2, v95, v2
	v_exp_f32_e32 v105, v3
	v_fma_f32 v3, v108, s70, -v1
	v_add_f32_e32 v2, v102, v2
	v_exp_f32_e32 v108, v3
	v_fma_f32 v3, v109, s70, -v1
	v_add_f32_e32 v2, v103, v2
	v_exp_f32_e32 v109, v3
	v_fma_f32 v3, v110, s70, -v1
	v_add_f32_e32 v2, v104, v2
	v_exp_f32_e32 v110, v3
	v_fma_f32 v3, v111, s70, -v1
	v_add_f32_e32 v2, v105, v2
	v_exp_f32_e32 v111, v3
	v_fma_f32 v3, v112, s70, -v1
	v_add_f32_e32 v2, v108, v2
	v_exp_f32_e32 v112, v3
	v_sub_f32_e32 v0, v0, v1
	v_add_f32_e32 v2, v109, v2
	v_exp_f32_e32 v113, v0
	v_add_f32_e32 v0, v110, v2
	v_add_f32_e32 v0, v111, v0
	v_add_f32_e32 v0, v112, v0
	v_add_f32_e32 v0, v113, v0
	v_mov_b32_e32 v1, v0
	s_nop 1
	v_permlane16_swap_b32_e32 v0, v1
	v_add_f32_e32 v0, v0, v1
	v_mov_b32_e32 v1, v0
	s_nop 1
	v_permlane32_swap_b32_e32 v0, v1
	s_and_saveexec_b64 s[22:23], s[4:5]
	v_add_f32_e32 v0, v0, v1
	ds_write_b32 v211, v0 offset:512
	s_or_b64 exec, exec, s[22:23]
	ds_read_b128 v[0:3], v214
	v_mov_b32_e32 v4, v75
	s_waitcnt lgkmcnt(0)
	v_max_f32_e32 v3, v3, v3
	v_max_f32_e32 v2, v2, v2
	v_max_f32_e32 v2, v2, v3
	v_max3_f32 v5, v0, v1, v2
	v_pk_mul_f32 v[0:1], v[4:5], s[70:71] op_sel_hi:[1,0]
	s_nop 0
	v_fma_f32 v2, v174, s70, -v1
	v_fma_f32 v3, v175, s70, -v1
	v_exp_f32_e32 v50, v2
	v_exp_f32_e32 v51, v3
	v_fma_f32 v2, v172, s70, -v1
	v_exp_f32_e32 v56, v2
	v_fma_f32 v2, v173, s70, -v1
	v_exp_f32_e32 v57, v2
	v_fma_f32 v3, v170, s70, -v1
	v_add_f32_e32 v2, 0, v50
	v_exp_f32_e32 v54, v3
	v_fma_f32 v3, v171, s70, -v1
	v_add_f32_e32 v2, v51, v2
	v_exp_f32_e32 v55, v3
	v_fma_f32 v3, v166, s70, -v1
	v_add_f32_e32 v2, v56, v2
	v_exp_f32_e32 v64, v3
	v_fma_f32 v3, v167, s70, -v1
	v_add_f32_e32 v2, v57, v2
	v_exp_f32_e32 v65, v3
	v_fma_f32 v3, v168, s70, -v1
	v_add_f32_e32 v2, v54, v2
	v_exp_f32_e32 v52, v3
	v_fma_f32 v3, v169, s70, -v1
	v_add_f32_e32 v2, v55, v2
	v_exp_f32_e32 v53, v3
	v_fma_f32 v3, v164, s70, -v1
	v_add_f32_e32 v2, v64, v2
	v_exp_f32_e32 v62, v3
	v_fma_f32 v3, v165, s70, -v1
	v_add_f32_e32 v2, v65, v2
	v_exp_f32_e32 v63, v3
	v_fma_f32 v3, v68, s70, -v1
	v_add_f32_e32 v2, v52, v2
	v_exp_f32_e32 v68, v3
	v_fma_f32 v3, v69, s70, -v1
	v_add_f32_e32 v2, v53, v2
	v_exp_f32_e32 v69, v3
	v_fma_f32 v3, v74, s70, -v1
	v_add_f32_e32 v2, v62, v2
	v_exp_f32_e32 v74, v3
	v_sub_f32_e32 v0, v0, v1
	v_add_f32_e32 v2, v63, v2
	v_exp_f32_e32 v75, v0
	v_add_f32_e32 v0, v68, v2
	v_add_f32_e32 v0, v69, v0
	v_add_f32_e32 v0, v74, v0
	v_add_f32_e32 v0, v75, v0
	v_mov_b32_e32 v1, v0
	s_nop 1
	v_permlane16_swap_b32_e32 v0, v1
	v_add_f32_e32 v0, v0, v1
	v_mov_b32_e32 v1, v0
	s_nop 1
	v_permlane32_swap_b32_e32 v0, v1
	s_and_saveexec_b64 s[22:23], s[4:5]
	v_add_f32_e32 v0, v0, v1
	ds_write_b32 v211, v0 offset:768
	s_or_b64 exec, exec, s[22:23]
	ds_read_b128 v[0:3], v215
	v_mov_b32_e32 v4, v81
	s_waitcnt lgkmcnt(0)
; #define PG8_LAS __attribute__((address_space(3)))
;     __device__ __forceinline__ void operator()(f32x4 (&acc)[2][2][4][2], const Unit& u, int wr, int wc, int fr, int fq) const {
;     ...
;             for (int m = 0; m < 4; ++m) { const f32x4 q = *(const PG8_LAS f32x4*)(smax + (ai * HALF + wr * 64 + m * 16 + fr) * 4);
;                 const float mm = fmaxf(fmaxf(q[0], q[1]), fmaxf(q[2], q[3])) * SC; float s = 0.f;
; #pragma unroll
;                 for (int bj = 0; bj < 2; ++bj)
; #pragma unroll
;                     for (int n = 0; n < 2; ++n)
; #pragma unroll
;                         for (int e = 0; e < 4; ++e) { const float p = __builtin_amdgcn_exp2f(acc[ai][bj][m][n][e] * SC - mm); acc[ai][bj][m][n][e] = p; s += p; }
;                 s = rows_sum4(s);
;                 if (fq == 0) ssum[(ai * HALF + wr * 64 + m * 16 + fr) * 4 + wc] = s; }
	v_max_f32_e32 v3, v3, v3
	v_max_f32_e32 v2, v2, v2
	v_max_f32_e32 v2, v2, v3
	v_max3_f32 v5, v0, v1, v2
	v_pk_mul_f32 v[0:1], v[4:5], s[70:71] op_sel_hi:[1,0]
	s_nop 0
	v_fma_f32 v2, v60, s70, -v1
	v_fma_f32 v3, v61, s70, -v1
	v_exp_f32_e32 v58, v2
	v_exp_f32_e32 v59, v3
	v_fma_f32 v2, v72, s70, -v1
	v_exp_f32_e32 v60, v2
	v_fma_f32 v2, v73, s70, -v1
	v_exp_f32_e32 v61, v2
	v_fma_f32 v3, v66, s70, -v1
	v_add_f32_e32 v2, 0, v58
	v_exp_f32_e32 v66, v3
	v_fma_f32 v3, v67, s70, -v1
	v_add_f32_e32 v2, v59, v2
	v_exp_f32_e32 v67, v3
	v_fma_f32 v3, v70, s70, -v1
	v_add_f32_e32 v2, v60, v2
	v_exp_f32_e32 v72, v3
	v_fma_f32 v3, v71, s70, -v1
	v_add_f32_e32 v2, v61, v2
	v_exp_f32_e32 v73, v3
	v_fma_f32 v3, v162, s70, -v1
	v_add_f32_e32 v2, v66, v2
	v_exp_f32_e32 v70, v3
	v_fma_f32 v3, v163, s70, -v1
	v_add_f32_e32 v2, v67, v2
	v_exp_f32_e32 v71, v3
	v_fma_f32 v3, v76, s70, -v1
	v_add_f32_e32 v2, v72, v2
	v_exp_f32_e32 v76, v3
	v_fma_f32 v3, v77, s70, -v1
	v_add_f32_e32 v2, v73, v2
	v_exp_f32_e32 v77, v3
	v_fma_f32 v3, v78, s70, -v1
	v_add_f32_e32 v2, v70, v2
	v_exp_f32_e32 v78, v3
	v_fma_f32 v3, v79, s70, -v1
	v_add_f32_e32 v2, v71, v2
	v_exp_f32_e32 v79, v3
	v_fma_f32 v3, v80, s70, -v1
	v_add_f32_e32 v2, v76, v2
	v_exp_f32_e32 v80, v3
	v_sub_f32_e32 v0, v0, v1
	v_add_f32_e32 v2, v77, v2
	v_exp_f32_e32 v81, v0
	v_add_f32_e32 v0, v78, v2
	v_add_f32_e32 v0, v79, v0
	v_add_f32_e32 v0, v80, v0
	v_add_f32_e32 v0, v81, v0
	v_mov_b32_e32 v1, v0
	s_nop 1
	v_permlane16_swap_b32_e32 v0, v1
	v_add_f32_e32 v0, v0, v1
	v_mov_b32_e32 v1, v0
	s_nop 1
	v_permlane32_swap_b32_e32 v0, v1
	s_and_saveexec_b64 s[22:23], s[4:5]
	v_add_f32_e32 v0, v0, v1
	ds_write_b32 v211, v0 offset:2048
	s_or_b64 exec, exec, s[22:23]
	ds_read_b128 v[0:3], v216
	v_mov_b32_e32 v4, v43
	s_waitcnt lgkmcnt(0)
	v_max_f32_e32 v3, v3, v3
	v_max_f32_e32 v2, v2, v2
	v_max_f32_e32 v2, v2, v3
	v_max3_f32 v5, v0, v1, v2
	v_pk_mul_f32 v[0:1], v[4:5], s[70:71] op_sel_hi:[1,0]
	s_nop 0
	v_fma_f32 v2, v160, s70, -v1
	v_fma_f32 v3, v161, s70, -v1
	v_exp_f32_e32 v18, v2
	v_exp_f32_e32 v19, v3
	v_fma_f32 v2, v158, s70, -v1
	v_exp_f32_e32 v26, v2
	v_fma_f32 v2, v159, s70, -v1
	v_exp_f32_e32 v27, v2
	v_fma_f32 v3, v156, s70, -v1
	v_add_f32_e32 v2, 0, v18
	v_exp_f32_e32 v24, v3
	v_fma_f32 v3, v157, s70, -v1
	v_add_f32_e32 v2, v19, v2
	v_exp_f32_e32 v25, v3
	v_fma_f32 v3, v152, s70, -v1
	v_add_f32_e32 v2, v26, v2
	v_exp_f32_e32 v36, v3
	v_fma_f32 v3, v153, s70, -v1
	v_add_f32_e32 v2, v27, v2
	v_exp_f32_e32 v37, v3
	v_fma_f32 v3, v154, s70, -v1
	v_add_f32_e32 v2, v24, v2
	v_exp_f32_e32 v20, v3
	v_fma_f32 v3, v155, s70, -v1
	v_add_f32_e32 v2, v25, v2
	v_exp_f32_e32 v21, v3
	v_fma_f32 v3, v150, s70, -v1
	v_add_f32_e32 v2, v36, v2
	v_exp_f32_e32 v30, v3
	v_fma_f32 v3, v151, s70, -v1
	v_add_f32_e32 v2, v37, v2
	v_exp_f32_e32 v31, v3
	v_fma_f32 v3, v34, s70, -v1
	v_add_f32_e32 v2, v20, v2
	v_exp_f32_e32 v34, v3
	v_fma_f32 v3, v35, s70, -v1
	v_add_f32_e32 v2, v21, v2
	v_exp_f32_e32 v35, v3
	v_fma_f32 v3, v42, s70, -v1
	v_add_f32_e32 v2, v30, v2
	v_exp_f32_e32 v42, v3
	v_sub_f32_e32 v0, v0, v1
	v_add_f32_e32 v2, v31, v2
	v_exp_f32_e32 v43, v0
	v_add_f32_e32 v0, v34, v2
	v_add_f32_e32 v0, v35, v0
	v_add_f32_e32 v0, v42, v0
	v_add_f32_e32 v0, v43, v0
	v_mov_b32_e32 v1, v0
	s_nop 1
	v_permlane16_swap_b32_e32 v0, v1
	v_add_f32_e32 v0, v0, v1
	v_mov_b32_e32 v1, v0
	s_nop 1
	v_permlane32_swap_b32_e32 v0, v1
	s_and_saveexec_b64 s[22:23], s[4:5]
	v_add_f32_e32 v0, v0, v1
	ds_write_b32 v211, v0 offset:2304
	s_or_b64 exec, exec, s[22:23]
	ds_read_b128 v[0:3], v217
	v_mov_b32_e32 v4, v49
	s_waitcnt lgkmcnt(0)
	v_max_f32_e32 v3, v3, v3
	v_max_f32_e32 v2, v2, v2
	v_max_f32_e32 v2, v2, v3
	v_max3_f32 v5, v0, v1, v2
	v_pk_mul_f32 v[0:1], v[4:5], s[70:71] op_sel_hi:[1,0]
	s_nop 0
	v_fma_f32 v2, v28, s70, -v1
	v_fma_f32 v3, v29, s70, -v1
	v_exp_f32_e32 v22, v2
	v_exp_f32_e32 v23, v3
	v_fma_f32 v2, v40, s70, -v1
	v_exp_f32_e32 v28, v2
	v_fma_f32 v2, v41, s70, -v1
	v_exp_f32_e32 v29, v2
	v_fma_f32 v3, v32, s70, -v1
	v_add_f32_e32 v2, 0, v22
	v_exp_f32_e32 v32, v3
	v_fma_f32 v3, v33, s70, -v1
	v_add_f32_e32 v2, v23, v2
	v_exp_f32_e32 v33, v3
	v_fma_f32 v3, v38, s70, -v1
	v_add_f32_e32 v2, v28, v2
	v_exp_f32_e32 v40, v3
	v_fma_f32 v3, v39, s70, -v1
	v_add_f32_e32 v2, v29, v2
	v_exp_f32_e32 v41, v3
	v_fma_f32 v3, v148, s70, -v1
	v_add_f32_e32 v2, v32, v2
	v_exp_f32_e32 v38, v3
	v_fma_f32 v3, v149, s70, -v1
	v_add_f32_e32 v2, v33, v2
	v_exp_f32_e32 v39, v3
	v_fma_f32 v3, v44, s70, -v1
	v_add_f32_e32 v2, v40, v2
	v_exp_f32_e32 v44, v3
	v_fma_f32 v3, v45, s70, -v1
	v_add_f32_e32 v2, v41, v2
	v_exp_f32_e32 v45, v3
	v_fma_f32 v3, v46, s70, -v1
	v_add_f32_e32 v2, v38, v2
	v_exp_f32_e32 v46, v3
	v_fma_f32 v3, v47, s70, -v1
	v_add_f32_e32 v2, v39, v2
	v_exp_f32_e32 v47, v3
	v_fma_f32 v3, v48, s70, -v1
	v_add_f32_e32 v2, v44, v2
	v_exp_f32_e32 v48, v3
	v_sub_f32_e32 v0, v0, v1
	v_add_f32_e32 v2, v45, v2
	v_exp_f32_e32 v49, v0
	v_add_f32_e32 v0, v46, v2
	v_add_f32_e32 v0, v47, v0
	v_add_f32_e32 v0, v48, v0
	v_add_f32_e32 v0, v49, v0
	v_mov_b32_e32 v1, v0
	s_nop 1
	v_permlane16_swap_b32_e32 v0, v1
	v_add_f32_e32 v0, v0, v1
	v_mov_b32_e32 v1, v0
	s_nop 1
	v_permlane32_swap_b32_e32 v0, v1
	s_and_saveexec_b64 s[22:23], s[4:5]
	v_add_f32_e32 v0, v0, v1
	ds_write_b32 v211, v0 offset:2560
	s_or_b64 exec, exec, s[22:23]
	ds_read_b128 v[0:3], v218
	v_mov_b32_e32 v4, v15
	s_waitcnt lgkmcnt(0)
; #define PG8_LAS __attribute__((address_space(3)))
; __device__ __forceinline__ unsigned cvt_pk_bf16(float lo, float hi) { const f32x2c v = {lo, hi}; const bf16x2c b = __builtin_convertvector(v, bf16x2c); return __builtin_bit_cast(unsigned, b); }
;     __device__ __forceinline__ void operator()(f32x4 (&acc)[2][2][4][2], const Unit& u, int wr, int wc, int fr, int fq) const {
;     ...
;             for (int m = 0; m < 4; ++m) { const f32x4 q = *(const PG8_LAS f32x4*)(smax + (ai * HALF + wr * 64 + m * 16 + fr) * 4);
;                 const float mm = fmaxf(fmaxf(q[0], q[1]), fmaxf(q[2], q[3])) * SC; float s = 0.f;
; #pragma unroll
;                 for (int bj = 0; bj < 2; ++bj)
; #pragma unroll
;                     for (int n = 0; n < 2; ++n)
; #pragma unroll
;                         for (int e = 0; e < 4; ++e) { const float p = __builtin_amdgcn_exp2f(acc[ai][bj][m][n][e] * SC - mm); acc[ai][bj][m][n][e] = p; s += p; }
;                 s = rows_sum4(s);
;                 if (fq == 0) ssum[(ai * HALF + wr * 64 + m * 16 + fr) * 4 + wc] = s; }
;         asm volatile("s_waitcnt lgkmcnt(0)" ::: "memory"); __builtin_amdgcn_s_barrier(); asm volatile("" ::: "memory");
;         const int row0 = u.pm * BM + wr * 64 + fr, col0 = u.pn * 256 + wc * 32 + 8 * fq;
; #pragma unroll
;         for (int ai = 0; ai < 2; ++ai)
; #pragma unroll
;             for (int m = 0; m < 4; ++m) { const f32x4 q = *(const PG8_LAS f32x4*)(ssum + (ai * HALF + wr * 64 + m * 16 + fr) * 4);
;                 const float iv = 1.f / ((q[0] + q[1]) + (q[2] + q[3]));
;                 bf16* rowp = P + (size_t)(row0 + ai * HALF + m * 16) * D + col0;
; #pragma unroll
;                 for (int bj = 0; bj < 2; ++bj) { const f32x4 v0 = acc[ai][bj][m][0] * iv, v1 = acc[ai][bj][m][1] * iv; u32x4 w;
;                     w.x = cvt_pk_bf16(v0[0], v0[1]); w.y = cvt_pk_bf16(v0[2], v0[3]); w.z = cvt_pk_bf16(v1[0], v1[1]); w.w = cvt_pk_bf16(v1[2], v1[3]);
;                     *(u32x4*)(rowp + bj * HALF) = w; } }
	v_max_f32_e32 v3, v3, v3
	v_max_f32_e32 v2, v2, v2
	v_max_f32_e32 v2, v2, v3
	v_max3_f32 v5, v0, v1, v2
	v_pk_mul_f32 v[148:149], v[4:5], s[70:71] op_sel_hi:[1,0]
	s_nop 0
	v_fma_f32 v0, v146, s70, -v149
	v_fma_f32 v1, v147, s70, -v149
	v_exp_f32_e32 v0, v0
	v_exp_f32_e32 v1, v1
	v_fma_f32 v2, v116, s70, -v149
	v_exp_f32_e32 v6, v2
	v_fma_f32 v2, v117, s70, -v149
	v_exp_f32_e32 v7, v2
	v_fma_f32 v3, v114, s70, -v149
	v_add_f32_e32 v2, 0, v0
	v_exp_f32_e32 v4, v3
	v_fma_f32 v3, v115, s70, -v149
	v_add_f32_e32 v2, v1, v2
	v_exp_f32_e32 v5, v3
	v_fma_f32 v3, v12, s70, -v149
	v_add_f32_e32 v2, v6, v2
	v_exp_f32_e32 v12, v3
	v_fma_f32 v3, v13, s70, -v149
	v_add_f32_e32 v2, v7, v2
	v_exp_f32_e32 v13, v3
	v_add_f32_e32 v2, v4, v2
	v_add_f32_e32 v2, v5, v2
	v_add_f32_e32 v2, v12, v2
	v_add_f32_e32 v15, v13, v2
	v_fma_f32 v2, v16, s70, -v149
	v_exp_f32_e32 v2, v2
	v_fma_f32 v3, v17, s70, -v149
	v_exp_f32_e32 v3, v3
	v_fma_f32 v10, v10, s70, -v149
	v_exp_f32_e32 v10, v10
	v_fma_f32 v11, v11, s70, -v149
	v_exp_f32_e32 v11, v11
	v_add_f32_e32 v15, v2, v15
	v_fma_f32 v8, v8, s70, -v149
	v_add_f32_e32 v15, v3, v15
	v_exp_f32_e32 v8, v8
	v_fma_f32 v9, v9, s70, -v149
	v_add_f32_e32 v15, v10, v15
	v_exp_f32_e32 v9, v9
	v_fma_f32 v14, v14, s70, -v149
	v_add_f32_e32 v16, v11, v15
	v_exp_f32_e32 v14, v14
	v_sub_f32_e32 v15, v148, v149
	v_exp_f32_e32 v15, v15
	v_add_f32_e32 v16, v8, v16
	v_add_f32_e32 v16, v9, v16
	v_add_f32_e32 v16, v14, v16
	v_add_f32_e32 v16, v15, v16
	v_mov_b32_e32 v17, v16
	s_nop 1
	v_permlane16_swap_b32_e32 v16, v17
	v_add_f32_e32 v16, v16, v17
	v_mov_b32_e32 v17, v16
	s_nop 1
	v_permlane32_swap_b32_e32 v16, v17
	s_and_saveexec_b64 s[22:23], s[4:5]
	v_add_f32_e32 v16, v16, v17
	ds_write_b32 v211, v16 offset:2816
	s_or_b64 exec, exec, s[22:23]
	s_waitcnt lgkmcnt(0)
	s_barrier
	ds_read_b128 v[146:149], v220
	v_lshl_add_u32 v114, s20, 8, v198
	v_lshl_or_b32 v16, s21, 8, v200
	v_ashrrev_i32_e32 v17, 31, v16
	s_cmp_eq_u32 s44, 3
	s_waitcnt lgkmcnt(0)
	v_mov_b32_e32 v116, v147
	v_mov_b32_e32 v117, v148
	v_mov_b32_e32 v147, v149
	v_pk_add_f32 v[116:117], v[116:117], v[146:147]
	s_nop 0
	v_add_f32_e32 v115, v116, v117
	v_rcp_f32_e32 v117, v115
	s_nop 0
	v_fma_f32 v146, -v115, v117, 1.0
	v_fmac_f32_e32 v117, v146, v117
	v_div_fixup_f32 v146, v117, v115, 1.0
	v_ashrrev_i32_e32 v115, 31, v114
	v_lshlrev_b64 v[116:117], 11, v[114:115]
	v_lshl_add_u64 v[148:149], s[30:31], 0, v[116:117]
	v_lshlrev_b64 v[116:117], 1, v[16:17]
	v_pk_mul_f32 v[120:121], v[120:121], v[146:147] op_sel_hi:[1,0]
	v_pk_mul_f32 v[118:119], v[118:119], v[146:147] op_sel_hi:[1,0]
	v_pk_mul_f32 v[124:125], v[124:125], v[146:147] op_sel_hi:[1,0]
	v_pk_mul_f32 v[122:123], v[122:123], v[146:147] op_sel_hi:[1,0]
	v_lshl_add_u64 v[16:17], v[148:149], 0, v[116:117]
	v_cvt_pk_bf16_f32 v118, v118, v119
	v_cvt_pk_bf16_f32 v119, v120, v121
	v_cvt_pk_bf16_f32 v120, v122, v123
	v_cvt_pk_bf16_f32 v121, v124, v125
	global_store_dwordx4 v[16:17], v[118:121], off
	v_pk_mul_f32 v[122:123], v[144:145], v[146:147] op_sel_hi:[1,0]
	v_pk_mul_f32 v[124:125], v[142:143], v[146:147] op_sel_hi:[1,0]
	v_pk_mul_f32 v[120:121], v[140:141], v[146:147] op_sel_hi:[1,0]
	v_pk_mul_f32 v[118:119], v[126:127], v[146:147] op_sel_hi:[1,0]
	s_nop 0
	v_cvt_pk_bf16_f32 v118, v118, v119
	v_cvt_pk_bf16_f32 v119, v120, v121
	v_cvt_pk_bf16_f32 v120, v124, v125
	v_cvt_pk_bf16_f32 v121, v122, v123
	global_store_dwordx4 v[16:17], v[118:121], off offset:256
	ds_read_b128 v[118:121], v220 offset:256
	s_waitcnt lgkmcnt(0)
	v_mov_b32_e32 v122, v119
	v_mov_b32_e32 v123, v120
	v_mov_b32_e32 v119, v121
	v_pk_add_f32 v[118:119], v[122:123], v[118:119]
	s_nop 0
	v_add_f32_e32 v115, v118, v119
	v_div_scale_f32 v118, s[20:21], v115, v115, 1.0
	v_rcp_f32_e32 v119, v118
	s_nop 0
	v_fma_f32 v120, -v118, v119, 1.0
	v_fmac_f32_e32 v119, v120, v119
	v_div_scale_f32 v120, vcc, 1.0, v115, 1.0
	v_mul_f32_e32 v121, v120, v119
	v_fma_f32 v122, -v118, v121, v120
	v_fmac_f32_e32 v121, v122, v119
	v_fma_f32 v118, -v118, v121, v120
	v_or_b32_e32 v120, 16, v114
	v_div_fmas_f32 v118, v118, v119, v121
	v_ashrrev_i32_e32 v121, 31, v120
	v_div_fixup_f32 v118, v118, v115, 1.0
	v_lshlrev_b64 v[120:121], 11, v[120:121]
	v_lshl_add_u64 v[120:121], s[30:31], 0, v[120:121]
	v_pk_mul_f32 v[90:91], v[90:91], v[118:119] op_sel_hi:[1,0]
	v_pk_mul_f32 v[82:83], v[82:83], v[118:119] op_sel_hi:[1,0]
	v_pk_mul_f32 v[98:99], v[98:99], v[118:119] op_sel_hi:[1,0]
	v_pk_mul_f32 v[122:123], v[88:89], v[118:119] op_sel_hi:[1,0]
	v_lshl_add_u64 v[120:121], v[120:121], 0, v[116:117]
	v_cvt_pk_bf16_f32 v88, v82, v83
	v_cvt_pk_bf16_f32 v89, v90, v91
	v_cvt_pk_bf16_f32 v90, v122, v123
	v_cvt_pk_bf16_f32 v91, v98, v99
	global_store_dwordx4 v[120:121], v[88:91], off
	v_pk_mul_f32 v[82:83], v[96:97], v[118:119] op_sel_hi:[1,0]
	v_pk_mul_f32 v[86:87], v[86:87], v[118:119] op_sel_hi:[1,0]
	v_pk_mul_f32 v[90:91], v[106:107], v[118:119] op_sel_hi:[1,0]
	v_pk_mul_f32 v[88:89], v[100:101], v[118:119] op_sel_hi:[1,0]
	v_cvt_pk_bf16_f32 v86, v86, v87
	v_cvt_pk_bf16_f32 v87, v82, v83
	v_cvt_pk_bf16_f32 v88, v88, v89
	v_cvt_pk_bf16_f32 v89, v90, v91
	global_store_dwordx4 v[120:121], v[86:89], off offset:256
	ds_read_b128 v[86:89], v220 offset:512
	s_waitcnt lgkmcnt(0)
; #define PG8_LAS __attribute__((address_space(3)))
; __device__ __forceinline__ unsigned cvt_pk_bf16(float lo, float hi) { const f32x2c v = {lo, hi}; const bf16x2c b = __builtin_convertvector(v, bf16x2c); return __builtin_bit_cast(unsigned, b); }
;     __device__ __forceinline__ void operator()(f32x4 (&acc)[2][2][4][2], const Unit& u, int wr, int wc, int fr, int fq) const {
;     ...
;         for (int ai = 0; ai < 2; ++ai)
; #pragma unroll
;             for (int m = 0; m < 4; ++m) { const f32x4 q = *(const PG8_LAS f32x4*)(ssum + (ai * HALF + wr * 64 + m * 16 + fr) * 4);
;                 const float iv = 1.f / ((q[0] + q[1]) + (q[2] + q[3]));
;                 bf16* rowp = P + (size_t)(row0 + ai * HALF + m * 16) * D + col0;
; #pragma unroll
;                 for (int bj = 0; bj < 2; ++bj) { const f32x4 v0 = acc[ai][bj][m][0] * iv, v1 = acc[ai][bj][m][1] * iv; u32x4 w;
;                     w.x = cvt_pk_bf16(v0[0], v0[1]); w.y = cvt_pk_bf16(v0[2], v0[3]); w.z = cvt_pk_bf16(v1[0], v1[1]); w.w = cvt_pk_bf16(v1[2], v1[3]);
;                     *(u32x4*)(rowp + bj * HALF) = w; } }
	v_mov_b32_e32 v82, v87
	v_mov_b32_e32 v83, v88
	v_mov_b32_e32 v87, v89
	v_pk_add_f32 v[82:83], v[82:83], v[86:87]
	s_nop 0
	v_add_f32_e32 v82, v82, v83
	v_rcp_f32_e32 v86, v82
	s_nop 0
	v_fma_f32 v87, -v82, v86, 1.0
	v_fmac_f32_e32 v86, v87, v86
	v_div_fixup_f32 v86, v86, v82, 1.0
	v_or_b32_e32 v82, 32, v114
	v_ashrrev_i32_e32 v83, 31, v82
	v_lshlrev_b64 v[82:83], 11, v[82:83]
	v_lshl_add_u64 v[82:83], s[30:31], 0, v[82:83]
	v_lshl_add_u64 v[88:89], v[82:83], 0, v[116:117]
	v_pk_mul_f32 v[90:91], v[92:93], v[86:87] op_sel_hi:[1,0]
	v_pk_mul_f32 v[82:83], v[84:85], v[86:87] op_sel_hi:[1,0]
	v_pk_mul_f32 v[92:93], v[102:103], v[86:87] op_sel_hi:[1,0]
	v_pk_mul_f32 v[84:85], v[94:95], v[86:87] op_sel_hi:[1,0]
	v_cvt_pk_bf16_f32 v82, v82, v83
	v_cvt_pk_bf16_f32 v83, v90, v91
	v_cvt_pk_bf16_f32 v84, v84, v85
	v_cvt_pk_bf16_f32 v85, v92, v93
	global_store_dwordx4 v[88:89], v[82:85], off
	v_pk_mul_f32 v[90:91], v[112:113], v[86:87] op_sel_hi:[1,0]
	s_nop 0
	v_pk_mul_f32 v[84:85], v[108:109], v[86:87] op_sel_hi:[1,0]
	v_pk_mul_f32 v[82:83], v[104:105], v[86:87] op_sel_hi:[1,0]
	v_pk_mul_f32 v[86:87], v[110:111], v[86:87] op_sel_hi:[1,0]
	v_cvt_pk_bf16_f32 v82, v82, v83
	v_cvt_pk_bf16_f32 v83, v84, v85
	v_cvt_pk_bf16_f32 v84, v86, v87
	v_cvt_pk_bf16_f32 v85, v90, v91
	global_store_dwordx4 v[88:89], v[82:85], off offset:256
	ds_read_b128 v[82:85], v220 offset:768
	s_waitcnt lgkmcnt(0)
	v_mov_b32_e32 v86, v83
	v_mov_b32_e32 v87, v84
	v_mov_b32_e32 v83, v85
	v_pk_add_f32 v[82:83], v[86:87], v[82:83]
	s_nop 0
	v_add_f32_e32 v82, v82, v83
	v_div_scale_f32 v83, s[20:21], v82, v82, 1.0
	v_rcp_f32_e32 v84, v83
	s_nop 0
	v_fma_f32 v85, -v83, v84, 1.0
	v_fmac_f32_e32 v84, v85, v84
	v_div_scale_f32 v85, vcc, 1.0, v82, 1.0
	v_mul_f32_e32 v86, v85, v84
	v_fma_f32 v87, -v83, v86, v85
	v_fmac_f32_e32 v86, v87, v84
	v_fma_f32 v83, -v83, v86, v85
	v_div_fmas_f32 v83, v83, v84, v86
	v_or_b32_e32 v84, 48, v114
	v_ashrrev_i32_e32 v85, 31, v84
	v_div_fixup_f32 v82, v83, v82, 1.0
	v_lshlrev_b64 v[84:85], 11, v[84:85]
	v_lshl_add_u64 v[84:85], s[30:31], 0, v[84:85]
	v_pk_mul_f32 v[56:57], v[56:57], v[82:83] op_sel_hi:[1,0]
	v_pk_mul_f32 v[50:51], v[50:51], v[82:83] op_sel_hi:[1,0]
	v_pk_mul_f32 v[64:65], v[64:65], v[82:83] op_sel_hi:[1,0]
	v_pk_mul_f32 v[86:87], v[54:55], v[82:83] op_sel_hi:[1,0]
	v_lshl_add_u64 v[84:85], v[84:85], 0, v[116:117]
	v_cvt_pk_bf16_f32 v54, v50, v51
	v_cvt_pk_bf16_f32 v55, v56, v57
	v_cvt_pk_bf16_f32 v56, v86, v87
	v_cvt_pk_bf16_f32 v57, v64, v65
	global_store_dwordx4 v[84:85], v[54:57], off
	v_pk_mul_f32 v[50:51], v[52:53], v[82:83] op_sel_hi:[1,0]
	v_pk_mul_f32 v[52:53], v[68:69], v[82:83] op_sel_hi:[1,0]
	v_pk_mul_f32 v[54:55], v[62:63], v[82:83] op_sel_hi:[1,0]
	v_pk_mul_f32 v[56:57], v[74:75], v[82:83] op_sel_hi:[1,0]
	v_cvt_pk_bf16_f32 v50, v50, v51
	v_cvt_pk_bf16_f32 v51, v54, v55
	v_cvt_pk_bf16_f32 v52, v52, v53
	v_cvt_pk_bf16_f32 v53, v56, v57
	global_store_dwordx4 v[84:85], v[50:53], off offset:256
	ds_read_b128 v[50:53], v220 offset:2048
	v_lshl_add_u64 v[56:57], v[16:17], 0, s[58:59]
	s_waitcnt lgkmcnt(0)
	v_mov_b32_e32 v54, v51
	v_mov_b32_e32 v55, v52
	v_mov_b32_e32 v51, v53
	v_pk_add_f32 v[50:51], v[54:55], v[50:51]
	s_nop 0
	v_add_f32_e32 v50, v50, v51
	v_rcp_f32_e32 v52, v50
	s_nop 0
	v_fma_f32 v53, -v50, v52, 1.0
	v_fmac_f32_e32 v52, v53, v52
	v_div_fixup_f32 v54, v52, v50, 1.0
	v_pk_mul_f32 v[52:53], v[60:61], v[54:55] op_sel_hi:[1,0]
	v_pk_mul_f32 v[50:51], v[58:59], v[54:55] op_sel_hi:[1,0]
	v_pk_mul_f32 v[58:59], v[72:73], v[54:55] op_sel_hi:[1,0]
	v_pk_mul_f32 v[60:61], v[66:67], v[54:55] op_sel_hi:[1,0]
	v_cvt_pk_bf16_f32 v50, v50, v51
	v_cvt_pk_bf16_f32 v51, v52, v53
	v_cvt_pk_bf16_f32 v53, v58, v59
	v_add_co_u32_e32 v58, vcc, s35, v16
	v_cvt_pk_bf16_f32 v52, v60, v61
	s_nop 0
	v_addc_co_u32_e32 v59, vcc, 0, v17, vcc
	global_store_dwordx4 v[58:59], v[50:53], off
	v_pk_mul_f32 v[58:59], v[80:81], v[54:55] op_sel_hi:[1,0]
	s_nop 0
	v_pk_mul_f32 v[52:53], v[76:77], v[54:55] op_sel_hi:[1,0]
	v_pk_mul_f32 v[50:51], v[70:71], v[54:55] op_sel_hi:[1,0]
	v_pk_mul_f32 v[54:55], v[78:79], v[54:55] op_sel_hi:[1,0]
	v_cvt_pk_bf16_f32 v50, v50, v51
	v_cvt_pk_bf16_f32 v51, v52, v53
	v_cvt_pk_bf16_f32 v52, v54, v55
	v_cvt_pk_bf16_f32 v53, v58, v59
	global_store_dwordx4 v[56:57], v[50:53], off offset:256
	ds_read_b128 v[50:53], v220 offset:2304
	s_waitcnt lgkmcnt(0)
; #define PG8_LAS __attribute__((address_space(3)))
; __device__ __forceinline__ unsigned cvt_pk_bf16(float lo, float hi) { const f32x2c v = {lo, hi}; const bf16x2c b = __builtin_convertvector(v, bf16x2c); return __builtin_bit_cast(unsigned, b); }
;     __device__ __forceinline__ void operator()(f32x4 (&acc)[2][2][4][2], const Unit& u, int wr, int wc, int fr, int fq) const {
;     ...
;         for (int ai = 0; ai < 2; ++ai)
; #pragma unroll
;             for (int m = 0; m < 4; ++m) { const f32x4 q = *(const PG8_LAS f32x4*)(ssum + (ai * HALF + wr * 64 + m * 16 + fr) * 4);
;                 const float iv = 1.f / ((q[0] + q[1]) + (q[2] + q[3]));
;                 bf16* rowp = P + (size_t)(row0 + ai * HALF + m * 16) * D + col0;
; #pragma unroll
;                 for (int bj = 0; bj < 2; ++bj) { const f32x4 v0 = acc[ai][bj][m][0] * iv, v1 = acc[ai][bj][m][1] * iv; u32x4 w;
;                     w.x = cvt_pk_bf16(v0[0], v0[1]); w.y = cvt_pk_bf16(v0[2], v0[3]); w.z = cvt_pk_bf16(v1[0], v1[1]); w.w = cvt_pk_bf16(v1[2], v1[3]);
;                     *(u32x4*)(rowp + bj * HALF) = w; } }
	v_mov_b32_e32 v54, v51
	v_mov_b32_e32 v55, v52
	v_mov_b32_e32 v51, v53
	v_pk_add_f32 v[50:51], v[54:55], v[50:51]
	s_nop 0
	v_add_f32_e32 v50, v50, v51
	v_rcp_f32_e32 v52, v50
	s_nop 0
	v_fma_f32 v53, -v50, v52, 1.0
	v_fmac_f32_e32 v52, v53, v52
	v_div_fixup_f32 v50, v52, v50, 1.0
	v_pk_mul_f32 v[18:19], v[18:19], v[50:51] op_sel_hi:[1,0]
	v_pk_mul_f32 v[26:27], v[26:27], v[50:51] op_sel_hi:[1,0]
	v_pk_mul_f32 v[36:37], v[36:37], v[50:51] op_sel_hi:[1,0]
	v_pk_mul_f32 v[54:55], v[24:25], v[50:51] op_sel_hi:[1,0]
	v_cvt_pk_bf16_f32 v24, v18, v19
	v_add_co_u32_e32 v18, vcc, s87, v16
	v_cvt_pk_bf16_f32 v25, v26, v27
	v_cvt_pk_bf16_f32 v26, v54, v55
	v_cvt_pk_bf16_f32 v27, v36, v37
	v_addc_co_u32_e32 v19, vcc, 0, v17, vcc
	global_store_dwordx4 v[18:19], v[24:27], off
	v_pk_mul_f32 v[18:19], v[20:21], v[50:51] op_sel_hi:[1,0]
	v_pk_mul_f32 v[20:21], v[34:35], v[50:51] op_sel_hi:[1,0]
	v_pk_mul_f32 v[24:25], v[30:31], v[50:51] op_sel_hi:[1,0]
	v_pk_mul_f32 v[26:27], v[42:43], v[50:51] op_sel_hi:[1,0]
	v_lshl_add_u64 v[52:53], v[16:17], 0, s[72:73]
	v_cvt_pk_bf16_f32 v18, v18, v19
	v_cvt_pk_bf16_f32 v19, v24, v25
	v_cvt_pk_bf16_f32 v20, v20, v21
	v_cvt_pk_bf16_f32 v21, v26, v27
	global_store_dwordx4 v[52:53], v[18:21], off offset:256
	ds_read_b128 v[18:21], v220 offset:2560
	v_lshl_add_u64 v[26:27], v[16:17], 0, s[74:75]
	s_waitcnt lgkmcnt(0)
	v_mov_b32_e32 v24, v19
	v_mov_b32_e32 v25, v20
	v_mov_b32_e32 v19, v21
	v_pk_add_f32 v[18:19], v[24:25], v[18:19]
	s_nop 0
	v_add_f32_e32 v18, v18, v19
	v_rcp_f32_e32 v20, v18
	s_nop 0
	v_fma_f32 v21, -v18, v20, 1.0
	v_fmac_f32_e32 v20, v21, v20
	v_div_fixup_f32 v24, v20, v18, 1.0
	v_pk_mul_f32 v[20:21], v[28:29], v[24:25] op_sel_hi:[1,0]
	v_pk_mul_f32 v[18:19], v[22:23], v[24:25] op_sel_hi:[1,0]
	v_pk_mul_f32 v[22:23], v[40:41], v[24:25] op_sel_hi:[1,0]
	v_pk_mul_f32 v[28:29], v[32:33], v[24:25] op_sel_hi:[1,0]
	v_cvt_pk_bf16_f32 v18, v18, v19
	v_cvt_pk_bf16_f32 v19, v20, v21
	v_cvt_pk_bf16_f32 v21, v22, v23
	v_add_co_u32_e32 v22, vcc, s85, v16
	v_cvt_pk_bf16_f32 v20, v28, v29
	s_nop 0
	v_addc_co_u32_e32 v23, vcc, 0, v17, vcc
	global_store_dwordx4 v[22:23], v[18:21], off
	v_pk_mul_f32 v[22:23], v[48:49], v[24:25] op_sel_hi:[1,0]
	s_nop 0
	v_pk_mul_f32 v[20:21], v[44:45], v[24:25] op_sel_hi:[1,0]
	v_pk_mul_f32 v[18:19], v[38:39], v[24:25] op_sel_hi:[1,0]
	v_pk_mul_f32 v[24:25], v[46:47], v[24:25] op_sel_hi:[1,0]
	v_cvt_pk_bf16_f32 v18, v18, v19
	v_cvt_pk_bf16_f32 v19, v20, v21
	v_cvt_pk_bf16_f32 v20, v24, v25
	v_cvt_pk_bf16_f32 v21, v22, v23
	global_store_dwordx4 v[26:27], v[18:21], off offset:256
	ds_read_b128 v[18:21], v220 offset:2816
	s_waitcnt lgkmcnt(0)
	v_mov_b32_e32 v22, v19
	v_mov_b32_e32 v23, v20
	v_mov_b32_e32 v19, v21
	v_pk_add_f32 v[18:19], v[22:23], v[18:19]
	s_nop 0
	v_add_f32_e32 v18, v18, v19
	v_rcp_f32_e32 v20, v18
	s_mov_b64 s[20:21], -1
	v_fma_f32 v21, -v18, v20, 1.0
	v_fmac_f32_e32 v20, v21, v20
	v_div_fixup_f32 v18, v20, v18, 1.0
	v_pk_mul_f32 v[0:1], v[0:1], v[18:19] op_sel_hi:[1,0]
	v_pk_mul_f32 v[6:7], v[6:7], v[18:19] op_sel_hi:[1,0]
	v_pk_mul_f32 v[12:13], v[12:13], v[18:19] op_sel_hi:[1,0]
	v_pk_mul_f32 v[22:23], v[4:5], v[18:19] op_sel_hi:[1,0]
	v_cvt_pk_bf16_f32 v4, v0, v1
	v_add_co_u32_e32 v0, vcc, s65, v16
	v_cvt_pk_bf16_f32 v5, v6, v7
	v_cvt_pk_bf16_f32 v6, v22, v23
	v_cvt_pk_bf16_f32 v7, v12, v13
	v_addc_co_u32_e32 v1, vcc, 0, v17, vcc
	global_store_dwordx4 v[0:1], v[4:7], off
	v_pk_mul_f32 v[0:1], v[2:3], v[18:19] op_sel_hi:[1,0]
	v_pk_mul_f32 v[2:3], v[8:9], v[18:19] op_sel_hi:[1,0]
	v_pk_mul_f32 v[4:5], v[10:11], v[18:19] op_sel_hi:[1,0]
	v_pk_mul_f32 v[6:7], v[14:15], v[18:19] op_sel_hi:[1,0]
	v_lshl_add_u64 v[20:21], v[16:17], 0, s[76:77]
	v_cvt_pk_bf16_f32 v0, v0, v1
	v_cvt_pk_bf16_f32 v1, v4, v5
	v_cvt_pk_bf16_f32 v2, v2, v3
	v_cvt_pk_bf16_f32 v3, v6, v7
	global_store_dwordx4 v[20:21], v[0:3], off offset:256
	s_cbranch_scc1 .LBB0_2066
	s_andn2_b64 vcc, exec, s[8:9]
	s_cbranch_vccnz .LBB0_2065
	s_barrier
	s_branch .LBB0_2065

; __device__ __forceinline__ void router_ph(const int WID_, const bf16* __restrict__ x3, const float* __restrict__ nw, const float* __restrict__ wrg, const float* __restrict__ brg, ...
;     ...
;     for (int m = tile * 256 + wv; m < tile * 256 + 256; m += 8) {
;         float h[16]; float s = 0.f;
; #pragma unroll
;         for (int j = 0; j < 2; ++j) { const unsigned wd[4] = {nx[j].x, nx[j].y, nx[j].z, nx[j].w};
; #pragma unroll
;             for (int q = 0; q < 4; ++q) { const float lo = __builtin_bit_cast(float, wd[q] << 16), hi = __builtin_bit_cast(float, wd[q] & 0xffff0000u); h[8 * j + 2 * q] = lo; h[8 * j + 2 * q + 1] = hi; s += lo * lo + hi * hi; } }
;         { const int mn = min(m + 8, tile * 256 + 248 + wv); const uint4* xr = (const uint4*)(x3 + (size_t)mn * D);
; #pragma unroll
;           for (int j = 0; j < 2; ++j) nx[j] = xr[lane + 64 * j]; }
;         s = wave_sum(s);
;         const float rs = rsqrtf(s * (1.f / D) + 1e-6f);
;         float l1[4] = {0.f, 0.f, 0.f, 0.f};
; #pragma unroll
;         for (int j = 0; j < 2; ++j) {
;             const int k0 = (lane + 64 * j) * 8;
;             const float4 ga = gw[2 * j], gb = gw[2 * j + 1];
;             h[8 * j] *= rs * ga.x; h[8 * j + 1] *= rs * ga.y; h[8 * j + 2] *= rs * ga.z; h[8 * j + 3] *= rs * ga.w;
;             h[8 * j + 4] *= rs * gb.x; h[8 * j + 5] *= rs * gb.y; h[8 * j + 6] *= rs * gb.z; h[8 * j + 7] *= rs * gb.w;
; #pragma unroll
;             for (int e = 0; e < 8; ++e) { const h4 w = *(const h4*)(wg16 + (k0 + e) * 4); const float x = h[8 * j + e];
;                 l1[0] += x * (float)w[0]; l1[1] += x * (float)w[1]; l1[2] += x * (float)w[2]; l1[3] += x * (float)w[3]; }
;         }
; #pragma unroll
;         for (int i = 0; i < 4; ++i) l1[i] = wave_sum(l1[i]) + brg_l[i];
.LBB0_2145:
	v_and_b32_e32 v90, 0xffff0000, v16
	v_and_b32_e32 v92, 0xffff0000, v17
	v_lshlrev_b32_e32 v59, 16, v16
	v_mul_f32_e32 v14, v90, v90
	v_lshlrev_b32_e32 v91, 16, v17
	v_mul_f32_e32 v16, v92, v92
	v_fmac_f32_e32 v14, v59, v59
	v_fmac_f32_e32 v16, v91, v91
	v_and_b32_e32 v94, 0xffff0000, v18
	v_add_f32_e32 v14, v16, v14
	v_lshlrev_b32_e32 v93, 16, v18
	v_mul_f32_e32 v16, v94, v94
	v_fmac_f32_e32 v16, v93, v93
	v_and_b32_e32 v96, 0xffff0000, v19
	v_add_f32_e32 v14, v16, v14
	v_lshlrev_b32_e32 v95, 16, v19
	v_mul_f32_e32 v16, v96, v96
	v_and_b32_e32 v85, 0xffff0000, v13
	v_and_b32_e32 v84, 0xffff0000, v12
	v_fmac_f32_e32 v16, v95, v95
	v_lshlrev_b32_e32 v27, 16, v13
	v_lshlrev_b32_e32 v26, 16, v12
	v_pk_mul_f32 v[12:13], v[84:85], v[84:85]
	v_add_f32_e32 v14, v16, v14
	v_pk_fma_f32 v[16:17], v[26:27], v[26:27], v[12:13]
	v_and_b32_e32 v86, 0xffff0000, v2
	v_add_f32_e32 v14, v16, v14
	v_add_f32_e32 v88, v17, v14
	v_and_b32_e32 v14, 0xffff0000, v15
	v_lshlrev_b32_e32 v15, 16, v15
	v_lshlrev_b32_e32 v87, 16, v2
	v_mov_b32_e32 v82, v14
	v_mov_b32_e32 v83, v86
	v_mov_b32_e32 v80, v15
	v_mov_b32_e32 v81, v87
	v_pk_mul_f32 v[82:83], v[82:83], v[82:83]
	s_add_i32 s4, s44, 16
	v_pk_fma_f32 v[80:81], v[80:81], v[80:81], v[82:83]
	s_min_i32 s4, s4, s33
	v_add_f32_e32 v2, v81, v88
	v_add_f32_e32 v2, v80, v2
	v_mov_b32_e32 v80, 0
	s_ashr_i32 s5, s4, 31
	v_add_f32_dpp v2, v2, v2 quad_perm:[1,0,3,2] row_mask:0xf bank_mask:0xf bound_ctrl:1
	s_lshl_b64 s[4:5], s[4:5], 11
	v_lshl_add_u64 v[12:13], v[10:11], 0, s[4:5]
	v_add_f32_dpp v2, v2, v2 quad_perm:[2,3,0,1] row_mask:0xf bank_mask:0xf bound_ctrl:1
	ds_read_b128 v[16:19], v21 offset:256
	ds_read_b128 v[22:25], v52 offset:256
	ds_read_b128 v[60:63], v53 offset:256
	ds_read_b128 v[64:67], v54 offset:256
	ds_read_b128 v[68:71], v55 offset:256
	ds_read_b128 v[72:75], v56 offset:256
	ds_read_b128 v[76:79], v57 offset:256
	v_add_f32_dpp v2, v2, v2 row_half_mirror row_mask:0xf bank_mask:0xf bound_ctrl:1
	s_add_i32 s5, 0, 0x12100
	s_waitcnt lgkmcnt(0)
	v_cvt_f32_f16_sdwa v89, v77 dst_sel:DWORD dst_unused:UNUSED_PAD src0_sel:WORD_1
	v_add_f32_dpp v2, v2, v2 row_mirror row_mask:0xf bank_mask:0xf bound_ctrl:1
	v_cvt_f32_f16_sdwa v88, v79 dst_sel:DWORD dst_unused:UNUSED_PAD src0_sel:WORD_1
	s_nop 0
	v_mov_b32_dpp v80, v2 row_bcast:15 row_mask:0xa bank_mask:0xf
	v_add_f32_e32 v2, v2, v80
	v_mov_b32_e32 v80, 0
	s_nop 1
	v_mov_b32_dpp v80, v2 row_bcast:31 row_mask:0xc bank_mask:0xf
	v_add_f32_e32 v2, v2, v80
	s_nop 0
	v_readlane_b32 s4, v2, 63
	s_nop 1
	v_fma_f32 v2, s4, v196, v194
	v_mul_f32_e32 v80, 0x4b800000, v2
	v_cmp_gt_f32_e32 vcc, s64, v2
	s_nop 1
	v_cndmask_b32_e32 v2, v2, v80, vcc
	v_rsq_f32_e32 v2, v2
	ds_read_b128 v[80:83], v58 offset:256
	v_mul_f32_e32 v97, 0x45800000, v2
	v_cndmask_b32_e32 v2, v2, v97, vcc
	v_mul_f32_e32 v97, v29, v2
	v_mul_f32_e32 v97, v97, v59
	v_mul_f32_e32 v59, v31, v2
	v_mul_f32_e32 v90, v59, v90
	v_mul_f32_e32 v59, v30, v2
	v_mul_f32_e32 v91, v59, v91
	v_mul_f32_e32 v59, v3, v2
	v_mul_f32_e32 v92, v59, v92
	v_mul_f32_e32 v59, v33, v2
	v_mul_f32_e32 v93, v59, v93
	v_mul_f32_e32 v59, v32, v2
	v_mul_f32_e32 v94, v59, v94
	v_mul_f32_e32 v59, v6, v2
	v_mul_f32_e32 v95, v59, v95
	v_mul_f32_e32 v59, v7, v2
	v_mul_f32_e32 v96, v59, v96
	v_fma_mix_f32 v59, v97, v16, 0 op_sel_hi:[0,1,0]
	v_fma_mix_f32 v16, v97, v16, 0 op_sel:[0,1,0] op_sel_hi:[0,1,0]
	v_fma_mix_f32 v16, v90, v18, v16 op_sel:[0,1,0] op_sel_hi:[0,1,0]
	v_fma_mix_f32 v16, v91, v22, v16 op_sel:[0,1,0] op_sel_hi:[0,1,0]
	v_fma_mix_f32 v16, v92, v24, v16 op_sel:[0,1,0] op_sel_hi:[0,1,0]
	v_fma_mix_f32 v98, v97, v17, 0 op_sel_hi:[0,1,0]
	v_fma_mix_f32 v17, v97, v17, 0 op_sel:[0,1,0] op_sel_hi:[0,1,0]
	v_fma_mix_f32 v16, v93, v60, v16 op_sel:[0,1,0] op_sel_hi:[0,1,0]
	v_fma_mix_f32 v17, v90, v19, v17 op_sel:[0,1,0] op_sel_hi:[0,1,0]
	v_fma_mix_f32 v16, v94, v62, v16 op_sel:[0,1,0] op_sel_hi:[0,1,0]
	v_fma_mix_f32 v59, v90, v18, v59 op_sel_hi:[0,1,0]
	v_fma_mix_f32 v17, v91, v23, v17 op_sel:[0,1,0] op_sel_hi:[0,1,0]
	v_fma_mix_f32 v16, v95, v64, v16 op_sel:[0,1,0] op_sel_hi:[0,1,0]
	v_fma_mix_f32 v18, v90, v19, v98 op_sel_hi:[0,1,0]
	v_fma_mix_f32 v19, v91, v22, v59 op_sel_hi:[0,1,0]
	v_fma_mix_f32 v17, v92, v25, v17 op_sel:[0,1,0] op_sel_hi:[0,1,0]
	v_fma_mix_f32 v22, v96, v66, v16 op_sel:[0,1,0] op_sel_hi:[0,1,0]
	v_mul_f32_e32 v16, v8, v2
	v_fma_mix_f32 v18, v91, v23, v18 op_sel_hi:[0,1,0]
	v_fma_mix_f32 v19, v92, v24, v19 op_sel_hi:[0,1,0]
	v_fma_mix_f32 v17, v93, v61, v17 op_sel:[0,1,0] op_sel_hi:[0,1,0]
	v_mul_f32_e32 v98, v16, v26
	v_mul_f32_e32 v16, v9, v2
	v_fma_mix_f32 v18, v92, v25, v18 op_sel_hi:[0,1,0]
	v_fma_mix_f32 v19, v93, v60, v19 op_sel_hi:[0,1,0]
	v_fma_mix_f32 v17, v94, v63, v17 op_sel:[0,1,0] op_sel_hi:[0,1,0]
	v_mul_f32_e32 v84, v16, v84
	v_mul_f32_e32 v16, v35, v2
	v_fma_mix_f32 v18, v93, v61, v18 op_sel_hi:[0,1,0]
	v_fma_mix_f32 v19, v94, v62, v19 op_sel_hi:[0,1,0]
	v_fma_mix_f32 v17, v95, v65, v17 op_sel:[0,1,0] op_sel_hi:[0,1,0]
	v_mul_f32_e32 v99, v16, v27
	v_mul_f32_e32 v16, v34, v2
	v_fma_mix_f32 v18, v94, v63, v18 op_sel_hi:[0,1,0]
	v_fma_mix_f32 v19, v95, v64, v19 op_sel_hi:[0,1,0]
	v_fma_mix_f32 v23, v96, v67, v17 op_sel:[0,1,0] op_sel_hi:[0,1,0]
	v_mul_f32_e32 v85, v16, v85
	v_pk_mul_f32 v[16:17], v[0:1], v[2:3] op_sel_hi:[1,0]
	v_fma_mix_f32 v18, v95, v65, v18 op_sel_hi:[0,1,0]
	v_fma_mix_f32 v19, v96, v66, v19 op_sel_hi:[0,1,0]
	v_pk_mul_f32 v[26:27], v[16:17], v[86:87]
	v_pk_mul_f32 v[16:17], v[4:5], v[2:3] op_sel_hi:[1,0]
	v_fma_mix_f32 v18, v96, v67, v18 op_sel_hi:[0,1,0]
	v_pk_mul_f32 v[24:25], v[16:17], v[14:15]
	v_fma_mix_f32 v14, v98, v68, v19 op_sel_hi:[0,1,0]
	v_fma_mix_f32 v15, v98, v68, v22 op_sel:[0,1,0] op_sel_hi:[0,1,0]
	v_fma_mix_f32 v16, v98, v69, v18 op_sel_hi:[0,1,0]
	v_fma_mix_f32 v17, v98, v69, v23 op_sel:[0,1,0] op_sel_hi:[0,1,0]
	v_fma_mix_f32 v14, v84, v70, v14 op_sel_hi:[0,1,0]
	v_fma_mix_f32 v15, v84, v70, v15 op_sel:[0,1,0] op_sel_hi:[0,1,0]
	v_fma_mix_f32 v16, v84, v71, v16 op_sel_hi:[0,1,0]
	v_fma_mix_f32 v17, v84, v71, v17 op_sel:[0,1,0] op_sel_hi:[0,1,0]
	v_fma_mix_f32 v14, v99, v72, v14 op_sel_hi:[0,1,0]
	v_fma_mix_f32 v15, v99, v72, v15 op_sel:[0,1,0] op_sel_hi:[0,1,0]
	v_fma_mix_f32 v16, v99, v73, v16 op_sel_hi:[0,1,0]
	v_fma_mix_f32 v17, v99, v73, v17 op_sel:[0,1,0] op_sel_hi:[0,1,0]
	v_fma_mix_f32 v14, v85, v74, v14 op_sel_hi:[0,1,0]
	v_fma_mix_f32 v22, v85, v74, v15 op_sel:[0,1,0] op_sel_hi:[0,1,0]
	v_fma_mix_f32 v23, v85, v75, v16 op_sel_hi:[0,1,0]
	v_fma_mix_f32 v16, v85, v75, v17 op_sel:[0,1,0] op_sel_hi:[0,1,0]
	v_fma_mix_f32 v18, v27, v76, v14 op_sel_hi:[0,1,0]
	v_pk_mul_f32 v[14:15], v[26:27], v[88:89]
	v_cvt_f32_f16_sdwa v17, v76 dst_sel:DWORD dst_unused:UNUSED_PAD src0_sel:WORD_1
	v_add_f32_e32 v15, v15, v16
	v_cvt_f32_f16_sdwa v16, v78 dst_sel:DWORD dst_unused:UNUSED_PAD src0_sel:WORD_1
	v_fma_mix_f32 v59, v26, v78, v18 op_sel_hi:[0,1,0]
	v_cvt_f32_f16_e32 v19, v77
	v_cvt_f32_f16_e32 v18, v79
	v_pk_mul_f32 v[16:17], v[26:27], v[16:17]
	s_waitcnt lgkmcnt(0)
; __device__ __forceinline__ void router_ph(const int WID_, const bf16* __restrict__ x3, const float* __restrict__ nw, const float* __restrict__ wrg, const float* __restrict__ brg, ...
;     ...
;         { const int mn = min(m + 8, tile * 256 + 248 + wv); const uint4* xr = (const uint4*)(x3 + (size_t)mn * D);
; #pragma unroll
;           for (int j = 0; j < 2; ++j) nx[j] = xr[lane + 64 * j]; }
;         s = wave_sum(s);
;         const float rs = rsqrtf(s * (1.f / D) + 1e-6f);
;         float l1[4] = {0.f, 0.f, 0.f, 0.f};
; #pragma unroll
;         for (int j = 0; j < 2; ++j) {
;             const int k0 = (lane + 64 * j) * 8;
;             const float4 ga = gw[2 * j], gb = gw[2 * j + 1];
;             h[8 * j] *= rs * ga.x; h[8 * j + 1] *= rs * ga.y; h[8 * j + 2] *= rs * ga.z; h[8 * j + 3] *= rs * ga.w;
;             h[8 * j + 4] *= rs * gb.x; h[8 * j + 5] *= rs * gb.y; h[8 * j + 6] *= rs * gb.z; h[8 * j + 7] *= rs * gb.w;
; #pragma unroll
;             for (int e = 0; e < 8; ++e) { const h4 w = *(const h4*)(wg16 + (k0 + e) * 4); const float x = h[8 * j + e];
;                 l1[0] += x * (float)w[0]; l1[1] += x * (float)w[1]; l1[2] += x * (float)w[2]; l1[3] += x * (float)w[3]; }
;         }
; #pragma unroll
;         for (int i = 0; i < 4; ++i) l1[i] = wave_sum(l1[i]) + brg_l[i];
;         int grp = 0; float best = l1[0];
; #pragma unroll
;         for (int i = 1; i < 4; ++i) if (l1[i] > best) { best = l1[i]; grp = i; }
;         float se = 0.f;
; #pragma unroll
;         for (int i = 0; i < 4; ++i) se += __expf(l1[i] - best);
;         const float g1 = 1.f / se;
;         float l2[8] = {};
;         const _Float16* we = we16 + (size_t)grp * D * 8;
; #pragma unroll
;         for (int j = 0; j < 2; ++j) {
;             const int k0 = (lane + 64 * j) * 8;
; #pragma unroll
;             for (int e = 0; e < 8; ++e) { const float x = h[8 * j + e]; const h8 w = *(const h8*)(we + (k0 + e) * 8);
; #pragma unroll
;                 for (int q = 0; q < 8; ++q) l2[q] += x * (float)w[q]; }
	v_fma_mix_f32 v59, v25, v80, v59 op_sel_hi:[0,1,0]
	v_add_f32_e32 v17, v17, v22
	v_add_f32_e32 v22, v16, v17
	v_pk_mul_f32 v[16:17], v[26:27], v[18:19]
	v_cvt_f32_f16_sdwa v19, v81 dst_sel:DWORD dst_unused:UNUSED_PAD src0_sel:WORD_1
	v_cvt_f32_f16_sdwa v18, v83 dst_sel:DWORD dst_unused:UNUSED_PAD src0_sel:WORD_1
	v_add_f32_e32 v17, v17, v23
	v_add_f32_e32 v23, v16, v17
	v_add_f32_e32 v16, v14, v15
	v_pk_mul_f32 v[14:15], v[24:25], v[18:19]
	v_cvt_f32_f16_sdwa v17, v80 dst_sel:DWORD dst_unused:UNUSED_PAD src0_sel:WORD_1
	v_add_f32_e32 v15, v15, v16
	v_cvt_f32_f16_sdwa v16, v82 dst_sel:DWORD dst_unused:UNUSED_PAD src0_sel:WORD_1
	v_cvt_f32_f16_e32 v19, v81
	v_cvt_f32_f16_e32 v18, v83
	v_fma_mix_f32 v59, v24, v82, v59 op_sel_hi:[0,1,0]
	v_pk_mul_f32 v[16:17], v[24:25], v[16:17]
	s_nop 0
	v_add_f32_e32 v17, v17, v22
	v_add_f32_e32 v22, v16, v17
	v_pk_mul_f32 v[16:17], v[24:25], v[18:19]
	v_add_f32_e32 v19, v14, v15
	v_add_f32_dpp v14, v59, v59 quad_perm:[1,0,3,2] row_mask:0xf bank_mask:0xf bound_ctrl:1
	v_mov_b32_e32 v15, 0
	v_add_f32_e32 v17, v17, v23
	v_add_f32_dpp v14, v14, v14 quad_perm:[2,3,0,1] row_mask:0xf bank_mask:0xf bound_ctrl:1
	v_add_f32_e32 v18, v16, v17
	v_mov_b32_e32 v23, 0
	v_add_f32_dpp v14, v14, v14 row_half_mirror row_mask:0xf bank_mask:0xf bound_ctrl:1
	s_nop 1
	v_add_f32_dpp v14, v14, v14 row_mirror row_mask:0xf bank_mask:0xf bound_ctrl:1
	s_nop 1
	v_mov_b32_dpp v15, v14 row_bcast:15 row_mask:0xa bank_mask:0xf
	v_add_f32_e32 v14, v14, v15
	v_mov_b32_e32 v15, 0
	s_nop 1
	v_mov_b32_dpp v15, v14 row_bcast:31 row_mask:0xc bank_mask:0xf
	v_add_f32_e32 v14, v14, v15
	v_mov_b32_e32 v15, 0
	v_readlane_b32 s4, v14, 63
	v_add_f32_dpp v14, v22, v22 quad_perm:[1,0,3,2] row_mask:0xf bank_mask:0xf bound_ctrl:1
	s_nop 1
	v_add_f32_dpp v14, v14, v14 quad_perm:[2,3,0,1] row_mask:0xf bank_mask:0xf bound_ctrl:1
	s_nop 1
	v_add_f32_dpp v14, v14, v14 row_half_mirror row_mask:0xf bank_mask:0xf bound_ctrl:1
	s_nop 1
	v_add_f32_dpp v14, v14, v14 row_mirror row_mask:0xf bank_mask:0xf bound_ctrl:1
	s_nop 1
	v_mov_b32_dpp v15, v14 row_bcast:15 row_mask:0xa bank_mask:0xf
	v_add_f32_e32 v22, v14, v15
	v_mov_b32_e32 v14, s5
	ds_read_b128 v[14:17], v14
	v_mov_b32_dpp v23, v22 row_bcast:31 row_mask:0xc bank_mask:0xf
	v_add_f32_e32 v22, v22, v23
	s_nop 0
	v_readlane_b32 s5, v22, 63
	s_waitcnt lgkmcnt(0)
	s_nop 0
	v_pk_add_f32 v[22:23], s[4:5], v[14:15]
	v_add_f32_dpp v14, v18, v18 quad_perm:[1,0,3,2] row_mask:0xf bank_mask:0xf bound_ctrl:1
	v_mov_b32_e32 v15, 0
	s_nop 0
	v_add_f32_dpp v14, v14, v14 quad_perm:[2,3,0,1] row_mask:0xf bank_mask:0xf bound_ctrl:1
	s_nop 1
	v_add_f32_dpp v14, v14, v14 row_half_mirror row_mask:0xf bank_mask:0xf bound_ctrl:1
	s_nop 1
	v_add_f32_dpp v14, v14, v14 row_mirror row_mask:0xf bank_mask:0xf bound_ctrl:1
	s_nop 1
	v_mov_b32_dpp v15, v14 row_bcast:15 row_mask:0xa bank_mask:0xf
	v_add_f32_e32 v14, v14, v15
	v_mov_b32_e32 v15, 0
	s_nop 1
	v_mov_b32_dpp v15, v14 row_bcast:31 row_mask:0xc bank_mask:0xf
	v_add_f32_e32 v14, v14, v15
	v_mov_b32_e32 v15, 0
	v_readlane_b32 s4, v14, 63
	v_add_f32_dpp v14, v19, v19 quad_perm:[1,0,3,2] row_mask:0xf bank_mask:0xf bound_ctrl:1
	s_nop 0
	v_add_f32_e32 v59, s4, v16
	v_add_f32_dpp v14, v14, v14 quad_perm:[2,3,0,1] row_mask:0xf bank_mask:0xf bound_ctrl:1
	s_nop 1
	v_add_f32_dpp v14, v14, v14 row_half_mirror row_mask:0xf bank_mask:0xf bound_ctrl:1
	s_nop 1
	v_add_f32_dpp v14, v14, v14 row_mirror row_mask:0xf bank_mask:0xf bound_ctrl:1
	s_nop 1
	v_mov_b32_dpp v15, v14 row_bcast:15 row_mask:0xa bank_mask:0xf
	v_add_f32_e32 v14, v14, v15
	v_mov_b32_e32 v15, 0
	s_nop 1
	v_mov_b32_dpp v15, v14 row_bcast:31 row_mask:0xc bank_mask:0xf
	v_add_f32_e32 v14, v14, v15
	s_nop 0
	v_readlane_b32 s4, v14, 63
	s_nop 1
	v_add_f32_e32 v60, s4, v17
	v_cmp_gt_f32_e64 s[4:5], v23, v22
	s_nop 1
	v_cndmask_b32_e64 v14, v22, v23, s[4:5]
	v_cmp_gt_f32_e64 s[6:7], v59, v14
	s_nop 1
	v_cndmask_b32_e64 v61, v14, v59, s[6:7]
	v_cndmask_b32_e64 v14, 0, 1, s[4:5]
	s_and_b64 s[4:5], s[6:7], exec
	v_cmp_gt_f32_e32 vcc, v60, v61
	v_readfirstlane_b32 s4, v14
	s_cselect_b32 s6, 2, s4
	s_and_b64 s[4:5], vcc, exec
	s_cselect_b32 s49, 3, s6
	s_lshl_b32 s4, s49, 14
	s_add_i32 s48, s4, 0
	global_load_dwordx4 v[16:19], v[12:13], off
	s_nop 0
	global_load_dwordx4 v[12:15], v[12:13], off offset:1024
	v_add_u32_e32 v112, s48, v36
	ds_read_b128 v[132:135], v112 offset:8448
	v_add_u32_e32 v113, s48, v37
	ds_read_b128 v[136:139], v113 offset:8448
	v_add_u32_e32 v112, s48, v38
	ds_read_b128 v[140:143], v112 offset:8448
	v_add_u32_e32 v113, s48, v39
	ds_read_b128 v[144:147], v113 offset:8448
	v_add_u32_e32 v112, s48, v40
	ds_read_b128 v[148:151], v112 offset:8448
	v_add_u32_e32 v113, s48, v41
	ds_read_b128 v[152:155], v113 offset:8448
	v_add_u32_e32 v112, s48, v42
	ds_read_b128 v[156:159], v112 offset:8448
	v_add_u32_e32 v113, s48, v43
	ds_read_b128 v[160:163], v113 offset:8448
	v_add_u32_e32 v112, s48, v44
	ds_read_b128 v[164:167], v112 offset:8448
	v_add_u32_e32 v113, s48, v45
	ds_read_b128 v[168:171], v113 offset:8448
	v_add_u32_e32 v112, s48, v46
	ds_read_b128 v[172:175], v112 offset:8448
	v_add_u32_e32 v113, s48, v47
	ds_read_b128 v[176:179], v113 offset:8448
	s_waitcnt lgkmcnt(11)
	v_fma_mix_f32 v70, v97, v132, 0 op_sel_hi:[0,1,0]
	v_fma_mix_f32 v71, v97, v132, 0 op_sel:[0,1,0] op_sel_hi:[0,1,0]
	v_fma_mix_f32 v72, v97, v133, 0 op_sel_hi:[0,1,0]
	v_fma_mix_f32 v73, v97, v133, 0 op_sel:[0,1,0] op_sel_hi:[0,1,0]
	v_fma_mix_f32 v74, v97, v134, 0 op_sel_hi:[0,1,0]
	v_fma_mix_f32 v75, v97, v134, 0 op_sel:[0,1,0] op_sel_hi:[0,1,0]
	v_fma_mix_f32 v76, v97, v135, 0 op_sel_hi:[0,1,0]
	v_fma_mix_f32 v77, v97, v135, 0 op_sel:[0,1,0] op_sel_hi:[0,1,0]
	s_waitcnt lgkmcnt(10)
; __device__ __forceinline__ void router_ph(const int WID_, const bf16* __restrict__ x3, const float* __restrict__ nw, const float* __restrict__ wrg, const float* __restrict__ brg, ...
;     ...
;         float l2[8] = {};
;         const _Float16* we = we16 + (size_t)grp * D * 8;
; #pragma unroll
;         for (int j = 0; j < 2; ++j) {
;             const int k0 = (lane + 64 * j) * 8;
; #pragma unroll
;             for (int e = 0; e < 8; ++e) { const float x = h[8 * j + e]; const h8 w = *(const h8*)(we + (k0 + e) * 8);
; #pragma unroll
;                 for (int q = 0; q < 8; ++q) l2[q] += x * (float)w[q]; }
	v_fma_mix_f32 v70, v90, v136, v70 op_sel_hi:[0,1,0]
	v_fma_mix_f32 v71, v90, v136, v71 op_sel:[0,1,0] op_sel_hi:[0,1,0]
	v_fma_mix_f32 v72, v90, v137, v72 op_sel_hi:[0,1,0]
	v_fma_mix_f32 v73, v90, v137, v73 op_sel:[0,1,0] op_sel_hi:[0,1,0]
	v_fma_mix_f32 v74, v90, v138, v74 op_sel_hi:[0,1,0]
	v_fma_mix_f32 v75, v90, v138, v75 op_sel:[0,1,0] op_sel_hi:[0,1,0]
	v_fma_mix_f32 v76, v90, v139, v76 op_sel_hi:[0,1,0]
	v_fma_mix_f32 v77, v90, v139, v77 op_sel:[0,1,0] op_sel_hi:[0,1,0]
	s_waitcnt lgkmcnt(9)
	v_fma_mix_f32 v70, v91, v140, v70 op_sel_hi:[0,1,0]
	v_fma_mix_f32 v71, v91, v140, v71 op_sel:[0,1,0] op_sel_hi:[0,1,0]
	v_fma_mix_f32 v72, v91, v141, v72 op_sel_hi:[0,1,0]
	v_fma_mix_f32 v73, v91, v141, v73 op_sel:[0,1,0] op_sel_hi:[0,1,0]
	v_fma_mix_f32 v74, v91, v142, v74 op_sel_hi:[0,1,0]
	v_fma_mix_f32 v75, v91, v142, v75 op_sel:[0,1,0] op_sel_hi:[0,1,0]
	v_fma_mix_f32 v76, v91, v143, v76 op_sel_hi:[0,1,0]
	v_fma_mix_f32 v77, v91, v143, v77 op_sel:[0,1,0] op_sel_hi:[0,1,0]
	s_waitcnt lgkmcnt(8)
	v_fma_mix_f32 v70, v92, v144, v70 op_sel_hi:[0,1,0]
	v_fma_mix_f32 v71, v92, v144, v71 op_sel:[0,1,0] op_sel_hi:[0,1,0]
	v_fma_mix_f32 v72, v92, v145, v72 op_sel_hi:[0,1,0]
	v_fma_mix_f32 v73, v92, v145, v73 op_sel:[0,1,0] op_sel_hi:[0,1,0]
	v_fma_mix_f32 v74, v92, v146, v74 op_sel_hi:[0,1,0]
	v_fma_mix_f32 v75, v92, v146, v75 op_sel:[0,1,0] op_sel_hi:[0,1,0]
	v_fma_mix_f32 v76, v92, v147, v76 op_sel_hi:[0,1,0]
	v_fma_mix_f32 v77, v92, v147, v77 op_sel:[0,1,0] op_sel_hi:[0,1,0]
	v_add_u32_e32 v112, s48, v48
	ds_read_b128 v[180:183], v112 offset:8448
	v_add_u32_e32 v113, s48, v49
	ds_read_b128 v[184:187], v113 offset:8448
	v_add_u32_e32 v112, s48, v50
	ds_read_b128 v[188:191], v112 offset:8448
	v_add_u32_e32 v113, s48, v51
	ds_read_b128 v[108:111], v113 offset:8448
	s_waitcnt lgkmcnt(11)
	v_fma_mix_f32 v70, v93, v148, v70 op_sel_hi:[0,1,0]
	v_fma_mix_f32 v71, v93, v148, v71 op_sel:[0,1,0] op_sel_hi:[0,1,0]
	v_fma_mix_f32 v72, v93, v149, v72 op_sel_hi:[0,1,0]
	v_fma_mix_f32 v73, v93, v149, v73 op_sel:[0,1,0] op_sel_hi:[0,1,0]
	v_fma_mix_f32 v74, v93, v150, v74 op_sel_hi:[0,1,0]
	v_fma_mix_f32 v75, v93, v150, v75 op_sel:[0,1,0] op_sel_hi:[0,1,0]
	v_fma_mix_f32 v76, v93, v151, v76 op_sel_hi:[0,1,0]
	v_fma_mix_f32 v77, v93, v151, v77 op_sel:[0,1,0] op_sel_hi:[0,1,0]
	s_waitcnt lgkmcnt(10)
	v_fma_mix_f32 v70, v94, v152, v70 op_sel_hi:[0,1,0]
	v_fma_mix_f32 v71, v94, v152, v71 op_sel:[0,1,0] op_sel_hi:[0,1,0]
	v_fma_mix_f32 v72, v94, v153, v72 op_sel_hi:[0,1,0]
	v_fma_mix_f32 v73, v94, v153, v73 op_sel:[0,1,0] op_sel_hi:[0,1,0]
	v_fma_mix_f32 v74, v94, v154, v74 op_sel_hi:[0,1,0]
	v_fma_mix_f32 v75, v94, v154, v75 op_sel:[0,1,0] op_sel_hi:[0,1,0]
	v_fma_mix_f32 v76, v94, v155, v76 op_sel_hi:[0,1,0]
	v_fma_mix_f32 v77, v94, v155, v77 op_sel:[0,1,0] op_sel_hi:[0,1,0]
	s_waitcnt lgkmcnt(9)
	v_fma_mix_f32 v70, v95, v156, v70 op_sel_hi:[0,1,0]
	v_fma_mix_f32 v71, v95, v156, v71 op_sel:[0,1,0] op_sel_hi:[0,1,0]
	v_fma_mix_f32 v72, v95, v157, v72 op_sel_hi:[0,1,0]
	v_fma_mix_f32 v73, v95, v157, v73 op_sel:[0,1,0] op_sel_hi:[0,1,0]
	v_fma_mix_f32 v74, v95, v158, v74 op_sel_hi:[0,1,0]
	v_fma_mix_f32 v75, v95, v158, v75 op_sel:[0,1,0] op_sel_hi:[0,1,0]
	v_fma_mix_f32 v76, v95, v159, v76 op_sel_hi:[0,1,0]
	v_fma_mix_f32 v77, v95, v159, v77 op_sel:[0,1,0] op_sel_hi:[0,1,0]
	s_waitcnt lgkmcnt(8)
	v_fma_mix_f32 v70, v96, v160, v70 op_sel_hi:[0,1,0]
	v_fma_mix_f32 v71, v96, v160, v71 op_sel:[0,1,0] op_sel_hi:[0,1,0]
	v_fma_mix_f32 v72, v96, v161, v72 op_sel_hi:[0,1,0]
	v_fma_mix_f32 v73, v96, v161, v73 op_sel:[0,1,0] op_sel_hi:[0,1,0]
	v_fma_mix_f32 v74, v96, v162, v74 op_sel_hi:[0,1,0]
	v_fma_mix_f32 v75, v96, v162, v75 op_sel:[0,1,0] op_sel_hi:[0,1,0]
	v_fma_mix_f32 v76, v96, v163, v76 op_sel_hi:[0,1,0]
	v_fma_mix_f32 v77, v96, v163, v77 op_sel:[0,1,0] op_sel_hi:[0,1,0]
	s_waitcnt lgkmcnt(7)
	v_fma_mix_f32 v70, v98, v164, v70 op_sel_hi:[0,1,0]
	v_fma_mix_f32 v71, v98, v164, v71 op_sel:[0,1,0] op_sel_hi:[0,1,0]
	v_fma_mix_f32 v72, v98, v165, v72 op_sel_hi:[0,1,0]
	v_fma_mix_f32 v73, v98, v165, v73 op_sel:[0,1,0] op_sel_hi:[0,1,0]
	v_fma_mix_f32 v74, v98, v166, v74 op_sel_hi:[0,1,0]
	v_fma_mix_f32 v75, v98, v166, v75 op_sel:[0,1,0] op_sel_hi:[0,1,0]
	v_fma_mix_f32 v76, v98, v167, v76 op_sel_hi:[0,1,0]
	v_fma_mix_f32 v77, v98, v167, v77 op_sel:[0,1,0] op_sel_hi:[0,1,0]
	s_waitcnt lgkmcnt(6)
	v_fma_mix_f32 v70, v84, v168, v70 op_sel_hi:[0,1,0]
	v_fma_mix_f32 v71, v84, v168, v71 op_sel:[0,1,0] op_sel_hi:[0,1,0]
	v_fma_mix_f32 v72, v84, v169, v72 op_sel_hi:[0,1,0]
	v_fma_mix_f32 v73, v84, v169, v73 op_sel:[0,1,0] op_sel_hi:[0,1,0]
	v_fma_mix_f32 v74, v84, v170, v74 op_sel_hi:[0,1,0]
	v_fma_mix_f32 v75, v84, v170, v75 op_sel:[0,1,0] op_sel_hi:[0,1,0]
	v_fma_mix_f32 v76, v84, v171, v76 op_sel_hi:[0,1,0]
	v_fma_mix_f32 v77, v84, v171, v77 op_sel:[0,1,0] op_sel_hi:[0,1,0]
	s_waitcnt lgkmcnt(5)
	v_fma_mix_f32 v70, v99, v172, v70 op_sel_hi:[0,1,0]
	v_fma_mix_f32 v71, v99, v172, v71 op_sel:[0,1,0] op_sel_hi:[0,1,0]
	v_fma_mix_f32 v72, v99, v173, v72 op_sel_hi:[0,1,0]
	v_fma_mix_f32 v73, v99, v173, v73 op_sel:[0,1,0] op_sel_hi:[0,1,0]
	v_fma_mix_f32 v74, v99, v174, v74 op_sel_hi:[0,1,0]
	v_fma_mix_f32 v75, v99, v174, v75 op_sel:[0,1,0] op_sel_hi:[0,1,0]
	v_fma_mix_f32 v76, v99, v175, v76 op_sel_hi:[0,1,0]
	v_fma_mix_f32 v77, v99, v175, v77 op_sel:[0,1,0] op_sel_hi:[0,1,0]
	s_waitcnt lgkmcnt(4)
	v_fma_mix_f32 v70, v85, v176, v70 op_sel_hi:[0,1,0]
	v_fma_mix_f32 v71, v85, v176, v71 op_sel:[0,1,0] op_sel_hi:[0,1,0]
	v_fma_mix_f32 v72, v85, v177, v72 op_sel_hi:[0,1,0]
	v_fma_mix_f32 v73, v85, v177, v73 op_sel:[0,1,0] op_sel_hi:[0,1,0]
	v_fma_mix_f32 v74, v85, v178, v74 op_sel_hi:[0,1,0]
	v_fma_mix_f32 v75, v85, v178, v75 op_sel:[0,1,0] op_sel_hi:[0,1,0]
	v_fma_mix_f32 v76, v85, v179, v76 op_sel_hi:[0,1,0]
	v_fma_mix_f32 v77, v85, v179, v77 op_sel:[0,1,0] op_sel_hi:[0,1,0]
	s_waitcnt lgkmcnt(3)
; __device__ __forceinline__ void router_ph(const int WID_, const bf16* __restrict__ x3, const float* __restrict__ nw, const float* __restrict__ wrg, const float* __restrict__ brg, ...
;     ...
; #pragma unroll
;         for (int j = 0; j < 2; ++j) {
;             const int k0 = (lane + 64 * j) * 8;
; #pragma unroll
;             for (int e = 0; e < 8; ++e) { const float x = h[8 * j + e]; const h8 w = *(const h8*)(we + (k0 + e) * 8);
; #pragma unroll
;                 for (int q = 0; q < 8; ++q) l2[q] += x * (float)w[q]; }
;         }
; #pragma unroll
;         for (int i = 0; i < 8; ++i) l2[i] = wave_sum(l2[i]) + bre_l[grp * 8 + i];
	v_fma_mix_f32 v70, v27, v180, v70 op_sel_hi:[0,1,0]
	v_fma_mix_f32 v71, v27, v180, v71 op_sel:[0,1,0] op_sel_hi:[0,1,0]
	v_fma_mix_f32 v72, v27, v181, v72 op_sel_hi:[0,1,0]
	v_fma_mix_f32 v73, v27, v181, v73 op_sel:[0,1,0] op_sel_hi:[0,1,0]
	v_fma_mix_f32 v74, v27, v182, v74 op_sel_hi:[0,1,0]
	v_fma_mix_f32 v75, v27, v182, v75 op_sel:[0,1,0] op_sel_hi:[0,1,0]
	v_fma_mix_f32 v76, v27, v183, v76 op_sel_hi:[0,1,0]
	v_fma_mix_f32 v77, v27, v183, v77 op_sel:[0,1,0] op_sel_hi:[0,1,0]
	s_waitcnt lgkmcnt(2)
	v_fma_mix_f32 v70, v26, v184, v70 op_sel_hi:[0,1,0]
	v_fma_mix_f32 v71, v26, v184, v71 op_sel:[0,1,0] op_sel_hi:[0,1,0]
	v_fma_mix_f32 v72, v26, v185, v72 op_sel_hi:[0,1,0]
	v_fma_mix_f32 v73, v26, v185, v73 op_sel:[0,1,0] op_sel_hi:[0,1,0]
	v_fma_mix_f32 v74, v26, v186, v74 op_sel_hi:[0,1,0]
	v_fma_mix_f32 v75, v26, v186, v75 op_sel:[0,1,0] op_sel_hi:[0,1,0]
	v_fma_mix_f32 v76, v26, v187, v76 op_sel_hi:[0,1,0]
	v_fma_mix_f32 v77, v26, v187, v77 op_sel:[0,1,0] op_sel_hi:[0,1,0]
	s_waitcnt lgkmcnt(1)
	v_fma_mix_f32 v70, v25, v188, v70 op_sel_hi:[0,1,0]
	v_fma_mix_f32 v71, v25, v188, v71 op_sel:[0,1,0] op_sel_hi:[0,1,0]
	v_fma_mix_f32 v72, v25, v189, v72 op_sel_hi:[0,1,0]
	v_fma_mix_f32 v73, v25, v189, v73 op_sel:[0,1,0] op_sel_hi:[0,1,0]
	v_fma_mix_f32 v74, v25, v190, v74 op_sel_hi:[0,1,0]
	v_fma_mix_f32 v75, v25, v190, v75 op_sel:[0,1,0] op_sel_hi:[0,1,0]
	v_fma_mix_f32 v76, v25, v191, v76 op_sel_hi:[0,1,0]
	v_fma_mix_f32 v77, v25, v191, v77 op_sel:[0,1,0] op_sel_hi:[0,1,0]
	s_waitcnt lgkmcnt(0)
	v_fma_mix_f32 v70, v24, v108, v70 op_sel_hi:[0,1,0]
	v_fma_mix_f32 v71, v24, v108, v71 op_sel:[0,1,0] op_sel_hi:[0,1,0]
	v_fma_mix_f32 v72, v24, v109, v72 op_sel_hi:[0,1,0]
	v_fma_mix_f32 v73, v24, v109, v73 op_sel:[0,1,0] op_sel_hi:[0,1,0]
	v_fma_mix_f32 v74, v24, v110, v74 op_sel_hi:[0,1,0]
	v_fma_mix_f32 v75, v24, v110, v75 op_sel:[0,1,0] op_sel_hi:[0,1,0]
	v_fma_mix_f32 v76, v24, v111, v76 op_sel_hi:[0,1,0]
	v_fma_mix_f32 v77, v24, v111, v77 op_sel:[0,1,0] op_sel_hi:[0,1,0]
	v_mov_b32_e32 v26, v70
	v_mov_b32_e32 v27, v71
	v_mov_b32_e32 v62, v72
	v_mov_b32_e32 v63, v73
	v_mov_b32_e32 v65, v74
	v_mov_b32_e32 v64, v75
	v_mov_b32_e32 v66, v76
	v_mov_b32_e32 v24, v77
	v_add_f32_dpp v26, v26, v26 quad_perm:[1,0,3,2] row_mask:0xf bank_mask:0xf bound_ctrl:1
	v_add_f32_dpp v27, v27, v27 quad_perm:[1,0,3,2] row_mask:0xf bank_mask:0xf bound_ctrl:1
	v_add_f32_dpp v62, v62, v62 quad_perm:[1,0,3,2] row_mask:0xf bank_mask:0xf bound_ctrl:1
	v_add_f32_dpp v63, v63, v63 quad_perm:[1,0,3,2] row_mask:0xf bank_mask:0xf bound_ctrl:1
	v_add_f32_dpp v65, v65, v65 quad_perm:[1,0,3,2] row_mask:0xf bank_mask:0xf bound_ctrl:1
	v_add_f32_dpp v64, v64, v64 quad_perm:[1,0,3,2] row_mask:0xf bank_mask:0xf bound_ctrl:1
	v_add_f32_dpp v66, v66, v66 quad_perm:[1,0,3,2] row_mask:0xf bank_mask:0xf bound_ctrl:1
	v_add_f32_dpp v24, v24, v24 quad_perm:[1,0,3,2] row_mask:0xf bank_mask:0xf bound_ctrl:1
	v_add_f32_dpp v26, v26, v26 quad_perm:[2,3,0,1] row_mask:0xf bank_mask:0xf bound_ctrl:1
	v_add_f32_dpp v27, v27, v27 quad_perm:[2,3,0,1] row_mask:0xf bank_mask:0xf bound_ctrl:1
	v_add_f32_dpp v62, v62, v62 quad_perm:[2,3,0,1] row_mask:0xf bank_mask:0xf bound_ctrl:1
	v_add_f32_dpp v63, v63, v63 quad_perm:[2,3,0,1] row_mask:0xf bank_mask:0xf bound_ctrl:1
	v_add_f32_dpp v65, v65, v65 quad_perm:[2,3,0,1] row_mask:0xf bank_mask:0xf bound_ctrl:1
	v_add_f32_dpp v64, v64, v64 quad_perm:[2,3,0,1] row_mask:0xf bank_mask:0xf bound_ctrl:1
	v_add_f32_dpp v66, v66, v66 quad_perm:[2,3,0,1] row_mask:0xf bank_mask:0xf bound_ctrl:1
	v_add_f32_dpp v24, v24, v24 quad_perm:[2,3,0,1] row_mask:0xf bank_mask:0xf bound_ctrl:1
	v_add_f32_dpp v26, v26, v26 row_half_mirror row_mask:0xf bank_mask:0xf bound_ctrl:1
	v_add_f32_dpp v27, v27, v27 row_half_mirror row_mask:0xf bank_mask:0xf bound_ctrl:1
	v_add_f32_dpp v62, v62, v62 row_half_mirror row_mask:0xf bank_mask:0xf bound_ctrl:1
	v_add_f32_dpp v63, v63, v63 row_half_mirror row_mask:0xf bank_mask:0xf bound_ctrl:1
	v_add_f32_dpp v65, v65, v65 row_half_mirror row_mask:0xf bank_mask:0xf bound_ctrl:1
	v_add_f32_dpp v64, v64, v64 row_half_mirror row_mask:0xf bank_mask:0xf bound_ctrl:1
	v_add_f32_dpp v66, v66, v66 row_half_mirror row_mask:0xf bank_mask:0xf bound_ctrl:1
	v_add_f32_dpp v24, v24, v24 row_half_mirror row_mask:0xf bank_mask:0xf bound_ctrl:1
	v_add_f32_dpp v26, v26, v26 row_mirror row_mask:0xf bank_mask:0xf bound_ctrl:1
	v_add_f32_dpp v27, v27, v27 row_mirror row_mask:0xf bank_mask:0xf bound_ctrl:1
	v_add_f32_dpp v62, v62, v62 row_mirror row_mask:0xf bank_mask:0xf bound_ctrl:1
	v_add_f32_dpp v63, v63, v63 row_mirror row_mask:0xf bank_mask:0xf bound_ctrl:1
	v_add_f32_dpp v65, v65, v65 row_mirror row_mask:0xf bank_mask:0xf bound_ctrl:1
	v_add_f32_dpp v64, v64, v64 row_mirror row_mask:0xf bank_mask:0xf bound_ctrl:1
	v_add_f32_dpp v66, v66, v66 row_mirror row_mask:0xf bank_mask:0xf bound_ctrl:1
	v_add_f32_dpp v24, v24, v24 row_mirror row_mask:0xf bank_mask:0xf bound_ctrl:1
	v_mov_b32_e32 v100, 0
	v_mov_b32_e32 v101, 0
	v_mov_b32_e32 v102, 0
	v_mov_b32_e32 v103, 0
	v_mov_b32_e32 v104, 0
	v_mov_b32_e32 v105, 0
	v_mov_b32_e32 v106, 0
	v_mov_b32_e32 v107, 0
	v_mov_b32_dpp v100, v26 row_bcast:15 row_mask:0xa bank_mask:0xf
	v_mov_b32_dpp v101, v27 row_bcast:15 row_mask:0xa bank_mask:0xf
	v_mov_b32_dpp v102, v62 row_bcast:15 row_mask:0xa bank_mask:0xf
	v_mov_b32_dpp v103, v63 row_bcast:15 row_mask:0xa bank_mask:0xf
	v_mov_b32_dpp v104, v65 row_bcast:15 row_mask:0xa bank_mask:0xf
	v_mov_b32_dpp v105, v64 row_bcast:15 row_mask:0xa bank_mask:0xf
	v_mov_b32_dpp v106, v66 row_bcast:15 row_mask:0xa bank_mask:0xf
	v_mov_b32_dpp v107, v24 row_bcast:15 row_mask:0xa bank_mask:0xf
; __device__ __forceinline__ void router_ph(const int WID_, const bf16* __restrict__ x3, const float* __restrict__ nw, const float* __restrict__ wrg, const float* __restrict__ brg, ...
;     ...
;         for (int i = 0; i < 8; ++i) l2[i] = wave_sum(l2[i]) + bre_l[grp * 8 + i];
;         int i0 = 0; float v0 = l2[0];
; #pragma unroll
;         for (int i = 1; i < 8; ++i) if (l2[i] > v0) { v0 = l2[i]; i0 = i; }
;         int i1 = -1; float v1 = -3.0e38f;
; #pragma unroll
;         for (int i = 0; i < 8; ++i) if (i != i0 && l2[i] > v1) { v1 = l2[i]; i1 = i; }
;         const float e1 = __expf(v1 - v0), inv = 1.f / (1.f + e1);
;         if (lane == 0) {
;             const int ea = grp * 8 + i0, eb = grp * 8 + i1;
;             mb.tok_e[2 * m] = ea; mb.tok_e[2 * m + 1] = eb; mb.tok_rs[m] = rs;
;             mb.tok_g[2 * m] = g1 * inv; mb.tok_g[2 * m + 1] = g1 * e1 * inv;
;             atomicAdd(&lcnt[ea], 1); atomicAdd(&lcnt[eb], 1);
	v_add_f32_e32 v26, v26, v100
	v_add_f32_e32 v27, v27, v101
	v_add_f32_e32 v62, v62, v102
	v_add_f32_e32 v63, v63, v103
	v_add_f32_e32 v65, v65, v104
	v_add_f32_e32 v64, v64, v105
	v_add_f32_e32 v66, v66, v106
	v_add_f32_e32 v24, v24, v107
	v_mov_b32_e32 v100, 0
	v_mov_b32_e32 v101, 0
	v_mov_b32_e32 v102, 0
	v_mov_b32_e32 v103, 0
	v_mov_b32_e32 v104, 0
	v_mov_b32_e32 v105, 0
	v_mov_b32_e32 v106, 0
	v_mov_b32_e32 v107, 0
	v_mov_b32_dpp v100, v26 row_bcast:31 row_mask:0xc bank_mask:0xf
	v_mov_b32_dpp v101, v27 row_bcast:31 row_mask:0xc bank_mask:0xf
	v_mov_b32_dpp v102, v62 row_bcast:31 row_mask:0xc bank_mask:0xf
	v_mov_b32_dpp v103, v63 row_bcast:31 row_mask:0xc bank_mask:0xf
	v_mov_b32_dpp v104, v65 row_bcast:31 row_mask:0xc bank_mask:0xf
	v_mov_b32_dpp v105, v64 row_bcast:31 row_mask:0xc bank_mask:0xf
	v_mov_b32_dpp v106, v66 row_bcast:31 row_mask:0xc bank_mask:0xf
	v_mov_b32_dpp v107, v24 row_bcast:31 row_mask:0xc bank_mask:0xf
	v_add_f32_e32 v26, v26, v100
	v_add_f32_e32 v27, v27, v101
	v_add_f32_e32 v62, v62, v102
	v_add_f32_e32 v63, v63, v103
	v_add_f32_e32 v65, v65, v104
	v_add_f32_e32 v64, v64, v105
	v_add_f32_e32 v66, v66, v106
	v_add_f32_e32 v24, v24, v107
	v_readlane_b32 s4, v26, 63
	v_readlane_b32 s5, v27, 63
	v_readlane_b32 s6, v62, 63
	v_readlane_b32 s7, v63, 63
	v_readlane_b32 s8, v65, 63
	v_readlane_b32 s9, v64, 63
	v_readlane_b32 s10, v66, 63
	v_readlane_b32 s11, v24, 63
	s_and_saveexec_b64 s[82:83], s[2:3]
	s_cbranch_execz .LBB0_2144
	s_mul_i32 s12, s49, 0xffffc020
	s_add_i32 s48, s48, s12
	v_mov_b32_e32 v62, s48
	ds_read_b128 v[24:27], v62 offset:128
	ds_read_b128 v[62:65], v62 offset:144
	s_waitcnt lgkmcnt(1)
	v_pk_add_f32 v[24:25], s[4:5], v[24:25]
	s_nop 0
	v_cmp_gt_f32_e64 s[4:5], v25, v24
	v_add_f32_e32 v26, s6, v26
	v_add_f32_e32 v27, s7, v27
	v_cndmask_b32_e64 v66, v24, v25, s[4:5]
	v_cmp_gt_f32_e64 s[6:7], v26, v66
	s_waitcnt lgkmcnt(0)
	v_add_f32_e32 v63, s9, v63
	v_add_f32_e32 v62, s8, v62
	v_cndmask_b32_e64 v66, v66, v26, s[6:7]
	v_cmp_gt_f32_e64 s[8:9], v27, v66
	v_add_f32_e32 v65, s11, v65
	v_add_f32_e32 v64, s10, v64
	v_cndmask_b32_e64 v66, v66, v27, s[8:9]
	v_cmp_gt_f32_e64 s[10:11], v62, v66
	v_cndmask_b32_e64 v67, 0, 1, s[4:5]
	s_nop 0
	v_cndmask_b32_e64 v66, v66, v62, s[10:11]
	v_cmp_gt_f32_e64 s[12:13], v63, v66
	s_nop 1
	v_cndmask_b32_e64 v66, v66, v63, s[12:13]
	v_cmp_gt_f32_e64 s[14:15], v64, v66
	s_nop 1
	v_cndmask_b32_e64 v66, v66, v64, s[14:15]
	v_cmp_ngt_f32_e64 s[16:17], v65, v66
	s_and_b64 s[22:23], s[14:15], s[16:17]
	s_and_b64 s[4:5], s[6:7], exec
	v_readfirstlane_b32 s4, v67
	s_cselect_b32 s6, 2, s4
	s_and_b64 s[4:5], s[8:9], exec
	s_cselect_b32 s6, 3, s6
	s_and_b64 s[4:5], s[10:11], exec
	s_cselect_b32 s6, 4, s6
	s_and_b64 s[4:5], s[12:13], exec
	s_cselect_b32 s6, 5, s6
	s_and_b64 s[4:5], s[14:15], exec
	s_cselect_b32 s6, 6, s6
	s_and_b64 s[4:5], s[16:17], exec
	s_cselect_b32 s46, s6, 7
	s_cmp_lg_u32 s46, 5
	s_cselect_b64 s[20:21], -1, 0
	s_cmp_lg_u32 s46, 4
	s_cselect_b64 s[14:15], -1, 0
	s_cmp_lg_u32 s46, 3
	s_cselect_b64 s[12:13], -1, 0
	s_cmp_lg_u32 s46, 2
	s_cselect_b64 s[10:11], -1, 0
	s_cmp_lg_u32 s46, 1
	s_cselect_b64 s[8:9], -1, 0
	s_cmp_eq_u32 s46, 0
	s_cselect_b64 s[6:7], -1, 0
	v_cmp_nlt_f32_e64 s[4:5], s34, v24
	s_or_b64 s[4:5], s[6:7], s[4:5]
	s_nop 0
	v_cndmask_b32_e64 v24, v24, v197, s[4:5]
	v_cmp_gt_f32_e64 s[6:7], v25, v24
	s_and_b64 s[6:7], s[8:9], s[6:7]
	s_nop 0
	v_cndmask_b32_e64 v24, v24, v25, s[6:7]
	v_cmp_gt_f32_e64 s[8:9], v26, v24
	s_and_b64 s[8:9], s[10:11], s[8:9]
	v_cndmask_b32_e64 v25, 0, -1, s[4:5]
	v_cndmask_b32_e64 v24, v24, v26, s[8:9]
	v_cndmask_b32_e32 v26, v61, v60, vcc
	v_sub_f32_e32 v22, v22, v26
	v_mul_f32_e32 v22, 0x3fb8aa3b, v22
	v_sub_f32_e32 v23, v23, v26
	v_exp_f32_e32 v22, v22
	v_mul_f32_e32 v23, 0x3fb8aa3b, v23
	v_exp_f32_e32 v23, v23
	v_cmp_gt_f32_e64 s[10:11], v27, v24
	s_and_b64 s[10:11], s[12:13], s[10:11]
	v_add_f32_e32 v22, 0, v22
	v_cndmask_b32_e64 v24, v24, v27, s[10:11]
	v_cmp_gt_f32_e64 s[12:13], v62, v24
	v_add_f32_e32 v22, v23, v22
	v_sub_f32_e32 v23, v59, v26
	s_and_b64 s[12:13], s[14:15], s[12:13]
	v_mul_f32_e32 v23, 0x3fb8aa3b, v23
	v_cndmask_b32_e64 v24, v24, v62, s[12:13]
	v_exp_f32_e32 v23, v23
	v_cmp_gt_f32_e64 s[14:15], v63, v24
	s_and_b64 s[14:15], s[20:21], s[14:15]
	v_add_f32_e32 v22, v23, v22
	v_cndmask_b32_e64 v24, v24, v63, s[14:15]
	v_cmp_ngt_f32_e64 s[20:21], v64, v24
	v_sub_f32_e32 v23, v60, v26
	s_or_b64 s[20:21], s[22:23], s[20:21]
	v_mul_f32_e32 v23, 0x3fb8aa3b, v23
	v_cndmask_b32_e64 v24, v64, v24, s[20:21]
	v_exp_f32_e32 v23, v23
	v_cmp_gt_f32_e64 s[22:23], v65, v24
	s_and_b64 s[22:23], s[16:17], s[22:23]
	s_and_b64 s[4:5], s[6:7], exec
	v_readfirstlane_b32 s4, v25
	v_add_f32_e32 v22, v23, v22
	s_cselect_b32 s6, 1, s4
	v_rcp_f32_e32 v26, v22
	v_cndmask_b32_e64 v24, v24, v65, s[22:23]
	v_cndmask_b32_e64 v25, v65, v66, s[16:17]
	s_and_b64 s[4:5], s[8:9], exec
	v_fma_f32 v27, -v22, v26, 1.0
	v_fmac_f32_e32 v26, v27, v26
	v_div_fixup_f32 v26, v26, v22, 1.0
	v_sub_f32_e32 v22, v24, v25
	v_mul_f32_e32 v22, 0x3fb8aa3b, v22
	v_exp_f32_e32 v24, v22
	s_cselect_b32 s6, 2, s6
	s_and_b64 s[4:5], s[10:11], exec
	s_cselect_b32 s6, 3, s6
	v_add_f32_e32 v22, 1.0, v24
	v_rcp_f32_e32 v25, v22
	s_and_b64 s[4:5], s[12:13], exec
	s_cselect_b32 s6, 4, s6
	s_and_b64 s[4:5], s[14:15], exec
	s_cselect_b32 s6, 5, s6
	s_and_b64 s[4:5], s[20:21], exec
	v_fma_f32 v27, -v22, v25, 1.0
	s_cselect_b32 s6, s6, 6
	s_and_b64 s[4:5], s[22:23], exec
	v_fmac_f32_e32 v25, v27, v25
	s_cselect_b32 s8, 7, s6
	s_lshl_b32 s4, s49, 3
	s_ashr_i32 s81, s80, 31
	s_or_b32 s9, s46, s4
	s_add_i32 s12, s8, s4
	s_lshl_b64 s[4:5], s[80:81], 2
	s_add_u32 s6, s52, s4
	s_addc_u32 s7, s53, s5
	s_add_i32 s10, s80, 1
	s_ashr_i32 s11, s10, 31
	v_div_fixup_f32 v25, v25, v22, 1.0
	v_mov_b32_e32 v22, s9
	v_mov_b32_e32 v23, s12
	s_add_u32 s4, s40, s4
	global_store_dwordx2 v129, v[22:23], s[6:7]
	global_store_dword v129, v2, s[78:79]
	v_mul_f32_e32 v2, v26, v25
	s_addc_u32 s5, s41, s5
	global_store_dword v129, v2, s[4:5]
	s_lshl_b64 s[4:5], s[10:11], 2
	v_mul_f32_e32 v2, v26, v24
	s_add_u32 s4, s40, s4
	v_mul_f32_e32 v2, v2, v25
	s_addc_u32 s5, s41, s5
	global_store_dword v129, v2, s[4:5]
	s_waitcnt vmcnt(4)
	s_mov_b64 s[4:5], exec
	v_mbcnt_lo_u32_b32 v2, s4, 0
	v_mbcnt_hi_u32_b32 v2, s5, v2
	v_cmp_eq_u32_e32 vcc, 0, v2
	s_and_saveexec_b64 s[6:7], vcc
	s_cbranch_execz .LBB0_2148
	s_lshl_b32 s9, s9, 2
	s_add_i32 s9, s9, 0
	s_bcnt1_i32_b64 s4, s[4:5]
	v_mov_b32_e32 v2, s9
	v_mov_b32_e32 v22, s4
	ds_add_u32 v2, v22
